# dead zero-initialisations before fp8 packs removed (both 16-bit halves are written by the two converts); wait states they provided re-padded
# baseline (speedup 1.0000x reference)
.LBB0_181:
	v_mul_f32_e32 v106, 0x41800000, v106
	v_mul_f32_e32 v107, 0x41800000, v107
	v_mul_f32_e32 v108, 0x41800000, v108
	v_mul_f32_e32 v109, 0x41800000, v109
	v_mul_f32_e32 v110, 0x41800000, v110
	v_mul_f32_e32 v111, 0x41800000, v111
	v_mul_f32_e32 v112, 0x41800000, v112
	v_mul_f32_e32 v113, 0x41800000, v113
	v_mul_f32_e32 v114, 0x41800000, v114
	v_mul_f32_e32 v115, 0x41800000, v115
	v_mul_f32_e32 v116, 0x41800000, v116
	v_mul_f32_e32 v117, 0x41800000, v117
	v_mul_f32_e32 v118, 0x41800000, v118
	v_mul_f32_e32 v119, 0x41800000, v119
	v_mul_f32_e32 v120, 0x41800000, v120
	v_mul_f32_e32 v121, 0x41800000, v121
	v_cvt_f32_i32_e32 v143, v143
	v_cvt_f32_i32_e32 v145, v145
	v_cvt_f32_i32_e32 v144, v144
	v_cvt_f32_i32_e32 v142, v142
	v_cvt_f32_i32_e32 v139, v139
	v_cvt_f32_i32_e32 v141, v141
	v_cvt_f32_i32_e32 v140, v140
	v_cvt_f32_i32_e32 v138, v138
	s_waitcnt lgkmcnt(0)
	v_pk_mul_f32 v[190:191], v[116:117], v[188:189] op_sel_hi:[1,0]
	v_pk_mul_f32 v[192:193], v[114:115], v[188:189] op_sel_hi:[1,0]
	v_pk_mul_f32 v[144:145], v[190:191], v[144:145]
	v_pk_mul_f32 v[142:143], v[192:193], v[142:143]
	v_pk_mul_f32 v[190:191], v[120:121], v[188:189] op_sel_hi:[1,0]
	v_pk_mul_f32 v[192:193], v[118:119], v[188:189] op_sel_hi:[1,0]
	v_pk_mul_f32 v[140:141], v[190:191], v[140:141]
	v_pk_mul_f32 v[190:191], v[192:193], v[138:139]
	v_cvt_pk_fp8_f32 v138, v142, v143
	v_cvt_pk_fp8_f32 v139, v190, v191
	v_cvt_f32_i32_e32 v135, v135
	v_cvt_f32_i32_e32 v137, v137
	v_cvt_f32_i32_e32 v136, v136
	v_cvt_f32_i32_e32 v134, v134
	v_cvt_f32_i32_e32 v131, v131
	v_cvt_f32_i32_e32 v133, v133
	v_cvt_f32_i32_e32 v132, v132
	v_cvt_f32_i32_e32 v130, v130
	s_mul_hi_i32 s0, s10, 0x2aaaaaab
	v_cvt_pk_fp8_f32 v138, v144, v145 op_sel:[0,0,1]
	v_cvt_pk_fp8_f32 v139, v140, v141 op_sel:[0,0,1]
	v_pk_mul_f32 v[140:141], v[108:109], v[188:189] op_sel_hi:[1,0]
	v_pk_mul_f32 v[142:143], v[106:107], v[188:189] op_sel_hi:[1,0]
	s_lshr_b32 s1, s0, 31
	s_ashr_i32 s0, s0, 1
	v_pk_mul_f32 v[136:137], v[140:141], v[136:137]
	v_pk_mul_f32 v[134:135], v[142:143], v[134:135]
	v_pk_mul_f32 v[140:141], v[112:113], v[188:189] op_sel_hi:[1,0]
	v_pk_mul_f32 v[142:143], v[110:111], v[188:189] op_sel_hi:[1,0]
	s_add_i32 s0, s0, s1
	v_pk_mul_f32 v[132:133], v[140:141], v[132:133]
	v_pk_mul_f32 v[140:141], v[142:143], v[130:131]
	s_mul_i32 s1, s0, 12
	v_cvt_pk_fp8_f32 v130, v134, v135
	s_sub_i32 s1, s10, s1
	v_cvt_pk_fp8_f32 v131, v140, v141
	s_ashr_i32 s4, s1, 2
	s_lshl_b32 s31, s4, 1
	s_sub_i32 s35, 11, s31
	v_and_b32_e32 v194, 0x7cf, v146
	v_cvt_pk_fp8_f32 v131, v132, v133 op_sel:[0,0,1]
	v_lshlrev_b32_e32 v132, s35, v146
	v_and_b32_e32 v132, 0x7fe, v132
	v_lshrrev_b32_e32 v133, s31, v194
	v_add_u32_e32 v134, v132, v133
	v_or_b32_e32 v132, 16, v194
	v_lshlrev_b32_e32 v133, s35, v132
	v_cvt_f32_i32_e32 v129, v129
	v_cvt_f32_i32_e32 v128, v128
	v_and_b32_e32 v133, 0x7fe, v133
	v_lshrrev_b32_e32 v132, s31, v132
	v_cvt_f32_i32_e32 v123, v123
	v_cvt_f32_i32_e32 v122, v122
	v_cvt_pk_fp8_f32 v130, v136, v137 op_sel:[0,0,1]
	v_add_u32_e32 v135, v133, v132
	v_mov_b32_e32 v132, v189
	v_cvt_f32_i32_e32 v127, v127
	v_cvt_f32_i32_e32 v126, v126
	v_pk_mul_f32 v[136:137], v[120:121], v[132:133] op_sel_hi:[1,0]
	v_pk_mul_f32 v[140:141], v[118:119], v[132:133] op_sel_hi:[1,0]
	v_pk_mul_f32 v[128:129], v[136:137], v[128:129]
	v_pk_mul_f32 v[136:137], v[114:115], v[132:133] op_sel_hi:[1,0]
	v_cvt_f32_i32_e32 v125, v125
	v_cvt_f32_i32_e32 v124, v124
	v_pk_mul_f32 v[122:123], v[136:137], v[122:123]
	v_pk_mul_f32 v[126:127], v[140:141], v[126:127]
	v_cvt_pk_fp8_f32 v140, v122, v123
	v_cvt_pk_fp8_f32 v141, v126, v127
	v_pk_mul_f32 v[126:127], v[116:117], v[132:133] op_sel_hi:[1,0]
	v_pk_mul_f32 v[122:123], v[126:127], v[124:125]
	v_add_u32_e32 v143, 0x80, v146
	v_cvt_pk_fp8_f32 v140, v122, v123 op_sel:[0,0,1]
	v_cvt_pk_fp8_f32 v141, v128, v129 op_sel:[0,0,1]
	v_or_b32_e32 v122, 32, v194
	v_lshlrev_b32_e32 v123, s35, v122
	v_and_b32_e32 v123, 0x7fe, v123
	v_lshrrev_b32_e32 v122, s31, v122
	v_add_u32_e32 v123, v123, v122
	v_or_b32_e32 v122, 48, v194
	v_lshlrev_b32_e32 v124, s35, v122
	v_and_b32_e32 v124, 0x7fe, v124
	v_lshrrev_b32_e32 v122, s31, v122
	v_add_u32_e32 v142, v124, v122
	v_and_b32_e32 v124, 0x7cf, v143
	v_lshlrev_b32_e32 v122, s35, v124
	v_and_b32_e32 v122, 0x7fe, v122
	v_lshrrev_b32_e32 v125, s31, v124
	v_add_u32_e32 v125, v122, v125
	v_or_b32_e32 v122, 16, v124
	s_mul_hi_i32 s10, s0, 0x6000000
	s_mul_i32 s12, s0, 0x6000000
	s_lshl_b32 s0, s1, 22
	v_lshlrev_b32_e32 v126, s35, v122
	s_ashr_i32 s5, s4, 31
	s_and_b32 s1, s0, 0xc00000
	s_ashr_i32 s0, s11, 11
	v_and_b32_e32 v126, 0x7fe, v126
	v_lshrrev_b32_e32 v122, s31, v122
	s_add_u32 s12, s48, s12
	v_cmp_ne_u64_e32 vcc, 0, v[162:163]
	v_add_u32_e32 v126, v126, v122
	s_addc_u32 s13, s49, s10
	v_cndmask_b32_e32 v127, v134, v135, vcc
	v_cndmask_b32_e32 v122, v125, v126, vcc
	v_cmp_eq_u32_e32 vcc, 2, v162
	v_cmp_eq_u32_e64 s[10:11], 3, v162
	s_or_b64 s[14:15], s[10:11], vcc
	s_lshl_b64 s[4:5], s[4:5], 24
	v_cndmask_b32_e64 v127, v127, 0, s[14:15]
	v_lshlrev_b32_e32 v146, 7, v127
	s_add_u32 s4, s12, s4
	v_mov_b32_e32 v127, s0
	s_addc_u32 s5, s13, s5
	v_cndmask_b32_e64 v128, v127, 0, s[14:15]
	s_add_u32 s40, s4, s1
	v_ashrrev_i32_e32 v129, 31, v128
	s_addc_u32 s41, s5, 0
	v_lshlrev_b64 v[128:129], 18, v[128:129]
	v_lshl_add_u64 v[136:137], s[40:41], 0, v[128:129]
	v_lshl_add_u64 v[136:137], v[136:137], 0, v[146:147]
	v_lshl_add_u64 v[136:137], v[136:137], 0, s[20:21]
	v_cvt_f32_i32_e32 v103, v103
	v_cvt_f32_i32_e32 v102, v102
	v_lshl_add_u64 v[136:137], v[136:137], 0, v[160:161]
	v_permlane16_swap_b32_e32 v138, v140
	v_permlane16_swap_b32_e32 v139, v141
	v_lshl_add_u64 v[136:137], v[136:137], 0, v[164:165]
	global_store_dwordx4 v[136:137], v[138:141], off
	v_pk_mul_f32 v[136:137], v[112:113], v[132:133] op_sel_hi:[1,0]
	v_cvt_f32_i32_e32 v105, v105
	v_pk_mul_f32 v[138:139], v[110:111], v[132:133] op_sel_hi:[1,0]
	v_pk_mul_f32 v[102:103], v[138:139], v[102:103]
	v_cvt_f32_i32_e32 v104, v104
	v_cvt_pk_fp8_f32 v133, v102, v103
	v_cvt_f32_i32_e32 v99, v99
	v_cvt_f32_i32_e32 v98, v98
	v_pk_mul_f32 v[104:105], v[136:137], v[104:105]
	v_pk_mul_f32 v[136:137], v[106:107], v[132:133] op_sel_hi:[1,0]
	v_cvt_f32_i32_e32 v101, v101
	v_cvt_f32_i32_e32 v100, v100
	v_pk_mul_f32 v[98:99], v[136:137], v[98:99]
	v_pk_mul_f32 v[102:103], v[108:109], v[132:133] op_sel_hi:[1,0]
	v_cvt_pk_fp8_f32 v132, v98, v99
	v_pk_mul_f32 v[98:99], v[102:103], v[100:101]
	s_add_u32 s4, s40, 0x200000
	v_cvt_pk_fp8_f32 v132, v98, v99 op_sel:[0,0,1]
	s_addc_u32 s5, s41, 0
	v_cvt_pk_fp8_f32 v133, v104, v105 op_sel:[0,0,1]
	v_lshl_add_u64 v[98:99], s[4:5], 0, v[128:129]
	v_lshl_add_u64 v[98:99], v[98:99], 0, v[146:147]
	v_lshl_add_u64 v[98:99], v[98:99], 0, s[20:21]
	v_cvt_f32_i32_e32 v95, v95
	v_cvt_f32_i32_e32 v97, v97
	v_cvt_f32_i32_e32 v96, v96
	v_cvt_f32_i32_e32 v94, v94
	v_lshl_add_u64 v[98:99], v[98:99], 0, v[160:161]
	v_cvt_f32_i32_e32 v91, v91
	v_cvt_f32_i32_e32 v93, v93
	v_cvt_f32_i32_e32 v92, v92
	v_cvt_f32_i32_e32 v90, v90
	v_permlane16_swap_b32_e32 v130, v132
	v_permlane16_swap_b32_e32 v131, v133
	v_lshl_add_u64 v[98:99], v[98:99], 0, v[164:165]
	global_store_dwordx4 v[98:99], v[130:133], off
	v_pk_mul_f32 v[98:99], v[116:117], v[186:187] op_sel_hi:[1,0]
	v_pk_mul_f32 v[100:101], v[114:115], v[186:187] op_sel_hi:[1,0]
	v_pk_mul_f32 v[96:97], v[98:99], v[96:97]
	v_pk_mul_f32 v[94:95], v[100:101], v[94:95]
	v_pk_mul_f32 v[98:99], v[120:121], v[186:187] op_sel_hi:[1,0]
	v_pk_mul_f32 v[100:101], v[118:119], v[186:187] op_sel_hi:[1,0]
	v_pk_mul_f32 v[92:93], v[98:99], v[92:93]
	v_pk_mul_f32 v[98:99], v[100:101], v[90:91]
	v_cvt_pk_fp8_f32 v90, v94, v95
	v_cvt_pk_fp8_f32 v91, v98, v99
	v_cvt_f32_i32_e32 v87, v87
	v_cvt_f32_i32_e32 v89, v89
	v_cvt_f32_i32_e32 v88, v88
	v_cvt_f32_i32_e32 v86, v86
	v_cvt_f32_i32_e32 v79, v79
	v_cvt_f32_i32_e32 v81, v81
	v_cvt_f32_i32_e32 v80, v80
	v_cvt_f32_i32_e32 v78, v78
	v_cvt_pk_fp8_f32 v90, v96, v97 op_sel:[0,0,1]
	v_cvt_pk_fp8_f32 v91, v92, v93 op_sel:[0,0,1]
	v_pk_mul_f32 v[92:93], v[108:109], v[186:187] op_sel_hi:[1,0]
	v_pk_mul_f32 v[94:95], v[106:107], v[186:187] op_sel_hi:[1,0]
	v_pk_mul_f32 v[88:89], v[92:93], v[88:89]
	v_pk_mul_f32 v[86:87], v[94:95], v[86:87]
	v_pk_mul_f32 v[92:93], v[112:113], v[186:187] op_sel_hi:[1,0]
	v_pk_mul_f32 v[94:95], v[110:111], v[186:187] op_sel_hi:[1,0]
	v_pk_mul_f32 v[80:81], v[92:93], v[80:81]
	v_pk_mul_f32 v[92:93], v[94:95], v[78:79]
	v_cvt_pk_fp8_f32 v78, v86, v87
	v_cvt_pk_fp8_f32 v79, v92, v93
	v_cvt_f32_i32_e32 v85, v85
	v_cvt_f32_i32_e32 v84, v84
	v_cvt_pk_fp8_f32 v79, v80, v81 op_sel:[0,0,1]
	v_mov_b32_e32 v80, v187
	v_cvt_pk_fp8_f32 v78, v88, v89 op_sel:[0,0,1]
	v_pk_mul_f32 v[86:87], v[120:121], v[80:81] op_sel_hi:[1,0]
	v_cvt_f32_i32_e32 v75, v75
	v_cvt_f32_i32_e32 v74, v74
	v_cvt_f32_i32_e32 v83, v83
	v_cvt_f32_i32_e32 v82, v82
	v_pk_mul_f32 v[84:85], v[86:87], v[84:85]
	v_pk_mul_f32 v[88:89], v[118:119], v[80:81] op_sel_hi:[1,0]
	v_pk_mul_f32 v[86:87], v[114:115], v[80:81] op_sel_hi:[1,0]
	v_cvt_f32_i32_e32 v77, v77
	v_cvt_f32_i32_e32 v76, v76
	v_pk_mul_f32 v[74:75], v[86:87], v[74:75]
	v_pk_mul_f32 v[82:83], v[88:89], v[82:83]
	v_cvt_pk_fp8_f32 v92, v74, v75
	v_cvt_pk_fp8_f32 v93, v82, v83
	v_pk_mul_f32 v[82:83], v[116:117], v[80:81] op_sel_hi:[1,0]
	v_cndmask_b32_e32 v122, v122, v123, vcc
	v_pk_mul_f32 v[74:75], v[82:83], v[76:77]
	v_cmp_eq_u32_e32 vcc, 1, v166
	v_cvt_pk_fp8_f32 v92, v74, v75 op_sel:[0,0,1]
	v_cndmask_b32_e64 v122, v122, v142, s[10:11]
	v_cvt_pk_fp8_f32 v93, v84, v85 op_sel:[0,0,1]
	v_cndmask_b32_e32 v74, v134, v135, vcc
	v_cmp_eq_u32_e64 s[10:11], 2, v166
	s_ashr_i32 s1, s0, 31
	v_cmp_eq_u32_e64 s[12:13], 3, v166
	v_cndmask_b32_e64 v74, v74, v123, s[10:11]
	s_lshl_b64 s[0:1], s[0:1], 18
	v_cndmask_b32_e64 v74, v74, v142, s[12:13]
	s_add_u32 s42, s40, s0
	v_ashrrev_i32_e32 v75, 31, v74
	s_addc_u32 s43, s41, s1
	v_lshlrev_b64 v[74:75], 7, v[74:75]
	v_cvt_f32_i32_e32 v71, v71
	v_cvt_f32_i32_e32 v70, v70
	v_lshl_add_u64 v[76:77], s[42:43], 0, v[74:75]
	v_lshl_add_u64 v[76:77], v[76:77], 0, s[20:21]
	v_lshl_add_u64 v[76:77], v[76:77], 0, v[160:161]
	v_pk_mul_f32 v[82:83], v[110:111], v[80:81] op_sel_hi:[1,0]
	v_permlane16_swap_b32_e32 v90, v92
	v_permlane16_swap_b32_e32 v91, v93
	v_lshl_add_u64 v[76:77], v[76:77], 0, v[164:165]
	v_pk_mul_f32 v[70:71], v[82:83], v[70:71]
	global_store_dwordx4 v[76:77], v[90:93], off
	v_pk_mul_f32 v[76:77], v[112:113], v[80:81] op_sel_hi:[1,0]
	v_cvt_f32_i32_e32 v73, v73
	v_cvt_f32_i32_e32 v72, v72
	v_cvt_pk_fp8_f32 v81, v70, v71
	v_cvt_f32_i32_e32 v59, v59
	v_cvt_f32_i32_e32 v58, v58
	v_cvt_f32_i32_e32 v61, v61
	v_cvt_f32_i32_e32 v60, v60
	v_pk_mul_f32 v[72:73], v[76:77], v[72:73]
	v_pk_mul_f32 v[76:77], v[106:107], v[80:81] op_sel_hi:[1,0]
	v_cvt_f32_i32_e32 v55, v55
	v_cvt_f32_i32_e32 v57, v57
	v_cvt_f32_i32_e32 v56, v56
	v_cvt_f32_i32_e32 v54, v54
	v_pk_mul_f32 v[58:59], v[76:77], v[58:59]
	v_cvt_f32_i32_e32 v51, v51
	v_cvt_f32_i32_e32 v53, v53
	v_cvt_f32_i32_e32 v52, v52
	v_cvt_f32_i32_e32 v50, v50
	v_pk_mul_f32 v[70:71], v[108:109], v[80:81] op_sel_hi:[1,0]
	v_cvt_pk_fp8_f32 v80, v58, v59
	v_pk_mul_f32 v[58:59], v[70:71], v[60:61]
	v_pk_mul_f32 v[60:61], v[116:117], v[184:185] op_sel_hi:[1,0]
	v_pk_mul_f32 v[70:71], v[114:115], v[184:185] op_sel_hi:[1,0]
	v_pk_mul_f32 v[56:57], v[60:61], v[56:57]
	v_pk_mul_f32 v[54:55], v[70:71], v[54:55]
	v_pk_mul_f32 v[60:61], v[120:121], v[184:185] op_sel_hi:[1,0]
	v_pk_mul_f32 v[70:71], v[118:119], v[184:185] op_sel_hi:[1,0]
	v_pk_mul_f32 v[52:53], v[60:61], v[52:53]
	v_pk_mul_f32 v[60:61], v[70:71], v[50:51]
	v_cvt_pk_fp8_f32 v50, v54, v55
	v_cvt_pk_fp8_f32 v51, v60, v61
	v_cvt_pk_fp8_f32 v50, v56, v57 op_sel:[0,0,1]
	v_cvt_f32_i32_e32 v55, v69
	v_cvt_f32_i32_e32 v54, v68
	v_cvt_pk_fp8_f32 v51, v52, v53 op_sel:[0,0,1]
	v_cvt_f32_i32_e32 v53, v67
	v_cvt_f32_i32_e32 v52, v66
	v_cvt_pk_fp8_f32 v80, v58, v59 op_sel:[0,0,1]
	s_add_u32 s0, s4, s0
	v_cvt_pk_fp8_f32 v81, v72, v73 op_sel:[0,0,1]
	s_addc_u32 s1, s5, s1
	v_pk_mul_f32 v[56:57], v[108:109], v[184:185] op_sel_hi:[1,0]
	v_lshl_add_u64 v[58:59], s[0:1], 0, v[74:75]
	v_pk_mul_f32 v[60:61], v[106:107], v[184:185] op_sel_hi:[1,0]
	v_pk_mul_f32 v[54:55], v[56:57], v[54:55]
	v_cvt_f32_i32_e32 v57, v63
	v_cvt_f32_i32_e32 v56, v62
	v_lshl_add_u64 v[58:59], v[58:59], 0, s[20:21]
	v_pk_mul_f32 v[52:53], v[60:61], v[52:53]
	v_cvt_f32_i32_e32 v61, v65
	v_cvt_f32_i32_e32 v60, v64
	v_lshl_add_u64 v[58:59], v[58:59], 0, v[160:161]
	v_permlane16_swap_b32_e32 v78, v80
	v_permlane16_swap_b32_e32 v79, v81
	v_lshl_add_u64 v[58:59], v[58:59], 0, v[164:165]
	v_pk_mul_f32 v[64:65], v[110:111], v[184:185] op_sel_hi:[1,0]
	global_store_dwordx4 v[58:59], v[78:81], off
	v_pk_mul_f32 v[62:63], v[112:113], v[184:185] op_sel_hi:[1,0]
	v_pk_mul_f32 v[56:57], v[64:65], v[56:57]
	v_mov_b32_e32 v59, v54
	v_pk_mul_f32 v[60:61], v[62:63], v[60:61]
	v_mov_b32_e32 v62, v55
	v_cvt_pk_fp8_f32 v54, v52, v53
	v_cvt_f32_i32_e32 v39, v39
	v_cvt_f32_i32_e32 v38, v38
	v_cvt_pk_fp8_f32 v55, v56, v57
	v_cvt_f32_i32_e32 v35, v35
	v_cvt_f32_i32_e32 v34, v34
	v_mov_b32_e32 v56, v185
	v_cvt_f32_i32_e32 v41, v41
	v_cvt_f32_i32_e32 v40, v40
	v_mov_b32_e32 v52, v60
	v_mov_b32_e32 v53, v61
	v_pk_mul_f32 v[60:61], v[118:119], v[56:57] op_sel_hi:[1,0]
	v_cvt_pk_fp8_f32 v55, v52, v53 op_sel:[0,0,1]
	v_pk_mul_f32 v[38:39], v[60:61], v[38:39]
	v_pk_mul_f32 v[60:61], v[114:115], v[56:57] op_sel_hi:[1,0]
	v_pk_mul_f32 v[52:53], v[120:121], v[56:57] op_sel_hi:[1,0]
	v_cvt_f32_i32_e32 v37, v37
	v_cvt_f32_i32_e32 v36, v36
	v_pk_mul_f32 v[34:35], v[60:61], v[34:35]
	v_pk_mul_f32 v[40:41], v[52:53], v[40:41]
	v_cvt_pk_fp8_f32 v52, v34, v35
	v_cvt_pk_fp8_f32 v53, v38, v39
	v_pk_mul_f32 v[38:39], v[116:117], v[56:57] op_sel_hi:[1,0]
	v_ashrrev_i32_e32 v58, 11, v143
	v_pk_mul_f32 v[34:35], v[38:39], v[36:37]
	v_cvt_pk_fp8_f32 v52, v34, v35 op_sel:[0,0,1]
	v_cvt_pk_fp8_f32 v53, v40, v41 op_sel:[0,0,1]
	v_cndmask_b32_e64 v34, v58, v127, s[14:15]
	v_ashrrev_i32_e32 v35, 31, v34
	v_lshlrev_b64 v[34:35], 18, v[34:35]
	v_ashrrev_i32_e32 v123, 31, v122
	v_lshl_add_u64 v[36:37], s[40:41], 0, v[34:35]
	v_lshlrev_b64 v[38:39], 7, v[122:123]
	v_lshl_add_u64 v[36:37], v[36:37], 0, v[38:39]
	v_lshl_add_u64 v[36:37], v[36:37], 0, s[20:21]
	v_cvt_f32_i32_e32 v41, v47
	v_cvt_f32_i32_e32 v40, v46
	v_lshl_add_u64 v[36:37], v[36:37], 0, v[160:161]
	v_permlane16_swap_b32_e32 v50, v52
	v_permlane16_swap_b32_e32 v51, v53
	v_lshl_add_u64 v[36:37], v[36:37], 0, v[164:165]
	global_store_dwordx4 v[36:37], v[50:53], off
	v_cvt_f32_i32_e32 v37, v49
	v_cvt_f32_i32_e32 v36, v48
	v_pk_mul_f32 v[48:49], v[110:111], v[56:57] op_sel_hi:[1,0]
	v_pk_mul_f32 v[46:47], v[112:113], v[56:57] op_sel_hi:[1,0]
	v_pk_mul_f32 v[40:41], v[48:49], v[40:41]
	v_cvt_pk_fp8_f32 v57, v40, v41
	v_cvt_f32_i32_e32 v43, v43
	v_cvt_f32_i32_e32 v42, v42
	v_pk_mul_f32 v[36:37], v[46:47], v[36:37]
	v_pk_mul_f32 v[46:47], v[106:107], v[56:57] op_sel_hi:[1,0]
	v_cvt_f32_i32_e32 v45, v45
	v_cvt_f32_i32_e32 v44, v44
	v_pk_mul_f32 v[42:43], v[46:47], v[42:43]
	v_pk_mul_f32 v[40:41], v[108:109], v[56:57] op_sel_hi:[1,0]
	v_cvt_pk_fp8_f32 v56, v42, v43
	v_pk_mul_f32 v[40:41], v[40:41], v[44:45]
	v_cvt_pk_fp8_f32 v54, v59, v62 op_sel:[0,0,1]
	v_cvt_pk_fp8_f32 v56, v40, v41 op_sel:[0,0,1]
	v_cvt_pk_fp8_f32 v57, v36, v37 op_sel:[0,0,1]
	v_lshl_add_u64 v[34:35], s[4:5], 0, v[34:35]
	v_lshl_add_u64 v[34:35], v[34:35], 0, v[38:39]
	v_lshl_add_u64 v[34:35], v[34:35], 0, s[20:21]
	v_lshl_add_u64 v[34:35], v[34:35], 0, v[160:161]
	v_permlane16_swap_b32_e32 v54, v56
	v_permlane16_swap_b32_e32 v55, v57
	v_lshl_add_u64 v[34:35], v[34:35], 0, v[164:165]
	global_store_dwordx4 v[34:35], v[54:57], off
	v_or_b32_e32 v34, 32, v124
	v_cvt_f32_i32_e32 v23, v23
	v_cvt_f32_i32_e32 v25, v25
	v_cvt_f32_i32_e32 v24, v24
	v_cvt_f32_i32_e32 v22, v22
	v_lshlrev_b32_e32 v35, s35, v34
	v_cvt_f32_i32_e32 v19, v19
	v_cvt_f32_i32_e32 v21, v21
	v_cvt_f32_i32_e32 v20, v20
	v_cvt_f32_i32_e32 v18, v18
	v_and_b32_e32 v35, 0x7fe, v35
	v_lshrrev_b32_e32 v34, s31, v34
	v_add_u32_e32 v38, v35, v34
	v_pk_mul_f32 v[34:35], v[116:117], v[182:183] op_sel_hi:[1,0]
	v_pk_mul_f32 v[36:37], v[114:115], v[182:183] op_sel_hi:[1,0]
	v_pk_mul_f32 v[24:25], v[34:35], v[24:25]
	v_pk_mul_f32 v[22:23], v[36:37], v[22:23]
	v_pk_mul_f32 v[34:35], v[120:121], v[182:183] op_sel_hi:[1,0]
	v_pk_mul_f32 v[36:37], v[118:119], v[182:183] op_sel_hi:[1,0]
	v_pk_mul_f32 v[20:21], v[34:35], v[20:21]
	v_pk_mul_f32 v[34:35], v[36:37], v[18:19]
	v_cvt_pk_fp8_f32 v18, v22, v23
	v_cvt_pk_fp8_f32 v19, v34, v35
	v_cvt_pk_fp8_f32 v18, v24, v25 op_sel:[0,0,1]
	v_cvt_f32_i32_e32 v23, v33
	v_cvt_f32_i32_e32 v22, v32
	v_cvt_pk_fp8_f32 v19, v20, v21 op_sel:[0,0,1]
	v_cvt_f32_i32_e32 v21, v31
	v_cvt_f32_i32_e32 v20, v30
	v_pk_mul_f32 v[24:25], v[108:109], v[182:183] op_sel_hi:[1,0]
	v_cvt_f32_i32_e32 v29, v29
	v_pk_mul_f32 v[22:23], v[24:25], v[22:23]
	v_cvt_f32_i32_e32 v25, v27
	v_cvt_f32_i32_e32 v28, v28
	v_cvt_f32_i32_e32 v24, v26
	v_pk_mul_f32 v[30:31], v[106:107], v[182:183] op_sel_hi:[1,0]
	v_pk_mul_f32 v[26:27], v[112:113], v[182:183] op_sel_hi:[1,0]
	v_pk_mul_f32 v[20:21], v[30:31], v[20:21]
	v_pk_mul_f32 v[30:31], v[110:111], v[182:183] op_sel_hi:[1,0]
	v_pk_mul_f32 v[26:27], v[26:27], v[28:29]
	v_pk_mul_f32 v[24:25], v[30:31], v[24:25]
	v_mov_b32_e32 v28, v22
	v_mov_b32_e32 v29, v23
	v_cvt_pk_fp8_f32 v22, v20, v21
	v_cvt_pk_fp8_f32 v23, v24, v25
	v_cvt_f32_i32_e32 v7, v7
	v_cvt_pk_fp8_f32 v23, v26, v27 op_sel:[0,0,1]
	v_or_b32_e32 v20, 48, v124
	v_lshlrev_b32_e32 v21, s35, v20
	v_cvt_f32_i32_e32 v6, v6
	v_and_b32_e32 v21, 0x7fe, v21
	v_lshrrev_b32_e32 v20, s31, v20
	v_cvt_f32_i32_e32 v3, v3
	v_cvt_f32_i32_e32 v2, v2
	v_add_u32_e32 v25, v21, v20
	v_mov_b32_e32 v24, v183
	v_cvt_f32_i32_e32 v9, v9
	v_cvt_f32_i32_e32 v8, v8
	v_pk_mul_f32 v[26:27], v[118:119], v[24:25] op_sel_hi:[1,0]
	v_pk_mul_f32 v[20:21], v[120:121], v[24:25] op_sel_hi:[1,0]
	v_pk_mul_f32 v[6:7], v[26:27], v[6:7]
	v_pk_mul_f32 v[26:27], v[114:115], v[24:25] op_sel_hi:[1,0]
	v_cvt_f32_i32_e32 v5, v5
	v_cvt_f32_i32_e32 v4, v4
	v_pk_mul_f32 v[2:3], v[26:27], v[2:3]
	v_pk_mul_f32 v[8:9], v[20:21], v[8:9]
	v_cvt_pk_fp8_f32 v20, v2, v3
	v_cvt_pk_fp8_f32 v21, v6, v7
	v_pk_mul_f32 v[6:7], v[116:117], v[24:25] op_sel_hi:[1,0]
	v_pk_mul_f32 v[2:3], v[6:7], v[4:5]
	v_cndmask_b32_e32 v6, v125, v126, vcc
	v_cndmask_b32_e64 v6, v6, v38, s[10:11]
	v_cvt_pk_fp8_f32 v20, v2, v3 op_sel:[0,0,1]
	v_ashrrev_i32_e32 v59, 31, v58
	v_cndmask_b32_e64 v6, v6, v25, s[12:13]
	v_cvt_pk_fp8_f32 v21, v8, v9 op_sel:[0,0,1]
	v_lshlrev_b64 v[2:3], 18, v[58:59]
	v_ashrrev_i32_e32 v7, 31, v6
	v_lshl_add_u64 v[4:5], s[40:41], 0, v[2:3]
	v_lshlrev_b64 v[6:7], 7, v[6:7]
	v_lshl_add_u64 v[4:5], v[4:5], 0, v[6:7]
	v_lshl_add_u64 v[4:5], v[4:5], 0, s[20:21]
	v_cvt_f32_i32_e32 v9, v15
	v_cvt_f32_i32_e32 v8, v14
	v_lshl_add_u64 v[4:5], v[4:5], 0, v[160:161]
	v_permlane16_swap_b32_e32 v18, v20
	v_permlane16_swap_b32_e32 v19, v21
	v_lshl_add_u64 v[4:5], v[4:5], 0, v[164:165]
	global_store_dwordx4 v[4:5], v[18:21], off
	v_cvt_f32_i32_e32 v5, v17
	v_cvt_f32_i32_e32 v4, v16
	v_pk_mul_f32 v[16:17], v[110:111], v[24:25] op_sel_hi:[1,0]
	v_pk_mul_f32 v[14:15], v[112:113], v[24:25] op_sel_hi:[1,0]
	v_pk_mul_f32 v[8:9], v[16:17], v[8:9]
	v_cvt_pk_fp8_f32 v25, v8, v9
	v_cvt_f32_i32_e32 v11, v11
	v_cvt_f32_i32_e32 v10, v10
	v_pk_mul_f32 v[4:5], v[14:15], v[4:5]
	v_pk_mul_f32 v[14:15], v[106:107], v[24:25] op_sel_hi:[1,0]
	v_cvt_f32_i32_e32 v13, v13
	v_cvt_f32_i32_e32 v12, v12
	v_pk_mul_f32 v[10:11], v[14:15], v[10:11]
	v_pk_mul_f32 v[8:9], v[108:109], v[24:25] op_sel_hi:[1,0]
	v_cvt_pk_fp8_f32 v24, v10, v11
	v_pk_mul_f32 v[8:9], v[8:9], v[12:13]
	v_cvt_pk_fp8_f32 v22, v28, v29 op_sel:[0,0,1]
	v_cvt_pk_fp8_f32 v24, v8, v9 op_sel:[0,0,1]
	v_cvt_pk_fp8_f32 v25, v4, v5 op_sel:[0,0,1]
	v_lshl_add_u64 v[2:3], s[4:5], 0, v[2:3]
	v_lshl_add_u64 v[2:3], v[2:3], 0, v[6:7]
	v_lshl_add_u64 v[2:3], v[2:3], 0, s[20:21]
	v_lshl_add_u64 v[2:3], v[2:3], 0, v[160:161]
	v_permlane16_swap_b32_e32 v22, v24
	v_permlane16_swap_b32_e32 v23, v25
	v_lshl_add_u64 v[2:3], v[2:3], 0, v[164:165]
	global_store_dwordx4 v[2:3], v[22:25], off
	s_and_b64 vcc, exec, s[8:9]
	s_mov_b64 s[0:1], -1
	s_cbranch_vccnz .LBB0_152

.LBB0_187:
	v_mul_f32_e32 v151, 0x42800000, v54
	v_mul_f32_e32 v153, 0x42800000, v58
	v_cvt_pk_fp8_f32 v152, v151, v153
	v_mul_f32_e32 v151, 0x42800000, v78
	v_mul_f32_e32 v156, 0x42800000, v82
	v_cvt_pk_fp8_f32 v153, v151, v156
	v_mul_f32_e32 v154, 0x42800000, v66
	v_mul_f32_e32 v155, 0x42800000, v70
	v_cvt_pk_fp8_f32 v152, v154, v155 op_sel:[0,0,1]
	v_mul_f32_e32 v151, 0x42800000, v90
	v_mul_f32_e32 v154, 0x42800000, v94
	v_cvt_pk_fp8_f32 v153, v151, v154 op_sel:[0,0,1]
	v_mul_f32_e32 v151, 0x42800000, v98
	v_mul_f32_e32 v155, 0x42800000, v102
	v_cvt_pk_fp8_f32 v154, v151, v155
	v_mul_f32_e32 v151, 0x42800000, v114
	v_mul_f32_e32 v158, 0x42800000, v118
	v_cvt_pk_fp8_f32 v155, v151, v158
	v_mul_f32_e32 v156, 0x42800000, v106
	v_mul_f32_e32 v157, 0x42800000, v110
	v_cvt_pk_fp8_f32 v154, v156, v157 op_sel:[0,0,1]
	v_mul_f32_e32 v151, 0x42800000, v122
	v_mul_f32_e32 v156, 0x42800000, v126
	v_cvt_pk_fp8_f32 v155, v151, v156 op_sel:[0,0,1]
	v_mul_f32_e32 v151, 0x42800000, v55
	v_mul_f32_e32 v157, 0x42800000, v59
	v_cvt_pk_fp8_f32 v156, v151, v157
	v_mul_f32_e32 v151, 0x42800000, v79
	v_mul_f32_e32 v160, 0x42800000, v83
	v_cvt_pk_fp8_f32 v157, v151, v160
	v_mul_f32_e32 v158, 0x42800000, v67
	v_mul_f32_e32 v159, 0x42800000, v71
	v_cvt_pk_fp8_f32 v156, v158, v159 op_sel:[0,0,1]
	v_mul_f32_e32 v151, 0x42800000, v91
	v_mul_f32_e32 v158, 0x42800000, v95
	v_cvt_pk_fp8_f32 v157, v151, v158 op_sel:[0,0,1]
	v_mul_f32_e32 v151, 0x42800000, v99
	v_mul_f32_e32 v159, 0x42800000, v103
	v_cvt_pk_fp8_f32 v158, v151, v159
	v_mul_f32_e32 v151, 0x42800000, v115
	v_mul_f32_e32 v162, 0x42800000, v119
	v_cvt_pk_fp8_f32 v159, v151, v162
	v_mul_f32_e32 v160, 0x42800000, v107
	v_mul_f32_e32 v161, 0x42800000, v111
	v_cvt_pk_fp8_f32 v158, v160, v161 op_sel:[0,0,1]
	v_mul_f32_e32 v151, 0x42800000, v123
	v_mul_f32_e32 v160, 0x42800000, v127
	v_cvt_pk_fp8_f32 v159, v151, v160 op_sel:[0,0,1]
	v_mul_f32_e32 v151, 0x42800000, v56
	v_mul_f32_e32 v161, 0x42800000, v60
	v_cvt_pk_fp8_f32 v160, v151, v161
	v_mul_f32_e32 v151, 0x42800000, v80
	v_mul_f32_e32 v164, 0x42800000, v84
	s_ashr_i32 s0, s26, 31
	v_cvt_pk_fp8_f32 v161, v151, v164
	s_lshr_b32 s0, s0, 19
	s_add_i32 s0, s26, s0
	v_mul_f32_e32 v162, 0x42800000, v68
	v_mul_f32_e32 v163, 0x42800000, v72
	s_and_b32 s0, s0, 0xffffe000
	v_cvt_pk_fp8_f32 v160, v162, v163 op_sel:[0,0,1]
	v_mul_f32_e32 v151, 0x42800000, v92
	v_mul_f32_e32 v162, 0x42800000, v96
	s_sub_i32 s1, s26, s0
	v_cvt_pk_fp8_f32 v161, v151, v162 op_sel:[0,0,1]
	v_mul_f32_e32 v151, 0x42800000, v100
	v_mul_f32_e32 v163, 0x42800000, v104
	s_sext_i32_i16 s0, s1
	v_cvt_pk_fp8_f32 v162, v151, v163
	v_mul_f32_e32 v151, 0x42800000, v116
	v_mul_f32_e32 v166, 0x42800000, v120
	s_bfe_u32 s0, s0, 0x80017
	v_cvt_pk_fp8_f32 v163, v151, v166
	s_add_i32 s0, s1, s0
	s_sext_i32_i16 s4, s0
	v_mul_f32_e32 v164, 0x42800000, v108
	v_mul_f32_e32 v165, 0x42800000, v112
	s_lshr_b32 s0, s4, 8
	s_and_b32 s4, s4, 0xffffff00
	v_cvt_pk_fp8_f32 v162, v164, v165 op_sel:[0,0,1]
	v_mul_f32_e32 v151, 0x42800000, v124
	v_mul_f32_e32 v164, 0x42800000, v128
	s_sub_i32 s4, s1, s4
	v_cvt_pk_fp8_f32 v163, v151, v164 op_sel:[0,0,1]
	v_mul_f32_e32 v151, 0x42800000, v57
	v_mul_f32_e32 v165, 0x42800000, v61
	s_bfe_u32 s1, s4, 0x4001b
	v_cvt_pk_fp8_f32 v164, v151, v165
	v_mul_f32_e32 v151, 0x42800000, v81
	v_mul_f32_e32 v168, 0x42800000, v85
	s_add_i32 s1, s4, s1
	v_cvt_pk_fp8_f32 v165, v151, v168
	s_sext_i32_i16 s1, s1
	s_add_i32 s25, s26, s90
	v_mul_f32_e32 v166, 0x42800000, v69
	v_mul_f32_e32 v167, 0x42800000, v73
	s_ashr_i32 s26, s1, 4
	s_bfe_i64 s[0:1], s[0:1], 0x100000
	v_cvt_pk_fp8_f32 v164, v166, v167 op_sel:[0,0,1]
	v_mul_f32_e32 v151, 0x42800000, v93
	v_mul_f32_e32 v166, 0x42800000, v97
	s_lshl_b64 s[0:1], s[0:1], 23
	v_cvt_pk_fp8_f32 v165, v151, v166 op_sel:[0,0,1]
	v_mul_f32_e32 v151, 0x42800000, v101
	v_mul_f32_e32 v167, 0x42800000, v105
	s_add_u32 s0, s5, s0
	v_cvt_pk_fp8_f32 v166, v151, v167
	v_mul_f32_e32 v151, 0x42800000, v117
	v_mul_f32_e32 v170, 0x42800000, v121
	s_addc_u32 s1, s6, s1
	s_lshl_b32 s27, s26, 7
	v_cvt_pk_fp8_f32 v167, v151, v170
	s_ashr_i32 s28, s27, 31
	s_add_u32 s0, s0, s27
	v_mul_f32_e32 v168, 0x42800000, v109
	v_mul_f32_e32 v169, 0x42800000, v113
	s_addc_u32 s1, s1, s28
	s_lshl_b32 s26, s26, 12
	s_lshl_b32 s4, s4, 8
	v_cvt_pk_fp8_f32 v166, v168, v169 op_sel:[0,0,1]
	v_mul_f32_e32 v151, 0x42800000, v125
	v_mul_f32_e32 v168, 0x42800000, v129
	s_sub_i32 s4, s4, s26
	v_cvt_pk_fp8_f32 v167, v151, v168 op_sel:[0,0,1]
	v_add_u32_e32 v151, s4, v138
	ds_write_b128 v146, v[152:155] offset:36864
	ds_write_b128 v146, v[156:159] offset:37008
	ds_write_b128 v146, v[160:163] offset:37152
	ds_write_b128 v146, v[164:167] offset:37296
	v_lshlrev_b32_e32 v152, 1, v151
	v_ashrrev_i32_e32 v151, 4, v151
	v_and_b32_e32 v152, 0xf00, v152
	v_and_b32_e32 v151, 0xffffff80, v151
	v_add_u32_e32 v151, v152, v151
	s_waitcnt lgkmcnt(0)
	s_barrier
	v_or_b32_e32 v156, v151, v139
	ds_read_b128 v[152:155], v147 offset:36864
	v_ashrrev_i32_e32 v157, 31, v156
	v_lshlrev_b64 v[156:157], 11, v[156:157]
	v_lshl_add_u64 v[156:157], s[0:1], 0, v[156:157]
	v_lshl_add_u64 v[160:161], v[156:157], 0, v[132:133]
	v_add_u32_e32 v151, s4, v140
	ds_read_b128 v[156:159], v148 offset:36864
	s_waitcnt lgkmcnt(1)
	global_store_dwordx4 v[160:161], v[152:155], off nt
	s_cmpk_gt_i32 s25, 0x1fff
	s_nop 0
	v_lshlrev_b32_e32 v152, 1, v151
	v_ashrrev_i32_e32 v151, 4, v151
	v_and_b32_e32 v152, 0xf00, v152
	v_and_b32_e32 v151, 0xffffff80, v151
	v_add_u32_e32 v151, v152, v151
	v_or_b32_e32 v152, v151, v141
	v_ashrrev_i32_e32 v153, 31, v152
	v_lshlrev_b64 v[152:153], 11, v[152:153]
	v_lshl_add_u64 v[152:153], s[0:1], 0, v[152:153]
	v_lshl_add_u64 v[152:153], v[152:153], 0, v[134:135]
	v_add_u32_e32 v151, s4, v142
	s_waitcnt lgkmcnt(0)
	global_store_dwordx4 v[152:153], v[156:159], off nt
	v_lshlrev_b32_e32 v152, 1, v151
	v_ashrrev_i32_e32 v151, 4, v151
	v_and_b32_e32 v152, 0xf00, v152
	v_and_b32_e32 v151, 0xffffff80, v151
	v_add_u32_e32 v151, v152, v151
	v_or_b32_e32 v156, v151, v143
	ds_read_b128 v[152:155], v149 offset:36864
	v_ashrrev_i32_e32 v157, 31, v156
	v_lshlrev_b64 v[156:157], 11, v[156:157]
	v_lshl_add_u64 v[156:157], s[0:1], 0, v[156:157]
	v_lshl_add_u64 v[160:161], v[156:157], 0, v[132:133]
	v_add_u32_e32 v151, s4, v144
	ds_read_b128 v[156:159], v150 offset:36864
	s_waitcnt lgkmcnt(1)
	global_store_dwordx4 v[160:161], v[152:155], off nt
	s_nop 1
	v_lshlrev_b32_e32 v152, 1, v151
	v_ashrrev_i32_e32 v151, 4, v151
	v_and_b32_e32 v152, 0xf00, v152
	v_and_b32_e32 v151, 0xffffff80, v151
	v_add_u32_e32 v151, v152, v151
	v_or_b32_e32 v152, v151, v145
	v_ashrrev_i32_e32 v153, 31, v152
	v_lshlrev_b64 v[152:153], 11, v[152:153]
	v_lshl_add_u64 v[152:153], s[0:1], 0, v[152:153]
	v_lshl_add_u64 v[152:153], v[152:153], 0, v[136:137]
	s_cselect_b64 s[0:1], -1, 0
	s_waitcnt lgkmcnt(0)
	global_store_dwordx4 v[152:153], v[156:159], off nt

.Lcvgu_a:
	v_mul_f32_e32 v151, 0x42800000, v30
	v_mul_f32_e32 v153, 0x42800000, v2
	v_cvt_pk_fp8_f32 v152, v151, v153
	v_mul_f32_e32 v151, 0x42800000, v14
	v_mul_f32_e32 v156, 0x42800000, v18
	v_cvt_pk_fp8_f32 v153, v151, v156
	v_mul_f32_e32 v154, 0x42800000, v6
	v_mul_f32_e32 v155, 0x42800000, v10
	v_cvt_pk_fp8_f32 v152, v154, v155 op_sel:[0,0,1]
	v_mul_f32_e32 v151, 0x42800000, v22
	v_mul_f32_e32 v154, 0x42800000, v26
	v_cvt_pk_fp8_f32 v153, v151, v154 op_sel:[0,0,1]
	v_mul_f32_e32 v151, 0x42800000, v34
	v_mul_f32_e32 v155, 0x42800000, v38
	v_cvt_pk_fp8_f32 v154, v151, v155
	v_mul_f32_e32 v151, 0x42800000, v50
	v_mul_f32_e32 v158, 0x42800000, v62
	v_cvt_pk_fp8_f32 v155, v151, v158
	v_mul_f32_e32 v156, 0x42800000, v42
	v_mul_f32_e32 v157, 0x42800000, v46
	v_cvt_pk_fp8_f32 v154, v156, v157 op_sel:[0,0,1]
	v_mul_f32_e32 v151, 0x42800000, v74
	v_mul_f32_e32 v156, 0x42800000, v86
	v_cvt_pk_fp8_f32 v155, v151, v156 op_sel:[0,0,1]
	v_mul_f32_e32 v151, 0x42800000, v31
	v_mul_f32_e32 v157, 0x42800000, v3
	v_cvt_pk_fp8_f32 v156, v151, v157
	v_mul_f32_e32 v151, 0x42800000, v15
	v_mul_f32_e32 v160, 0x42800000, v19
	v_cvt_pk_fp8_f32 v157, v151, v160
	v_mul_f32_e32 v158, 0x42800000, v7
	v_mul_f32_e32 v159, 0x42800000, v11
	v_cvt_pk_fp8_f32 v156, v158, v159 op_sel:[0,0,1]
	v_mul_f32_e32 v151, 0x42800000, v23
	v_mul_f32_e32 v158, 0x42800000, v27
	v_cvt_pk_fp8_f32 v157, v151, v158 op_sel:[0,0,1]
	v_mul_f32_e32 v151, 0x42800000, v35
	v_mul_f32_e32 v159, 0x42800000, v39
	v_cvt_pk_fp8_f32 v158, v151, v159
	v_mul_f32_e32 v151, 0x42800000, v51
	v_mul_f32_e32 v162, 0x42800000, v63
	v_cvt_pk_fp8_f32 v159, v151, v162
	v_mul_f32_e32 v160, 0x42800000, v43
	v_mul_f32_e32 v161, 0x42800000, v47
	v_cvt_pk_fp8_f32 v158, v160, v161 op_sel:[0,0,1]
	v_mul_f32_e32 v151, 0x42800000, v75
	v_mul_f32_e32 v160, 0x42800000, v87
	v_cvt_pk_fp8_f32 v159, v151, v160 op_sel:[0,0,1]
	v_mul_f32_e32 v151, 0x42800000, v32
	v_mul_f32_e32 v161, 0x42800000, v4
	v_cvt_pk_fp8_f32 v160, v151, v161
	v_mul_f32_e32 v151, 0x42800000, v16
	v_mul_f32_e32 v164, 0x42800000, v20
	s_ashr_i32 s4, s25, 31
	v_cvt_pk_fp8_f32 v161, v151, v164
	s_lshr_b32 s4, s4, 19
	s_add_i32 s4, s25, s4
	v_mul_f32_e32 v162, 0x42800000, v8
	v_mul_f32_e32 v163, 0x42800000, v12
	s_and_b32 s4, s4, 0xffffe000
	v_cvt_pk_fp8_f32 v160, v162, v163 op_sel:[0,0,1]
	v_mul_f32_e32 v151, 0x42800000, v24
	v_mul_f32_e32 v162, 0x42800000, v28
	s_sub_i32 s27, s25, s4
	v_cvt_pk_fp8_f32 v161, v151, v162 op_sel:[0,0,1]
	v_mul_f32_e32 v151, 0x42800000, v36
	v_mul_f32_e32 v163, 0x42800000, v40
	s_sext_i32_i16 s4, s27
	v_cvt_pk_fp8_f32 v162, v151, v163
	v_mul_f32_e32 v151, 0x42800000, v52
	v_mul_f32_e32 v166, 0x42800000, v64
	s_bfe_u32 s4, s4, 0x80017
	v_cvt_pk_fp8_f32 v163, v151, v166
	s_add_i32 s4, s27, s4
	s_sext_i32_i16 s28, s4
	v_mul_f32_e32 v164, 0x42800000, v44
	v_mul_f32_e32 v165, 0x42800000, v48
	s_lshr_b32 s4, s28, 8
	s_and_b32 s28, s28, 0xffffff00
	v_cvt_pk_fp8_f32 v162, v164, v165 op_sel:[0,0,1]
	v_mul_f32_e32 v151, 0x42800000, v76
	v_mul_f32_e32 v164, 0x42800000, v88
	s_sub_i32 s27, s27, s28
	v_cvt_pk_fp8_f32 v163, v151, v164 op_sel:[0,0,1]
	v_mul_f32_e32 v151, 0x42800000, v33
	v_mul_f32_e32 v165, 0x42800000, v5
	s_bfe_u32 s28, s27, 0x4001b
	v_cvt_pk_fp8_f32 v164, v151, v165
	v_mul_f32_e32 v151, 0x42800000, v17
	v_mul_f32_e32 v168, 0x42800000, v21
	s_add_i32 s28, s27, s28
	v_cvt_pk_fp8_f32 v165, v151, v168
	s_sext_i32_i16 s28, s28
	v_mul_f32_e32 v166, 0x42800000, v9
	v_mul_f32_e32 v167, 0x42800000, v13
	s_ashr_i32 s30, s28, 4
	s_bfe_i64 s[28:29], s[4:5], 0x100000
	v_cvt_pk_fp8_f32 v164, v166, v167 op_sel:[0,0,1]
	v_mul_f32_e32 v151, 0x42800000, v25
	v_mul_f32_e32 v166, 0x42800000, v29
	s_lshl_b64 s[28:29], s[28:29], 23
	v_cvt_pk_fp8_f32 v165, v151, v166 op_sel:[0,0,1]
	v_mul_f32_e32 v151, 0x42800000, v37
	v_mul_f32_e32 v167, 0x42800000, v41
	s_add_u32 s4, s5, s28
	v_cvt_pk_fp8_f32 v166, v151, v167
	v_mul_f32_e32 v151, 0x42800000, v53
	v_mul_f32_e32 v170, 0x42800000, v65
	s_addc_u32 s29, s6, s29
	s_lshl_b32 s28, s30, 7
	v_cvt_pk_fp8_f32 v167, v151, v170
	s_ashr_i32 s31, s28, 31
	s_add_u32 s28, s4, s28
	v_mul_f32_e32 v168, 0x42800000, v45
	v_mul_f32_e32 v169, 0x42800000, v49
	s_addc_u32 s29, s29, s31
	s_lshl_b32 s4, s30, 12
	s_lshl_b32 s27, s27, 8
	v_cvt_pk_fp8_f32 v166, v168, v169 op_sel:[0,0,1]
	v_mul_f32_e32 v151, 0x42800000, v77
	v_mul_f32_e32 v168, 0x42800000, v89
	s_sub_i32 s4, s27, s4
	v_cvt_pk_fp8_f32 v167, v151, v168 op_sel:[0,0,1]
	v_add_u32_e32 v151, s4, v138
	ds_write_b128 v146, v[152:155]
	ds_write_b128 v146, v[156:159] offset:144
	ds_write_b128 v146, v[160:163] offset:288
	ds_write_b128 v146, v[164:167] offset:432
	v_lshlrev_b32_e32 v152, 1, v151
	v_ashrrev_i32_e32 v151, 4, v151
	v_and_b32_e32 v152, 0xf00, v152
	v_and_b32_e32 v151, 0xffffff80, v151
	v_add_u32_e32 v151, v152, v151
	s_waitcnt lgkmcnt(0)
	s_barrier
	v_or_b32_e32 v156, v151, v139
	ds_read_b128 v[152:155], v147
	v_ashrrev_i32_e32 v157, 31, v156
	v_lshlrev_b64 v[156:157], 11, v[156:157]
	v_lshl_add_u64 v[156:157], s[28:29], 0, v[156:157]
	v_lshl_add_u64 v[160:161], v[156:157], 0, v[132:133]
	v_add_u32_e32 v151, s4, v140
	ds_read_b128 v[156:159], v148
	s_waitcnt lgkmcnt(1)
	global_store_dwordx4 v[160:161], v[152:155], off nt
	s_andn2_b64 vcc, exec, s[0:1]
	s_mov_b64 s[0:1], -1
	v_lshlrev_b32_e32 v152, 1, v151
	v_ashrrev_i32_e32 v151, 4, v151
	v_and_b32_e32 v152, 0xf00, v152
	v_and_b32_e32 v151, 0xffffff80, v151
	v_add_u32_e32 v151, v152, v151
	v_or_b32_e32 v152, v151, v141
	v_ashrrev_i32_e32 v153, 31, v152
	v_lshlrev_b64 v[152:153], 11, v[152:153]
	v_lshl_add_u64 v[152:153], s[28:29], 0, v[152:153]
	v_lshl_add_u64 v[152:153], v[152:153], 0, v[134:135]
	v_add_u32_e32 v151, s4, v142
	s_waitcnt lgkmcnt(0)
	global_store_dwordx4 v[152:153], v[156:159], off nt
	v_lshlrev_b32_e32 v152, 1, v151
	v_ashrrev_i32_e32 v151, 4, v151
	v_and_b32_e32 v152, 0xf00, v152
	v_and_b32_e32 v151, 0xffffff80, v151
	v_add_u32_e32 v151, v152, v151
	v_or_b32_e32 v156, v151, v143
	ds_read_b128 v[152:155], v149
	v_ashrrev_i32_e32 v157, 31, v156
	v_lshlrev_b64 v[156:157], 11, v[156:157]
	v_lshl_add_u64 v[156:157], s[28:29], 0, v[156:157]
	v_lshl_add_u64 v[160:161], v[156:157], 0, v[132:133]
	v_add_u32_e32 v151, s4, v144
	ds_read_b128 v[156:159], v150
	s_waitcnt lgkmcnt(1)
	global_store_dwordx4 v[160:161], v[152:155], off nt
	s_nop 1
	v_lshlrev_b32_e32 v152, 1, v151
	v_ashrrev_i32_e32 v151, 4, v151
	v_and_b32_e32 v152, 0xf00, v152
	v_and_b32_e32 v151, 0xffffff80, v151
	v_add_u32_e32 v151, v152, v151
	v_or_b32_e32 v152, v151, v145
	v_ashrrev_i32_e32 v153, 31, v152
	v_lshlrev_b64 v[152:153], 11, v[152:153]
	v_lshl_add_u64 v[152:153], s[28:29], 0, v[152:153]
	v_lshl_add_u64 v[152:153], v[152:153], 0, v[136:137]
	s_waitcnt lgkmcnt(0)
	global_store_dwordx4 v[152:153], v[156:159], off nt
	s_cbranch_vccnz .LBB0_188
	s_add_i32 s0, s24, s25
	s_cmpk_gt_i32 s0, 0x1fff
	s_cbranch_scc1 .Lcvgu_t
	s_ashr_i32 s1, s0, 31
	s_lshr_b32 s1, s1, 19
	s_add_i32 s1, s0, s1
	s_and_b32 s1, s1, 0xffffe000
	s_sub_i32 s1, s0, s1
	s_sext_i32_i16 s0, s1
	s_bfe_u32 s0, s0, 0x80017
	s_add_i32 s0, s1, s0
	s_sext_i32_i16 s4, s0
	s_lshr_b32 s0, s4, 8
	s_and_b32 s4, s4, 0xffffff00
	s_sub_i32 s4, s1, s4
	s_bfe_u32 s1, s4, 0x4001b
	s_add_i32 s1, s4, s1
	s_sext_i32_i16 s1, s1
	s_ashr_i32 s25, s1, 4
	s_bfe_i64 s[0:1], s[0:1], 0x100000
	s_lshl_b64 s[0:1], s[0:1], 25
	s_add_u32 s27, s62, s0
	s_addc_u32 s28, s63, s1
	s_lshl_b32 s0, s25, 7
	s_add_i32 s0, s0, s7
	s_ashr_i32 s1, s0, 31
	s_lshl_b64 s[0:1], s[0:1], 14
	s_add_u32 s27, s27, s0
	s_addc_u32 s28, s28, s1
	s_lshl_b32 s0, s25, 12
	s_lshl_b32 s1, s4, 8
	s_sub_i32 s0, s1, s0
	s_ashr_i32 s1, s0, 31
	s_lshl_b64 s[0:1], s[0:1], 2
	s_add_u32 s0, s27, s0
	s_addc_u32 s1, s28, s1
	v_lshl_add_u64 v[74:75], s[0:1], 0, v[130:131]
	v_add_co_u32_e32 v2, vcc, s8, v74
	s_nop 1
	v_addc_co_u32_e32 v3, vcc, 0, v75, vcc
	v_add_co_u32_e32 v6, vcc, s9, v74
	global_load_dwordx4 v[30:33], v[74:75], off nt
	s_nop 0
	global_load_dwordx4 v[2:5], v[2:3], off nt
	v_addc_co_u32_e32 v7, vcc, 0, v75, vcc
	v_add_co_u32_e32 v10, vcc, s10, v74
	s_nop 1
	v_addc_co_u32_e32 v11, vcc, 0, v75, vcc
	v_add_co_u32_e32 v14, vcc, s11, v74
	global_load_dwordx4 v[6:9], v[6:7], off nt
	s_nop 0
	global_load_dwordx4 v[10:13], v[10:11], off nt
	v_addc_co_u32_e32 v15, vcc, 0, v75, vcc
	v_add_co_u32_e32 v18, vcc, s12, v74
	s_nop 1
	v_addc_co_u32_e32 v19, vcc, 0, v75, vcc
	v_add_co_u32_e32 v22, vcc, s13, v74
	global_load_dwordx4 v[14:17], v[14:15], off nt
	s_nop 0
	global_load_dwordx4 v[18:21], v[18:19], off nt
	v_addc_co_u32_e32 v23, vcc, 0, v75, vcc
	v_add_co_u32_e32 v26, vcc, s14, v74
	s_nop 1
	v_addc_co_u32_e32 v27, vcc, 0, v75, vcc
	v_add_co_u32_e32 v34, vcc, s15, v74
	global_load_dwordx4 v[22:25], v[22:23], off nt
	s_nop 0
	global_load_dwordx4 v[26:29], v[26:27], off nt
	v_addc_co_u32_e32 v35, vcc, 0, v75, vcc
	v_add_co_u32_e32 v38, vcc, s20, v74
	s_nop 1
	v_addc_co_u32_e32 v39, vcc, 0, v75, vcc
	v_add_co_u32_e32 v42, vcc, s21, v74
	global_load_dwordx4 v[34:37], v[34:35], off nt
	s_nop 0
	global_load_dwordx4 v[38:41], v[38:39], off nt
	v_addc_co_u32_e32 v43, vcc, 0, v75, vcc
	v_add_co_u32_e32 v46, vcc, s22, v74
	s_nop 1
	v_addc_co_u32_e32 v47, vcc, 0, v75, vcc
	v_add_co_u32_e32 v50, vcc, s23, v74
	global_load_dwordx4 v[42:45], v[42:43], off nt
	s_nop 0
	global_load_dwordx4 v[46:49], v[46:47], off nt
	v_addc_co_u32_e32 v51, vcc, 0, v75, vcc
	v_add_co_u32_e32 v62, vcc, 0x34000, v74
	s_nop 1
	v_addc_co_u32_e32 v63, vcc, 0, v75, vcc
	v_add_co_u32_e32 v76, vcc, 0x38000, v74
	global_load_dwordx4 v[50:53], v[50:51], off nt
	s_nop 0
	global_load_dwordx4 v[62:65], v[62:63], off nt
	v_addc_co_u32_e32 v77, vcc, 0, v75, vcc
	v_add_co_u32_e32 v86, vcc, 0x3c000, v74
	s_nop 1
	v_addc_co_u32_e32 v87, vcc, 0, v75, vcc
	global_load_dwordx4 v[74:77], v[76:77], off nt
	s_nop 0
	global_load_dwordx4 v[86:89], v[86:87], off nt
	s_waitcnt vmcnt(20)
	s_branch .LBB0_187

.LBB0_197:
	v_mul_f32_e32 v141, 0x42800000, v50
	v_mul_f32_e32 v142, 0x42800000, v54
	v_cvt_pk_fp8_f32 v145, v141, v142
	v_mul_f32_e32 v141, 0x42800000, v51
	v_mul_f32_e32 v142, 0x42800000, v55
	v_cvt_pk_fp8_f32 v146, v141, v142
	v_mul_f32_e32 v141, 0x42800000, v63
	v_mul_f32_e32 v142, 0x42800000, v67
	v_cvt_pk_fp8_f32 v146, v141, v142 op_sel:[0,0,1]
	v_mul_f32_e32 v141, 0x42800000, v52
	v_mul_f32_e32 v142, 0x42800000, v56
	v_cvt_pk_fp8_f32 v147, v141, v142
	v_mul_f32_e32 v141, 0x42800000, v53
	v_mul_f32_e32 v142, 0x42800000, v57
	v_cvt_pk_fp8_f32 v148, v141, v142
	v_mul_f32_e32 v141, 0x42800000, v65
	v_mul_f32_e32 v142, 0x42800000, v69
	v_cvt_pk_fp8_f32 v148, v141, v142 op_sel:[0,0,1]
	v_mul_f32_e32 v141, 0x42800000, v74
	v_mul_f32_e32 v142, 0x42800000, v78
	v_cvt_pk_fp8_f32 v149, v141, v142
	v_mul_f32_e32 v141, 0x42800000, v75
	v_mul_f32_e32 v142, 0x42800000, v79
	v_cvt_pk_fp8_f32 v150, v141, v142
	v_mul_f32_e32 v141, 0x42800000, v87
	v_mul_f32_e32 v142, 0x42800000, v91
	v_cvt_pk_fp8_f32 v150, v141, v142 op_sel:[0,0,1]
	v_mul_f32_e32 v141, 0x42800000, v76
	v_mul_f32_e32 v142, 0x42800000, v80
	v_cvt_pk_fp8_f32 v151, v141, v142
	v_mul_f32_e32 v141, 0x42800000, v77
	v_mul_f32_e32 v142, 0x42800000, v81
	v_mul_f32_e32 v143, 0x42800000, v62
	v_mul_f32_e32 v144, 0x42800000, v66
	v_cvt_pk_fp8_f32 v152, v141, v142
	v_cvt_pk_fp8_f32 v145, v143, v144 op_sel:[0,0,1]
	v_mul_f32_e32 v143, 0x42800000, v64
	v_mul_f32_e32 v144, 0x42800000, v68
	v_cvt_pk_fp8_f32 v147, v143, v144 op_sel:[0,0,1]
	v_mul_f32_e32 v143, 0x42800000, v86
	v_mul_f32_e32 v144, 0x42800000, v90
	v_cvt_pk_fp8_f32 v149, v143, v144 op_sel:[0,0,1]
	v_mul_f32_e32 v143, 0x42800000, v88
	v_mul_f32_e32 v144, 0x42800000, v92
	v_mul_f32_e32 v141, 0x42800000, v89
	v_mul_f32_e32 v142, 0x42800000, v93
	v_cvt_pk_fp8_f32 v151, v143, v144 op_sel:[0,0,1]
	v_cvt_pk_fp8_f32 v152, v141, v142 op_sel:[0,0,1]
	ds_write2_b32 v134, v145, v146 offset1:32
	ds_write2_b32 v134, v147, v148 offset0:64 offset1:96
	ds_write2_b32 v135, v149, v150 offset1:32
	ds_write2_b32 v135, v151, v152 offset0:64 offset1:96
	v_mul_f32_e32 v141, 0x42800000, v98
	v_mul_f32_e32 v142, 0x42800000, v102
	v_cvt_pk_fp8_f32 v145, v141, v142
	v_mul_f32_e32 v141, 0x42800000, v99
	v_mul_f32_e32 v142, 0x42800000, v103
	v_cvt_pk_fp8_f32 v146, v141, v142
	v_mul_f32_e32 v141, 0x42800000, v107
	v_mul_f32_e32 v142, 0x42800000, v111
	v_cvt_pk_fp8_f32 v146, v141, v142 op_sel:[0,0,1]
	v_mul_f32_e32 v141, 0x42800000, v100
	v_mul_f32_e32 v142, 0x42800000, v104
	v_cvt_pk_fp8_f32 v147, v141, v142
	v_mul_f32_e32 v141, 0x42800000, v101
	v_mul_f32_e32 v142, 0x42800000, v105
	v_cvt_pk_fp8_f32 v148, v141, v142
	v_mul_f32_e32 v141, 0x42800000, v109
	v_mul_f32_e32 v142, 0x42800000, v113
	v_cvt_pk_fp8_f32 v148, v141, v142 op_sel:[0,0,1]
	v_mul_f32_e32 v141, 0x42800000, v114
	v_mul_f32_e32 v142, 0x42800000, v118
	s_ashr_i32 s4, s29, 31
	v_cvt_pk_fp8_f32 v149, v141, v142
	v_mul_f32_e32 v141, 0x42800000, v115
	v_mul_f32_e32 v142, 0x42800000, v119
	s_lshr_b32 s4, s4, 23
	v_cvt_pk_fp8_f32 v150, v141, v142
	s_add_i32 s4, s29, s4
	s_and_b32 s4, s4, 0xfffffe00
	s_sub_i32 s4, s29, s4
	v_mul_f32_e32 v141, 0x42800000, v123
	v_mul_f32_e32 v142, 0x42800000, v127
	s_bfe_u32 s5, s4, 0x60019
	v_cvt_pk_fp8_f32 v150, v141, v142 op_sel:[0,0,1]
	v_mul_f32_e32 v141, 0x42800000, v116
	v_mul_f32_e32 v142, 0x42800000, v120
	s_add_i32 s5, s4, s5
	v_cvt_pk_fp8_f32 v151, v141, v142
	v_mul_f32_e32 v141, 0x42800000, v117
	v_mul_f32_e32 v142, 0x42800000, v121
	s_sext_i32_i16 s5, s5
	v_mul_f32_e32 v143, 0x42800000, v106
	v_mul_f32_e32 v144, 0x42800000, v110
	v_cvt_pk_fp8_f32 v152, v141, v142
	s_add_i32 s28, s29, s6
	v_cvt_pk_fp8_f32 v145, v143, v144 op_sel:[0,0,1]
	v_mul_f32_e32 v143, 0x42800000, v108
	v_mul_f32_e32 v144, 0x42800000, v112
	s_ashr_i32 s29, s5, 6
	v_cvt_pk_fp8_f32 v147, v143, v144 op_sel:[0,0,1]
	v_mul_f32_e32 v143, 0x42800000, v122
	v_mul_f32_e32 v144, 0x42800000, v126
	s_lshl_b32 s5, s29, 11
	s_lshl_b32 s4, s4, 5
	v_cvt_pk_fp8_f32 v149, v143, v144 op_sel:[0,0,1]
	v_mul_f32_e32 v143, 0x42800000, v124
	v_mul_f32_e32 v144, 0x42800000, v128
	v_mul_f32_e32 v141, 0x42800000, v125
	v_mul_f32_e32 v142, 0x42800000, v129
	s_sub_i32 s4, s4, s5
	v_cvt_pk_fp8_f32 v151, v143, v144 op_sel:[0,0,1]
	v_cvt_pk_fp8_f32 v152, v141, v142 op_sel:[0,0,1]
	s_ashr_i32 s5, s4, 31
	ds_write2_b32 v136, v145, v146 offset1:32
	ds_write2_b32 v136, v147, v148 offset0:64 offset1:96
	ds_write2_b32 v137, v149, v150 offset1:32
	ds_write2_b32 v137, v151, v152 offset0:64 offset1:96
	s_lshl_b64 s[4:5], s[4:5], 10
	s_waitcnt lgkmcnt(0)
	s_add_u32 s4, s9, s4
	s_addc_u32 s5, s10, s5
	s_lshl_b32 s29, s29, 7
	ds_read_b128 v[142:145], v138
	ds_read_b128 v[146:149], v138 offset:2048
	s_ashr_i32 s30, s29, 31
	s_add_u32 s4, s4, s29
	s_addc_u32 s5, s5, s30
	v_lshl_add_u64 v[154:155], s[4:5], 0, v[132:133]
	s_waitcnt lgkmcnt(1)
	global_store_dwordx4 v[154:155], v[142:145], off nt
	ds_read_b128 v[142:145], v139
	ds_read_b128 v[150:153], v140
	v_add_co_u32_e32 v156, vcc, s11, v154
	s_cmpk_gt_i32 s28, 0x1ff
	s_nop 0
	v_addc_co_u32_e32 v157, vcc, 0, v155, vcc
	s_waitcnt lgkmcnt(1)
	global_store_dwordx4 v[156:157], v[142:145], off nt
	s_cselect_b64 s[4:5], -1, 0
	s_nop 0
	v_add_co_u32_e32 v142, vcc, 0x4000, v154
	s_nop 1
	v_addc_co_u32_e32 v143, vcc, 0, v155, vcc
	global_store_dwordx4 v[142:143], v[146:149], off nt
	v_add_co_u32_e32 v142, vcc, 0x6000, v154
	s_nop 1
	v_addc_co_u32_e32 v143, vcc, 0, v155, vcc
	s_waitcnt lgkmcnt(0)
	global_store_dwordx4 v[142:143], v[150:153], off nt
	s_waitcnt lgkmcnt(0)

.LBB0_201:
	s_waitcnt vmcnt(1)
	v_mul_f32_e32 v141, 0x42800000, v30
	v_mul_f32_e32 v142, 0x42800000, v2
	v_cvt_pk_fp8_f32 v145, v141, v142
	v_mul_f32_e32 v141, 0x42800000, v31
	v_mul_f32_e32 v142, 0x42800000, v3
	v_cvt_pk_fp8_f32 v146, v141, v142
	v_mul_f32_e32 v141, 0x42800000, v7
	v_mul_f32_e32 v142, 0x42800000, v11
	v_cvt_pk_fp8_f32 v146, v141, v142 op_sel:[0,0,1]
	v_mul_f32_e32 v141, 0x42800000, v32
	v_mul_f32_e32 v142, 0x42800000, v4
	v_cvt_pk_fp8_f32 v147, v141, v142
	v_mul_f32_e32 v141, 0x42800000, v33
	v_mul_f32_e32 v142, 0x42800000, v5
	v_cvt_pk_fp8_f32 v148, v141, v142
	v_mul_f32_e32 v141, 0x42800000, v9
	v_mul_f32_e32 v142, 0x42800000, v13
	v_cvt_pk_fp8_f32 v148, v141, v142 op_sel:[0,0,1]
	v_mul_f32_e32 v141, 0x42800000, v14
	v_mul_f32_e32 v142, 0x42800000, v18
	v_cvt_pk_fp8_f32 v149, v141, v142
	v_mul_f32_e32 v141, 0x42800000, v15
	v_mul_f32_e32 v142, 0x42800000, v19
	v_cvt_pk_fp8_f32 v150, v141, v142
	v_mul_f32_e32 v141, 0x42800000, v23
	v_mul_f32_e32 v142, 0x42800000, v27
	v_cvt_pk_fp8_f32 v150, v141, v142 op_sel:[0,0,1]
	v_mul_f32_e32 v141, 0x42800000, v16
	v_mul_f32_e32 v142, 0x42800000, v20
	v_cvt_pk_fp8_f32 v151, v141, v142
	v_mul_f32_e32 v141, 0x42800000, v17
	v_mul_f32_e32 v142, 0x42800000, v21
	v_mul_f32_e32 v143, 0x42800000, v6
	v_mul_f32_e32 v144, 0x42800000, v10
	v_cvt_pk_fp8_f32 v152, v141, v142
	v_cvt_pk_fp8_f32 v145, v143, v144 op_sel:[0,0,1]
	v_mul_f32_e32 v143, 0x42800000, v8
	v_mul_f32_e32 v144, 0x42800000, v12
	v_cvt_pk_fp8_f32 v147, v143, v144 op_sel:[0,0,1]
	v_mul_f32_e32 v143, 0x42800000, v22
	v_mul_f32_e32 v144, 0x42800000, v26
	v_cvt_pk_fp8_f32 v149, v143, v144 op_sel:[0,0,1]
	v_mul_f32_e32 v143, 0x42800000, v24
	v_mul_f32_e32 v144, 0x42800000, v28
	v_mul_f32_e32 v141, 0x42800000, v25
	v_mul_f32_e32 v142, 0x42800000, v29
	v_cvt_pk_fp8_f32 v151, v143, v144 op_sel:[0,0,1]
	v_cvt_pk_fp8_f32 v152, v141, v142 op_sel:[0,0,1]
	ds_write2_b32 v134, v145, v146 offset1:32
	ds_write2_b32 v134, v147, v148 offset0:64 offset1:96
	ds_write2_b32 v135, v149, v150 offset1:32
	ds_write2_b32 v135, v151, v152 offset0:64 offset1:96
	v_mul_f32_e32 v141, 0x42800000, v34
	v_mul_f32_e32 v142, 0x42800000, v38
	v_cvt_pk_fp8_f32 v145, v141, v142
	v_mul_f32_e32 v141, 0x42800000, v35
	v_mul_f32_e32 v142, 0x42800000, v39
	v_cvt_pk_fp8_f32 v146, v141, v142
	v_mul_f32_e32 v141, 0x42800000, v43
	v_mul_f32_e32 v142, 0x42800000, v47
	v_cvt_pk_fp8_f32 v146, v141, v142 op_sel:[0,0,1]
	v_mul_f32_e32 v141, 0x42800000, v36
	v_mul_f32_e32 v142, 0x42800000, v40
	v_cvt_pk_fp8_f32 v147, v141, v142
	v_mul_f32_e32 v141, 0x42800000, v37
	v_mul_f32_e32 v142, 0x42800000, v41
	v_cvt_pk_fp8_f32 v148, v141, v142
	v_mul_f32_e32 v141, 0x42800000, v45
	v_mul_f32_e32 v142, 0x42800000, v49
	v_cvt_pk_fp8_f32 v148, v141, v142 op_sel:[0,0,1]
	v_mul_f32_e32 v141, 0x42800000, v58
	v_mul_f32_e32 v142, 0x42800000, v70
	s_ashr_i32 s30, s28, 31
	v_cvt_pk_fp8_f32 v149, v141, v142
	v_mul_f32_e32 v141, 0x42800000, v59
	v_mul_f32_e32 v142, 0x42800000, v71
	s_lshr_b32 s30, s30, 23
	v_cvt_pk_fp8_f32 v150, v141, v142
	s_add_i32 s30, s28, s30
	s_and_b32 s30, s30, 0xfffffe00
	s_sub_i32 s30, s28, s30
	v_mul_f32_e32 v141, 0x42800000, v83
	s_waitcnt vmcnt(0)
	v_mul_f32_e32 v142, 0x42800000, v95
	s_bfe_u32 s31, s30, 0x60019
	v_cvt_pk_fp8_f32 v150, v141, v142 op_sel:[0,0,1]
	v_mul_f32_e32 v141, 0x42800000, v60
	v_mul_f32_e32 v142, 0x42800000, v72
	s_add_i32 s31, s30, s31
	v_cvt_pk_fp8_f32 v151, v141, v142
	v_mul_f32_e32 v141, 0x42800000, v61
	v_mul_f32_e32 v142, 0x42800000, v73
	s_sext_i32_i16 s31, s31
	v_mul_f32_e32 v143, 0x42800000, v42
	v_mul_f32_e32 v144, 0x42800000, v46
	v_cvt_pk_fp8_f32 v152, v141, v142
	v_cvt_pk_fp8_f32 v145, v143, v144 op_sel:[0,0,1]
	v_mul_f32_e32 v143, 0x42800000, v44
	v_mul_f32_e32 v144, 0x42800000, v48
	s_ashr_i32 s34, s31, 6
	v_cvt_pk_fp8_f32 v147, v143, v144 op_sel:[0,0,1]
	v_mul_f32_e32 v143, 0x42800000, v82
	v_mul_f32_e32 v144, 0x42800000, v94
	s_lshl_b32 s31, s34, 11
	s_lshl_b32 s30, s30, 5
	v_cvt_pk_fp8_f32 v149, v143, v144 op_sel:[0,0,1]
	v_mul_f32_e32 v143, 0x42800000, v84
	v_mul_f32_e32 v144, 0x42800000, v96
	v_mul_f32_e32 v141, 0x42800000, v85
	v_mul_f32_e32 v142, 0x42800000, v97
	s_sub_i32 s30, s30, s31
	v_cvt_pk_fp8_f32 v151, v143, v144 op_sel:[0,0,1]
	v_cvt_pk_fp8_f32 v152, v141, v142 op_sel:[0,0,1]
	s_ashr_i32 s31, s30, 31
	ds_write2_b32 v136, v145, v146 offset1:32
	ds_write2_b32 v136, v147, v148 offset0:64 offset1:96
	ds_write2_b32 v137, v149, v150 offset1:32
	ds_write2_b32 v137, v151, v152 offset0:64 offset1:96
	s_lshl_b64 s[30:31], s[30:31], 10
	s_waitcnt lgkmcnt(0)
	s_add_u32 s30, s9, s30
	s_addc_u32 s31, s10, s31
	s_lshl_b32 s34, s34, 7
	ds_read_b128 v[142:145], v138
	ds_read_b128 v[146:149], v138 offset:2048
	s_ashr_i32 s35, s34, 31
	s_add_u32 s30, s30, s34
	s_addc_u32 s31, s31, s35
	v_lshl_add_u64 v[154:155], s[30:31], 0, v[132:133]
	s_waitcnt lgkmcnt(1)
	global_store_dwordx4 v[154:155], v[142:145], off nt
	ds_read_b128 v[142:145], v139
	ds_read_b128 v[150:153], v140
	v_add_co_u32_e32 v156, vcc, s11, v154
	s_nop 1
	v_addc_co_u32_e32 v157, vcc, 0, v155, vcc
	s_waitcnt lgkmcnt(1)
	global_store_dwordx4 v[156:157], v[142:145], off nt
	s_nop 1
	v_add_co_u32_e32 v142, vcc, 0x4000, v154
	s_nop 1
	v_addc_co_u32_e32 v143, vcc, 0, v155, vcc
	global_store_dwordx4 v[142:143], v[146:149], off nt
	v_add_co_u32_e32 v142, vcc, 0x6000, v154
	s_nop 1
	v_addc_co_u32_e32 v143, vcc, 0, v155, vcc
	s_waitcnt lgkmcnt(0)
	global_store_dwordx4 v[142:143], v[150:153], off nt
	s_waitcnt lgkmcnt(0)
	s_andn2_b64 vcc, exec, s[4:5]
	s_mov_b64 s[4:5], -1
	s_cbranch_vccnz .LBB0_198
	s_add_i32 s4, s27, s28
	s_cmpk_gt_i32 s4, 0x1ff
	s_cbranch_scc1 .LBB0_197
	s_ashr_i32 s5, s4, 31
	s_lshr_b32 s5, s5, 23
	s_add_i32 s5, s4, s5
	s_and_b32 s5, s5, 0xfffffe00
	s_sub_i32 s5, s4, s5
	s_bfe_u32 s4, s5, 0x60019
	s_add_i32 s4, s5, s4
	s_sext_i32_i16 s4, s4
	s_lshr_b32 s4, s4, 6
	s_bfe_i64 s[30:31], s[4:5], 0x100000
	v_readlane_b32 s56, v254, 13
	s_lshl_b64 s[30:31], s[30:31], 20
	v_readlane_b32 s70, v254, 27
	v_readlane_b32 s71, v254, 28
	s_add_u32 s28, s70, s30
	s_addc_u32 s30, s71, s31
	s_lshl_b32 s4, s4, 11
	s_lshl_b32 s5, s5, 5
	s_sub_i32 s4, s5, s4
	s_ashr_i32 s5, s4, 31
	s_lshl_b64 s[4:5], s[4:5], 2
	s_add_u32 s4, s28, s4
	s_addc_u32 s5, s30, s5
	v_lshl_add_u64 v[82:83], s[4:5], 0, v[130:131]
	v_add_co_u32_e32 v2, vcc, s11, v82
	v_readlane_b32 s57, v254, 14
	s_nop 0
	v_addc_co_u32_e32 v3, vcc, 0, v83, vcc
	v_add_co_u32_e32 v6, vcc, s12, v82
	global_load_dwordx4 v[30:33], v[82:83], off nt
	s_nop 0
	global_load_dwordx4 v[2:5], v[2:3], off nt
	v_addc_co_u32_e32 v7, vcc, 0, v83, vcc
	v_add_co_u32_e32 v10, vcc, s13, v82
	v_readlane_b32 s58, v254, 15
	s_nop 0
	v_addc_co_u32_e32 v11, vcc, 0, v83, vcc
	v_add_co_u32_e32 v14, vcc, s14, v82
	global_load_dwordx4 v[6:9], v[6:7], off nt
	s_nop 0
	global_load_dwordx4 v[10:13], v[10:11], off nt
	v_addc_co_u32_e32 v15, vcc, 0, v83, vcc
	v_add_co_u32_e32 v18, vcc, s15, v82
	v_readlane_b32 s59, v254, 16
	s_nop 0
	v_addc_co_u32_e32 v19, vcc, 0, v83, vcc
	v_add_co_u32_e32 v22, vcc, s20, v82
	global_load_dwordx4 v[14:17], v[14:15], off nt
	s_nop 0
	global_load_dwordx4 v[18:21], v[18:19], off nt
	v_addc_co_u32_e32 v23, vcc, 0, v83, vcc
	v_add_co_u32_e32 v26, vcc, s21, v82
	v_readlane_b32 s60, v254, 17
	s_nop 0
	v_addc_co_u32_e32 v27, vcc, 0, v83, vcc
	v_add_co_u32_e32 v34, vcc, s22, v82
	global_load_dwordx4 v[22:25], v[22:23], off nt
	s_nop 0
	global_load_dwordx4 v[26:29], v[26:27], off nt
	v_addc_co_u32_e32 v35, vcc, 0, v83, vcc
	v_add_co_u32_e32 v38, vcc, s23, v82
	v_readlane_b32 s61, v254, 18
	s_nop 0
	v_addc_co_u32_e32 v39, vcc, 0, v83, vcc
	v_add_co_u32_e32 v42, vcc, s24, v82
	global_load_dwordx4 v[34:37], v[34:35], off nt
	s_nop 0
	global_load_dwordx4 v[38:41], v[38:39], off nt
	v_addc_co_u32_e32 v43, vcc, 0, v83, vcc
	v_add_co_u32_e32 v46, vcc, s25, v82
	v_readlane_b32 s62, v254, 19
	s_nop 0
	v_addc_co_u32_e32 v47, vcc, 0, v83, vcc
	v_add_co_u32_e32 v58, vcc, s26, v82
	global_load_dwordx4 v[42:45], v[42:43], off nt
	s_nop 0
	global_load_dwordx4 v[46:49], v[46:47], off nt
	v_addc_co_u32_e32 v59, vcc, 0, v83, vcc
	v_add_co_u32_e32 v70, vcc, 0xc2000, v82
	v_readlane_b32 s63, v254, 20
	s_nop 0
	v_addc_co_u32_e32 v71, vcc, 0, v83, vcc
	v_add_co_u32_e32 v84, vcc, 0xc4000, v82
	global_load_dwordx4 v[58:61], v[58:59], off nt
	s_nop 0
	global_load_dwordx4 v[70:73], v[70:71], off nt
	v_addc_co_u32_e32 v85, vcc, 0, v83, vcc
	v_add_co_u32_e32 v94, vcc, 0xc6000, v82
	v_readlane_b32 s64, v254, 21
	s_nop 0
	v_addc_co_u32_e32 v95, vcc, 0, v83, vcc
	global_load_dwordx4 v[82:85], v[84:85], off nt
	s_nop 0
	global_load_dwordx4 v[94:97], v[94:95], off nt
	v_readlane_b32 s65, v254, 22
	v_readlane_b32 s66, v254, 23
	v_readlane_b32 s67, v254, 24
	v_readlane_b32 s68, v254, 25
	v_readlane_b32 s69, v254, 26
	s_branch .LBB0_197

.LBB0_206:
	v_mul_f32_e32 v141, 0x42800000, v50
	v_mul_f32_e32 v142, 0x42800000, v54
	v_cvt_pk_fp8_f32 v145, v141, v142
	v_mul_f32_e32 v141, 0x42800000, v51
	v_mul_f32_e32 v142, 0x42800000, v55
	v_cvt_pk_fp8_f32 v146, v141, v142
	v_mul_f32_e32 v141, 0x42800000, v63
	v_mul_f32_e32 v142, 0x42800000, v67
	v_cvt_pk_fp8_f32 v146, v141, v142 op_sel:[0,0,1]
	v_mul_f32_e32 v141, 0x42800000, v52
	v_mul_f32_e32 v142, 0x42800000, v56
	v_cvt_pk_fp8_f32 v147, v141, v142
	v_mul_f32_e32 v141, 0x42800000, v53
	v_mul_f32_e32 v142, 0x42800000, v57
	v_cvt_pk_fp8_f32 v148, v141, v142
	v_mul_f32_e32 v141, 0x42800000, v65
	v_mul_f32_e32 v142, 0x42800000, v69
	v_cvt_pk_fp8_f32 v148, v141, v142 op_sel:[0,0,1]
	v_mul_f32_e32 v141, 0x42800000, v74
	v_mul_f32_e32 v142, 0x42800000, v78
	v_cvt_pk_fp8_f32 v149, v141, v142
	v_mul_f32_e32 v141, 0x42800000, v75
	v_mul_f32_e32 v142, 0x42800000, v79
	v_cvt_pk_fp8_f32 v150, v141, v142
	v_mul_f32_e32 v141, 0x42800000, v87
	v_mul_f32_e32 v142, 0x42800000, v91
	v_cvt_pk_fp8_f32 v150, v141, v142 op_sel:[0,0,1]
	v_mul_f32_e32 v141, 0x42800000, v76
	v_mul_f32_e32 v142, 0x42800000, v80
	v_cvt_pk_fp8_f32 v151, v141, v142
	v_mul_f32_e32 v141, 0x42800000, v77
	v_mul_f32_e32 v142, 0x42800000, v81
	v_mul_f32_e32 v143, 0x42800000, v62
	v_mul_f32_e32 v144, 0x42800000, v66
	v_cvt_pk_fp8_f32 v152, v141, v142
	v_cvt_pk_fp8_f32 v145, v143, v144 op_sel:[0,0,1]
	v_mul_f32_e32 v143, 0x42800000, v64
	v_mul_f32_e32 v144, 0x42800000, v68
	v_cvt_pk_fp8_f32 v147, v143, v144 op_sel:[0,0,1]
	v_mul_f32_e32 v143, 0x42800000, v86
	v_mul_f32_e32 v144, 0x42800000, v90
	v_cvt_pk_fp8_f32 v149, v143, v144 op_sel:[0,0,1]
	v_mul_f32_e32 v143, 0x42800000, v88
	v_mul_f32_e32 v144, 0x42800000, v92
	v_mul_f32_e32 v141, 0x42800000, v89
	v_mul_f32_e32 v142, 0x42800000, v93
	v_cvt_pk_fp8_f32 v151, v143, v144 op_sel:[0,0,1]
	v_cvt_pk_fp8_f32 v152, v141, v142 op_sel:[0,0,1]
	ds_write2_b32 v134, v145, v146 offset1:32
	ds_write2_b32 v134, v147, v148 offset0:64 offset1:96
	ds_write2_b32 v135, v149, v150 offset1:32
	ds_write2_b32 v135, v151, v152 offset0:64 offset1:96
	v_mul_f32_e32 v141, 0x42800000, v98
	v_mul_f32_e32 v142, 0x42800000, v102
	v_cvt_pk_fp8_f32 v145, v141, v142
	v_mul_f32_e32 v141, 0x42800000, v99
	v_mul_f32_e32 v142, 0x42800000, v103
	v_cvt_pk_fp8_f32 v146, v141, v142
	v_mul_f32_e32 v141, 0x42800000, v107
	v_mul_f32_e32 v142, 0x42800000, v111
	v_cvt_pk_fp8_f32 v146, v141, v142 op_sel:[0,0,1]
	v_mul_f32_e32 v141, 0x42800000, v100
	v_mul_f32_e32 v142, 0x42800000, v104
	v_cvt_pk_fp8_f32 v147, v141, v142
	v_mul_f32_e32 v141, 0x42800000, v101
	v_mul_f32_e32 v142, 0x42800000, v105
	v_cvt_pk_fp8_f32 v148, v141, v142
	v_mul_f32_e32 v141, 0x42800000, v109
	v_mul_f32_e32 v142, 0x42800000, v113
	v_cvt_pk_fp8_f32 v148, v141, v142 op_sel:[0,0,1]
	v_mul_f32_e32 v141, 0x42800000, v114
	v_mul_f32_e32 v142, 0x42800000, v118
	s_ashr_i32 s0, s29, 31
	v_cvt_pk_fp8_f32 v149, v141, v142
	v_mul_f32_e32 v141, 0x42800000, v115
	v_mul_f32_e32 v142, 0x42800000, v119
	s_lshr_b32 s0, s0, 23
	v_cvt_pk_fp8_f32 v150, v141, v142
	s_add_i32 s0, s29, s0
	s_and_b32 s0, s0, 0xfffffe00
	s_sub_i32 s0, s29, s0
	v_mul_f32_e32 v141, 0x42800000, v123
	v_mul_f32_e32 v142, 0x42800000, v127
	s_bfe_u32 s1, s0, 0x60019
	v_cvt_pk_fp8_f32 v150, v141, v142 op_sel:[0,0,1]
	v_mul_f32_e32 v141, 0x42800000, v116
	v_mul_f32_e32 v142, 0x42800000, v120
	s_add_i32 s1, s0, s1
	v_cvt_pk_fp8_f32 v151, v141, v142
	v_mul_f32_e32 v141, 0x42800000, v117
	v_mul_f32_e32 v142, 0x42800000, v121
	s_sext_i32_i16 s1, s1
	v_mul_f32_e32 v143, 0x42800000, v106
	v_mul_f32_e32 v144, 0x42800000, v110
	v_cvt_pk_fp8_f32 v152, v141, v142
	s_add_i32 s28, s29, s6
	v_cvt_pk_fp8_f32 v145, v143, v144 op_sel:[0,0,1]
	v_mul_f32_e32 v143, 0x42800000, v108
	v_mul_f32_e32 v144, 0x42800000, v112
	s_ashr_i32 s29, s1, 6
	v_cvt_pk_fp8_f32 v147, v143, v144 op_sel:[0,0,1]
	v_mul_f32_e32 v143, 0x42800000, v122
	v_mul_f32_e32 v144, 0x42800000, v126
	s_lshl_b32 s1, s29, 11
	s_lshl_b32 s0, s0, 5
	v_cvt_pk_fp8_f32 v149, v143, v144 op_sel:[0,0,1]
	v_mul_f32_e32 v143, 0x42800000, v124
	v_mul_f32_e32 v144, 0x42800000, v128
	v_mul_f32_e32 v141, 0x42800000, v125
	v_mul_f32_e32 v142, 0x42800000, v129
	s_sub_i32 s0, s0, s1
	v_cvt_pk_fp8_f32 v151, v143, v144 op_sel:[0,0,1]
	v_cvt_pk_fp8_f32 v152, v141, v142 op_sel:[0,0,1]
	s_ashr_i32 s1, s0, 31
	ds_write2_b32 v136, v145, v146 offset1:32
	ds_write2_b32 v136, v147, v148 offset0:64 offset1:96
	ds_write2_b32 v137, v149, v150 offset1:32
	ds_write2_b32 v137, v151, v152 offset0:64 offset1:96
	s_lshl_b64 s[0:1], s[0:1], 10
	s_waitcnt lgkmcnt(0)
	s_add_u32 s0, s9, s0
	s_addc_u32 s1, s10, s1
	s_lshl_b32 s29, s29, 7
	ds_read_b128 v[142:145], v138
	ds_read_b128 v[146:149], v138 offset:2048
	s_ashr_i32 s30, s29, 31
	s_add_u32 s0, s0, s29
	s_addc_u32 s1, s1, s30
	v_lshl_add_u64 v[154:155], s[0:1], 0, v[132:133]
	s_waitcnt lgkmcnt(1)
	global_store_dwordx4 v[154:155], v[142:145], off nt
	ds_read_b128 v[142:145], v139
	ds_read_b128 v[150:153], v140
	v_add_co_u32_e32 v156, vcc, s11, v154
	s_cmpk_gt_i32 s28, 0x1ff
	s_nop 0
	v_addc_co_u32_e32 v157, vcc, 0, v155, vcc
	s_waitcnt lgkmcnt(1)
	global_store_dwordx4 v[156:157], v[142:145], off nt
	s_cselect_b64 s[0:1], -1, 0
	s_nop 0
	v_add_co_u32_e32 v142, vcc, 0x4000, v154
	s_nop 1
	v_addc_co_u32_e32 v143, vcc, 0, v155, vcc
	global_store_dwordx4 v[142:143], v[146:149], off nt
	v_add_co_u32_e32 v142, vcc, 0x6000, v154
	s_nop 1
	v_addc_co_u32_e32 v143, vcc, 0, v155, vcc
	s_waitcnt lgkmcnt(0)
	global_store_dwordx4 v[142:143], v[150:153], off nt
	s_waitcnt lgkmcnt(0)

.LBB0_210:
	s_waitcnt vmcnt(1)
	v_mul_f32_e32 v141, 0x42800000, v30
	v_mul_f32_e32 v142, 0x42800000, v2
	v_cvt_pk_fp8_f32 v145, v141, v142
	v_mul_f32_e32 v141, 0x42800000, v31
	v_mul_f32_e32 v142, 0x42800000, v3
	v_cvt_pk_fp8_f32 v146, v141, v142
	v_mul_f32_e32 v141, 0x42800000, v7
	v_mul_f32_e32 v142, 0x42800000, v11
	v_cvt_pk_fp8_f32 v146, v141, v142 op_sel:[0,0,1]
	v_mul_f32_e32 v141, 0x42800000, v32
	v_mul_f32_e32 v142, 0x42800000, v4
	v_cvt_pk_fp8_f32 v147, v141, v142
	v_mul_f32_e32 v141, 0x42800000, v33
	v_mul_f32_e32 v142, 0x42800000, v5
	v_cvt_pk_fp8_f32 v148, v141, v142
	v_mul_f32_e32 v141, 0x42800000, v9
	v_mul_f32_e32 v142, 0x42800000, v13
	v_cvt_pk_fp8_f32 v148, v141, v142 op_sel:[0,0,1]
	v_mul_f32_e32 v141, 0x42800000, v14
	v_mul_f32_e32 v142, 0x42800000, v18
	v_cvt_pk_fp8_f32 v149, v141, v142
	v_mul_f32_e32 v141, 0x42800000, v15
	v_mul_f32_e32 v142, 0x42800000, v19
	v_cvt_pk_fp8_f32 v150, v141, v142
	v_mul_f32_e32 v141, 0x42800000, v23
	v_mul_f32_e32 v142, 0x42800000, v27
	v_cvt_pk_fp8_f32 v150, v141, v142 op_sel:[0,0,1]
	v_mul_f32_e32 v141, 0x42800000, v16
	v_mul_f32_e32 v142, 0x42800000, v20
	v_cvt_pk_fp8_f32 v151, v141, v142
	v_mul_f32_e32 v141, 0x42800000, v17
	v_mul_f32_e32 v142, 0x42800000, v21
	v_mul_f32_e32 v143, 0x42800000, v6
	v_mul_f32_e32 v144, 0x42800000, v10
	v_cvt_pk_fp8_f32 v152, v141, v142
	v_cvt_pk_fp8_f32 v145, v143, v144 op_sel:[0,0,1]
	v_mul_f32_e32 v143, 0x42800000, v8
	v_mul_f32_e32 v144, 0x42800000, v12
	v_cvt_pk_fp8_f32 v147, v143, v144 op_sel:[0,0,1]
	v_mul_f32_e32 v143, 0x42800000, v22
	v_mul_f32_e32 v144, 0x42800000, v26
	v_cvt_pk_fp8_f32 v149, v143, v144 op_sel:[0,0,1]
	v_mul_f32_e32 v143, 0x42800000, v24
	v_mul_f32_e32 v144, 0x42800000, v28
	v_mul_f32_e32 v141, 0x42800000, v25
	v_mul_f32_e32 v142, 0x42800000, v29
	v_cvt_pk_fp8_f32 v151, v143, v144 op_sel:[0,0,1]
	v_cvt_pk_fp8_f32 v152, v141, v142 op_sel:[0,0,1]
	ds_write2_b32 v134, v145, v146 offset1:32
	ds_write2_b32 v134, v147, v148 offset0:64 offset1:96
	ds_write2_b32 v135, v149, v150 offset1:32
	ds_write2_b32 v135, v151, v152 offset0:64 offset1:96
	v_mul_f32_e32 v141, 0x42800000, v34
	v_mul_f32_e32 v142, 0x42800000, v38
	v_cvt_pk_fp8_f32 v145, v141, v142
	v_mul_f32_e32 v141, 0x42800000, v35
	v_mul_f32_e32 v142, 0x42800000, v39
	v_cvt_pk_fp8_f32 v146, v141, v142
	v_mul_f32_e32 v141, 0x42800000, v43
	v_mul_f32_e32 v142, 0x42800000, v47
	v_cvt_pk_fp8_f32 v146, v141, v142 op_sel:[0,0,1]
	v_mul_f32_e32 v141, 0x42800000, v36
	v_mul_f32_e32 v142, 0x42800000, v40
	v_cvt_pk_fp8_f32 v147, v141, v142
	v_mul_f32_e32 v141, 0x42800000, v37
	v_mul_f32_e32 v142, 0x42800000, v41
	v_cvt_pk_fp8_f32 v148, v141, v142
	v_mul_f32_e32 v141, 0x42800000, v45
	v_mul_f32_e32 v142, 0x42800000, v49
	v_cvt_pk_fp8_f32 v148, v141, v142 op_sel:[0,0,1]
	v_mul_f32_e32 v141, 0x42800000, v58
	v_mul_f32_e32 v142, 0x42800000, v70
	s_ashr_i32 s30, s28, 31
	v_cvt_pk_fp8_f32 v149, v141, v142
	v_mul_f32_e32 v141, 0x42800000, v59
	v_mul_f32_e32 v142, 0x42800000, v71
	s_lshr_b32 s30, s30, 23
	v_cvt_pk_fp8_f32 v150, v141, v142
	s_add_i32 s30, s28, s30
	s_and_b32 s30, s30, 0xfffffe00
	s_sub_i32 s30, s28, s30
	v_mul_f32_e32 v141, 0x42800000, v83
	s_waitcnt vmcnt(0)
	v_mul_f32_e32 v142, 0x42800000, v95
	s_bfe_u32 s31, s30, 0x60019
	v_cvt_pk_fp8_f32 v150, v141, v142 op_sel:[0,0,1]
	v_mul_f32_e32 v141, 0x42800000, v60
	v_mul_f32_e32 v142, 0x42800000, v72
	s_add_i32 s31, s30, s31
	v_cvt_pk_fp8_f32 v151, v141, v142
	v_mul_f32_e32 v141, 0x42800000, v61
	v_mul_f32_e32 v142, 0x42800000, v73
	s_sext_i32_i16 s31, s31
	v_mul_f32_e32 v143, 0x42800000, v42
	v_mul_f32_e32 v144, 0x42800000, v46
	v_cvt_pk_fp8_f32 v152, v141, v142
	v_cvt_pk_fp8_f32 v145, v143, v144 op_sel:[0,0,1]
	v_mul_f32_e32 v143, 0x42800000, v44
	v_mul_f32_e32 v144, 0x42800000, v48
	s_ashr_i32 s34, s31, 6
	v_cvt_pk_fp8_f32 v147, v143, v144 op_sel:[0,0,1]
	v_mul_f32_e32 v143, 0x42800000, v82
	v_mul_f32_e32 v144, 0x42800000, v94
	s_lshl_b32 s31, s34, 11
	s_lshl_b32 s30, s30, 5
	v_cvt_pk_fp8_f32 v149, v143, v144 op_sel:[0,0,1]
	v_mul_f32_e32 v143, 0x42800000, v84
	v_mul_f32_e32 v144, 0x42800000, v96
	v_mul_f32_e32 v141, 0x42800000, v85
	v_mul_f32_e32 v142, 0x42800000, v97
	s_sub_i32 s30, s30, s31
	v_cvt_pk_fp8_f32 v151, v143, v144 op_sel:[0,0,1]
	v_cvt_pk_fp8_f32 v152, v141, v142 op_sel:[0,0,1]
	s_ashr_i32 s31, s30, 31
	ds_write2_b32 v136, v145, v146 offset1:32
	ds_write2_b32 v136, v147, v148 offset0:64 offset1:96
	ds_write2_b32 v137, v149, v150 offset1:32
	ds_write2_b32 v137, v151, v152 offset0:64 offset1:96
	s_lshl_b64 s[30:31], s[30:31], 10
	s_waitcnt lgkmcnt(0)
	s_add_u32 s30, s9, s30
	s_addc_u32 s31, s10, s31
	s_lshl_b32 s34, s34, 7
	ds_read_b128 v[142:145], v138
	ds_read_b128 v[146:149], v138 offset:2048
	s_ashr_i32 s35, s34, 31
	s_add_u32 s30, s30, s34
	s_addc_u32 s31, s31, s35
	v_lshl_add_u64 v[154:155], s[30:31], 0, v[132:133]
	s_waitcnt lgkmcnt(1)
	global_store_dwordx4 v[154:155], v[142:145], off nt
	ds_read_b128 v[142:145], v139
	ds_read_b128 v[150:153], v140
	v_add_co_u32_e32 v156, vcc, s11, v154
	s_nop 1
	v_addc_co_u32_e32 v157, vcc, 0, v155, vcc
	s_waitcnt lgkmcnt(1)
	global_store_dwordx4 v[156:157], v[142:145], off nt
	s_nop 1
	v_add_co_u32_e32 v142, vcc, 0x4000, v154
	s_nop 1
	v_addc_co_u32_e32 v143, vcc, 0, v155, vcc
	global_store_dwordx4 v[142:143], v[146:149], off nt
	v_add_co_u32_e32 v142, vcc, 0x6000, v154
	s_nop 1
	v_addc_co_u32_e32 v143, vcc, 0, v155, vcc
	s_waitcnt lgkmcnt(0)
	global_store_dwordx4 v[142:143], v[150:153], off nt
	s_waitcnt lgkmcnt(0)
	s_andn2_b64 vcc, exec, s[0:1]
	s_mov_b64 s[0:1], -1
	s_cbranch_vccnz .LBB0_207
	s_add_i32 s0, s27, s28
	s_cmpk_gt_i32 s0, 0x1ff
	s_cbranch_scc1 .LBB0_206
	s_ashr_i32 s1, s0, 31
	s_lshr_b32 s1, s1, 23
	s_add_i32 s1, s0, s1
	s_and_b32 s1, s1, 0xfffffe00
	s_sub_i32 s1, s0, s1
	s_bfe_u32 s0, s1, 0x60019
	s_add_i32 s0, s1, s0
	s_sext_i32_i16 s0, s0
	s_lshr_b32 s0, s0, 6
	s_bfe_i64 s[30:31], s[0:1], 0x100000
	s_lshl_b64 s[30:31], s[30:31], 20
	s_add_u32 s28, s4, s30
	s_addc_u32 s30, s5, s31
	s_lshl_b32 s0, s0, 11
	s_lshl_b32 s1, s1, 5
	s_sub_i32 s0, s1, s0
	s_ashr_i32 s1, s0, 31
	s_lshl_b64 s[0:1], s[0:1], 2
	s_add_u32 s0, s28, s0
	s_addc_u32 s1, s30, s1
	v_lshl_add_u64 v[82:83], s[0:1], 0, v[130:131]
	v_add_co_u32_e32 v2, vcc, s11, v82
	s_nop 1
	v_addc_co_u32_e32 v3, vcc, 0, v83, vcc
	v_add_co_u32_e32 v6, vcc, s12, v82
	global_load_dwordx4 v[30:33], v[82:83], off nt
	s_nop 0
	global_load_dwordx4 v[2:5], v[2:3], off nt
	v_addc_co_u32_e32 v7, vcc, 0, v83, vcc
	v_add_co_u32_e32 v10, vcc, s13, v82
	s_nop 1
	v_addc_co_u32_e32 v11, vcc, 0, v83, vcc
	v_add_co_u32_e32 v14, vcc, s14, v82
	global_load_dwordx4 v[6:9], v[6:7], off nt
	s_nop 0
	global_load_dwordx4 v[10:13], v[10:11], off nt
	v_addc_co_u32_e32 v15, vcc, 0, v83, vcc
	v_add_co_u32_e32 v18, vcc, s15, v82
	s_nop 1
	v_addc_co_u32_e32 v19, vcc, 0, v83, vcc
	v_add_co_u32_e32 v22, vcc, s20, v82
	global_load_dwordx4 v[14:17], v[14:15], off nt
	s_nop 0
	global_load_dwordx4 v[18:21], v[18:19], off nt
	v_addc_co_u32_e32 v23, vcc, 0, v83, vcc
	v_add_co_u32_e32 v26, vcc, s21, v82
	s_nop 1
	v_addc_co_u32_e32 v27, vcc, 0, v83, vcc
	v_add_co_u32_e32 v34, vcc, s22, v82
	global_load_dwordx4 v[22:25], v[22:23], off nt
	s_nop 0
	global_load_dwordx4 v[26:29], v[26:27], off nt
	v_addc_co_u32_e32 v35, vcc, 0, v83, vcc
	v_add_co_u32_e32 v38, vcc, s23, v82
	s_nop 1
	v_addc_co_u32_e32 v39, vcc, 0, v83, vcc
	v_add_co_u32_e32 v42, vcc, s24, v82
	global_load_dwordx4 v[34:37], v[34:35], off nt
	s_nop 0
	global_load_dwordx4 v[38:41], v[38:39], off nt
	v_addc_co_u32_e32 v43, vcc, 0, v83, vcc
	v_add_co_u32_e32 v46, vcc, s25, v82
	s_nop 1
	v_addc_co_u32_e32 v47, vcc, 0, v83, vcc
	v_add_co_u32_e32 v58, vcc, s26, v82
	global_load_dwordx4 v[42:45], v[42:43], off nt
	s_nop 0
	global_load_dwordx4 v[46:49], v[46:47], off nt
	v_addc_co_u32_e32 v59, vcc, 0, v83, vcc
	v_add_co_u32_e32 v70, vcc, 0xc2000, v82
	s_nop 1
	v_addc_co_u32_e32 v71, vcc, 0, v83, vcc
	v_add_co_u32_e32 v84, vcc, 0xc4000, v82
	global_load_dwordx4 v[58:61], v[58:59], off nt
	s_nop 0
	global_load_dwordx4 v[70:73], v[70:71], off nt
	v_addc_co_u32_e32 v85, vcc, 0, v83, vcc
	v_add_co_u32_e32 v94, vcc, 0xc6000, v82
	s_nop 1
	v_addc_co_u32_e32 v95, vcc, 0, v83, vcc
	global_load_dwordx4 v[82:85], v[84:85], off nt
	s_nop 0
	global_load_dwordx4 v[94:97], v[94:95], off nt
	s_branch .LBB0_206

.LBB0_215:
	v_mul_f32_e32 v141, 0x42800000, v50
	v_mul_f32_e32 v142, 0x42800000, v54
	v_cvt_pk_fp8_f32 v145, v141, v142
	v_mul_f32_e32 v141, 0x42800000, v51
	v_mul_f32_e32 v142, 0x42800000, v55
	v_cvt_pk_fp8_f32 v146, v141, v142
	v_mul_f32_e32 v141, 0x42800000, v63
	v_mul_f32_e32 v142, 0x42800000, v67
	v_cvt_pk_fp8_f32 v146, v141, v142 op_sel:[0,0,1]
	v_mul_f32_e32 v141, 0x42800000, v52
	v_mul_f32_e32 v142, 0x42800000, v56
	v_cvt_pk_fp8_f32 v147, v141, v142
	v_mul_f32_e32 v141, 0x42800000, v53
	v_mul_f32_e32 v142, 0x42800000, v57
	v_cvt_pk_fp8_f32 v148, v141, v142
	v_mul_f32_e32 v141, 0x42800000, v65
	v_mul_f32_e32 v142, 0x42800000, v69
	v_cvt_pk_fp8_f32 v148, v141, v142 op_sel:[0,0,1]
	v_mul_f32_e32 v141, 0x42800000, v74
	v_mul_f32_e32 v142, 0x42800000, v78
	v_cvt_pk_fp8_f32 v149, v141, v142
	v_mul_f32_e32 v141, 0x42800000, v75
	v_mul_f32_e32 v142, 0x42800000, v79
	v_cvt_pk_fp8_f32 v150, v141, v142
	v_mul_f32_e32 v141, 0x42800000, v87
	v_mul_f32_e32 v142, 0x42800000, v91
	v_cvt_pk_fp8_f32 v150, v141, v142 op_sel:[0,0,1]
	v_mul_f32_e32 v141, 0x42800000, v76
	v_mul_f32_e32 v142, 0x42800000, v80
	v_cvt_pk_fp8_f32 v151, v141, v142
	v_mul_f32_e32 v141, 0x42800000, v77
	v_mul_f32_e32 v142, 0x42800000, v81
	v_mul_f32_e32 v143, 0x42800000, v62
	v_mul_f32_e32 v144, 0x42800000, v66
	v_cvt_pk_fp8_f32 v152, v141, v142
	v_cvt_pk_fp8_f32 v145, v143, v144 op_sel:[0,0,1]
	v_mul_f32_e32 v143, 0x42800000, v64
	v_mul_f32_e32 v144, 0x42800000, v68
	v_cvt_pk_fp8_f32 v147, v143, v144 op_sel:[0,0,1]
	v_mul_f32_e32 v143, 0x42800000, v86
	v_mul_f32_e32 v144, 0x42800000, v90
	v_cvt_pk_fp8_f32 v149, v143, v144 op_sel:[0,0,1]
	v_mul_f32_e32 v143, 0x42800000, v88
	v_mul_f32_e32 v144, 0x42800000, v92
	v_mul_f32_e32 v141, 0x42800000, v89
	v_mul_f32_e32 v142, 0x42800000, v93
	v_cvt_pk_fp8_f32 v151, v143, v144 op_sel:[0,0,1]
	v_cvt_pk_fp8_f32 v152, v141, v142 op_sel:[0,0,1]
	ds_write2_b32 v134, v145, v146 offset1:32
	ds_write2_b32 v134, v147, v148 offset0:64 offset1:96
	ds_write2_b32 v135, v149, v150 offset1:32
	ds_write2_b32 v135, v151, v152 offset0:64 offset1:96
	v_mul_f32_e32 v141, 0x42800000, v98
	v_mul_f32_e32 v142, 0x42800000, v102
	v_cvt_pk_fp8_f32 v145, v141, v142
	v_mul_f32_e32 v141, 0x42800000, v99
	v_mul_f32_e32 v142, 0x42800000, v103
	v_cvt_pk_fp8_f32 v146, v141, v142
	v_mul_f32_e32 v141, 0x42800000, v107
	v_mul_f32_e32 v142, 0x42800000, v111
	v_cvt_pk_fp8_f32 v146, v141, v142 op_sel:[0,0,1]
	v_mul_f32_e32 v141, 0x42800000, v100
	v_mul_f32_e32 v142, 0x42800000, v104
	v_cvt_pk_fp8_f32 v147, v141, v142
	v_mul_f32_e32 v141, 0x42800000, v101
	v_mul_f32_e32 v142, 0x42800000, v105
	v_cvt_pk_fp8_f32 v148, v141, v142
	v_mul_f32_e32 v141, 0x42800000, v109
	v_mul_f32_e32 v142, 0x42800000, v113
	v_cvt_pk_fp8_f32 v148, v141, v142 op_sel:[0,0,1]
	v_mul_f32_e32 v141, 0x42800000, v114
	v_mul_f32_e32 v142, 0x42800000, v118
	s_ashr_i32 s0, s25, 31
	v_cvt_pk_fp8_f32 v149, v141, v142
	v_mul_f32_e32 v141, 0x42800000, v115
	v_mul_f32_e32 v142, 0x42800000, v119
	s_lshr_b32 s0, s0, 22
	v_cvt_pk_fp8_f32 v150, v141, v142
	s_add_i32 s0, s25, s0
	s_and_b32 s0, s0, 0xfffffc00
	s_sub_i32 s0, s25, s0
	v_mul_f32_e32 v141, 0x42800000, v123
	v_mul_f32_e32 v142, 0x42800000, v127
	s_bfe_u32 s1, s0, 0x60019
	v_cvt_pk_fp8_f32 v150, v141, v142 op_sel:[0,0,1]
	v_mul_f32_e32 v141, 0x42800000, v116
	v_mul_f32_e32 v142, 0x42800000, v120
	s_add_i32 s1, s0, s1
	v_cvt_pk_fp8_f32 v151, v141, v142
	v_mul_f32_e32 v141, 0x42800000, v117
	v_mul_f32_e32 v142, 0x42800000, v121
	s_sext_i32_i16 s1, s1
	v_mul_f32_e32 v143, 0x42800000, v106
	v_mul_f32_e32 v144, 0x42800000, v110
	v_cvt_pk_fp8_f32 v152, v141, v142
	s_add_i32 s7, s25, s6
	v_cvt_pk_fp8_f32 v145, v143, v144 op_sel:[0,0,1]
	v_mul_f32_e32 v143, 0x42800000, v108
	v_mul_f32_e32 v144, 0x42800000, v112
	s_ashr_i32 s25, s1, 6
	v_cvt_pk_fp8_f32 v147, v143, v144 op_sel:[0,0,1]
	v_mul_f32_e32 v143, 0x42800000, v122
	v_mul_f32_e32 v144, 0x42800000, v126
	s_lshl_b32 s1, s25, 11
	s_lshl_b32 s0, s0, 5
	v_cvt_pk_fp8_f32 v149, v143, v144 op_sel:[0,0,1]
	v_mul_f32_e32 v143, 0x42800000, v124
	v_mul_f32_e32 v144, 0x42800000, v128
	v_mul_f32_e32 v141, 0x42800000, v125
	v_mul_f32_e32 v142, 0x42800000, v129
	s_sub_i32 s0, s0, s1
	v_cvt_pk_fp8_f32 v151, v143, v144 op_sel:[0,0,1]
	v_cvt_pk_fp8_f32 v152, v141, v142 op_sel:[0,0,1]
	s_ashr_i32 s1, s0, 31
	ds_write2_b32 v136, v145, v146 offset1:32
	ds_write2_b32 v136, v147, v148 offset0:64 offset1:96
	ds_write2_b32 v137, v149, v150 offset1:32
	ds_write2_b32 v137, v151, v152 offset0:64 offset1:96
	s_lshl_b64 s[0:1], s[0:1], 11
	s_waitcnt lgkmcnt(0)
	s_add_u32 s0, s4, s0
	s_addc_u32 s1, s5, s1
	s_lshl_b32 s25, s25, 7
	ds_read_b128 v[142:145], v138
	ds_read_b128 v[146:149], v138 offset:2048
	s_ashr_i32 s26, s25, 31
	s_add_u32 s0, s0, s25
	s_addc_u32 s1, s1, s26
	v_lshl_add_u64 v[154:155], s[0:1], 0, v[132:133]
	s_waitcnt lgkmcnt(1)
	global_store_dwordx4 v[154:155], v[142:145], off nt
	ds_read_b128 v[142:145], v139
	ds_read_b128 v[150:153], v140
	v_add_co_u32_e32 v156, vcc, s10, v154
	s_cmpk_gt_i32 s7, 0x3ff
	s_nop 0
	v_addc_co_u32_e32 v157, vcc, 0, v155, vcc
	s_waitcnt lgkmcnt(1)
	global_store_dwordx4 v[156:157], v[142:145], off nt
	s_cselect_b64 s[0:1], -1, 0
	s_nop 0
	v_add_co_u32_e32 v142, vcc, 0x8000, v154
	s_nop 1
	v_addc_co_u32_e32 v143, vcc, 0, v155, vcc
	global_store_dwordx4 v[142:143], v[146:149], off nt
	v_add_co_u32_e32 v142, vcc, 0xc000, v154
	s_nop 1
	v_addc_co_u32_e32 v143, vcc, 0, v155, vcc
	s_waitcnt lgkmcnt(0)
	global_store_dwordx4 v[142:143], v[150:153], off nt
	s_waitcnt lgkmcnt(0)

.LBB0_219:
	s_waitcnt vmcnt(1)
	v_mul_f32_e32 v141, 0x42800000, v30
	v_mul_f32_e32 v142, 0x42800000, v2
	v_cvt_pk_fp8_f32 v145, v141, v142
	v_mul_f32_e32 v141, 0x42800000, v31
	v_mul_f32_e32 v142, 0x42800000, v3
	v_cvt_pk_fp8_f32 v146, v141, v142
	v_mul_f32_e32 v141, 0x42800000, v7
	v_mul_f32_e32 v142, 0x42800000, v11
	v_cvt_pk_fp8_f32 v146, v141, v142 op_sel:[0,0,1]
	v_mul_f32_e32 v141, 0x42800000, v32
	v_mul_f32_e32 v142, 0x42800000, v4
	v_cvt_pk_fp8_f32 v147, v141, v142
	v_mul_f32_e32 v141, 0x42800000, v33
	v_mul_f32_e32 v142, 0x42800000, v5
	v_cvt_pk_fp8_f32 v148, v141, v142
	v_mul_f32_e32 v141, 0x42800000, v9
	v_mul_f32_e32 v142, 0x42800000, v13
	v_cvt_pk_fp8_f32 v148, v141, v142 op_sel:[0,0,1]
	v_mul_f32_e32 v141, 0x42800000, v14
	v_mul_f32_e32 v142, 0x42800000, v18
	v_cvt_pk_fp8_f32 v149, v141, v142
	v_mul_f32_e32 v141, 0x42800000, v15
	v_mul_f32_e32 v142, 0x42800000, v19
	v_cvt_pk_fp8_f32 v150, v141, v142
	v_mul_f32_e32 v141, 0x42800000, v23
	v_mul_f32_e32 v142, 0x42800000, v27
	v_cvt_pk_fp8_f32 v150, v141, v142 op_sel:[0,0,1]
	v_mul_f32_e32 v141, 0x42800000, v16
	v_mul_f32_e32 v142, 0x42800000, v20
	v_cvt_pk_fp8_f32 v151, v141, v142
	v_mul_f32_e32 v141, 0x42800000, v17
	v_mul_f32_e32 v142, 0x42800000, v21
	v_mul_f32_e32 v143, 0x42800000, v6
	v_mul_f32_e32 v144, 0x42800000, v10
	v_cvt_pk_fp8_f32 v152, v141, v142
	v_cvt_pk_fp8_f32 v145, v143, v144 op_sel:[0,0,1]
	v_mul_f32_e32 v143, 0x42800000, v8
	v_mul_f32_e32 v144, 0x42800000, v12
	v_cvt_pk_fp8_f32 v147, v143, v144 op_sel:[0,0,1]
	v_mul_f32_e32 v143, 0x42800000, v22
	v_mul_f32_e32 v144, 0x42800000, v26
	v_cvt_pk_fp8_f32 v149, v143, v144 op_sel:[0,0,1]
	v_mul_f32_e32 v143, 0x42800000, v24
	v_mul_f32_e32 v144, 0x42800000, v28
	v_mul_f32_e32 v141, 0x42800000, v25
	v_mul_f32_e32 v142, 0x42800000, v29
	v_cvt_pk_fp8_f32 v151, v143, v144 op_sel:[0,0,1]
	v_cvt_pk_fp8_f32 v152, v141, v142 op_sel:[0,0,1]
	ds_write2_b32 v134, v145, v146 offset1:32
	ds_write2_b32 v134, v147, v148 offset0:64 offset1:96
	ds_write2_b32 v135, v149, v150 offset1:32
	ds_write2_b32 v135, v151, v152 offset0:64 offset1:96
	v_mul_f32_e32 v141, 0x42800000, v34
	v_mul_f32_e32 v142, 0x42800000, v38
	v_cvt_pk_fp8_f32 v145, v141, v142
	v_mul_f32_e32 v141, 0x42800000, v35
	v_mul_f32_e32 v142, 0x42800000, v39
	v_cvt_pk_fp8_f32 v146, v141, v142
	v_mul_f32_e32 v141, 0x42800000, v43
	v_mul_f32_e32 v142, 0x42800000, v47
	v_cvt_pk_fp8_f32 v146, v141, v142 op_sel:[0,0,1]
	v_mul_f32_e32 v141, 0x42800000, v36
	v_mul_f32_e32 v142, 0x42800000, v40
	v_cvt_pk_fp8_f32 v147, v141, v142
	v_mul_f32_e32 v141, 0x42800000, v37
	v_mul_f32_e32 v142, 0x42800000, v41
	v_cvt_pk_fp8_f32 v148, v141, v142
	v_mul_f32_e32 v141, 0x42800000, v45
	v_mul_f32_e32 v142, 0x42800000, v49
	v_cvt_pk_fp8_f32 v148, v141, v142 op_sel:[0,0,1]
	v_mul_f32_e32 v141, 0x42800000, v58
	v_mul_f32_e32 v142, 0x42800000, v70
	s_ashr_i32 s26, s7, 31
	v_cvt_pk_fp8_f32 v149, v141, v142
	v_mul_f32_e32 v141, 0x42800000, v59
	v_mul_f32_e32 v142, 0x42800000, v71
	s_lshr_b32 s26, s26, 22
	v_cvt_pk_fp8_f32 v150, v141, v142
	s_add_i32 s26, s7, s26
	s_and_b32 s26, s26, 0xfffffc00
	s_sub_i32 s26, s7, s26
	v_mul_f32_e32 v141, 0x42800000, v83
	s_waitcnt vmcnt(0)
	v_mul_f32_e32 v142, 0x42800000, v95
	s_bfe_u32 s27, s26, 0x60019
	v_cvt_pk_fp8_f32 v150, v141, v142 op_sel:[0,0,1]
	v_mul_f32_e32 v141, 0x42800000, v60
	v_mul_f32_e32 v142, 0x42800000, v72
	s_add_i32 s27, s26, s27
	v_cvt_pk_fp8_f32 v151, v141, v142
	v_mul_f32_e32 v141, 0x42800000, v61
	v_mul_f32_e32 v142, 0x42800000, v73
	s_sext_i32_i16 s27, s27
	v_mul_f32_e32 v143, 0x42800000, v42
	v_mul_f32_e32 v144, 0x42800000, v46
	v_cvt_pk_fp8_f32 v152, v141, v142
	v_cvt_pk_fp8_f32 v145, v143, v144 op_sel:[0,0,1]
	v_mul_f32_e32 v143, 0x42800000, v44
	v_mul_f32_e32 v144, 0x42800000, v48
	s_ashr_i32 s28, s27, 6
	v_cvt_pk_fp8_f32 v147, v143, v144 op_sel:[0,0,1]
	v_mul_f32_e32 v143, 0x42800000, v82
	v_mul_f32_e32 v144, 0x42800000, v94
	s_lshl_b32 s27, s28, 11
	s_lshl_b32 s26, s26, 5
	v_cvt_pk_fp8_f32 v149, v143, v144 op_sel:[0,0,1]
	v_mul_f32_e32 v143, 0x42800000, v84
	v_mul_f32_e32 v144, 0x42800000, v96
	v_mul_f32_e32 v141, 0x42800000, v85
	v_mul_f32_e32 v142, 0x42800000, v97
	s_sub_i32 s26, s26, s27
	v_cvt_pk_fp8_f32 v151, v143, v144 op_sel:[0,0,1]
	v_cvt_pk_fp8_f32 v152, v141, v142 op_sel:[0,0,1]
	s_ashr_i32 s27, s26, 31
	ds_write2_b32 v136, v145, v146 offset1:32
	ds_write2_b32 v136, v147, v148 offset0:64 offset1:96
	ds_write2_b32 v137, v149, v150 offset1:32
	ds_write2_b32 v137, v151, v152 offset0:64 offset1:96
	s_lshl_b64 s[26:27], s[26:27], 11
	s_waitcnt lgkmcnt(0)
	s_add_u32 s26, s4, s26
	s_addc_u32 s27, s5, s27
	s_lshl_b32 s28, s28, 7
	ds_read_b128 v[142:145], v138
	ds_read_b128 v[146:149], v138 offset:2048
	s_ashr_i32 s29, s28, 31
	s_add_u32 s26, s26, s28
	s_addc_u32 s27, s27, s29
	v_lshl_add_u64 v[154:155], s[26:27], 0, v[132:133]
	s_waitcnt lgkmcnt(1)
	global_store_dwordx4 v[154:155], v[142:145], off nt
	ds_read_b128 v[142:145], v139
	ds_read_b128 v[150:153], v140
	v_add_co_u32_e32 v156, vcc, s10, v154
	s_nop 1
	v_addc_co_u32_e32 v157, vcc, 0, v155, vcc
	s_waitcnt lgkmcnt(1)
	global_store_dwordx4 v[156:157], v[142:145], off nt
	s_nop 1
	v_add_co_u32_e32 v142, vcc, 0x8000, v154
	s_nop 1
	v_addc_co_u32_e32 v143, vcc, 0, v155, vcc
	global_store_dwordx4 v[142:143], v[146:149], off nt
	v_add_co_u32_e32 v142, vcc, 0xc000, v154
	s_nop 1
	v_addc_co_u32_e32 v143, vcc, 0, v155, vcc
	s_waitcnt lgkmcnt(0)
	global_store_dwordx4 v[142:143], v[150:153], off nt
	s_waitcnt lgkmcnt(0)
	s_andn2_b64 vcc, exec, s[0:1]
	s_mov_b64 s[0:1], -1
	s_cbranch_vccnz .LBB0_216
	s_add_i32 s0, s8, s7
	s_cmpk_gt_i32 s0, 0x3ff
	s_cbranch_scc1 .LBB0_215
	s_ashr_i32 s1, s0, 31
	s_lshr_b32 s1, s1, 22
	s_add_i32 s1, s0, s1
	s_and_b32 s1, s1, 0xfffffc00
	s_sub_i32 s1, s0, s1
	s_bfe_u32 s0, s1, 0x60019
	s_add_i32 s0, s1, s0
	s_sext_i32_i16 s0, s0
	s_lshr_b32 s0, s0, 6
	s_bfe_i64 s[26:27], s[0:1], 0x100000
	s_lshl_b64 s[26:27], s[26:27], 20
	s_add_u32 s7, s52, s26
	s_addc_u32 s26, s53, s27
	s_lshl_b32 s0, s0, 11
	s_lshl_b32 s1, s1, 5
	s_sub_i32 s0, s1, s0
	s_ashr_i32 s1, s0, 31
	s_lshl_b64 s[0:1], s[0:1], 2
	s_add_u32 s0, s7, s0
	s_addc_u32 s1, s26, s1
	v_lshl_add_u64 v[82:83], s[0:1], 0, v[130:131]
	v_add_co_u32_e32 v2, vcc, s9, v82
	s_nop 1
	v_addc_co_u32_e32 v3, vcc, 0, v83, vcc
	v_add_co_u32_e32 v6, vcc, s10, v82
	global_load_dwordx4 v[30:33], v[82:83], off nt
	s_nop 0
	global_load_dwordx4 v[2:5], v[2:3], off nt
	v_addc_co_u32_e32 v7, vcc, 0, v83, vcc
	v_add_co_u32_e32 v10, vcc, s11, v82
	s_nop 1
	v_addc_co_u32_e32 v11, vcc, 0, v83, vcc
	v_add_co_u32_e32 v14, vcc, s12, v82
	global_load_dwordx4 v[6:9], v[6:7], off nt
	s_nop 0
	global_load_dwordx4 v[10:13], v[10:11], off nt
	v_addc_co_u32_e32 v15, vcc, 0, v83, vcc
	v_add_co_u32_e32 v18, vcc, s13, v82
	s_nop 1
	v_addc_co_u32_e32 v19, vcc, 0, v83, vcc
	v_add_co_u32_e32 v22, vcc, s14, v82
	global_load_dwordx4 v[14:17], v[14:15], off nt
	s_nop 0
	global_load_dwordx4 v[18:21], v[18:19], off nt
	v_addc_co_u32_e32 v23, vcc, 0, v83, vcc
	v_add_co_u32_e32 v26, vcc, s15, v82
	s_nop 1
	v_addc_co_u32_e32 v27, vcc, 0, v83, vcc
	v_add_co_u32_e32 v34, vcc, s20, v82
	global_load_dwordx4 v[22:25], v[22:23], off nt
	s_nop 0
	global_load_dwordx4 v[26:29], v[26:27], off nt
	v_addc_co_u32_e32 v35, vcc, 0, v83, vcc
	v_add_co_u32_e32 v38, vcc, s21, v82
	s_nop 1
	v_addc_co_u32_e32 v39, vcc, 0, v83, vcc
	v_add_co_u32_e32 v42, vcc, s22, v82
	global_load_dwordx4 v[34:37], v[34:35], off nt
	s_nop 0
	global_load_dwordx4 v[38:41], v[38:39], off nt
	v_addc_co_u32_e32 v43, vcc, 0, v83, vcc
	v_add_co_u32_e32 v46, vcc, s23, v82
	s_nop 1
	v_addc_co_u32_e32 v47, vcc, 0, v83, vcc
	v_add_co_u32_e32 v58, vcc, s24, v82
	global_load_dwordx4 v[42:45], v[42:43], off nt
	s_nop 0
	global_load_dwordx4 v[46:49], v[46:47], off nt
	v_addc_co_u32_e32 v59, vcc, 0, v83, vcc
	v_add_co_u32_e32 v70, vcc, 0xc2000, v82
	s_nop 1
	v_addc_co_u32_e32 v71, vcc, 0, v83, vcc
	v_add_co_u32_e32 v84, vcc, 0xc4000, v82
	global_load_dwordx4 v[58:61], v[58:59], off nt
	s_nop 0
	global_load_dwordx4 v[70:73], v[70:71], off nt
	v_addc_co_u32_e32 v85, vcc, 0, v83, vcc
	v_add_co_u32_e32 v94, vcc, 0xc6000, v82
	s_nop 1
	v_addc_co_u32_e32 v95, vcc, 0, v83, vcc
	global_load_dwordx4 v[82:85], v[84:85], off nt
	s_nop 0
	global_load_dwordx4 v[94:97], v[94:95], off nt
	s_branch .LBB0_215

.LBB0_263:
	v_mul_f32_e32 v106, 0x41800000, v106
	v_mul_f32_e32 v107, 0x41800000, v107
	v_mul_f32_e32 v108, 0x41800000, v108
	v_mul_f32_e32 v109, 0x41800000, v109
	v_mul_f32_e32 v110, 0x41800000, v110
	v_mul_f32_e32 v111, 0x41800000, v111
	v_mul_f32_e32 v112, 0x41800000, v112
	v_mul_f32_e32 v113, 0x41800000, v113
	v_mul_f32_e32 v114, 0x41800000, v114
	v_mul_f32_e32 v115, 0x41800000, v115
	v_mul_f32_e32 v116, 0x41800000, v116
	v_mul_f32_e32 v117, 0x41800000, v117
	v_mul_f32_e32 v118, 0x41800000, v118
	v_mul_f32_e32 v119, 0x41800000, v119
	v_mul_f32_e32 v120, 0x41800000, v120
	v_mul_f32_e32 v121, 0x41800000, v121
	v_cvt_f32_i32_e32 v143, v143
	v_cvt_f32_i32_e32 v145, v145
	v_cvt_f32_i32_e32 v144, v144
	v_cvt_f32_i32_e32 v142, v142
	v_cvt_f32_i32_e32 v139, v139
	v_cvt_f32_i32_e32 v141, v141
	v_cvt_f32_i32_e32 v140, v140
	v_cvt_f32_i32_e32 v138, v138
	s_waitcnt lgkmcnt(0)
	v_pk_mul_f32 v[190:191], v[116:117], v[188:189] op_sel_hi:[1,0]
	v_pk_mul_f32 v[192:193], v[114:115], v[188:189] op_sel_hi:[1,0]
	v_pk_mul_f32 v[144:145], v[190:191], v[144:145]
	v_pk_mul_f32 v[142:143], v[192:193], v[142:143]
	v_pk_mul_f32 v[190:191], v[120:121], v[188:189] op_sel_hi:[1,0]
	v_pk_mul_f32 v[192:193], v[118:119], v[188:189] op_sel_hi:[1,0]
	v_pk_mul_f32 v[140:141], v[190:191], v[140:141]
	v_pk_mul_f32 v[190:191], v[192:193], v[138:139]
	v_cvt_pk_fp8_f32 v138, v142, v143
	v_cvt_pk_fp8_f32 v139, v190, v191
	v_cvt_f32_i32_e32 v135, v135
	v_cvt_f32_i32_e32 v137, v137
	v_cvt_f32_i32_e32 v136, v136
	v_cvt_f32_i32_e32 v134, v134
	v_cvt_f32_i32_e32 v131, v131
	v_cvt_f32_i32_e32 v133, v133
	v_cvt_f32_i32_e32 v132, v132
	v_cvt_f32_i32_e32 v130, v130
	s_mul_hi_i32 s0, s10, 0x2aaaaaab
	v_cvt_pk_fp8_f32 v138, v144, v145 op_sel:[0,0,1]
	v_cvt_pk_fp8_f32 v139, v140, v141 op_sel:[0,0,1]
	v_pk_mul_f32 v[140:141], v[108:109], v[188:189] op_sel_hi:[1,0]
	v_pk_mul_f32 v[142:143], v[106:107], v[188:189] op_sel_hi:[1,0]
	s_lshr_b32 s1, s0, 31
	s_ashr_i32 s0, s0, 1
	v_pk_mul_f32 v[136:137], v[140:141], v[136:137]
	v_pk_mul_f32 v[134:135], v[142:143], v[134:135]
	v_pk_mul_f32 v[140:141], v[112:113], v[188:189] op_sel_hi:[1,0]
	v_pk_mul_f32 v[142:143], v[110:111], v[188:189] op_sel_hi:[1,0]
	s_add_i32 s0, s0, s1
	v_pk_mul_f32 v[132:133], v[140:141], v[132:133]
	v_pk_mul_f32 v[140:141], v[142:143], v[130:131]
	s_mul_i32 s1, s0, 12
	v_cvt_pk_fp8_f32 v130, v134, v135
	s_sub_i32 s1, s10, s1
	v_cvt_pk_fp8_f32 v131, v140, v141
	s_ashr_i32 s4, s1, 2
	s_lshl_b32 s19, s4, 1
	s_sub_i32 s29, 11, s19
	v_and_b32_e32 v194, 0x7cf, v146
	v_cvt_pk_fp8_f32 v131, v132, v133 op_sel:[0,0,1]
	v_lshlrev_b32_e32 v132, s29, v146
	v_and_b32_e32 v132, 0x7fe, v132
	v_lshrrev_b32_e32 v133, s19, v194
	v_add_u32_e32 v134, v132, v133
	v_or_b32_e32 v132, 16, v194
	v_lshlrev_b32_e32 v133, s29, v132
	v_cvt_f32_i32_e32 v129, v129
	v_cvt_f32_i32_e32 v128, v128
	v_and_b32_e32 v133, 0x7fe, v133
	v_lshrrev_b32_e32 v132, s19, v132
	v_cvt_f32_i32_e32 v123, v123
	v_cvt_f32_i32_e32 v122, v122
	v_cvt_pk_fp8_f32 v130, v136, v137 op_sel:[0,0,1]
	v_add_u32_e32 v135, v133, v132
	v_mov_b32_e32 v132, v189
	v_cvt_f32_i32_e32 v127, v127
	v_cvt_f32_i32_e32 v126, v126
	v_pk_mul_f32 v[136:137], v[120:121], v[132:133] op_sel_hi:[1,0]
	v_pk_mul_f32 v[140:141], v[118:119], v[132:133] op_sel_hi:[1,0]
	v_pk_mul_f32 v[128:129], v[136:137], v[128:129]
	v_pk_mul_f32 v[136:137], v[114:115], v[132:133] op_sel_hi:[1,0]
	v_cvt_f32_i32_e32 v125, v125
	v_cvt_f32_i32_e32 v124, v124
	v_pk_mul_f32 v[122:123], v[136:137], v[122:123]
	v_pk_mul_f32 v[126:127], v[140:141], v[126:127]
	v_cvt_pk_fp8_f32 v140, v122, v123
	v_cvt_pk_fp8_f32 v141, v126, v127
	v_pk_mul_f32 v[126:127], v[116:117], v[132:133] op_sel_hi:[1,0]
	v_pk_mul_f32 v[122:123], v[126:127], v[124:125]
	v_add_u32_e32 v143, 0x80, v146
	v_cvt_pk_fp8_f32 v140, v122, v123 op_sel:[0,0,1]
	v_cvt_pk_fp8_f32 v141, v128, v129 op_sel:[0,0,1]
	v_or_b32_e32 v122, 32, v194
	v_lshlrev_b32_e32 v123, s29, v122
	v_and_b32_e32 v123, 0x7fe, v123
	v_lshrrev_b32_e32 v122, s19, v122
	v_add_u32_e32 v123, v123, v122
	v_or_b32_e32 v122, 48, v194
	v_lshlrev_b32_e32 v124, s29, v122
	v_and_b32_e32 v124, 0x7fe, v124
	v_lshrrev_b32_e32 v122, s19, v122
	v_add_u32_e32 v142, v124, v122
	v_and_b32_e32 v124, 0x7cf, v143
	v_lshlrev_b32_e32 v122, s29, v124
	v_and_b32_e32 v122, 0x7fe, v122
	v_lshrrev_b32_e32 v125, s19, v124
	v_add_u32_e32 v125, v122, v125
	v_or_b32_e32 v122, 16, v124
	s_mul_hi_i32 s10, s0, 0x6000000
	s_mul_i32 s12, s0, 0x6000000
	s_lshl_b32 s0, s1, 22
	v_lshlrev_b32_e32 v126, s29, v122
	s_ashr_i32 s5, s4, 31
	s_and_b32 s1, s0, 0xc00000
	s_ashr_i32 s0, s11, 11
	v_and_b32_e32 v126, 0x7fe, v126
	v_lshrrev_b32_e32 v122, s19, v122
	s_add_u32 s12, s48, s12
	v_cmp_ne_u64_e32 vcc, 0, v[162:163]
	v_add_u32_e32 v126, v126, v122
	s_addc_u32 s13, s49, s10
	v_cndmask_b32_e32 v127, v134, v135, vcc
	v_cndmask_b32_e32 v122, v125, v126, vcc
	v_cmp_eq_u32_e32 vcc, 2, v162
	v_cmp_eq_u32_e64 s[10:11], 3, v162
	s_or_b64 s[14:15], s[10:11], vcc
	s_lshl_b64 s[4:5], s[4:5], 24
	v_cndmask_b32_e64 v127, v127, 0, s[14:15]
	v_lshlrev_b32_e32 v146, 7, v127
	s_add_u32 s4, s12, s4
	v_mov_b32_e32 v127, s0
	s_addc_u32 s5, s13, s5
	v_cndmask_b32_e64 v128, v127, 0, s[14:15]
	s_add_u32 s36, s4, s1
	v_ashrrev_i32_e32 v129, 31, v128
	s_addc_u32 s37, s5, 0
	v_lshlrev_b64 v[128:129], 18, v[128:129]
	v_lshl_add_u64 v[136:137], s[36:37], 0, v[128:129]
	v_lshl_add_u64 v[136:137], v[136:137], 0, v[146:147]
	v_lshl_add_u64 v[136:137], v[136:137], 0, s[20:21]
	v_cvt_f32_i32_e32 v103, v103
	v_cvt_f32_i32_e32 v102, v102
	v_lshl_add_u64 v[136:137], v[136:137], 0, v[160:161]
	v_permlane16_swap_b32_e32 v138, v140
	v_permlane16_swap_b32_e32 v139, v141
	v_lshl_add_u64 v[136:137], v[136:137], 0, v[164:165]
	global_store_dwordx4 v[136:137], v[138:141], off
	v_pk_mul_f32 v[136:137], v[112:113], v[132:133] op_sel_hi:[1,0]
	v_cvt_f32_i32_e32 v105, v105
	v_pk_mul_f32 v[138:139], v[110:111], v[132:133] op_sel_hi:[1,0]
	v_pk_mul_f32 v[102:103], v[138:139], v[102:103]
	v_cvt_f32_i32_e32 v104, v104
	v_cvt_pk_fp8_f32 v133, v102, v103
	v_cvt_f32_i32_e32 v99, v99
	v_cvt_f32_i32_e32 v98, v98
	v_pk_mul_f32 v[104:105], v[136:137], v[104:105]
	v_pk_mul_f32 v[136:137], v[106:107], v[132:133] op_sel_hi:[1,0]
	v_cvt_f32_i32_e32 v101, v101
	v_cvt_f32_i32_e32 v100, v100
	v_pk_mul_f32 v[98:99], v[136:137], v[98:99]
	v_pk_mul_f32 v[102:103], v[108:109], v[132:133] op_sel_hi:[1,0]
	v_cvt_pk_fp8_f32 v132, v98, v99
	v_pk_mul_f32 v[98:99], v[102:103], v[100:101]
	s_add_u32 s4, s36, 0x200000
	v_cvt_pk_fp8_f32 v132, v98, v99 op_sel:[0,0,1]
	s_addc_u32 s5, s37, 0
	v_cvt_pk_fp8_f32 v133, v104, v105 op_sel:[0,0,1]
	v_lshl_add_u64 v[98:99], s[4:5], 0, v[128:129]
	v_lshl_add_u64 v[98:99], v[98:99], 0, v[146:147]
	v_lshl_add_u64 v[98:99], v[98:99], 0, s[20:21]
	v_cvt_f32_i32_e32 v95, v95
	v_cvt_f32_i32_e32 v97, v97
	v_cvt_f32_i32_e32 v96, v96
	v_cvt_f32_i32_e32 v94, v94
	v_lshl_add_u64 v[98:99], v[98:99], 0, v[160:161]
	v_cvt_f32_i32_e32 v91, v91
	v_cvt_f32_i32_e32 v93, v93
	v_cvt_f32_i32_e32 v92, v92
	v_cvt_f32_i32_e32 v90, v90
	v_permlane16_swap_b32_e32 v130, v132
	v_permlane16_swap_b32_e32 v131, v133
	v_lshl_add_u64 v[98:99], v[98:99], 0, v[164:165]
	global_store_dwordx4 v[98:99], v[130:133], off
	v_pk_mul_f32 v[98:99], v[116:117], v[186:187] op_sel_hi:[1,0]
	v_pk_mul_f32 v[100:101], v[114:115], v[186:187] op_sel_hi:[1,0]
	v_pk_mul_f32 v[96:97], v[98:99], v[96:97]
	v_pk_mul_f32 v[94:95], v[100:101], v[94:95]
	v_pk_mul_f32 v[98:99], v[120:121], v[186:187] op_sel_hi:[1,0]
	v_pk_mul_f32 v[100:101], v[118:119], v[186:187] op_sel_hi:[1,0]
	v_pk_mul_f32 v[92:93], v[98:99], v[92:93]
	v_pk_mul_f32 v[98:99], v[100:101], v[90:91]
	v_cvt_pk_fp8_f32 v90, v94, v95
	v_cvt_pk_fp8_f32 v91, v98, v99
	v_cvt_f32_i32_e32 v87, v87
	v_cvt_f32_i32_e32 v89, v89
	v_cvt_f32_i32_e32 v88, v88
	v_cvt_f32_i32_e32 v86, v86
	v_cvt_f32_i32_e32 v79, v79
	v_cvt_f32_i32_e32 v81, v81
	v_cvt_f32_i32_e32 v80, v80
	v_cvt_f32_i32_e32 v78, v78
	v_cvt_pk_fp8_f32 v90, v96, v97 op_sel:[0,0,1]
	v_cvt_pk_fp8_f32 v91, v92, v93 op_sel:[0,0,1]
	v_pk_mul_f32 v[92:93], v[108:109], v[186:187] op_sel_hi:[1,0]
	v_pk_mul_f32 v[94:95], v[106:107], v[186:187] op_sel_hi:[1,0]
	v_pk_mul_f32 v[88:89], v[92:93], v[88:89]
	v_pk_mul_f32 v[86:87], v[94:95], v[86:87]
	v_pk_mul_f32 v[92:93], v[112:113], v[186:187] op_sel_hi:[1,0]
	v_pk_mul_f32 v[94:95], v[110:111], v[186:187] op_sel_hi:[1,0]
	v_pk_mul_f32 v[80:81], v[92:93], v[80:81]
	v_pk_mul_f32 v[92:93], v[94:95], v[78:79]
	v_cvt_pk_fp8_f32 v78, v86, v87
	v_cvt_pk_fp8_f32 v79, v92, v93
	v_cvt_f32_i32_e32 v85, v85
	v_cvt_f32_i32_e32 v84, v84
	v_cvt_pk_fp8_f32 v79, v80, v81 op_sel:[0,0,1]
	v_mov_b32_e32 v80, v187
	v_cvt_pk_fp8_f32 v78, v88, v89 op_sel:[0,0,1]
	v_pk_mul_f32 v[86:87], v[120:121], v[80:81] op_sel_hi:[1,0]
	v_cvt_f32_i32_e32 v75, v75
	v_cvt_f32_i32_e32 v74, v74
	v_cvt_f32_i32_e32 v83, v83
	v_cvt_f32_i32_e32 v82, v82
	v_pk_mul_f32 v[84:85], v[86:87], v[84:85]
	v_pk_mul_f32 v[88:89], v[118:119], v[80:81] op_sel_hi:[1,0]
	v_pk_mul_f32 v[86:87], v[114:115], v[80:81] op_sel_hi:[1,0]
	v_cvt_f32_i32_e32 v77, v77
	v_cvt_f32_i32_e32 v76, v76
	v_pk_mul_f32 v[74:75], v[86:87], v[74:75]
	v_pk_mul_f32 v[82:83], v[88:89], v[82:83]
	v_cvt_pk_fp8_f32 v92, v74, v75
	v_cvt_pk_fp8_f32 v93, v82, v83
	v_pk_mul_f32 v[82:83], v[116:117], v[80:81] op_sel_hi:[1,0]
	v_cndmask_b32_e32 v122, v122, v123, vcc
	v_pk_mul_f32 v[74:75], v[82:83], v[76:77]
	v_cmp_eq_u32_e32 vcc, 1, v166
	v_cvt_pk_fp8_f32 v92, v74, v75 op_sel:[0,0,1]
	v_cndmask_b32_e64 v122, v122, v142, s[10:11]
	v_cvt_pk_fp8_f32 v93, v84, v85 op_sel:[0,0,1]
	v_cndmask_b32_e32 v74, v134, v135, vcc
	v_cmp_eq_u32_e64 s[10:11], 2, v166
	s_ashr_i32 s1, s0, 31
	v_cmp_eq_u32_e64 s[12:13], 3, v166
	v_cndmask_b32_e64 v74, v74, v123, s[10:11]
	s_lshl_b64 s[0:1], s[0:1], 18
	v_cndmask_b32_e64 v74, v74, v142, s[12:13]
	s_add_u32 s38, s36, s0
	v_ashrrev_i32_e32 v75, 31, v74
	s_addc_u32 s39, s37, s1
	v_lshlrev_b64 v[74:75], 7, v[74:75]
	v_cvt_f32_i32_e32 v71, v71
	v_cvt_f32_i32_e32 v70, v70
	v_lshl_add_u64 v[76:77], s[38:39], 0, v[74:75]
	v_lshl_add_u64 v[76:77], v[76:77], 0, s[20:21]
	v_lshl_add_u64 v[76:77], v[76:77], 0, v[160:161]
	v_pk_mul_f32 v[82:83], v[110:111], v[80:81] op_sel_hi:[1,0]
	v_permlane16_swap_b32_e32 v90, v92
	v_permlane16_swap_b32_e32 v91, v93
	v_lshl_add_u64 v[76:77], v[76:77], 0, v[164:165]
	v_pk_mul_f32 v[70:71], v[82:83], v[70:71]
	global_store_dwordx4 v[76:77], v[90:93], off
	v_pk_mul_f32 v[76:77], v[112:113], v[80:81] op_sel_hi:[1,0]
	v_cvt_f32_i32_e32 v73, v73
	v_cvt_f32_i32_e32 v72, v72
	v_cvt_pk_fp8_f32 v81, v70, v71
	v_cvt_f32_i32_e32 v59, v59
	v_cvt_f32_i32_e32 v58, v58
	v_cvt_f32_i32_e32 v61, v61
	v_cvt_f32_i32_e32 v60, v60
	v_pk_mul_f32 v[72:73], v[76:77], v[72:73]
	v_pk_mul_f32 v[76:77], v[106:107], v[80:81] op_sel_hi:[1,0]
	v_cvt_f32_i32_e32 v55, v55
	v_cvt_f32_i32_e32 v57, v57
	v_cvt_f32_i32_e32 v56, v56
	v_cvt_f32_i32_e32 v54, v54
	v_pk_mul_f32 v[58:59], v[76:77], v[58:59]
	v_cvt_f32_i32_e32 v51, v51
	v_cvt_f32_i32_e32 v53, v53
	v_cvt_f32_i32_e32 v52, v52
	v_cvt_f32_i32_e32 v50, v50
	v_pk_mul_f32 v[70:71], v[108:109], v[80:81] op_sel_hi:[1,0]
	v_cvt_pk_fp8_f32 v80, v58, v59
	v_pk_mul_f32 v[58:59], v[70:71], v[60:61]
	v_pk_mul_f32 v[60:61], v[116:117], v[184:185] op_sel_hi:[1,0]
	v_pk_mul_f32 v[70:71], v[114:115], v[184:185] op_sel_hi:[1,0]
	v_pk_mul_f32 v[56:57], v[60:61], v[56:57]
	v_pk_mul_f32 v[54:55], v[70:71], v[54:55]
	v_pk_mul_f32 v[60:61], v[120:121], v[184:185] op_sel_hi:[1,0]
	v_pk_mul_f32 v[70:71], v[118:119], v[184:185] op_sel_hi:[1,0]
	v_pk_mul_f32 v[52:53], v[60:61], v[52:53]
	v_pk_mul_f32 v[60:61], v[70:71], v[50:51]
	v_cvt_pk_fp8_f32 v50, v54, v55
	v_cvt_pk_fp8_f32 v51, v60, v61
	v_cvt_pk_fp8_f32 v50, v56, v57 op_sel:[0,0,1]
	v_cvt_f32_i32_e32 v55, v69
	v_cvt_f32_i32_e32 v54, v68
	v_cvt_pk_fp8_f32 v51, v52, v53 op_sel:[0,0,1]
	v_cvt_f32_i32_e32 v53, v67
	v_cvt_f32_i32_e32 v52, v66
	v_cvt_pk_fp8_f32 v80, v58, v59 op_sel:[0,0,1]
	s_add_u32 s0, s4, s0
	v_cvt_pk_fp8_f32 v81, v72, v73 op_sel:[0,0,1]
	s_addc_u32 s1, s5, s1
	v_pk_mul_f32 v[56:57], v[108:109], v[184:185] op_sel_hi:[1,0]
	v_lshl_add_u64 v[58:59], s[0:1], 0, v[74:75]
	v_pk_mul_f32 v[60:61], v[106:107], v[184:185] op_sel_hi:[1,0]
	v_pk_mul_f32 v[54:55], v[56:57], v[54:55]
	v_cvt_f32_i32_e32 v57, v63
	v_cvt_f32_i32_e32 v56, v62
	v_lshl_add_u64 v[58:59], v[58:59], 0, s[20:21]
	v_pk_mul_f32 v[52:53], v[60:61], v[52:53]
	v_cvt_f32_i32_e32 v61, v65
	v_cvt_f32_i32_e32 v60, v64
	v_lshl_add_u64 v[58:59], v[58:59], 0, v[160:161]
	v_permlane16_swap_b32_e32 v78, v80
	v_permlane16_swap_b32_e32 v79, v81
	v_lshl_add_u64 v[58:59], v[58:59], 0, v[164:165]
	v_pk_mul_f32 v[64:65], v[110:111], v[184:185] op_sel_hi:[1,0]
	global_store_dwordx4 v[58:59], v[78:81], off
	v_pk_mul_f32 v[62:63], v[112:113], v[184:185] op_sel_hi:[1,0]
	v_pk_mul_f32 v[56:57], v[64:65], v[56:57]
	v_mov_b32_e32 v59, v54
	v_pk_mul_f32 v[60:61], v[62:63], v[60:61]
	v_mov_b32_e32 v62, v55
	v_cvt_pk_fp8_f32 v54, v52, v53
	v_cvt_f32_i32_e32 v39, v39
	v_cvt_f32_i32_e32 v38, v38
	v_cvt_pk_fp8_f32 v55, v56, v57
	v_cvt_f32_i32_e32 v35, v35
	v_cvt_f32_i32_e32 v34, v34
	v_mov_b32_e32 v56, v185
	v_cvt_f32_i32_e32 v41, v41
	v_cvt_f32_i32_e32 v40, v40
	v_mov_b32_e32 v52, v60
	v_mov_b32_e32 v53, v61
	v_pk_mul_f32 v[60:61], v[118:119], v[56:57] op_sel_hi:[1,0]
	v_cvt_pk_fp8_f32 v55, v52, v53 op_sel:[0,0,1]
	v_pk_mul_f32 v[38:39], v[60:61], v[38:39]
	v_pk_mul_f32 v[60:61], v[114:115], v[56:57] op_sel_hi:[1,0]
	v_pk_mul_f32 v[52:53], v[120:121], v[56:57] op_sel_hi:[1,0]
	v_cvt_f32_i32_e32 v37, v37
	v_cvt_f32_i32_e32 v36, v36
	v_pk_mul_f32 v[34:35], v[60:61], v[34:35]
	v_pk_mul_f32 v[40:41], v[52:53], v[40:41]
	v_cvt_pk_fp8_f32 v52, v34, v35
	v_cvt_pk_fp8_f32 v53, v38, v39
	v_pk_mul_f32 v[38:39], v[116:117], v[56:57] op_sel_hi:[1,0]
	v_ashrrev_i32_e32 v58, 11, v143
	v_pk_mul_f32 v[34:35], v[38:39], v[36:37]
	v_cvt_pk_fp8_f32 v52, v34, v35 op_sel:[0,0,1]
	v_cvt_pk_fp8_f32 v53, v40, v41 op_sel:[0,0,1]
	v_cndmask_b32_e64 v34, v58, v127, s[14:15]
	v_ashrrev_i32_e32 v35, 31, v34
	v_lshlrev_b64 v[34:35], 18, v[34:35]
	v_ashrrev_i32_e32 v123, 31, v122
	v_lshl_add_u64 v[36:37], s[36:37], 0, v[34:35]
	v_lshlrev_b64 v[38:39], 7, v[122:123]
	v_lshl_add_u64 v[36:37], v[36:37], 0, v[38:39]
	v_lshl_add_u64 v[36:37], v[36:37], 0, s[20:21]
	v_cvt_f32_i32_e32 v41, v47
	v_cvt_f32_i32_e32 v40, v46
	v_lshl_add_u64 v[36:37], v[36:37], 0, v[160:161]
	v_permlane16_swap_b32_e32 v50, v52
	v_permlane16_swap_b32_e32 v51, v53
	v_lshl_add_u64 v[36:37], v[36:37], 0, v[164:165]
	global_store_dwordx4 v[36:37], v[50:53], off
	v_cvt_f32_i32_e32 v37, v49
	v_cvt_f32_i32_e32 v36, v48
	v_pk_mul_f32 v[48:49], v[110:111], v[56:57] op_sel_hi:[1,0]
	v_pk_mul_f32 v[46:47], v[112:113], v[56:57] op_sel_hi:[1,0]
	v_pk_mul_f32 v[40:41], v[48:49], v[40:41]
	v_cvt_pk_fp8_f32 v57, v40, v41
	v_cvt_f32_i32_e32 v43, v43
	v_cvt_f32_i32_e32 v42, v42
	v_pk_mul_f32 v[36:37], v[46:47], v[36:37]
	v_pk_mul_f32 v[46:47], v[106:107], v[56:57] op_sel_hi:[1,0]
	v_cvt_f32_i32_e32 v45, v45
	v_cvt_f32_i32_e32 v44, v44
	v_pk_mul_f32 v[42:43], v[46:47], v[42:43]
	v_pk_mul_f32 v[40:41], v[108:109], v[56:57] op_sel_hi:[1,0]
	v_cvt_pk_fp8_f32 v56, v42, v43
	v_pk_mul_f32 v[40:41], v[40:41], v[44:45]
	v_cvt_pk_fp8_f32 v54, v59, v62 op_sel:[0,0,1]
	v_cvt_pk_fp8_f32 v56, v40, v41 op_sel:[0,0,1]
	v_cvt_pk_fp8_f32 v57, v36, v37 op_sel:[0,0,1]
	v_lshl_add_u64 v[34:35], s[4:5], 0, v[34:35]
	v_lshl_add_u64 v[34:35], v[34:35], 0, v[38:39]
	v_lshl_add_u64 v[34:35], v[34:35], 0, s[20:21]
	v_lshl_add_u64 v[34:35], v[34:35], 0, v[160:161]
	v_permlane16_swap_b32_e32 v54, v56
	v_permlane16_swap_b32_e32 v55, v57
	v_lshl_add_u64 v[34:35], v[34:35], 0, v[164:165]
	global_store_dwordx4 v[34:35], v[54:57], off
	v_or_b32_e32 v34, 32, v124
	v_cvt_f32_i32_e32 v23, v23
	v_cvt_f32_i32_e32 v25, v25
	v_cvt_f32_i32_e32 v24, v24
	v_cvt_f32_i32_e32 v22, v22
	v_lshlrev_b32_e32 v35, s29, v34
	v_cvt_f32_i32_e32 v19, v19
	v_cvt_f32_i32_e32 v21, v21
	v_cvt_f32_i32_e32 v20, v20
	v_cvt_f32_i32_e32 v18, v18
	v_and_b32_e32 v35, 0x7fe, v35
	v_lshrrev_b32_e32 v34, s19, v34
	v_add_u32_e32 v38, v35, v34
	v_pk_mul_f32 v[34:35], v[116:117], v[182:183] op_sel_hi:[1,0]
	v_pk_mul_f32 v[36:37], v[114:115], v[182:183] op_sel_hi:[1,0]
	v_pk_mul_f32 v[24:25], v[34:35], v[24:25]
	v_pk_mul_f32 v[22:23], v[36:37], v[22:23]
	v_pk_mul_f32 v[34:35], v[120:121], v[182:183] op_sel_hi:[1,0]
	v_pk_mul_f32 v[36:37], v[118:119], v[182:183] op_sel_hi:[1,0]
	v_pk_mul_f32 v[20:21], v[34:35], v[20:21]
	v_pk_mul_f32 v[34:35], v[36:37], v[18:19]
	v_cvt_pk_fp8_f32 v18, v22, v23
	v_cvt_pk_fp8_f32 v19, v34, v35
	v_cvt_pk_fp8_f32 v18, v24, v25 op_sel:[0,0,1]
	v_cvt_f32_i32_e32 v23, v33
	v_cvt_f32_i32_e32 v22, v32
	v_cvt_pk_fp8_f32 v19, v20, v21 op_sel:[0,0,1]
	v_cvt_f32_i32_e32 v21, v31
	v_cvt_f32_i32_e32 v20, v30
	v_pk_mul_f32 v[24:25], v[108:109], v[182:183] op_sel_hi:[1,0]
	v_cvt_f32_i32_e32 v29, v29
	v_pk_mul_f32 v[22:23], v[24:25], v[22:23]
	v_cvt_f32_i32_e32 v25, v27
	v_cvt_f32_i32_e32 v28, v28
	v_cvt_f32_i32_e32 v24, v26
	v_pk_mul_f32 v[30:31], v[106:107], v[182:183] op_sel_hi:[1,0]
	v_pk_mul_f32 v[26:27], v[112:113], v[182:183] op_sel_hi:[1,0]
	v_pk_mul_f32 v[20:21], v[30:31], v[20:21]
	v_pk_mul_f32 v[30:31], v[110:111], v[182:183] op_sel_hi:[1,0]
	v_pk_mul_f32 v[26:27], v[26:27], v[28:29]
	v_pk_mul_f32 v[24:25], v[30:31], v[24:25]
	v_mov_b32_e32 v28, v22
	v_mov_b32_e32 v29, v23
	v_cvt_pk_fp8_f32 v22, v20, v21
	v_cvt_pk_fp8_f32 v23, v24, v25
	v_cvt_f32_i32_e32 v7, v7
	v_cvt_pk_fp8_f32 v23, v26, v27 op_sel:[0,0,1]
	v_or_b32_e32 v20, 48, v124
	v_lshlrev_b32_e32 v21, s29, v20
	v_cvt_f32_i32_e32 v6, v6
	v_and_b32_e32 v21, 0x7fe, v21
	v_lshrrev_b32_e32 v20, s19, v20
	v_cvt_f32_i32_e32 v3, v3
	v_cvt_f32_i32_e32 v2, v2
	v_add_u32_e32 v25, v21, v20
	v_mov_b32_e32 v24, v183
	v_cvt_f32_i32_e32 v9, v9
	v_cvt_f32_i32_e32 v8, v8
	v_pk_mul_f32 v[26:27], v[118:119], v[24:25] op_sel_hi:[1,0]
	v_pk_mul_f32 v[20:21], v[120:121], v[24:25] op_sel_hi:[1,0]
	v_pk_mul_f32 v[6:7], v[26:27], v[6:7]
	v_pk_mul_f32 v[26:27], v[114:115], v[24:25] op_sel_hi:[1,0]
	v_cvt_f32_i32_e32 v5, v5
	v_cvt_f32_i32_e32 v4, v4
	v_pk_mul_f32 v[2:3], v[26:27], v[2:3]
	v_pk_mul_f32 v[8:9], v[20:21], v[8:9]
	v_cvt_pk_fp8_f32 v20, v2, v3
	v_cvt_pk_fp8_f32 v21, v6, v7
	v_pk_mul_f32 v[6:7], v[116:117], v[24:25] op_sel_hi:[1,0]
	v_pk_mul_f32 v[2:3], v[6:7], v[4:5]
	v_cndmask_b32_e32 v6, v125, v126, vcc
	v_cndmask_b32_e64 v6, v6, v38, s[10:11]
	v_cvt_pk_fp8_f32 v20, v2, v3 op_sel:[0,0,1]
	v_ashrrev_i32_e32 v59, 31, v58
	v_cndmask_b32_e64 v6, v6, v25, s[12:13]
	v_cvt_pk_fp8_f32 v21, v8, v9 op_sel:[0,0,1]
	v_lshlrev_b64 v[2:3], 18, v[58:59]
	v_ashrrev_i32_e32 v7, 31, v6
	v_lshl_add_u64 v[4:5], s[36:37], 0, v[2:3]
	v_lshlrev_b64 v[6:7], 7, v[6:7]
	v_lshl_add_u64 v[4:5], v[4:5], 0, v[6:7]
	v_lshl_add_u64 v[4:5], v[4:5], 0, s[20:21]
	v_cvt_f32_i32_e32 v9, v15
	v_cvt_f32_i32_e32 v8, v14
	v_lshl_add_u64 v[4:5], v[4:5], 0, v[160:161]
	v_permlane16_swap_b32_e32 v18, v20
	v_permlane16_swap_b32_e32 v19, v21
	v_lshl_add_u64 v[4:5], v[4:5], 0, v[164:165]
	global_store_dwordx4 v[4:5], v[18:21], off
	v_cvt_f32_i32_e32 v5, v17
	v_cvt_f32_i32_e32 v4, v16
	v_pk_mul_f32 v[16:17], v[110:111], v[24:25] op_sel_hi:[1,0]
	v_pk_mul_f32 v[14:15], v[112:113], v[24:25] op_sel_hi:[1,0]
	v_pk_mul_f32 v[8:9], v[16:17], v[8:9]
	v_cvt_pk_fp8_f32 v25, v8, v9
	v_cvt_f32_i32_e32 v11, v11
	v_cvt_f32_i32_e32 v10, v10
	v_pk_mul_f32 v[4:5], v[14:15], v[4:5]
	v_pk_mul_f32 v[14:15], v[106:107], v[24:25] op_sel_hi:[1,0]
	v_cvt_f32_i32_e32 v13, v13
	v_cvt_f32_i32_e32 v12, v12
	v_pk_mul_f32 v[10:11], v[14:15], v[10:11]
	v_pk_mul_f32 v[8:9], v[108:109], v[24:25] op_sel_hi:[1,0]
	v_cvt_pk_fp8_f32 v24, v10, v11
	v_pk_mul_f32 v[8:9], v[8:9], v[12:13]
	v_cvt_pk_fp8_f32 v22, v28, v29 op_sel:[0,0,1]
	v_cvt_pk_fp8_f32 v24, v8, v9 op_sel:[0,0,1]
	v_cvt_pk_fp8_f32 v25, v4, v5 op_sel:[0,0,1]
	v_lshl_add_u64 v[2:3], s[4:5], 0, v[2:3]
	v_lshl_add_u64 v[2:3], v[2:3], 0, v[6:7]
	v_lshl_add_u64 v[2:3], v[2:3], 0, s[20:21]
	v_lshl_add_u64 v[2:3], v[2:3], 0, v[160:161]
	v_permlane16_swap_b32_e32 v22, v24
	v_permlane16_swap_b32_e32 v23, v25
	v_lshl_add_u64 v[2:3], v[2:3], 0, v[164:165]
	global_store_dwordx4 v[2:3], v[22:25], off
	s_and_b64 vcc, exec, s[8:9]
	s_mov_b64 s[0:1], -1
	s_cbranch_vccnz .LBB0_234

.LBB0_338:
	global_load_dword v181, v[118:119], off
	v_lshl_add_u64 v[190:191], s[92:93], 0, v[116:117]
	global_load_dwordx2 v[66:67], v[190:191], off offset:-128
	global_load_dwordx2 v[68:69], v[190:191], off offset:-64
	global_load_dwordx2 v[138:139], v[190:191], off offset:-32
	global_load_dwordx2 v[136:137], v[190:191], off
	global_load_dwordx2 v[134:135], v[190:191], off offset:32
	global_load_dwordx2 v[132:133], v[190:191], off offset:64
	global_load_dwordx2 v[130:131], v[190:191], off offset:96
	ds_read_b128 v[62:65], v160
	ds_read_b128 v[58:61], v161
	ds_read_b128 v[54:57], v162
	ds_read_b128 v[50:53], v163
	ds_read_b64_tr_b16 v[182:183], v164 offset:32768
	ds_read_b64_tr_b16 v[184:185], v165 offset:33792
	ds_read_b64_tr_b16 v[186:187], v164 offset:40960
	ds_read_b64_tr_b16 v[188:189], v165 offset:41984
	s_add_u32 s74, s74, 0x10000
	s_waitcnt lgkmcnt(2)
	v_mfma_f32_16x16x32_bf16 v[182:185], v[182:185], v[62:65], 0
	s_addc_u32 s75, s75, 0
	s_mov_b64 s[76:77], 0x200
	v_lshl_add_u64 v[124:125], v[124:125], 0, s[4:5]
	s_waitcnt lgkmcnt(0)
	v_mfma_f32_16x16x32_bf16 v[182:185], v[186:189], v[58:61], v[182:185]
	ds_read_b64_tr_b16 v[186:187], v164 offset:49152
	ds_read_b64_tr_b16 v[188:189], v165 offset:50176
	v_lshl_add_u64 v[126:127], v[126:127], 0, s[4:5]
	v_lshl_add_u64 v[128:129], v[128:129], 0, s[4:5]
	s_waitcnt lgkmcnt(0)
	v_mfma_f32_16x16x32_bf16 v[182:185], v[186:189], v[54:57], v[182:185]
	ds_read_b64_tr_b16 v[186:187], v164 offset:57344
	ds_read_b64_tr_b16 v[188:189], v165 offset:58368
	global_load_dwordx2 v[190:191], v[190:191], off offset:-96
	v_lshl_add_u64 v[108:109], v[108:109], 0, s[4:5]
	s_waitcnt lgkmcnt(0)
	v_mfma_f32_16x16x32_bf16 v[182:185], v[186:189], v[50:53], v[182:185]
	v_add_u32_e32 v180, 0x200, v180
	v_lshl_add_u64 v[116:117], v[116:117], 0, s[4:5]
	v_lshl_add_u64 v[118:119], v[118:119], 0, s[76:77]
	s_cmp_lg_u32 s74, 0x40000
	s_waitcnt vmcnt(7)
	v_lshlrev_b32_e32 v186, 16, v66
	v_and_b32_e32 v66, 0xffff0000, v66
	s_nop 0
	v_add_f32_e32 v183, v181, v183
	v_mul_f32_e32 v66, v183, v66
	v_mul_f32_e32 v183, 0x41800000, v66
	v_lshlrev_b32_e32 v66, 16, v67
	v_add_f32_e32 v184, v181, v184
	v_mul_f32_e32 v66, v184, v66
	v_add_f32_e32 v182, v181, v182
	v_mul_f32_e32 v184, 0x41800000, v66
	v_and_b32_e32 v66, 0xffff0000, v67
	v_add_f32_e32 v67, v181, v185
	v_mul_f32_e32 v182, v182, v186
	v_mul_f32_e32 v66, v67, v66
	v_mul_f32_e32 v182, 0x41800000, v182
	v_mul_f32_e32 v67, 0x41800000, v66
	v_cvt_pk_fp8_f32 v66, v182, v183
	v_cvt_pk_fp8_f32 v66, v184, v67 op_sel:[0,0,1]
	ds_read_b64_tr_b16 v[182:183], v166 offset:32768
	ds_read_b64_tr_b16 v[184:185], v167 offset:33792
	ds_read_b64_tr_b16 v[186:187], v166 offset:40960
	ds_read_b64_tr_b16 v[188:189], v167 offset:41984
	s_waitcnt lgkmcnt(2)
	v_mfma_f32_16x16x32_bf16 v[182:185], v[182:185], v[62:65], 0
	s_waitcnt vmcnt(0)
	v_lshlrev_b32_e32 v67, 16, v190
	s_waitcnt lgkmcnt(0)
	v_mfma_f32_16x16x32_bf16 v[182:185], v[186:189], v[58:61], v[182:185]
	ds_read_b64_tr_b16 v[186:187], v166 offset:49152
	ds_read_b64_tr_b16 v[188:189], v167 offset:50176
	s_waitcnt lgkmcnt(0)
	v_mfma_f32_16x16x32_bf16 v[182:185], v[186:189], v[54:57], v[182:185]
	ds_read_b64_tr_b16 v[186:187], v166 offset:57344
	ds_read_b64_tr_b16 v[188:189], v167 offset:58368
	s_waitcnt lgkmcnt(0)
	v_mfma_f32_16x16x32_bf16 v[182:185], v[186:189], v[50:53], v[182:185]
	s_nop 7
	v_add_f32_e32 v182, v181, v182
	v_mul_f32_e32 v67, v182, v67
	v_mul_f32_e32 v182, 0x41800000, v67
	v_and_b32_e32 v67, 0xffff0000, v190
	v_add_f32_e32 v183, v181, v183
	v_mul_f32_e32 v67, v183, v67
	v_mul_f32_e32 v183, 0x41800000, v67
	v_lshlrev_b32_e32 v67, 16, v191
	v_add_f32_e32 v184, v181, v184
	v_mul_f32_e32 v67, v184, v67
	v_mul_f32_e32 v184, 0x41800000, v67
	v_and_b32_e32 v67, 0xffff0000, v191
	v_add_f32_e32 v185, v181, v185
	v_mul_f32_e32 v67, v185, v67
	v_mul_f32_e32 v185, 0x41800000, v67
	v_cvt_pk_fp8_f32 v67, v182, v183
	v_cvt_pk_fp8_f32 v67, v184, v185 op_sel:[0,0,1]
	ds_read_b64_tr_b16 v[182:183], v168 offset:32768
	ds_read_b64_tr_b16 v[184:185], v169 offset:33792
	ds_read_b64_tr_b16 v[186:187], v168 offset:40960
	ds_read_b64_tr_b16 v[188:189], v169 offset:41984
	s_waitcnt lgkmcnt(2)
	v_mfma_f32_16x16x32_bf16 v[182:185], v[182:185], v[62:65], 0
	v_permlane16_swap_b32_e32 v66, v67
	s_waitcnt lgkmcnt(0)
	v_mfma_f32_16x16x32_bf16 v[182:185], v[186:189], v[58:61], v[182:185]
	ds_read_b64_tr_b16 v[186:187], v168 offset:49152
	ds_read_b64_tr_b16 v[188:189], v169 offset:50176
	s_waitcnt lgkmcnt(0)
	v_mfma_f32_16x16x32_bf16 v[182:185], v[186:189], v[54:57], v[182:185]
	ds_read_b64_tr_b16 v[186:187], v168 offset:57344
	ds_read_b64_tr_b16 v[188:189], v169 offset:58368
	s_waitcnt lgkmcnt(0)
	v_mfma_f32_16x16x32_bf16 v[182:185], v[186:189], v[50:53], v[182:185]
	v_lshlrev_b32_e32 v186, 16, v68
	v_and_b32_e32 v68, 0xffff0000, v68
	s_nop 5
	v_add_f32_e32 v183, v181, v183
	v_mul_f32_e32 v68, v183, v68
	v_mul_f32_e32 v183, 0x41800000, v68
	v_lshlrev_b32_e32 v68, 16, v69
	v_add_f32_e32 v184, v181, v184
	v_mul_f32_e32 v68, v184, v68
	v_add_f32_e32 v182, v181, v182
	v_mul_f32_e32 v184, 0x41800000, v68
	v_and_b32_e32 v68, 0xffff0000, v69
	v_add_f32_e32 v69, v181, v185
	v_mul_f32_e32 v182, v182, v186
	v_mul_f32_e32 v68, v69, v68
	v_mul_f32_e32 v182, 0x41800000, v182
	v_mul_f32_e32 v69, 0x41800000, v68
	v_cvt_pk_fp8_f32 v68, v182, v183
	v_cvt_pk_fp8_f32 v68, v184, v69 op_sel:[0,0,1]
	ds_read_b64_tr_b16 v[182:183], v170 offset:32768
	ds_read_b64_tr_b16 v[184:185], v171 offset:33792
	ds_read_b64_tr_b16 v[186:187], v170 offset:40960
	ds_read_b64_tr_b16 v[188:189], v171 offset:41984
	s_waitcnt lgkmcnt(2)
	v_mfma_f32_16x16x32_bf16 v[182:185], v[182:185], v[62:65], 0
	s_waitcnt lgkmcnt(0)
	v_mfma_f32_16x16x32_bf16 v[182:185], v[186:189], v[58:61], v[182:185]
	ds_read_b64_tr_b16 v[186:187], v170 offset:49152
	ds_read_b64_tr_b16 v[188:189], v171 offset:50176
	s_waitcnt lgkmcnt(0)
	v_mfma_f32_16x16x32_bf16 v[182:185], v[186:189], v[54:57], v[182:185]
	ds_read_b64_tr_b16 v[186:187], v170 offset:57344
	ds_read_b64_tr_b16 v[188:189], v171 offset:58368
	s_waitcnt lgkmcnt(0)
	v_mfma_f32_16x16x32_bf16 v[182:185], v[186:189], v[50:53], v[182:185]
	s_nop 7
	v_add_f32_e32 v69, v181, v184
	v_lshlrev_b32_e32 v184, 16, v139
	v_mul_f32_e32 v69, v69, v184
	v_mul_f32_e32 v184, 0x41800000, v69
	v_add_f32_e32 v69, v181, v185
	v_and_b32_e32 v139, 0xffff0000, v139
	v_mul_f32_e32 v69, v69, v139
	v_mul_f32_e32 v139, 0x41800000, v69
	v_add_f32_e32 v69, v181, v182
	v_lshlrev_b32_e32 v182, 16, v138
	v_mul_f32_e32 v69, v69, v182
	v_mul_f32_e32 v182, 0x41800000, v69
	v_add_f32_e32 v69, v181, v183
	v_and_b32_e32 v138, 0xffff0000, v138
	v_mul_f32_e32 v69, v69, v138
	v_mul_f32_e32 v138, 0x41800000, v69
	v_cvt_pk_fp8_f32 v69, v182, v138
	v_cvt_pk_fp8_f32 v69, v184, v139 op_sel:[0,0,1]
	v_lshl_add_u64 v[138:139], s[92:93], 0, v[122:123]
	v_lshl_add_u64 v[122:123], v[122:123], 0, s[96:97]
	v_permlane16_swap_b32_e32 v68, v69
	s_nop 1
	v_permlane32_swap_b32_e32 v66, v68
	v_permlane32_swap_b32_e32 v67, v69
	global_store_dwordx4 v[138:139], v[66:69], off
	ds_read_b64_tr_b16 v[66:67], v172 offset:32768
	ds_read_b64_tr_b16 v[68:69], v173 offset:33792
	ds_read_b64_tr_b16 v[182:183], v172 offset:40960
	ds_read_b64_tr_b16 v[184:185], v173 offset:41984
	s_waitcnt lgkmcnt(2)
	v_mfma_f32_16x16x32_bf16 v[66:69], v[66:69], v[62:65], 0
	v_lshlrev_b32_e32 v138, 16, v136
	s_waitcnt lgkmcnt(0)
	v_mfma_f32_16x16x32_bf16 v[66:69], v[182:185], v[58:61], v[66:69]
	ds_read_b64_tr_b16 v[182:183], v172 offset:49152
	ds_read_b64_tr_b16 v[184:185], v173 offset:50176
	s_waitcnt lgkmcnt(0)
	v_mfma_f32_16x16x32_bf16 v[66:69], v[182:185], v[54:57], v[66:69]
	ds_read_b64_tr_b16 v[182:183], v172 offset:57344
	ds_read_b64_tr_b16 v[184:185], v173 offset:58368
	s_waitcnt lgkmcnt(0)
	v_mfma_f32_16x16x32_bf16 v[66:69], v[182:185], v[50:53], v[66:69]
	s_nop 7
	v_add_f32_e32 v66, v181, v66
	v_mul_f32_e32 v66, v66, v138
	v_mul_f32_e32 v138, 0x41800000, v66
	v_and_b32_e32 v66, 0xffff0000, v136
	v_add_f32_e32 v67, v181, v67
	v_mul_f32_e32 v66, v67, v66
	v_mul_f32_e32 v67, 0x41800000, v66
	v_lshlrev_b32_e32 v66, 16, v137
	v_add_f32_e32 v68, v181, v68
	v_mul_f32_e32 v66, v68, v66
	v_mul_f32_e32 v68, 0x41800000, v66
	v_and_b32_e32 v66, 0xffff0000, v137
	v_add_f32_e32 v69, v181, v69
	v_mul_f32_e32 v66, v69, v66
	v_mul_f32_e32 v69, 0x41800000, v66
	v_cvt_pk_fp8_f32 v66, v138, v67
	ds_read_b64_tr_b16 v[136:137], v174 offset:32768
	ds_read_b64_tr_b16 v[138:139], v175 offset:33792
	ds_read_b64_tr_b16 v[182:183], v174 offset:40960
	ds_read_b64_tr_b16 v[184:185], v175 offset:41984
	s_waitcnt lgkmcnt(2)
	v_mfma_f32_16x16x32_bf16 v[136:139], v[136:139], v[62:65], 0
	v_cvt_pk_fp8_f32 v66, v68, v69 op_sel:[0,0,1]
	v_lshlrev_b32_e32 v67, 16, v134
	s_waitcnt lgkmcnt(0)
	v_mfma_f32_16x16x32_bf16 v[136:139], v[182:185], v[58:61], v[136:139]
	ds_read_b64_tr_b16 v[182:183], v174 offset:49152
	ds_read_b64_tr_b16 v[184:185], v175 offset:50176
	s_waitcnt lgkmcnt(0)
	v_mfma_f32_16x16x32_bf16 v[136:139], v[182:185], v[54:57], v[136:139]
	ds_read_b64_tr_b16 v[182:183], v174 offset:57344
	ds_read_b64_tr_b16 v[184:185], v175 offset:58368
	s_waitcnt lgkmcnt(0)
	v_mfma_f32_16x16x32_bf16 v[136:139], v[182:185], v[50:53], v[136:139]
	s_nop 7
	v_add_f32_e32 v68, v181, v136
	v_mul_f32_e32 v67, v68, v67
	v_mul_f32_e32 v68, 0x41800000, v67
	v_and_b32_e32 v67, 0xffff0000, v134
	v_add_f32_e32 v69, v181, v137
	v_mul_f32_e32 v67, v69, v67
	v_mul_f32_e32 v69, 0x41800000, v67
	v_lshlrev_b32_e32 v67, 16, v135
	v_add_f32_e32 v134, v181, v138
	v_mul_f32_e32 v67, v134, v67
	v_mul_f32_e32 v134, 0x41800000, v67
	v_and_b32_e32 v67, 0xffff0000, v135
	v_add_f32_e32 v135, v181, v139
	v_mul_f32_e32 v67, v135, v67
	v_mul_f32_e32 v135, 0x41800000, v67
	v_cvt_pk_fp8_f32 v67, v68, v69
	v_lshlrev_b32_e32 v68, 16, v132
	v_cvt_pk_fp8_f32 v67, v134, v135 op_sel:[0,0,1]
	ds_read_b64_tr_b16 v[134:135], v176 offset:32768
	ds_read_b64_tr_b16 v[136:137], v177 offset:33792
	ds_read_b64_tr_b16 v[182:183], v176 offset:40960
	ds_read_b64_tr_b16 v[184:185], v177 offset:41984
	s_waitcnt lgkmcnt(2)
	v_mfma_f32_16x16x32_bf16 v[134:137], v[134:137], v[62:65], 0
	v_permlane16_swap_b32_e32 v66, v67
	s_waitcnt lgkmcnt(0)
	v_mfma_f32_16x16x32_bf16 v[134:137], v[182:185], v[58:61], v[134:137]
	ds_read_b64_tr_b16 v[182:183], v176 offset:49152
	ds_read_b64_tr_b16 v[184:185], v177 offset:50176
	s_waitcnt lgkmcnt(0)
	v_mfma_f32_16x16x32_bf16 v[134:137], v[182:185], v[54:57], v[134:137]
	ds_read_b64_tr_b16 v[182:183], v176 offset:57344
	ds_read_b64_tr_b16 v[184:185], v177 offset:58368
	s_waitcnt lgkmcnt(0)
	v_mfma_f32_16x16x32_bf16 v[134:137], v[182:185], v[50:53], v[134:137]
	s_nop 7
	v_add_f32_e32 v69, v181, v134
	v_mul_f32_e32 v68, v69, v68
	v_mul_f32_e32 v69, 0x41800000, v68
	v_and_b32_e32 v68, 0xffff0000, v132
	v_add_f32_e32 v132, v181, v135
	v_mul_f32_e32 v68, v132, v68
	v_mul_f32_e32 v132, 0x41800000, v68
	v_lshlrev_b32_e32 v68, 16, v133
	v_add_f32_e32 v134, v181, v136
	v_mul_f32_e32 v68, v134, v68
	v_mul_f32_e32 v134, 0x41800000, v68
	v_and_b32_e32 v68, 0xffff0000, v133
	v_add_f32_e32 v133, v181, v137
	v_mul_f32_e32 v68, v133, v68
	v_mul_f32_e32 v133, 0x41800000, v68
	v_cvt_pk_fp8_f32 v68, v69, v132
	v_cvt_pk_fp8_f32 v68, v134, v133 op_sel:[0,0,1]
	ds_read_b64_tr_b16 v[132:133], v178 offset:32768
	ds_read_b64_tr_b16 v[134:135], v179 offset:33792
	s_waitcnt lgkmcnt(0)
	v_mfma_f32_16x16x32_bf16 v[62:65], v[132:135], v[62:65], 0
	ds_read_b64_tr_b16 v[132:133], v178 offset:40960
	ds_read_b64_tr_b16 v[134:135], v179 offset:41984
	s_waitcnt lgkmcnt(0)
	v_mfma_f32_16x16x32_bf16 v[58:61], v[132:135], v[58:61], v[62:65]
	s_nop 3
	ds_read_b64_tr_b16 v[62:63], v178 offset:49152
	ds_read_b64_tr_b16 v[64:65], v179 offset:50176
	s_waitcnt lgkmcnt(0)
	v_mfma_f32_16x16x32_bf16 v[54:57], v[62:65], v[54:57], v[58:61]
	s_nop 2
	ds_read_b64_tr_b16 v[58:59], v178 offset:57344
	ds_read_b64_tr_b16 v[60:61], v179 offset:58368
	s_waitcnt lgkmcnt(0)
	v_mfma_f32_16x16x32_bf16 v[50:53], v[58:61], v[50:53], v[54:57]
	s_nop 2
	v_lshlrev_b32_e32 v54, 16, v131
	s_nop 3
	v_add_f32_e32 v52, v181, v52
	v_mul_f32_e32 v52, v52, v54
	v_add_f32_e32 v53, v181, v53
	v_and_b32_e32 v54, 0xffff0000, v131
	v_mul_f32_e32 v53, v53, v54
	v_add_f32_e32 v50, v181, v50
	v_lshlrev_b32_e32 v54, 16, v130
	v_mul_f32_e32 v50, v50, v54
	v_add_f32_e32 v51, v181, v51
	v_and_b32_e32 v54, 0xffff0000, v130
	v_mul_f32_e32 v51, v51, v54
	v_mul_f32_e32 v50, 0x41800000, v50
	v_mul_f32_e32 v51, 0x41800000, v51
	v_cvt_pk_fp8_f32 v69, v50, v51
	v_mul_f32_e32 v52, 0x41800000, v52
	v_mul_f32_e32 v53, 0x41800000, v53
	v_lshl_add_u64 v[50:51], s[92:93], 0, v[120:121]
	v_cvt_pk_fp8_f32 v69, v52, v53 op_sel:[0,0,1]
	v_lshl_add_u64 v[120:121], v[120:121], 0, s[96:97]
	s_nop 0
	v_permlane16_swap_b32_e32 v68, v69
	s_nop 1
	v_permlane32_swap_b32_e32 v66, v68
	v_permlane32_swap_b32_e32 v67, v69
	global_store_dwordx4 v[50:51], v[66:69], off
	s_barrier
	s_cbranch_scc0 .LBB0_330

.LBB0_396:
	v_add_u32_e32 v10, s86, v157
	v_add_u32_e32 v12, v10, v149
	v_cvt_pk_bf16_f32 v82, v81, v82
	v_cvt_pk_bf16_f32 v83, v83, v84
	v_cvt_pk_bf16_f32 v84, v85, v86
	v_cvt_pk_bf16_f32 v85, v87, v89
	ds_read_b64_tr_b16 v[86:87], v12 offset:32768
	ds_read_b64_tr_b16 v[88:89], v12 offset:36864
	v_add_u32_e32 v12, v10, v150
	s_waitcnt lgkmcnt(0)
	v_mfma_f32_16x16x32_bf16 v[86:89], v[86:89], v[82:85], v[2:5]
	s_nop 2
	v_add_u32_e32 v4, v10, v151
	ds_read_b64_tr_b16 v[90:91], v12 offset:32768
	ds_read_b64_tr_b16 v[92:93], v12 offset:36864
	ds_read_b64_tr_b16 v[2:3], v4 offset:32768
	ds_read_b64_tr_b16 v[4:5], v4 offset:36864
	v_add_u32_e32 v12, v10, v152
	s_waitcnt lgkmcnt(0)
	v_mfma_f32_16x16x32_bf16 v[58:61], v[2:5], v[82:85], v[58:61]
	v_add_u32_e32 v4, v10, v153
	s_ashr_i32 s43, s42, 31
	v_mfma_f32_16x16x32_bf16 v[6:9], v[90:93], v[82:85], v[6:9]
	ds_read_b64_tr_b16 v[90:91], v12 offset:32768
	ds_read_b64_tr_b16 v[92:93], v12 offset:36864
	ds_read_b64_tr_b16 v[2:3], v4 offset:32768
	ds_read_b64_tr_b16 v[4:5], v4 offset:36864
	v_add_u32_e32 v12, v10, v154
	s_waitcnt lgkmcnt(0)
	v_mfma_f32_16x16x32_bf16 v[66:69], v[2:5], v[82:85], v[66:69]
	v_add_u32_e32 v4, v10, v155
	v_add_u32_e32 v10, v10, v156
	s_lshl_b64 s[16:17], s[42:43], 11
	v_mfma_f32_16x16x32_bf16 v[62:65], v[90:93], v[82:85], v[62:65]
	ds_read_b64_tr_b16 v[90:91], v12 offset:32768
	ds_read_b64_tr_b16 v[92:93], v12 offset:36864
	ds_read_b64_tr_b16 v[2:3], v4 offset:32768
	ds_read_b64_tr_b16 v[4:5], v4 offset:36864
	s_waitcnt lgkmcnt(0)
	v_mfma_f32_16x16x32_bf16 v[70:73], v[2:5], v[82:85], v[70:73]
	v_add_f32_e32 v4, v79, v80
	v_rcp_f32_e32 v5, v4
	v_mfma_f32_16x16x32_bf16 v[74:77], v[90:93], v[82:85], v[74:77]
	ds_read_b64_tr_b16 v[90:91], v10 offset:32768
	ds_read_b64_tr_b16 v[92:93], v10 offset:36864
	v_lshl_add_u32 v10, s5, 7, v108
	v_mul_lo_u32 v2, v10, s30
	v_mul_f32_e32 v10, v5, v86
	v_mul_f32_e32 v79, v5, v87
	v_mul_f32_e32 v6, v5, v6
	v_mul_f32_e32 v7, v5, v7
	v_cvt_pk_fp8_f32 v80, v10, v79
	v_cvt_pk_fp8_f32 v81, v6, v7
	s_waitcnt lgkmcnt(0)
	v_mfma_f32_16x16x32_bf16 v[54:57], v[90:93], v[82:85], v[54:57]
	v_mul_f32_e32 v82, v5, v88
	v_mul_f32_e32 v83, v5, v89
	v_mul_f32_e32 v6, v5, v8
	v_mul_f32_e32 v7, v5, v9
	v_cvt_pk_fp8_f32 v80, v82, v83 op_sel:[0,0,1]
	v_cvt_pk_fp8_f32 v81, v6, v7 op_sel:[0,0,1]
	v_mul_f32_e32 v6, v5, v58
	v_mul_f32_e32 v7, v5, v59
	v_cvt_pk_fp8_f32 v82, v6, v7
	v_mul_f32_e32 v6, v5, v62
	v_mul_f32_e32 v7, v5, v63
	v_cvt_pk_fp8_f32 v83, v6, v7
	v_mul_f32_e32 v8, v5, v60
	v_mul_f32_e32 v9, v5, v61
	v_mul_f32_e32 v6, v5, v64
	v_mul_f32_e32 v7, v5, v65
	v_cvt_pk_fp8_f32 v82, v8, v9 op_sel:[0,0,1]
	v_cvt_pk_fp8_f32 v83, v6, v7 op_sel:[0,0,1]
	v_mul_f32_e32 v7, v5, v66
	v_mul_f32_e32 v8, v5, v67
	v_cvt_pk_fp8_f32 v6, v7, v8
	v_mul_f32_e32 v8, v5, v74
	v_mul_f32_e32 v58, v5, v75
	v_cvt_pk_fp8_f32 v7, v8, v58
	v_mul_f32_e32 v9, v5, v68
	v_mul_f32_e32 v10, v5, v69
	v_cvt_pk_fp8_f32 v6, v9, v10 op_sel:[0,0,1]
	v_mul_f32_e32 v8, v5, v76
	v_mul_f32_e32 v9, v5, v77
	v_cvt_pk_fp8_f32 v7, v8, v9 op_sel:[0,0,1]
	v_mul_f32_e32 v9, v5, v70
	v_mul_f32_e32 v10, v5, v71
	v_cvt_pk_fp8_f32 v8, v9, v10
	v_mul_f32_e32 v10, v5, v54
	v_mul_f32_e32 v54, v5, v55
	v_cvt_pk_fp8_f32 v9, v10, v54
	s_ashr_i32 s5, s4, 31
	s_lshl_b64 s[4:5], s[4:5], 14
	v_add_u32_e32 v2, s1, v2
	s_add_u32 s4, s4, s16
	v_mul_f32_e32 v58, v5, v72
	v_mul_f32_e32 v59, v5, v73
	v_mul_f32_e32 v10, v5, v56
	v_mul_f32_e32 v5, v5, v57
	v_ashrrev_i32_e32 v3, 31, v2
	s_addc_u32 s5, s5, s17
	v_cvt_pk_fp8_f32 v8, v58, v59 op_sel:[0,0,1]
	v_cvt_pk_fp8_f32 v9, v10, v5 op_sel:[0,0,1]
	v_lshl_add_u64 v[2:3], s[4:5], 0, v[2:3]
	v_lshlrev_b64 v[12:13], 10, v[2:3]
	s_lshl_b32 s30, s0, 7
	v_lshl_add_u64 v[12:13], s[34:35], 0, v[12:13]
	v_lshl_add_u64 v[12:13], v[12:13], 0, s[30:31]
	v_permlane16_swap_b32_e32 v80, v81
	v_permlane16_swap_b32_e32 v82, v83
	v_permlane16_swap_b32_e32 v6, v7
	v_permlane16_swap_b32_e32 v8, v9
	v_permlane32_swap_b32_e32 v80, v82
	v_permlane32_swap_b32_e32 v81, v83
	v_lshl_add_u64 v[12:13], v[12:13], 0, v[100:101]
	v_permlane32_swap_b32_e32 v6, v8
	v_permlane32_swap_b32_e32 v7, v9
	global_store_dwordx4 v[12:13], v[80:83], off
	global_store_dwordx4 v[12:13], v[6:9], off offset:64
	s_and_saveexec_b64 s[4:5], s[8:9]
	s_cbranch_execz .LBB0_354
	v_log_f32_e32 v4, v4
	v_lshlrev_b64 v[2:3], 5, v[2:3]
	s_mov_b32 s1, s31
	v_lshl_add_u64 v[2:3], s[40:41], 0, v[2:3]
	v_add_f32_e32 v4, v78, v4
	v_mul_f32_e32 v4, 0x3f317218, v4
	v_lshl_add_u64 v[2:3], s[0:1], 2, v[2:3]
	global_store_dword v[2:3], v4, off
	s_branch .LBB0_354

.LBB0_457:
	v_alignbit_b32 v24, v3, v2, 1
	v_add_co_u32_e32 v16, vcc, s3, v6
	v_and_b32_e32 v4, 0x7ffe0, v24
	s_nop 0
	v_addc_co_u32_e32 v17, vcc, 0, v7, vcc
	v_add_co_u32_e32 v20, vcc, s14, v6
	v_lshl_add_u64 v[22:23], s[4:5], 0, v[4:5]
	v_and_b32_e32 v4, 28, v24
	v_addc_co_u32_e32 v21, vcc, 0, v7, vcc
	v_lshl_add_u64 v[22:23], v[22:23], 0, v[4:5]
	v_add_co_u32_e32 v24, vcc, 0x80000, v22
	global_load_dword v4, v[22:23], off
	s_nop 0
	v_addc_co_u32_e32 v25, vcc, 0, v23, vcc
	v_add_co_u32_e32 v22, vcc, 0x100000, v22
	global_load_dwordx4 v[8:11], v[6:7], off
	s_nop 0
	v_addc_co_u32_e32 v23, vcc, 0, v23, vcc
	global_load_dwordx4 v[16:19], v[16:17], off
	s_nop 0
	global_load_dword v60, v[24:25], off
	global_load_dword v61, v[22:23], off
	s_nop 0
	global_load_dwordx4 v[20:23], v[20:21], off
	v_lshl_add_u64 v[2:3], v[2:3], 0, s[6:7]
	v_cmp_lt_u64_e32 vcc, s[12:13], v[2:3]
	s_or_b64 s[10:11], vcc, s[10:11]
	s_waitcnt vmcnt(0)
	v_cvt_pk_f32_fp8_e32 v[24:25], v8
	v_cvt_pk_f32_fp8_sdwa v[26:27], v8 src0_sel:WORD_1
	v_cvt_pk_f32_fp8_e32 v[28:29], v9
	v_max3_f32 v62, v4, v60, v61
	v_sub_f32_e32 v4, v4, v62
	v_sub_f32_e32 v60, v60, v62
	v_sub_f32_e32 v61, v61, v62
	v_mul_f32_e32 v4, 0x3fb8aa3b, v4
	v_mul_f32_e32 v60, 0x3fb8aa3b, v60
	v_mul_f32_e32 v61, 0x3fb8aa3b, v61
	v_exp_f32_e32 v4, v4
	v_exp_f32_e32 v62, v60
	v_exp_f32_e32 v61, v61
	v_cvt_pk_f32_fp8_e32 v[36:37], v16
	v_cvt_pk_f32_fp8_sdwa v[40:41], v16 src0_sel:WORD_1
	v_add_f32_e32 v60, v4, v62
	v_add_f32_e32 v63, v61, v60
	v_div_scale_f32 v60, s[16:17], v63, v63, 1.0
	v_rcp_f32_e32 v65, v60
	v_div_scale_f32 v64, vcc, 1.0, v63, 1.0
	v_cvt_pk_f32_fp8_e32 v[44:45], v17
	v_fma_f32 v66, -v60, v65, 1.0
	v_fmac_f32_e32 v65, v66, v65
	v_mul_f32_e32 v66, v64, v65
	v_fma_f32 v67, -v60, v66, v64
	v_fmac_f32_e32 v66, v67, v65
	v_cvt_pk_f32_fp8_sdwa v[16:17], v17 src0_sel:WORD_1
	v_cvt_pk_f32_fp8_e32 v[48:49], v18
	v_cvt_pk_f32_fp8_sdwa v[52:53], v18 src0_sel:WORD_1
	v_cvt_pk_f32_fp8_e32 v[56:57], v19
	v_fma_f32 v60, -v60, v66, v64
	v_cvt_pk_f32_fp8_sdwa v[8:9], v9 src0_sel:WORD_1
	v_cvt_pk_f32_fp8_e32 v[30:31], v10
	v_cvt_pk_f32_fp8_sdwa v[32:33], v10 src0_sel:WORD_1
	v_cvt_pk_f32_fp8_e32 v[34:35], v11
	v_cvt_pk_f32_fp8_sdwa v[18:19], v19 src0_sel:WORD_1
	v_div_fmas_f32 v64, v60, v65, v66
	v_cvt_pk_f32_fp8_sdwa v[10:11], v11 src0_sel:WORD_1
	v_cvt_pk_f32_fp8_e32 v[38:39], v20
	v_cvt_pk_f32_fp8_sdwa v[42:43], v20 src0_sel:WORD_1
	v_cvt_pk_f32_fp8_e32 v[46:47], v21
	v_cvt_pk_f32_fp8_e32 v[50:51], v22
	v_cvt_pk_f32_fp8_e32 v[58:59], v23
	v_div_fixup_f32 v63, v64, v63, 1.0
	v_mul_f32_e32 v62, v62, v63
	v_mul_f32_e32 v4, v4, v63
	v_pk_mul_f32 v[36:37], v[62:63], v[36:37] op_sel_hi:[0,1]
	v_pk_mul_f32 v[40:41], v[62:63], v[40:41] op_sel_hi:[0,1]
	v_pk_mul_f32 v[44:45], v[62:63], v[44:45] op_sel_hi:[0,1]
	v_pk_mul_f32 v[16:17], v[62:63], v[16:17] op_sel_hi:[0,1]
	v_pk_mul_f32 v[48:49], v[62:63], v[48:49] op_sel_hi:[0,1]
	v_pk_mul_f32 v[52:53], v[62:63], v[52:53] op_sel_hi:[0,1]
	v_pk_mul_f32 v[56:57], v[62:63], v[56:57] op_sel_hi:[0,1]
	v_mul_f32_e32 v64, v61, v63
	v_pk_mul_f32 v[18:19], v[62:63], v[18:19] op_sel_hi:[0,1]
	v_pk_fma_f32 v[24:25], v[4:5], v[24:25], v[36:37] op_sel_hi:[0,1,1]
	v_pk_fma_f32 v[26:27], v[4:5], v[26:27], v[40:41] op_sel_hi:[0,1,1]
	v_pk_fma_f32 v[28:29], v[4:5], v[28:29], v[44:45] op_sel_hi:[0,1,1]
	v_pk_fma_f32 v[8:9], v[4:5], v[8:9], v[16:17] op_sel_hi:[0,1,1]
	v_pk_fma_f32 v[16:17], v[4:5], v[30:31], v[48:49] op_sel_hi:[0,1,1]
	v_pk_fma_f32 v[30:31], v[4:5], v[32:33], v[52:53] op_sel_hi:[0,1,1]
	v_pk_fma_f32 v[32:33], v[4:5], v[34:35], v[56:57] op_sel_hi:[0,1,1]
	v_cvt_pk_f32_fp8_sdwa v[20:21], v21 src0_sel:WORD_1
	v_cvt_pk_f32_fp8_sdwa v[54:55], v22 src0_sel:WORD_1
	v_cvt_pk_f32_fp8_sdwa v[22:23], v23 src0_sel:WORD_1
	v_pk_fma_f32 v[10:11], v[4:5], v[10:11], v[18:19] op_sel_hi:[0,1,1]
	v_pk_fma_f32 v[18:19], v[64:65], v[38:39], v[24:25] op_sel_hi:[0,1,1]
	v_pk_fma_f32 v[24:25], v[64:65], v[42:43], v[26:27] op_sel_hi:[0,1,1]
	v_pk_fma_f32 v[26:27], v[64:65], v[46:47], v[28:29] op_sel_hi:[0,1,1]
	v_pk_fma_f32 v[16:17], v[64:65], v[50:51], v[16:17] op_sel_hi:[0,1,1]
	v_pk_fma_f32 v[28:29], v[64:65], v[58:59], v[32:33] op_sel_hi:[0,1,1]
	v_cvt_pk_fp8_f32 v12, v18, v19
	v_cvt_pk_fp8_f32 v13, v26, v27
	v_cvt_pk_fp8_f32 v14, v16, v17
	v_cvt_pk_fp8_f32 v15, v28, v29
	v_pk_fma_f32 v[8:9], v[64:65], v[20:21], v[8:9] op_sel_hi:[0,1,1]
	v_pk_fma_f32 v[20:21], v[64:65], v[54:55], v[30:31] op_sel_hi:[0,1,1]
	v_pk_fma_f32 v[10:11], v[64:65], v[22:23], v[10:11] op_sel_hi:[0,1,1]
	v_cvt_pk_fp8_f32 v12, v24, v25 op_sel:[0,0,1]
	v_cvt_pk_fp8_f32 v13, v8, v9 op_sel:[0,0,1]
	v_cvt_pk_fp8_f32 v14, v20, v21 op_sel:[0,0,1]
	v_cvt_pk_fp8_f32 v15, v10, v11 op_sel:[0,0,1]
	v_add_co_u32_e32 v60, vcc, 0x6000000, v6
	s_nop 1
	v_addc_co_u32_e32 v61, vcc, 0, v7, vcc
	v_lshl_add_u64 v[6:7], v[6:7], 0, s[8:9]
	global_store_dwordx4 v[60:61], v[12:15], off
	s_andn2_b64 exec, exec, s[10:11]
	s_cbranch_execnz .LBB0_457

.LBB0_533:
	v_lshl_add_u32 v22, s26, 8, v190
	v_lshl_or_b32 v14, s52, 8, v194
	v_mov_b64_e32 v[16:17], s[88:89]
	v_ashrrev_i32_e32 v15, 31, v14
	v_mad_i64_i32 v[2:3], s[28:29], v22, s51, v[16:17]
	v_lshl_add_u64 v[2:3], v[2:3], 0, s[14:15]
	v_lshlrev_b64 v[18:19], 1, v[14:15]
	s_nop 11
	v_lshl_add_u64 v[4:5], v[2:3], 0, v[18:19]
	global_load_dwordx4 v[24:27], v[4:5], off
	v_or_b32_e32 v4, 0x80, v14
	v_ashrrev_i32_e32 v5, 31, v4
	v_lshlrev_b64 v[20:21], 1, v[4:5]
	v_lshl_add_u64 v[2:3], v[2:3], 0, v[20:21]
	global_load_dwordx4 v[28:31], v[2:3], off
	v_or_b32_e32 v2, 16, v22
	v_mad_i64_i32 v[2:3], s[28:29], v2, s51, v[16:17]
	v_lshl_add_u64 v[2:3], v[2:3], 0, s[14:15]
	v_lshl_add_u64 v[4:5], v[2:3], 0, v[18:19]
	v_pk_mul_f32 v[198:199], v[148:149], s[16:17] op_sel_hi:[1,0]
	v_pk_mul_f32 v[200:201], v[146:147], s[16:17] op_sel_hi:[1,0]
	global_load_dwordx4 v[146:149], v[4:5], off
	v_or_b32_e32 v6, 32, v22
	v_or_b32_e32 v7, 48, v22
	v_mad_i64_i32 v[4:5], s[28:29], v6, s51, v[16:17]
	v_mad_i64_i32 v[6:7], s[28:29], v7, s51, v[16:17]
	v_lshl_add_u64 v[4:5], v[4:5], 0, s[14:15]
	v_lshl_add_u64 v[6:7], v[6:7], 0, s[14:15]
	v_lshl_add_u64 v[2:3], v[2:3], 0, v[20:21]
	v_lshl_add_u64 v[8:9], v[4:5], 0, v[18:19]
	v_lshl_add_u64 v[4:5], v[4:5], 0, v[20:21]
	v_pk_mul_f32 v[32:33], v[160:161], s[16:17] op_sel_hi:[1,0]
	v_pk_mul_f32 v[182:183], v[158:159], s[16:17] op_sel_hi:[1,0]
	v_pk_mul_f32 v[186:187], v[152:153], s[16:17] op_sel_hi:[1,0]
	v_pk_mul_f32 v[188:189], v[150:151], s[16:17] op_sel_hi:[1,0]
	v_lshl_add_u64 v[202:203], v[6:7], 0, v[18:19]
	v_lshl_add_u64 v[204:205], v[6:7], 0, v[20:21]
	global_load_dwordx4 v[150:153], v[2:3], off
	global_load_dwordx4 v[158:161], v[8:9], off
	global_load_dwordx4 v[10:13], v[4:5], off
	s_nop 0
	global_load_dwordx4 v[6:9], v[202:203], off
	global_load_dwordx4 v[2:5], v[204:205], off
	v_pk_mul_f32 v[184:185], v[154:155], s[16:17] op_sel_hi:[1,0]
	v_pk_mul_f32 v[156:157], v[156:157], s[16:17] op_sel_hi:[1,0]
	s_and_b64 vcc, exec, s[6:7]
	s_mov_b64 s[6:7], -1
	s_waitcnt vmcnt(0)
	v_lshlrev_b32_e32 v23, 16, v24
	v_and_b32_e32 v24, 0xffff0000, v24
	v_lshlrev_b32_e32 v202, 16, v25
	v_and_b32_e32 v25, 0xffff0000, v25
	v_lshlrev_b32_e32 v203, 16, v26
	v_and_b32_e32 v26, 0xffff0000, v26
	v_mul_f32_e32 v23, v182, v23
	v_mul_f32_e32 v24, v183, v24
	v_mul_f32_e32 v25, v33, v25
	v_mul_f32_e32 v33, v184, v203
	v_mul_f32_e32 v26, v185, v26
	v_mul_f32_e32 v23, 0x41800000, v23
	v_mul_f32_e32 v24, 0x41800000, v24
	v_mul_f32_e32 v33, 0x41800000, v33
	v_mul_f32_e32 v26, 0x41800000, v26
	v_cvt_pk_fp8_f32 v154, v23, v24
	v_cvt_pk_fp8_f32 v155, v33, v26
	v_lshlrev_b32_e32 v204, 16, v27
	v_and_b32_e32 v27, 0xffff0000, v27
	v_mul_f32_e32 v32, v32, v202
	v_mul_f32_e32 v156, v156, v204
	v_mul_f32_e32 v27, v157, v27
	v_lshlrev_b32_e32 v157, 16, v28
	v_and_b32_e32 v28, 0xffff0000, v28
	v_lshlrev_b32_e32 v183, 16, v30
	v_and_b32_e32 v30, 0xffff0000, v30
	v_mul_f32_e32 v32, 0x41800000, v32
	v_mul_f32_e32 v25, 0x41800000, v25
	v_mul_f32_e32 v156, 0x41800000, v156
	v_mul_f32_e32 v27, 0x41800000, v27
	v_mul_f32_e32 v157, v188, v157
	v_mul_f32_e32 v28, v189, v28
	v_and_b32_e32 v24, 0xffff0000, v31
	v_mul_f32_e32 v183, v200, v183
	v_mul_f32_e32 v23, v201, v30
	v_cvt_pk_fp8_f32 v154, v32, v25 op_sel:[0,0,1]
	v_cvt_pk_fp8_f32 v155, v156, v27 op_sel:[0,0,1]
	v_mul_f32_e32 v27, v199, v24
	v_mul_f32_e32 v25, 0x41800000, v157
	v_mul_f32_e32 v28, 0x41800000, v28
	v_cvt_pk_fp8_f32 v24, v25, v28
	v_mul_f32_e32 v28, 0x41800000, v183
	v_mul_f32_e32 v23, 0x41800000, v23
	v_cvt_pk_fp8_f32 v25, v28, v23
	v_lshlrev_b32_e32 v182, 16, v29
	v_and_b32_e32 v29, 0xffff0000, v29
	v_lshlrev_b32_e32 v184, 16, v31
	v_mul_f32_e32 v182, v186, v182
	v_mul_f32_e32 v29, v187, v29
	v_mul_f32_e32 v26, v198, v184
	v_mul_f32_e32 v30, 0x41800000, v182
	v_mul_f32_e32 v29, 0x41800000, v29
	v_mul_f32_e32 v23, 0x41800000, v26
	v_mul_f32_e32 v26, 0x41800000, v27
	v_cvt_pk_fp8_f32 v24, v30, v29 op_sel:[0,0,1]
	v_cvt_pk_fp8_f32 v25, v23, v26 op_sel:[0,0,1]
	v_pk_mul_f32 v[28:29], v[144:145], s[16:17] op_sel_hi:[1,0]
	v_lshlrev_b32_e32 v23, 16, v149
	v_mul_f32_e32 v23, v28, v23
	v_and_b32_e32 v28, 0xffff0000, v149
	v_pk_mul_f32 v[30:31], v[142:143], s[16:17] op_sel_hi:[1,0]
	v_mul_f32_e32 v32, v29, v28
	v_lshlrev_b32_e32 v28, 16, v148
	v_and_b32_e32 v29, 0xffff0000, v148
	v_mul_f32_e32 v28, v30, v28
	v_mul_f32_e32 v29, v31, v29
	v_mul_f32_e32 v28, 0x41800000, v28
	v_mul_f32_e32 v29, 0x41800000, v29
	v_cvt_pk_fp8_f32 v157, v28, v29
	v_pk_mul_f32 v[28:29], v[140:141], s[16:17] op_sel_hi:[1,0]
	v_lshlrev_b32_e32 v33, 16, v147
	v_pk_mul_f32 v[30:31], v[138:139], s[16:17] op_sel_hi:[1,0]
	v_mul_f32_e32 v28, v28, v33
	v_lshlrev_b32_e32 v33, 16, v146
	v_mul_f32_e32 v30, v30, v33
	v_and_b32_e32 v33, 0xffff0000, v146
	v_mul_f32_e32 v31, v31, v33
	v_mul_f32_e32 v30, 0x41800000, v30
	v_mul_f32_e32 v31, 0x41800000, v31
	v_or_b32_e32 v26, v22, v192
	v_cvt_pk_fp8_f32 v156, v30, v31
	v_ashrrev_i32_e32 v27, 31, v26
	v_and_b32_e32 v30, 0xffff0000, v147
	v_lshlrev_b64 v[26:27], 11, v[26:27]
	v_mul_f32_e32 v29, v29, v30
	v_mul_f32_e32 v28, 0x41800000, v28
	v_mul_f32_e32 v29, 0x41800000, v29
	v_lshl_add_u64 v[26:27], s[8:9], 0, v[26:27]
	v_mul_f32_e32 v23, 0x41800000, v23
	v_cvt_pk_fp8_f32 v156, v28, v29 op_sel:[0,0,1]
	v_mul_f32_e32 v28, 0x41800000, v32
	v_lshl_add_u64 v[26:27], v[26:27], 0, v[14:15]
	v_cvt_pk_fp8_f32 v157, v23, v28 op_sel:[0,0,1]
	v_lshl_add_u64 v[28:29], v[26:27], 0, v[174:175]
	v_pk_mul_f32 v[26:27], v[136:137], s[16:17] op_sel_hi:[1,0]
	v_lshlrev_b32_e32 v23, 16, v153
	v_mul_f32_e32 v23, v26, v23
	v_and_b32_e32 v26, 0xffff0000, v153
	v_pk_mul_f32 v[30:31], v[134:135], s[16:17] op_sel_hi:[1,0]
	v_mul_f32_e32 v134, v27, v26
	v_lshlrev_b32_e32 v26, 16, v152
	v_and_b32_e32 v27, 0xffff0000, v152
	v_mul_f32_e32 v26, v30, v26
	v_mul_f32_e32 v27, v31, v27
	v_mul_f32_e32 v26, 0x41800000, v26
	v_mul_f32_e32 v30, 0x41800000, v27
	v_cvt_pk_fp8_f32 v27, v26, v30
	v_pk_mul_f32 v[30:31], v[132:133], s[16:17] op_sel_hi:[1,0]
	v_lshlrev_b32_e32 v26, 16, v151
	v_mul_f32_e32 v26, v30, v26
	v_pk_mul_f32 v[32:33], v[130:131], s[16:17] op_sel_hi:[1,0]
	v_mul_f32_e32 v30, 0x41800000, v26
	v_lshlrev_b32_e32 v26, 16, v150
	v_mul_f32_e32 v26, v32, v26
	v_mul_f32_e32 v32, 0x41800000, v26
	v_and_b32_e32 v26, 0xffff0000, v150
	v_mul_f32_e32 v26, v33, v26
	v_mul_f32_e32 v33, 0x41800000, v26
	v_cvt_pk_fp8_f32 v26, v32, v33
	v_and_b32_e32 v32, 0xffff0000, v151
	v_mul_f32_e32 v31, v31, v32
	v_mul_f32_e32 v31, 0x41800000, v31
	v_mul_f32_e32 v23, 0x41800000, v23
	v_cvt_pk_fp8_f32 v26, v30, v31 op_sel:[0,0,1]
	v_mul_f32_e32 v30, 0x41800000, v134
	v_cvt_pk_fp8_f32 v27, v23, v30 op_sel:[0,0,1]
	v_lshlrev_b32_e32 v23, 16, v158
	v_permlane16_swap_b32_e32 v24, v26
	v_permlane16_swap_b32_e32 v25, v27
	global_store_dwordx4 v[28:29], v[24:27], off offset:128
	v_pk_mul_f32 v[30:31], v[122:123], s[16:17] op_sel_hi:[1,0]
	v_permlane16_swap_b32_e32 v154, v156
	v_pk_mul_f32 v[26:27], v[126:127], s[16:17] op_sel_hi:[1,0]
	v_pk_mul_f32 v[24:25], v[128:129], s[16:17] op_sel_hi:[1,0]
	v_mul_f32_e32 v23, v26, v23
	v_and_b32_e32 v26, 0xffff0000, v158
	v_mul_f32_e32 v26, v27, v26
	v_lshlrev_b32_e32 v27, 16, v159
	v_mul_f32_e32 v24, v24, v27
	v_and_b32_e32 v27, 0xffff0000, v159
	v_mul_f32_e32 v25, v25, v27
	v_lshlrev_b32_e32 v27, 16, v160
	v_permlane16_swap_b32_e32 v155, v157
	v_mul_f32_e32 v27, v30, v27
	v_and_b32_e32 v30, 0xffff0000, v160
	global_store_dwordx4 v[28:29], v[154:157], off
	v_pk_mul_f32 v[28:29], v[124:125], s[16:17] op_sel_hi:[1,0]
	v_mul_f32_e32 v30, v31, v30
	v_lshlrev_b32_e32 v31, 16, v161
	v_mul_f32_e32 v28, v28, v31
	v_and_b32_e32 v31, 0xffff0000, v161
	v_mul_f32_e32 v29, v29, v31
	v_mul_f32_e32 v23, 0x41800000, v23
	v_mul_f32_e32 v26, 0x41800000, v26
	v_mul_f32_e32 v31, 0x41800000, v24
	v_mul_f32_e32 v32, 0x41800000, v25
	v_cvt_pk_fp8_f32 v24, v23, v26
	v_mul_f32_e32 v23, 0x41800000, v27
	v_mul_f32_e32 v26, 0x41800000, v30
	v_cvt_pk_fp8_f32 v25, v23, v26
	v_mul_f32_e32 v23, 0x41800000, v28
	v_mul_f32_e32 v26, 0x41800000, v29
	v_pk_mul_f32 v[28:29], v[118:119], s[16:17] op_sel_hi:[1,0]
	v_cvt_pk_fp8_f32 v25, v23, v26 op_sel:[0,0,1]
	v_lshlrev_b32_e32 v23, 16, v10
	v_and_b32_e32 v10, 0xffff0000, v10
	v_mul_f32_e32 v23, v28, v23
	v_mul_f32_e32 v10, v29, v10
	v_mul_f32_e32 v23, 0x41800000, v23
	v_mul_f32_e32 v29, 0x41800000, v10
	v_pk_mul_f32 v[26:27], v[120:121], s[16:17] op_sel_hi:[1,0]
	v_lshlrev_b32_e32 v28, 16, v11
	v_and_b32_e32 v11, 0xffff0000, v11
	v_cvt_pk_fp8_f32 v10, v23, v29
	v_cvt_pk_fp8_f32 v24, v31, v32 op_sel:[0,0,1]
	v_pk_mul_f32 v[32:33], v[114:115], s[16:17] op_sel_hi:[1,0]
	v_mul_f32_e32 v11, v27, v11
	v_lshlrev_b32_e32 v27, 16, v12
	v_and_b32_e32 v12, 0xffff0000, v12
	v_pk_mul_f32 v[30:31], v[116:117], s[16:17] op_sel_hi:[1,0]
	v_mul_f32_e32 v26, v26, v28
	v_mul_f32_e32 v27, v32, v27
	v_mul_f32_e32 v12, v33, v12
	v_lshlrev_b32_e32 v28, 16, v13
	v_mul_f32_e32 v28, v30, v28
	v_mul_f32_e32 v26, 0x41800000, v26
	v_mul_f32_e32 v30, 0x41800000, v11
	v_mul_f32_e32 v23, 0x41800000, v27
	v_mul_f32_e32 v12, 0x41800000, v12
	v_cvt_pk_fp8_f32 v11, v23, v12
	v_cvt_pk_fp8_f32 v10, v26, v30 op_sel:[0,0,1]
	v_pk_mul_f32 v[26:27], v[112:113], s[16:17] op_sel_hi:[1,0]
	v_lshlrev_b32_e32 v23, 16, v9
	v_and_b32_e32 v9, 0xffff0000, v9
	v_mul_f32_e32 v12, 0x41800000, v28
	v_pk_mul_f32 v[28:29], v[110:111], s[16:17] op_sel_hi:[1,0]
	v_mul_f32_e32 v30, v27, v9
	v_lshlrev_b32_e32 v9, 16, v8
	v_and_b32_e32 v8, 0xffff0000, v8
	v_mul_f32_e32 v9, v28, v9
	v_mul_f32_e32 v8, v29, v8
	v_mul_f32_e32 v9, 0x41800000, v9
	v_mul_f32_e32 v8, 0x41800000, v8
	v_mul_f32_e32 v23, v26, v23
	v_cvt_pk_fp8_f32 v27, v9, v8
	v_pk_mul_f32 v[8:9], v[108:109], s[16:17] op_sel_hi:[1,0]
	v_lshlrev_b32_e32 v26, 16, v7
	v_pk_mul_f32 v[28:29], v[106:107], s[16:17] op_sel_hi:[1,0]
	v_mul_f32_e32 v8, v8, v26
	v_lshlrev_b32_e32 v26, 16, v6
	v_and_b32_e32 v6, 0xffff0000, v6
	v_mul_f32_e32 v26, v28, v26
	v_mul_f32_e32 v6, v29, v6
	v_mul_f32_e32 v28, 0x41800000, v26
	v_mul_f32_e32 v6, 0x41800000, v6
	v_cvt_pk_fp8_f32 v26, v28, v6
	v_and_b32_e32 v13, 0xffff0000, v13
	v_and_b32_e32 v6, 0xffff0000, v7
	v_mul_f32_e32 v13, v31, v13
	v_mul_f32_e32 v6, v9, v6
	v_mul_f32_e32 v13, 0x41800000, v13
	v_mul_f32_e32 v8, 0x41800000, v8
	v_mul_f32_e32 v6, 0x41800000, v6
	v_cvt_pk_fp8_f32 v11, v12, v13 op_sel:[0,0,1]
	v_or_b32_e32 v12, v22, v193
	v_mul_f32_e32 v23, 0x41800000, v23
	v_cvt_pk_fp8_f32 v26, v8, v6 op_sel:[0,0,1]
	v_mul_f32_e32 v6, 0x41800000, v30
	v_ashrrev_i32_e32 v13, 31, v12
	v_cvt_pk_fp8_f32 v27, v23, v6 op_sel:[0,0,1]
	v_lshlrev_b64 v[12:13], 11, v[12:13]
	v_lshl_add_u64 v[6:7], s[8:9], 0, v[12:13]
	v_lshl_add_u64 v[6:7], v[6:7], 0, v[14:15]
	v_permlane16_swap_b32_e32 v24, v26
	v_permlane16_swap_b32_e32 v25, v27
	v_lshl_add_u64 v[6:7], v[6:7], 0, v[174:175]
	v_pk_mul_f32 v[8:9], v[104:105], s[16:17] op_sel_hi:[1,0]
	v_lshlrev_b32_e32 v23, 16, v5
	v_and_b32_e32 v5, 0xffff0000, v5
	global_store_dwordx4 v[6:7], v[24:27], off
	v_pk_mul_f32 v[12:13], v[102:103], s[16:17] op_sel_hi:[1,0]
	v_mul_f32_e32 v8, v8, v23
	v_mul_f32_e32 v24, v9, v5
	v_lshlrev_b32_e32 v5, 16, v4
	v_and_b32_e32 v4, 0xffff0000, v4
	v_mul_f32_e32 v5, v12, v5
	v_mul_f32_e32 v4, v13, v4
	v_mul_f32_e32 v5, 0x41800000, v5
	v_mul_f32_e32 v4, 0x41800000, v4
	v_cvt_pk_fp8_f32 v13, v5, v4
	v_pk_mul_f32 v[4:5], v[100:101], s[16:17] op_sel_hi:[1,0]
	v_lshlrev_b32_e32 v12, 16, v3
	v_mul_f32_e32 v23, 0x41800000, v8
	v_pk_mul_f32 v[8:9], v[98:99], s[16:17] op_sel_hi:[1,0]
	v_mul_f32_e32 v4, v4, v12
	v_lshlrev_b32_e32 v12, 16, v2
	v_and_b32_e32 v2, 0xffff0000, v2
	v_mul_f32_e32 v8, v8, v12
	v_mul_f32_e32 v2, v9, v2
	v_mul_f32_e32 v8, 0x41800000, v8
	v_mul_f32_e32 v2, 0x41800000, v2
	v_cvt_pk_fp8_f32 v12, v8, v2
	v_and_b32_e32 v2, 0xffff0000, v3
	v_mul_f32_e32 v2, v5, v2
	v_mul_f32_e32 v4, 0x41800000, v4
	v_mul_f32_e32 v2, 0x41800000, v2
	v_cvt_pk_fp8_f32 v12, v4, v2 op_sel:[0,0,1]
	v_mul_f32_e32 v2, 0x41800000, v24
	v_cvt_pk_fp8_f32 v13, v23, v2 op_sel:[0,0,1]
	v_add_u32_e32 v32, 0x80, v22
	v_mad_i64_i32 v[2:3], s[28:29], v32, s51, v[16:17]
	v_permlane16_swap_b32_e32 v10, v12
	v_permlane16_swap_b32_e32 v11, v13
	v_lshl_add_u64 v[2:3], v[2:3], 0, s[14:15]
	global_store_dwordx4 v[6:7], v[10:13], off offset:128
	v_lshl_add_u64 v[4:5], v[2:3], 0, v[18:19]
	global_load_dwordx4 v[24:27], v[4:5], off
	v_lshl_add_u64 v[2:3], v[2:3], 0, v[20:21]
	global_load_dwordx4 v[28:31], v[2:3], off
	v_add_u32_e32 v2, 0x90, v22
	v_mad_i64_i32 v[2:3], s[28:29], v2, s51, v[16:17]
	v_lshl_add_u64 v[2:3], v[2:3], 0, s[14:15]
	v_lshl_add_u64 v[4:5], v[2:3], 0, v[18:19]
	v_lshl_add_u64 v[2:3], v[2:3], 0, v[20:21]
	global_load_dwordx4 v[98:101], v[4:5], off
	global_load_dwordx4 v[102:105], v[2:3], off
	v_add_u32_e32 v2, 0xa0, v22
	v_mad_i64_i32 v[2:3], s[28:29], v2, s51, v[16:17]
	v_lshl_add_u64 v[2:3], v[2:3], 0, s[14:15]
	v_lshl_add_u64 v[4:5], v[2:3], 0, v[18:19]
	v_lshl_add_u64 v[2:3], v[2:3], 0, v[20:21]
	global_load_dwordx4 v[106:109], v[4:5], off
	global_load_dwordx4 v[10:13], v[2:3], off
	v_add_u32_e32 v2, 0xb0, v22
	v_mad_i64_i32 v[2:3], s[28:29], v2, s51, v[16:17]
	v_lshl_add_u64 v[2:3], v[2:3], 0, s[14:15]
	v_lshl_add_u64 v[4:5], v[2:3], 0, v[18:19]
	v_pk_mul_f32 v[18:19], v[86:87], s[16:17] op_sel_hi:[1,0]
	v_pk_mul_f32 v[16:17], v[88:89], s[16:17] op_sel_hi:[1,0]
	v_pk_mul_f32 v[22:23], v[82:83], s[16:17] op_sel_hi:[1,0]
	v_lshl_add_u64 v[2:3], v[2:3], 0, v[20:21]
	v_pk_mul_f32 v[20:21], v[84:85], s[16:17] op_sel_hi:[1,0]
	global_load_dwordx4 v[6:9], v[4:5], off
	s_nop 0
	global_load_dwordx4 v[2:5], v[2:3], off
	s_waitcnt vmcnt(7)
	v_lshlrev_b32_e32 v33, 16, v24
	v_and_b32_e32 v24, 0xffff0000, v24
	v_mul_f32_e32 v19, v19, v24
	v_lshlrev_b32_e32 v24, 16, v25
	v_mul_f32_e32 v16, v16, v24
	v_and_b32_e32 v24, 0xffff0000, v25
	v_mul_f32_e32 v17, v17, v24
	v_lshlrev_b32_e32 v24, 16, v26
	v_mul_f32_e32 v22, v22, v24
	v_and_b32_e32 v24, 0xffff0000, v26
	v_mul_f32_e32 v23, v23, v24
	v_lshlrev_b32_e32 v24, 16, v27
	v_mul_f32_e32 v18, v18, v33
	v_mul_f32_e32 v20, v20, v24
	v_and_b32_e32 v24, 0xffff0000, v27
	v_mul_f32_e32 v21, v21, v24
	v_mul_f32_e32 v18, 0x41800000, v18
	v_mul_f32_e32 v19, 0x41800000, v19
	v_mul_f32_e32 v24, 0x41800000, v16
	v_mul_f32_e32 v25, 0x41800000, v17
	v_cvt_pk_fp8_f32 v16, v18, v19
	v_mul_f32_e32 v18, 0x41800000, v22
	v_mul_f32_e32 v19, 0x41800000, v23
	v_cvt_pk_fp8_f32 v17, v18, v19
	v_mul_f32_e32 v18, 0x41800000, v20
	v_mul_f32_e32 v19, 0x41800000, v21
	v_pk_mul_f32 v[20:21], v[94:95], s[16:17] op_sel_hi:[1,0]
	s_waitcnt vmcnt(6)
	v_lshlrev_b32_e32 v26, 16, v28
	v_mul_f32_e32 v20, v20, v26
	v_and_b32_e32 v26, 0xffff0000, v28
	v_cvt_pk_fp8_f32 v17, v18, v19 op_sel:[0,0,1]
	v_pk_mul_f32 v[18:19], v[96:97], s[16:17] op_sel_hi:[1,0]
	v_mul_f32_e32 v21, v21, v26
	v_lshlrev_b32_e32 v26, 16, v29
	v_mul_f32_e32 v18, v18, v26
	v_and_b32_e32 v26, 0xffff0000, v29
	v_cvt_pk_fp8_f32 v16, v24, v25 op_sel:[0,0,1]
	v_pk_mul_f32 v[24:25], v[90:91], s[16:17] op_sel_hi:[1,0]
	v_mul_f32_e32 v19, v19, v26
	v_lshlrev_b32_e32 v26, 16, v30
	v_mul_f32_e32 v24, v24, v26
	v_and_b32_e32 v26, 0xffff0000, v30
	v_pk_mul_f32 v[22:23], v[92:93], s[16:17] op_sel_hi:[1,0]
	v_mul_f32_e32 v25, v25, v26
	v_lshlrev_b32_e32 v26, 16, v31
	v_mul_f32_e32 v22, v22, v26
	v_and_b32_e32 v26, 0xffff0000, v31
	v_mul_f32_e32 v23, v23, v26
	v_mul_f32_e32 v26, 0x41800000, v20
	v_mul_f32_e32 v21, 0x41800000, v21
	v_cvt_pk_fp8_f32 v20, v26, v21
	v_mul_f32_e32 v24, 0x41800000, v24
	v_mul_f32_e32 v25, 0x41800000, v25
	v_cvt_pk_fp8_f32 v21, v24, v25
	v_mul_f32_e32 v18, 0x41800000, v18
	v_mul_f32_e32 v19, 0x41800000, v19
	v_cvt_pk_fp8_f32 v20, v18, v19 op_sel:[0,0,1]
	v_mul_f32_e32 v18, 0x41800000, v22
	v_mul_f32_e32 v19, 0x41800000, v23
	v_cvt_pk_fp8_f32 v21, v18, v19 op_sel:[0,0,1]
	v_or_b32_e32 v18, v32, v192
	v_ashrrev_i32_e32 v19, 31, v18
	v_lshlrev_b64 v[22:23], 11, v[18:19]
	v_pk_mul_f32 v[18:19], v[72:73], s[16:17] op_sel_hi:[1,0]
	s_waitcnt vmcnt(5)
	v_lshlrev_b32_e32 v26, 16, v101
	v_mul_f32_e32 v18, v18, v26
	v_mul_f32_e32 v28, 0x41800000, v18
	v_and_b32_e32 v18, 0xffff0000, v101
	v_pk_mul_f32 v[24:25], v[70:71], s[16:17] op_sel_hi:[1,0]
	v_mul_f32_e32 v29, v19, v18
	v_lshlrev_b32_e32 v18, 16, v100
	v_and_b32_e32 v19, 0xffff0000, v100
	v_mul_f32_e32 v18, v24, v18
	v_mul_f32_e32 v19, v25, v19
	v_mul_f32_e32 v18, 0x41800000, v18
	v_mul_f32_e32 v24, 0x41800000, v19
	v_cvt_pk_fp8_f32 v19, v18, v24
	v_pk_mul_f32 v[24:25], v[68:69], s[16:17] op_sel_hi:[1,0]
	v_lshlrev_b32_e32 v18, 16, v99
	v_mul_f32_e32 v18, v24, v18
	v_pk_mul_f32 v[26:27], v[66:67], s[16:17] op_sel_hi:[1,0]
	v_mul_f32_e32 v24, 0x41800000, v18
	v_lshlrev_b32_e32 v18, 16, v98
	v_mul_f32_e32 v18, v26, v18
	v_mul_f32_e32 v26, 0x41800000, v18
	v_and_b32_e32 v18, 0xffff0000, v98
	v_mul_f32_e32 v18, v27, v18
	v_mul_f32_e32 v27, 0x41800000, v18
	v_cvt_pk_fp8_f32 v18, v26, v27
	v_and_b32_e32 v26, 0xffff0000, v99
	v_mul_f32_e32 v25, v25, v26
	v_mul_f32_e32 v25, 0x41800000, v25
	v_cvt_pk_fp8_f32 v18, v24, v25 op_sel:[0,0,1]
	v_mul_f32_e32 v24, 0x41800000, v29
	v_cvt_pk_fp8_f32 v19, v28, v24 op_sel:[0,0,1]
	v_lshl_add_u64 v[22:23], s[8:9], 0, v[22:23]
	v_lshl_add_u64 v[22:23], v[22:23], 0, v[14:15]
	v_permlane16_swap_b32_e32 v16, v18
	v_permlane16_swap_b32_e32 v17, v19
	v_lshl_add_u64 v[24:25], v[22:23], 0, v[174:175]
	global_store_dwordx4 v[24:25], v[16:19], off
	s_waitcnt vmcnt(5)
	v_lshlrev_b32_e32 v22, 16, v105
	v_pk_mul_f32 v[16:17], v[80:81], s[16:17] op_sel_hi:[1,0]
	v_pk_mul_f32 v[18:19], v[78:79], s[16:17] op_sel_hi:[1,0]
	v_mul_f32_e32 v16, v16, v22
	v_mul_f32_e32 v26, 0x41800000, v16
	v_and_b32_e32 v16, 0xffff0000, v105
	v_mul_f32_e32 v27, v17, v16
	v_lshlrev_b32_e32 v16, 16, v104
	v_and_b32_e32 v17, 0xffff0000, v104
	v_mul_f32_e32 v16, v18, v16
	v_mul_f32_e32 v17, v19, v17
	v_mul_f32_e32 v16, 0x41800000, v16
	v_mul_f32_e32 v17, 0x41800000, v17
	v_cvt_pk_fp8_f32 v23, v16, v17
	v_pk_mul_f32 v[16:17], v[76:77], s[16:17] op_sel_hi:[1,0]
	v_lshlrev_b32_e32 v22, 16, v103
	v_pk_mul_f32 v[18:19], v[74:75], s[16:17] op_sel_hi:[1,0]
	v_mul_f32_e32 v16, v16, v22
	v_lshlrev_b32_e32 v22, 16, v102
	v_mul_f32_e32 v18, v18, v22
	v_and_b32_e32 v22, 0xffff0000, v102
	v_mul_f32_e32 v19, v19, v22
	v_mul_f32_e32 v18, 0x41800000, v18
	v_mul_f32_e32 v19, 0x41800000, v19
	v_cvt_pk_fp8_f32 v22, v18, v19
	v_and_b32_e32 v18, 0xffff0000, v103
	v_mul_f32_e32 v17, v17, v18
	v_mul_f32_e32 v16, 0x41800000, v16
	v_mul_f32_e32 v17, 0x41800000, v17
	v_cvt_pk_fp8_f32 v22, v16, v17 op_sel:[0,0,1]
	v_mul_f32_e32 v16, 0x41800000, v27
	v_cvt_pk_fp8_f32 v23, v26, v16 op_sel:[0,0,1]
	v_pk_mul_f32 v[18:19], v[54:55], s[16:17] op_sel_hi:[1,0]
	v_permlane16_swap_b32_e32 v20, v22
	v_permlane16_swap_b32_e32 v21, v23
	global_store_dwordx4 v[24:25], v[20:23], off offset:128
	s_waitcnt vmcnt(5)
	v_lshlrev_b32_e32 v24, 16, v106
	v_mul_f32_e32 v18, v18, v24
	v_and_b32_e32 v24, 0xffff0000, v106
	v_pk_mul_f32 v[16:17], v[56:57], s[16:17] op_sel_hi:[1,0]
	v_mul_f32_e32 v19, v19, v24
	v_lshlrev_b32_e32 v24, 16, v107
	v_mul_f32_e32 v16, v16, v24
	v_and_b32_e32 v24, 0xffff0000, v107
	v_pk_mul_f32 v[22:23], v[50:51], s[16:17] op_sel_hi:[1,0]
	v_mul_f32_e32 v17, v17, v24
	v_lshlrev_b32_e32 v24, 16, v108
	v_mul_f32_e32 v22, v22, v24
	v_and_b32_e32 v24, 0xffff0000, v108
	v_pk_mul_f32 v[20:21], v[52:53], s[16:17] op_sel_hi:[1,0]
	v_mul_f32_e32 v23, v23, v24
	v_lshlrev_b32_e32 v24, 16, v109
	v_mul_f32_e32 v20, v20, v24
	v_and_b32_e32 v24, 0xffff0000, v109
	v_mul_f32_e32 v21, v21, v24
	v_mul_f32_e32 v18, 0x41800000, v18
	v_mul_f32_e32 v19, 0x41800000, v19
	v_mul_f32_e32 v24, 0x41800000, v16
	v_mul_f32_e32 v25, 0x41800000, v17
	v_cvt_pk_fp8_f32 v16, v18, v19
	v_mul_f32_e32 v18, 0x41800000, v22
	v_mul_f32_e32 v19, 0x41800000, v23
	v_cvt_pk_fp8_f32 v17, v18, v19
	v_mul_f32_e32 v18, 0x41800000, v20
	v_mul_f32_e32 v19, 0x41800000, v21
	v_pk_mul_f32 v[20:21], v[62:63], s[16:17] op_sel_hi:[1,0]
	s_waitcnt vmcnt(4)
	v_lshlrev_b32_e32 v26, 16, v10
	v_and_b32_e32 v10, 0xffff0000, v10
	v_cvt_pk_fp8_f32 v17, v18, v19 op_sel:[0,0,1]
	v_pk_mul_f32 v[18:19], v[64:65], s[16:17] op_sel_hi:[1,0]
	v_mul_f32_e32 v10, v21, v10
	v_lshlrev_b32_e32 v21, 16, v11
	v_pk_mul_f32 v[22:23], v[60:61], s[16:17] op_sel_hi:[1,0]
	v_mul_f32_e32 v20, v20, v26
	v_mul_f32_e32 v18, v18, v21
	v_lshlrev_b32_e32 v21, 16, v13
	v_mul_f32_e32 v21, v22, v21
	v_mul_f32_e32 v20, 0x41800000, v20
	v_mul_f32_e32 v22, 0x41800000, v10
	v_and_b32_e32 v11, 0xffff0000, v11
	v_cvt_pk_fp8_f32 v10, v20, v22
	v_cvt_pk_fp8_f32 v16, v24, v25 op_sel:[0,0,1]
	v_pk_mul_f32 v[24:25], v[58:59], s[16:17] op_sel_hi:[1,0]
	v_mul_f32_e32 v11, v19, v11
	v_lshlrev_b32_e32 v19, 16, v12
	v_and_b32_e32 v12, 0xffff0000, v12
	v_mul_f32_e32 v19, v24, v19
	v_mul_f32_e32 v12, v25, v12
	v_and_b32_e32 v13, 0xffff0000, v13
	v_mul_f32_e32 v13, v23, v13
	v_mul_f32_e32 v18, 0x41800000, v18
	v_mul_f32_e32 v23, 0x41800000, v11
	v_mul_f32_e32 v19, 0x41800000, v19
	v_mul_f32_e32 v12, 0x41800000, v12
	v_cvt_pk_fp8_f32 v11, v19, v12
	v_cvt_pk_fp8_f32 v10, v18, v23 op_sel:[0,0,1]
	v_pk_mul_f32 v[18:19], v[40:41], s[16:17] op_sel_hi:[1,0]
	s_waitcnt vmcnt(3)
	v_lshlrev_b32_e32 v22, 16, v9
	v_and_b32_e32 v9, 0xffff0000, v9
	v_mul_f32_e32 v12, 0x41800000, v21
	v_pk_mul_f32 v[20:21], v[38:39], s[16:17] op_sel_hi:[1,0]
	v_mul_f32_e32 v23, v19, v9
	v_lshlrev_b32_e32 v9, 16, v8
	v_and_b32_e32 v8, 0xffff0000, v8
	v_mul_f32_e32 v9, v20, v9
	v_mul_f32_e32 v8, v21, v8
	v_mul_f32_e32 v18, v18, v22
	v_mul_f32_e32 v9, 0x41800000, v9
	v_mul_f32_e32 v8, 0x41800000, v8
	v_mul_f32_e32 v22, 0x41800000, v18
	v_cvt_pk_fp8_f32 v19, v9, v8
	v_pk_mul_f32 v[8:9], v[36:37], s[16:17] op_sel_hi:[1,0]
	v_lshlrev_b32_e32 v18, 16, v7
	v_pk_mul_f32 v[20:21], v[34:35], s[16:17] op_sel_hi:[1,0]
	v_mul_f32_e32 v8, v8, v18
	v_lshlrev_b32_e32 v18, 16, v6
	v_and_b32_e32 v6, 0xffff0000, v6
	v_mul_f32_e32 v18, v20, v18
	v_mul_f32_e32 v6, v21, v6
	v_mul_f32_e32 v20, 0x41800000, v18
	v_mul_f32_e32 v6, 0x41800000, v6
	v_cvt_pk_fp8_f32 v18, v20, v6
	v_mul_f32_e32 v13, 0x41800000, v13
	v_and_b32_e32 v6, 0xffff0000, v7
	v_cvt_pk_fp8_f32 v11, v12, v13 op_sel:[0,0,1]
	v_or_b32_e32 v12, v32, v193
	v_mul_f32_e32 v6, v9, v6
	v_ashrrev_i32_e32 v13, 31, v12
	v_mul_f32_e32 v8, 0x41800000, v8
	v_mul_f32_e32 v6, 0x41800000, v6
	v_lshlrev_b64 v[12:13], 11, v[12:13]
	v_cvt_pk_fp8_f32 v18, v8, v6 op_sel:[0,0,1]
	v_mul_f32_e32 v6, 0x41800000, v23
	v_cvt_pk_fp8_f32 v19, v22, v6 op_sel:[0,0,1]
	v_lshl_add_u64 v[6:7], s[8:9], 0, v[12:13]
	v_lshl_add_u64 v[6:7], v[6:7], 0, v[14:15]
	v_pk_mul_f32 v[8:9], v[48:49], s[16:17] op_sel_hi:[1,0]
	s_waitcnt vmcnt(2)
	v_lshlrev_b32_e32 v14, 16, v5
	v_and_b32_e32 v5, 0xffff0000, v5
	v_pk_mul_f32 v[12:13], v[46:47], s[16:17] op_sel_hi:[1,0]
	v_mul_f32_e32 v15, v9, v5
	v_lshlrev_b32_e32 v5, 16, v4
	v_and_b32_e32 v4, 0xffff0000, v4
	v_mul_f32_e32 v5, v12, v5
	v_mul_f32_e32 v4, v13, v4
	v_mul_f32_e32 v5, 0x41800000, v5
	v_mul_f32_e32 v4, 0x41800000, v4
	v_mul_f32_e32 v8, v8, v14
	v_cvt_pk_fp8_f32 v13, v5, v4
	v_pk_mul_f32 v[4:5], v[44:45], s[16:17] op_sel_hi:[1,0]
	v_lshlrev_b32_e32 v12, 16, v3
	v_mul_f32_e32 v14, 0x41800000, v8
	v_pk_mul_f32 v[8:9], v[42:43], s[16:17] op_sel_hi:[1,0]
	v_mul_f32_e32 v4, v4, v12
	v_lshlrev_b32_e32 v12, 16, v2
	v_and_b32_e32 v2, 0xffff0000, v2
	v_mul_f32_e32 v8, v8, v12
	v_mul_f32_e32 v2, v9, v2
	v_mul_f32_e32 v8, 0x41800000, v8
	v_mul_f32_e32 v2, 0x41800000, v2
	v_cvt_pk_fp8_f32 v12, v8, v2
	v_and_b32_e32 v2, 0xffff0000, v3
	v_mul_f32_e32 v2, v5, v2
	v_mul_f32_e32 v4, 0x41800000, v4
	v_mul_f32_e32 v2, 0x41800000, v2
	v_cvt_pk_fp8_f32 v12, v4, v2 op_sel:[0,0,1]
	v_mul_f32_e32 v2, 0x41800000, v15
	v_cvt_pk_fp8_f32 v13, v14, v2 op_sel:[0,0,1]
	v_permlane16_swap_b32_e32 v16, v18
	v_permlane16_swap_b32_e32 v17, v19
	v_lshl_add_u64 v[6:7], v[6:7], 0, v[174:175]
	v_permlane16_swap_b32_e32 v10, v12
	v_permlane16_swap_b32_e32 v11, v13
	global_store_dwordx4 v[6:7], v[16:19], off
	global_store_dwordx4 v[6:7], v[10:13], off offset:128
	s_cbranch_vccnz .LBB0_522
	s_andn2_b64 vcc, exec, s[4:5]
	s_cbranch_vccnz .LBB0_521
	s_barrier
	s_branch .LBB0_521

.LBB0_557:
	v_lshl_or_b32 v30, s52, 8, v196
	v_lshl_add_u32 v32, s26, 8, v192
	v_mov_b64_e32 v[184:185], s[88:89]
	v_or_b32_e32 v6, 0x80, v30
	v_ashrrev_i32_e32 v31, 31, v30
	v_mad_i64_i32 v[2:3], s[28:29], v32, s51, v[184:185]
	v_ashrrev_i32_e32 v7, 31, v6
	v_lshl_add_u64 v[2:3], v[2:3], 0, s[14:15]
	v_lshlrev_b64 v[186:187], 1, v[30:31]
	v_pk_mul_f32 v[214:215], v[154:155], s[16:17] op_sel_hi:[1,0]
	v_lshlrev_b64 v[154:155], 1, v[6:7]
	s_nop 11
	v_lshl_add_u64 v[4:5], v[2:3], 0, v[186:187]
	v_ashrrev_i32_e32 v33, 31, v32
	v_lshl_add_u64 v[2:3], v[2:3], 0, v[154:155]
	global_load_dwordx4 v[200:203], v[4:5], off
	global_load_dwordx4 v[204:207], v[2:3], off
	v_lshlrev_b64 v[4:5], 11, v[32:33]
	v_lshl_add_u64 v[4:5], s[8:9], 0, v[4:5]
	v_lshl_add_u64 v[4:5], v[4:5], 0, v[30:31]
	global_load_dwordx2 v[26:27], v[4:5], off
	global_load_dwordx2 v[224:225], v[4:5], off offset:128
	v_or_b32_e32 v8, 16, v32
	v_or_b32_e32 v10, 32, v32
	v_or_b32_e32 v12, 48, v32
	v_ashrrev_i32_e32 v9, 31, v8
	v_ashrrev_i32_e32 v11, 31, v10
	v_mad_i64_i32 v[14:15], s[28:29], v8, s51, v[184:185]
	v_mad_i64_i32 v[16:17], s[28:29], v10, s51, v[184:185]
	v_ashrrev_i32_e32 v13, 31, v12
	v_mad_i64_i32 v[18:19], s[28:29], v12, s51, v[184:185]
	v_lshlrev_b64 v[8:9], 11, v[8:9]
	v_lshlrev_b64 v[10:11], 11, v[10:11]
	v_lshl_add_u64 v[6:7], v[14:15], 0, s[14:15]
	v_lshl_add_u64 v[14:15], v[16:17], 0, s[14:15]
	v_lshl_add_u64 v[16:17], v[18:19], 0, s[14:15]
	v_lshlrev_b64 v[12:13], 11, v[12:13]
	v_lshl_add_u64 v[8:9], s[8:9], 0, v[8:9]
	v_lshl_add_u64 v[10:11], s[8:9], 0, v[10:11]
	v_pk_mul_f32 v[210:211], v[158:159], s[16:17] op_sel_hi:[1,0]
	v_pk_mul_f32 v[212:213], v[156:157], s[16:17] op_sel_hi:[1,0]
	v_lshl_add_u64 v[18:19], v[6:7], 0, v[186:187]
	v_lshl_add_u64 v[6:7], v[6:7], 0, v[154:155]
	v_lshl_add_u64 v[156:157], v[14:15], 0, v[186:187]
	v_lshl_add_u64 v[158:159], v[14:15], 0, v[154:155]
	v_lshl_add_u64 v[12:13], s[8:9], 0, v[12:13]
	v_lshl_add_u64 v[2:3], v[16:17], 0, v[186:187]
	v_lshl_add_u64 v[4:5], v[8:9], 0, v[30:31]
	v_lshl_add_u64 v[8:9], v[10:11], 0, v[30:31]
	v_pk_mul_f32 v[208:209], v[160:161], s[16:17] op_sel_hi:[1,0]
	v_lshl_add_u64 v[222:223], v[16:17], 0, v[154:155]
	v_lshl_add_u64 v[226:227], v[12:13], 0, v[30:31]
	global_load_dwordx4 v[22:25], v[18:19], off
	global_load_dwordx2 v[190:191], v[4:5], off
	s_nop 0
	global_load_dwordx4 v[18:21], v[6:7], off
	global_load_dwordx2 v[28:29], v[4:5], off offset:128
	global_load_dwordx4 v[14:17], v[156:157], off
	global_load_dwordx2 v[188:189], v[8:9], off
	global_load_dwordx4 v[10:13], v[158:159], off
	global_load_dwordx2 v[160:161], v[8:9], off offset:128
	s_nop 0
	global_load_dwordx4 v[6:9], v[2:3], off
	global_load_dwordx2 v[158:159], v[226:227], off
	s_nop 0
	global_load_dwordx4 v[2:5], v[222:223], off
	global_load_dwordx2 v[156:157], v[226:227], off offset:128
	v_mov_b32_e32 v219, v183
	v_mov_b32_e32 v220, v210
	v_mov_b32_e32 v210, v208
	v_mov_b32_e32 v217, v183
	v_mov_b32_e32 v223, v183
	v_mov_b32_e32 v227, v183
	v_pk_mul_f32 v[150:151], v[150:151], s[16:17] op_sel_hi:[1,0]
	v_pk_mul_f32 v[146:147], v[146:147], s[16:17] op_sel_hi:[1,0]
	v_pk_mul_f32 v[148:149], v[148:149], s[16:17] op_sel_hi:[1,0]
	v_pk_mul_f32 v[144:145], v[144:145], s[16:17] op_sel_hi:[1,0]
	v_pk_mul_f32 v[142:143], v[142:143], s[16:17] op_sel_hi:[1,0]
	v_pk_mul_f32 v[138:139], v[138:139], s[16:17] op_sel_hi:[1,0]
	v_pk_mul_f32 v[134:135], v[134:135], s[16:17] op_sel_hi:[1,0]
	v_pk_mul_f32 v[130:131], v[130:131], s[16:17] op_sel_hi:[1,0]
	v_pk_mul_f32 v[94:95], v[94:95], s[16:17] op_sel_hi:[1,0]
	v_pk_mul_f32 v[96:97], v[96:97], s[16:17] op_sel_hi:[1,0]
	v_pk_mul_f32 v[90:91], v[90:91], s[16:17] op_sel_hi:[1,0]
	v_pk_mul_f32 v[92:93], v[92:93], s[16:17] op_sel_hi:[1,0]
	v_pk_mul_f32 v[86:87], v[86:87], s[16:17] op_sel_hi:[1,0]
	v_pk_mul_f32 v[82:83], v[82:83], s[16:17] op_sel_hi:[1,0]
	v_pk_mul_f32 v[84:85], v[84:85], s[16:17] op_sel_hi:[1,0]
	v_pk_mul_f32 v[80:81], v[80:81], s[16:17] op_sel_hi:[1,0]
	v_pk_mul_f32 v[78:79], v[78:79], s[16:17] op_sel_hi:[1,0]
	v_pk_mul_f32 v[70:71], v[70:71], s[16:17] op_sel_hi:[1,0]
	v_pk_mul_f32 v[66:67], v[66:67], s[16:17] op_sel_hi:[1,0]
	s_and_b64 vcc, exec, s[6:7]
	s_mov_b64 s[6:7], -1
	s_waitcnt vmcnt(0)
	v_lshlrev_b32_e32 v182, 16, v200
	v_and_b32_e32 v216, 0xffff0000, v200
	v_lshlrev_b32_e32 v218, 16, v201
	v_and_b32_e32 v200, 0xffff0000, v201
	v_mov_b32_e32 v201, v183
	v_cvt_pk_f32_fp8_e32 v[228:229], v26
	v_cvt_pk_f32_fp8_sdwa v[230:231], v26 src0_sel:WORD_1
	v_cvt_pk_f32_fp8_e32 v[232:233], v27
	v_cvt_pk_f32_fp8_sdwa v[26:27], v27 src0_sel:WORD_1
	v_mov_b32_e32 v221, v228
	v_mov_b32_e32 v228, v211
	v_mov_b32_e32 v211, v230
	v_mov_b32_e32 v230, v209
	v_pk_mul_f32 v[210:211], v[210:211], v[218:219]
	v_pk_mul_f32 v[200:201], v[230:231], v[200:201]
	v_lshlrev_b32_e32 v208, 16, v202
	v_add_f32_e32 v210, v210, v211
	v_add_f32_e32 v211, v200, v201
	v_mov_b32_e32 v200, v214
	v_mov_b32_e32 v201, v232
	v_mov_b32_e32 v209, v183
	v_and_b32_e32 v202, 0xffff0000, v202
	v_lshlrev_b32_e32 v222, 16, v203
	v_and_b32_e32 v226, 0xffff0000, v203
	v_pk_mul_f32 v[200:201], v[200:201], v[208:209]
	v_mov_b32_e32 v232, v215
	v_mov_b32_e32 v203, v183
	v_add_f32_e32 v208, v200, v201
	v_pk_mul_f32 v[200:201], v[232:233], v[202:203]
	v_pk_mul_f32 v[220:221], v[220:221], v[182:183]
	v_pk_mul_f32 v[216:217], v[228:229], v[216:217]
	v_add_f32_e32 v202, v200, v201
	v_mov_b32_e32 v200, v212
	v_mov_b32_e32 v201, v26
	v_mov_b32_e32 v26, v213
	v_add_f32_e32 v33, v220, v221
	v_add_f32_e32 v182, v216, v217
	v_pk_mul_f32 v[200:201], v[200:201], v[222:223]
	v_pk_mul_f32 v[26:27], v[26:27], v[226:227]
	v_add_f32_e32 v203, v200, v201
	v_add_f32_e32 v26, v26, v27
	v_mul_f32_e32 v27, 0x41800000, v33
	v_mul_f32_e32 v33, 0x41800000, v182
	v_cvt_pk_fp8_f32 v200, v27, v33
	v_mul_f32_e32 v27, 0x41800000, v208
	v_mul_f32_e32 v33, 0x41800000, v202
	v_cvt_pk_fp8_f32 v201, v27, v33
	v_cvt_pk_f32_fp8_e32 v[214:215], v224
	v_cvt_pk_f32_fp8_sdwa v[216:217], v224 src0_sel:WORD_1
	v_mul_f32_e32 v27, 0x41800000, v203
	v_mul_f32_e32 v26, 0x41800000, v26
	v_cvt_pk_fp8_f32 v201, v27, v26 op_sel:[0,0,1]
	v_pk_mul_f32 v[26:27], v[152:153], s[16:17] op_sel_hi:[1,0]
	v_and_b32_e32 v152, 0xffff0000, v204
	v_cvt_pk_f32_fp8_e32 v[218:219], v225
	v_mov_b32_e32 v223, v214
	v_mov_b32_e32 v214, v151
	v_mov_b32_e32 v153, v183
	v_mul_f32_e32 v182, 0x41800000, v210
	v_mul_f32_e32 v209, 0x41800000, v211
	v_mov_b32_e32 v222, v150
	v_pk_mul_f32 v[150:151], v[214:215], v[152:153]
	v_cvt_pk_fp8_f32 v200, v182, v209 op_sel:[0,0,1]
	v_lshlrev_b32_e32 v182, 16, v204
	v_lshlrev_b32_e32 v202, 16, v205
	v_and_b32_e32 v204, 0xffff0000, v205
	v_add_f32_e32 v152, v150, v151
	v_mov_b32_e32 v150, v26
	v_mov_b32_e32 v151, v216
	v_mov_b32_e32 v203, v183
	v_mov_b32_e32 v216, v27
	v_mov_b32_e32 v205, v183
	v_cvt_pk_f32_fp8_sdwa v[220:221], v225 src0_sel:WORD_1
	v_pk_mul_f32 v[150:151], v[150:151], v[202:203]
	v_pk_mul_f32 v[26:27], v[216:217], v[204:205]
	v_lshlrev_b32_e32 v208, 16, v206
	v_add_f32_e32 v150, v150, v151
	v_add_f32_e32 v151, v26, v27
	v_mov_b32_e32 v26, v146
	v_mov_b32_e32 v27, v218
	v_mov_b32_e32 v209, v183
	v_and_b32_e32 v206, 0xffff0000, v206
	v_lshlrev_b32_e32 v210, 16, v207
	v_and_b32_e32 v212, 0xffff0000, v207
	v_pk_mul_f32 v[26:27], v[26:27], v[208:209]
	v_mov_b32_e32 v218, v147
	v_mov_b32_e32 v207, v183
	v_add_f32_e32 v146, v26, v27
	v_pk_mul_f32 v[26:27], v[218:219], v[206:207]
	v_mov_b32_e32 v211, v183
	v_add_f32_e32 v147, v26, v27
	v_mov_b32_e32 v26, v148
	v_mov_b32_e32 v27, v220
	v_pk_mul_f32 v[222:223], v[222:223], v[182:183]
	v_pk_mul_f32 v[26:27], v[26:27], v[210:211]
	v_mov_b32_e32 v220, v149
	v_mov_b32_e32 v213, v183
	v_add_f32_e32 v33, v222, v223
	v_add_f32_e32 v148, v26, v27
	v_pk_mul_f32 v[26:27], v[220:221], v[212:213]
	v_mul_f32_e32 v150, 0x41800000, v150
	v_add_f32_e32 v149, v26, v27
	v_mul_f32_e32 v27, 0x41800000, v33
	v_mul_f32_e32 v33, 0x41800000, v152
	v_cvt_pk_fp8_f32 v26, v27, v33
	v_mul_f32_e32 v33, 0x41800000, v146
	v_mul_f32_e32 v146, 0x41800000, v147
	v_cvt_pk_fp8_f32 v27, v33, v146
	v_mul_f32_e32 v33, 0x41800000, v148
	v_mul_f32_e32 v146, 0x41800000, v149
	v_cvt_pk_f32_fp8_sdwa v[148:149], v191 src0_sel:WORD_1
	v_mul_f32_e32 v151, 0x41800000, v151
	v_cvt_pk_fp8_f32 v26, v150, v151 op_sel:[0,0,1]
	v_lshlrev_b32_e32 v182, 16, v25
	v_mov_b32_e32 v150, v144
	v_mov_b32_e32 v151, v148
	v_pk_mul_f32 v[150:151], v[150:151], v[182:183]
	v_and_b32_e32 v182, 0xffff0000, v25
	v_mov_b32_e32 v148, v145
	v_pk_mul_f32 v[144:145], v[148:149], v[182:183]
	v_cvt_pk_f32_fp8_e32 v[148:149], v191
	v_cvt_pk_fp8_f32 v27, v33, v146 op_sel:[0,0,1]
	v_add_f32_e32 v33, v150, v151
	v_add_f32_e32 v150, v144, v145
	v_lshlrev_b32_e32 v182, 16, v24
	v_mov_b32_e32 v144, v142
	v_mov_b32_e32 v145, v148
	v_pk_mul_f32 v[144:145], v[144:145], v[182:183]
	v_and_b32_e32 v182, 0xffff0000, v24
	v_add_f32_e32 v25, v144, v145
	v_mov_b32_e32 v148, v143
	v_mul_f32_e32 v142, 0x41800000, v25
	v_pk_mul_f32 v[24:25], v[148:149], v[182:183]
	v_add_f32_e32 v24, v24, v25
	v_mul_f32_e32 v24, 0x41800000, v24
	v_cvt_pk_fp8_f32 v203, v142, v24
	v_pk_mul_f32 v[24:25], v[140:141], s[16:17] op_sel_hi:[1,0]
	v_cvt_pk_f32_fp8_sdwa v[140:141], v190 src0_sel:WORD_1
	v_mov_b32_e32 v142, v24
	v_lshlrev_b32_e32 v182, 16, v23
	v_mov_b32_e32 v143, v140
	v_mov_b32_e32 v140, v25
	v_cvt_pk_f32_fp8_e32 v[24:25], v190
	v_pk_mul_f32 v[142:143], v[142:143], v[182:183]
	v_and_b32_e32 v182, 0xffff0000, v23
	v_add_f32_e32 v144, v142, v143
	v_pk_mul_f32 v[140:141], v[140:141], v[182:183]
	v_lshlrev_b32_e32 v182, 16, v22
	v_mov_b32_e32 v142, v138
	v_mov_b32_e32 v143, v24
	v_pk_mul_f32 v[142:143], v[142:143], v[182:183]
	v_and_b32_e32 v182, 0xffff0000, v22
	v_add_f32_e32 v23, v142, v143
	v_mov_b32_e32 v24, v139
	v_mul_f32_e32 v138, 0x41800000, v23
	v_pk_mul_f32 v[22:23], v[24:25], v[182:183]
	v_pk_mul_f32 v[24:25], v[136:137], s[16:17] op_sel_hi:[1,0]
	v_add_f32_e32 v22, v22, v23
	v_cvt_pk_f32_fp8_sdwa v[136:137], v29 src0_sel:WORD_1
	v_mul_f32_e32 v22, 0x41800000, v22
	v_cvt_pk_fp8_f32 v202, v138, v22
	v_add_f32_e32 v23, v140, v141
	v_lshlrev_b32_e32 v182, 16, v21
	v_mov_b32_e32 v138, v24
	v_mov_b32_e32 v139, v136
	v_mul_f32_e32 v22, 0x41800000, v144
	v_mul_f32_e32 v23, 0x41800000, v23
	v_pk_mul_f32 v[138:139], v[138:139], v[182:183]
	v_mul_f32_e32 v33, 0x41800000, v33
	v_cvt_pk_fp8_f32 v202, v22, v23 op_sel:[0,0,1]
	v_mul_f32_e32 v22, 0x41800000, v150
	v_add_f32_e32 v24, v138, v139
	v_and_b32_e32 v182, 0xffff0000, v21
	v_mov_b32_e32 v136, v25
	v_cvt_pk_fp8_f32 v203, v33, v22 op_sel:[0,0,1]
	v_mul_f32_e32 v33, 0x41800000, v24
	v_pk_mul_f32 v[24:25], v[136:137], v[182:183]
	v_cvt_pk_f32_fp8_e32 v[136:137], v29
	v_add_f32_e32 v138, v24, v25
	v_lshlrev_b32_e32 v182, 16, v20
	v_mov_b32_e32 v24, v134
	v_mov_b32_e32 v25, v136
	v_pk_mul_f32 v[24:25], v[24:25], v[182:183]
	v_and_b32_e32 v182, 0xffff0000, v20
	v_add_f32_e32 v21, v24, v25
	v_mov_b32_e32 v136, v135
	v_mul_f32_e32 v24, 0x41800000, v21
	v_pk_mul_f32 v[20:21], v[136:137], v[182:183]
	v_add_f32_e32 v20, v20, v21
	v_mul_f32_e32 v20, 0x41800000, v20
	v_cvt_pk_fp8_f32 v29, v24, v20
	v_cvt_pk_f32_fp8_sdwa v[24:25], v28 src0_sel:WORD_1
	v_pk_mul_f32 v[20:21], v[132:133], s[16:17] op_sel_hi:[1,0]
	v_lshlrev_b32_e32 v182, 16, v19
	v_mov_b32_e32 v132, v20
	v_mov_b32_e32 v133, v24
	v_mov_b32_e32 v24, v21
	v_cvt_pk_f32_fp8_e32 v[20:21], v28
	v_pk_mul_f32 v[132:133], v[132:133], v[182:183]
	v_and_b32_e32 v182, 0xffff0000, v19
	v_add_f32_e32 v134, v132, v133
	v_pk_mul_f32 v[24:25], v[24:25], v[182:183]
	v_lshlrev_b32_e32 v182, 16, v18
	v_mov_b32_e32 v132, v130
	v_mov_b32_e32 v133, v20
	v_pk_mul_f32 v[132:133], v[132:133], v[182:183]
	v_and_b32_e32 v182, 0xffff0000, v18
	v_add_f32_e32 v19, v132, v133
	v_mov_b32_e32 v20, v131
	v_mul_f32_e32 v130, 0x41800000, v19
	v_pk_mul_f32 v[18:19], v[20:21], v[182:183]
	v_add_f32_e32 v18, v18, v19
	v_mul_f32_e32 v18, 0x41800000, v18
	v_cvt_pk_fp8_f32 v28, v130, v18
	v_add_f32_e32 v19, v24, v25
	v_mul_f32_e32 v18, 0x41800000, v134
	v_mul_f32_e32 v19, 0x41800000, v19
	v_or_b32_e32 v146, v32, v194
	v_cvt_pk_fp8_f32 v28, v18, v19 op_sel:[0,0,1]
	v_mul_f32_e32 v18, 0x41800000, v138
	v_ashrrev_i32_e32 v147, 31, v146
	v_cvt_pk_fp8_f32 v29, v33, v18 op_sel:[0,0,1]
	v_lshlrev_b64 v[146:147], 11, v[146:147]
	v_pk_mul_f32 v[18:19], v[128:129], s[16:17] op_sel_hi:[1,0]
	v_cvt_pk_f32_fp8_e32 v[128:129], v188
	v_lshl_add_u64 v[22:23], s[4:5], 0, v[146:147]
	v_lshl_add_u64 v[22:23], v[22:23], 0, v[30:31]
	v_cvt_pk_f32_fp8_sdwa v[130:131], v188 src0_sel:WORD_1
	v_lshl_add_u64 v[22:23], v[22:23], 0, v[174:175]
	v_permlane16_swap_b32_e32 v26, v28
	v_permlane16_swap_b32_e32 v27, v29
	v_pk_mul_f32 v[20:21], v[126:127], s[16:17] op_sel_hi:[1,0]
	global_store_dwordx4 v[22:23], v[26:29], off offset:128
	v_lshlrev_b32_e32 v182, 16, v14
	v_and_b32_e32 v14, 0xffff0000, v14
	v_lshlrev_b32_e32 v26, 16, v15
	v_and_b32_e32 v28, 0xffff0000, v15
	v_mov_b32_e32 v137, v128
	v_mov_b32_e32 v128, v21
	v_mov_b32_e32 v15, v183
	v_cvt_pk_f32_fp8_e32 v[132:133], v189
	v_pk_mul_f32 v[14:15], v[128:129], v[14:15]
	v_mov_b32_e32 v27, v183
	v_add_f32_e32 v21, v14, v15
	v_mov_b32_e32 v14, v18
	v_mov_b32_e32 v15, v130
	v_pk_mul_f32 v[14:15], v[14:15], v[26:27]
	v_mov_b32_e32 v130, v19
	v_mov_b32_e32 v29, v183
	v_pk_mul_f32 v[24:25], v[122:123], s[16:17] op_sel_hi:[1,0]
	v_cvt_pk_f32_fp8_sdwa v[134:135], v189 src0_sel:WORD_1
	v_add_f32_e32 v18, v14, v15
	v_pk_mul_f32 v[14:15], v[130:131], v[28:29]
	v_permlane16_swap_b32_e32 v200, v202
	v_permlane16_swap_b32_e32 v201, v203
	v_lshlrev_b32_e32 v122, 16, v16
	v_add_f32_e32 v19, v14, v15
	v_mov_b32_e32 v14, v24
	v_mov_b32_e32 v15, v132
	v_mov_b32_e32 v123, v183
	global_store_dwordx4 v[22:23], v[200:203], off
	v_pk_mul_f32 v[22:23], v[124:125], s[16:17] op_sel_hi:[1,0]
	v_and_b32_e32 v16, 0xffff0000, v16
	v_lshlrev_b32_e32 v124, 16, v17
	v_and_b32_e32 v126, 0xffff0000, v17
	v_pk_mul_f32 v[14:15], v[14:15], v[122:123]
	v_mov_b32_e32 v132, v25
	v_mov_b32_e32 v17, v183
	v_add_f32_e32 v24, v14, v15
	v_pk_mul_f32 v[14:15], v[132:133], v[16:17]
	v_mov_b32_e32 v136, v20
	v_add_f32_e32 v16, v14, v15
	v_mov_b32_e32 v14, v22
	v_mov_b32_e32 v15, v134
	v_mov_b32_e32 v125, v183
	v_pk_mul_f32 v[136:137], v[136:137], v[182:183]
	v_pk_mul_f32 v[14:15], v[14:15], v[124:125]
	v_mov_b32_e32 v134, v23
	v_mov_b32_e32 v127, v183
	v_add_f32_e32 v20, v136, v137
	v_add_f32_e32 v17, v14, v15
	v_pk_mul_f32 v[14:15], v[134:135], v[126:127]
	v_mul_f32_e32 v16, 0x41800000, v16
	v_add_f32_e32 v22, v14, v15
	v_mul_f32_e32 v15, 0x41800000, v20
	v_mul_f32_e32 v20, 0x41800000, v21
	v_cvt_pk_fp8_f32 v14, v15, v20
	v_mul_f32_e32 v20, 0x41800000, v24
	v_cvt_pk_fp8_f32 v15, v20, v16
	v_mul_f32_e32 v18, 0x41800000, v18
	v_mul_f32_e32 v19, 0x41800000, v19
	v_cvt_pk_fp8_f32 v14, v18, v19 op_sel:[0,0,1]
	v_pk_mul_f32 v[18:19], v[118:119], s[16:17] op_sel_hi:[1,0]
	v_cvt_pk_f32_fp8_e32 v[118:119], v160
	v_mul_f32_e32 v16, 0x41800000, v17
	v_mul_f32_e32 v17, 0x41800000, v22
	v_cvt_pk_fp8_f32 v15, v16, v17 op_sel:[0,0,1]
	v_pk_mul_f32 v[16:17], v[120:121], s[16:17] op_sel_hi:[1,0]
	v_cvt_pk_f32_fp8_sdwa v[120:121], v160 src0_sel:WORD_1
	v_lshlrev_b32_e32 v182, 16, v10
	v_and_b32_e32 v10, 0xffff0000, v10
	v_lshlrev_b32_e32 v24, 16, v11
	v_and_b32_e32 v26, 0xffff0000, v11
	v_mov_b32_e32 v127, v118
	v_mov_b32_e32 v118, v19
	v_mov_b32_e32 v11, v183
	v_cvt_pk_f32_fp8_e32 v[122:123], v161
	v_pk_mul_f32 v[10:11], v[118:119], v[10:11]
	v_mov_b32_e32 v25, v183
	v_add_f32_e32 v19, v10, v11
	v_mov_b32_e32 v10, v16
	v_mov_b32_e32 v11, v120
	v_pk_mul_f32 v[10:11], v[10:11], v[24:25]
	v_mov_b32_e32 v120, v17
	v_pk_mul_f32 v[22:23], v[114:115], s[16:17] op_sel_hi:[1,0]
	v_cvt_pk_f32_fp8_sdwa v[124:125], v161 src0_sel:WORD_1
	v_add_f32_e32 v16, v10, v11
	v_pk_mul_f32 v[10:11], v[120:121], v[26:27]
	v_lshlrev_b32_e32 v28, 16, v12
	v_add_f32_e32 v17, v10, v11
	v_mov_b32_e32 v10, v22
	v_mov_b32_e32 v11, v122
	v_pk_mul_f32 v[20:21], v[116:117], s[16:17] op_sel_hi:[1,0]
	v_and_b32_e32 v12, 0xffff0000, v12
	v_lshlrev_b32_e32 v114, 16, v13
	v_and_b32_e32 v116, 0xffff0000, v13
	v_pk_mul_f32 v[10:11], v[10:11], v[28:29]
	v_mov_b32_e32 v122, v23
	v_mov_b32_e32 v13, v183
	v_add_f32_e32 v22, v10, v11
	v_pk_mul_f32 v[10:11], v[122:123], v[12:13]
	v_mov_b32_e32 v126, v18
	v_add_f32_e32 v12, v10, v11
	v_mov_b32_e32 v10, v20
	v_mov_b32_e32 v11, v124
	v_mov_b32_e32 v115, v183
	v_pk_mul_f32 v[126:127], v[126:127], v[182:183]
	v_pk_mul_f32 v[10:11], v[10:11], v[114:115]
	v_mov_b32_e32 v124, v21
	v_mov_b32_e32 v117, v183
	v_add_f32_e32 v18, v126, v127
	v_add_f32_e32 v13, v10, v11
	v_pk_mul_f32 v[10:11], v[124:125], v[116:117]
	v_mul_f32_e32 v12, 0x41800000, v12
	v_add_f32_e32 v20, v10, v11
	v_mul_f32_e32 v11, 0x41800000, v18
	v_mul_f32_e32 v18, 0x41800000, v19
	v_cvt_pk_fp8_f32 v10, v11, v18
	v_mul_f32_e32 v18, 0x41800000, v22
	v_cvt_pk_fp8_f32 v11, v18, v12
	v_cvt_pk_f32_fp8_sdwa v[18:19], v159 src0_sel:WORD_1
	v_mul_f32_e32 v16, 0x41800000, v16
	v_mul_f32_e32 v17, 0x41800000, v17
	v_cvt_pk_fp8_f32 v10, v16, v17 op_sel:[0,0,1]
	v_pk_mul_f32 v[16:17], v[112:113], s[16:17] op_sel_hi:[1,0]
	v_lshlrev_b32_e32 v182, 16, v9
	v_mov_b32_e32 v22, v16
	v_mov_b32_e32 v23, v18
	v_pk_mul_f32 v[22:23], v[22:23], v[182:183]
	v_and_b32_e32 v182, 0xffff0000, v9
	v_add_f32_e32 v16, v22, v23
	v_mov_b32_e32 v18, v17
	v_mul_f32_e32 v24, 0x41800000, v16
	v_pk_mul_f32 v[16:17], v[18:19], v[182:183]
	v_cvt_pk_f32_fp8_e32 v[18:19], v159
	v_mul_f32_e32 v12, 0x41800000, v13
	v_mul_f32_e32 v13, 0x41800000, v20
	v_pk_mul_f32 v[20:21], v[110:111], s[16:17] op_sel_hi:[1,0]
	v_add_f32_e32 v25, v16, v17
	v_lshlrev_b32_e32 v182, 16, v8
	v_mov_b32_e32 v16, v20
	v_mov_b32_e32 v17, v18
	v_pk_mul_f32 v[16:17], v[16:17], v[182:183]
	v_and_b32_e32 v182, 0xffff0000, v8
	v_add_f32_e32 v9, v16, v17
	v_mov_b32_e32 v18, v21
	v_mul_f32_e32 v16, 0x41800000, v9
	v_pk_mul_f32 v[8:9], v[18:19], v[182:183]
	v_cvt_pk_f32_fp8_sdwa v[18:19], v158 src0_sel:WORD_1
	v_add_f32_e32 v8, v8, v9
	v_mul_f32_e32 v8, 0x41800000, v8
	v_cvt_pk_fp8_f32 v17, v16, v8
	v_pk_mul_f32 v[8:9], v[108:109], s[16:17] op_sel_hi:[1,0]
	v_mov_b32_e32 v23, v18
	v_mov_b32_e32 v22, v8
	v_mov_b32_e32 v18, v9
	v_cvt_pk_f32_fp8_e32 v[8:9], v158
	v_lshlrev_b32_e32 v182, 16, v7
	v_pk_mul_f32 v[20:21], v[106:107], s[16:17] op_sel_hi:[1,0]
	v_pk_mul_f32 v[22:23], v[22:23], v[182:183]
	v_and_b32_e32 v182, 0xffff0000, v7
	v_add_f32_e32 v26, v22, v23
	v_pk_mul_f32 v[18:19], v[18:19], v[182:183]
	v_lshlrev_b32_e32 v182, 16, v6
	v_mov_b32_e32 v22, v20
	v_mov_b32_e32 v23, v8
	v_pk_mul_f32 v[22:23], v[22:23], v[182:183]
	v_and_b32_e32 v182, 0xffff0000, v6
	v_add_f32_e32 v7, v22, v23
	v_mov_b32_e32 v8, v21
	v_mul_f32_e32 v20, 0x41800000, v7
	v_pk_mul_f32 v[6:7], v[8:9], v[182:183]
	v_add_f32_e32 v6, v6, v7
	v_mul_f32_e32 v6, 0x41800000, v6
	v_cvt_pk_fp8_f32 v16, v20, v6
	v_add_f32_e32 v7, v18, v19
	v_cvt_pk_fp8_f32 v11, v12, v13 op_sel:[0,0,1]
	v_or_b32_e32 v12, v32, v195
	v_mul_f32_e32 v6, 0x41800000, v26
	v_mul_f32_e32 v7, 0x41800000, v7
	v_ashrrev_i32_e32 v13, 31, v12
	v_cvt_pk_fp8_f32 v16, v6, v7 op_sel:[0,0,1]
	v_mul_f32_e32 v6, 0x41800000, v25
	v_lshlrev_b64 v[12:13], 11, v[12:13]
	v_cvt_pk_fp8_f32 v17, v24, v6 op_sel:[0,0,1]
	v_lshl_add_u64 v[6:7], s[4:5], 0, v[12:13]
	v_cvt_pk_f32_fp8_sdwa v[12:13], v157 src0_sel:WORD_1
	v_lshl_add_u64 v[6:7], v[6:7], 0, v[30:31]
	v_permlane16_swap_b32_e32 v14, v16
	v_permlane16_swap_b32_e32 v15, v17
	v_lshl_add_u64 v[6:7], v[6:7], 0, v[174:175]
	v_pk_mul_f32 v[8:9], v[104:105], s[16:17] op_sel_hi:[1,0]
	global_store_dwordx4 v[6:7], v[14:17], off
	v_lshlrev_b32_e32 v182, 16, v5
	v_mov_b32_e32 v134, v94
	v_mov_b32_e32 v16, v8
	v_mov_b32_e32 v17, v12
	v_pk_mul_f32 v[16:17], v[16:17], v[182:183]
	v_and_b32_e32 v182, 0xffff0000, v5
	v_add_f32_e32 v8, v16, v17
	v_mov_b32_e32 v12, v9
	v_mul_f32_e32 v18, 0x41800000, v8
	v_pk_mul_f32 v[8:9], v[12:13], v[182:183]
	v_cvt_pk_f32_fp8_e32 v[12:13], v157
	v_pk_mul_f32 v[14:15], v[102:103], s[16:17] op_sel_hi:[1,0]
	v_add_f32_e32 v19, v8, v9
	v_lshlrev_b32_e32 v182, 16, v4
	v_mov_b32_e32 v8, v14
	v_mov_b32_e32 v9, v12
	v_pk_mul_f32 v[8:9], v[8:9], v[182:183]
	v_and_b32_e32 v182, 0xffff0000, v4
	v_add_f32_e32 v5, v8, v9
	v_mov_b32_e32 v12, v15
	v_mul_f32_e32 v8, 0x41800000, v5
	v_pk_mul_f32 v[4:5], v[12:13], v[182:183]
	v_add_f32_e32 v4, v4, v5
	v_mul_f32_e32 v4, 0x41800000, v4
	v_cvt_pk_fp8_f32 v13, v8, v4
	v_cvt_pk_f32_fp8_sdwa v[8:9], v156 src0_sel:WORD_1
	v_pk_mul_f32 v[4:5], v[100:101], s[16:17] op_sel_hi:[1,0]
	v_lshlrev_b32_e32 v182, 16, v3
	v_mov_b32_e32 v16, v4
	v_mov_b32_e32 v17, v8
	v_mov_b32_e32 v8, v5
	v_cvt_pk_f32_fp8_e32 v[4:5], v156
	v_pk_mul_f32 v[14:15], v[98:99], s[16:17] op_sel_hi:[1,0]
	v_pk_mul_f32 v[16:17], v[16:17], v[182:183]
	v_and_b32_e32 v182, 0xffff0000, v3
	v_add_f32_e32 v20, v16, v17
	v_pk_mul_f32 v[8:9], v[8:9], v[182:183]
	v_lshlrev_b32_e32 v182, 16, v2
	v_mov_b32_e32 v16, v14
	v_mov_b32_e32 v17, v4
	v_pk_mul_f32 v[16:17], v[16:17], v[182:183]
	v_and_b32_e32 v182, 0xffff0000, v2
	v_add_f32_e32 v3, v16, v17
	v_mov_b32_e32 v4, v15
	v_mul_f32_e32 v14, 0x41800000, v3
	v_pk_mul_f32 v[2:3], v[4:5], v[182:183]
	v_add_f32_e32 v2, v2, v3
	v_mul_f32_e32 v2, 0x41800000, v2
	v_cvt_pk_fp8_f32 v12, v14, v2
	v_add_f32_e32 v3, v8, v9
	v_mul_f32_e32 v2, 0x41800000, v20
	v_mul_f32_e32 v3, 0x41800000, v3
	v_cvt_pk_fp8_f32 v12, v2, v3 op_sel:[0,0,1]
	v_mul_f32_e32 v2, 0x41800000, v19
	v_cvt_pk_fp8_f32 v13, v18, v2 op_sel:[0,0,1]
	v_add_u32_e32 v100, 0x80, v32
	v_mad_i64_i32 v[2:3], s[28:29], v100, s51, v[184:185]
	v_permlane16_swap_b32_e32 v10, v12
	v_permlane16_swap_b32_e32 v11, v13
	v_lshl_add_u64 v[2:3], v[2:3], 0, s[14:15]
	global_store_dwordx4 v[6:7], v[10:13], off offset:128
	v_lshl_add_u64 v[4:5], v[2:3], 0, v[186:187]
	v_ashrrev_i32_e32 v101, 31, v100
	global_load_dwordx4 v[108:111], v[4:5], off
	v_lshlrev_b64 v[4:5], 11, v[100:101]
	v_lshl_add_u64 v[4:5], s[8:9], 0, v[4:5]
	v_lshl_add_u64 v[4:5], v[4:5], 0, v[30:31]
	global_load_dwordx2 v[26:27], v[4:5], off
	v_lshl_add_u64 v[2:3], v[2:3], 0, v[154:155]
	global_load_dwordx4 v[112:115], v[2:3], off
	global_load_dwordx2 v[116:117], v[4:5], off offset:128
	v_add_u32_e32 v2, 0x90, v32
	v_ashrrev_i32_e32 v3, 31, v2
	v_mad_i64_i32 v[4:5], s[28:29], v2, s51, v[184:185]
	v_lshl_add_u64 v[4:5], v[4:5], 0, s[14:15]
	v_lshlrev_b64 v[2:3], 11, v[2:3]
	v_lshl_add_u64 v[2:3], s[8:9], 0, v[2:3]
	v_lshl_add_u64 v[6:7], v[4:5], 0, v[186:187]
	v_lshl_add_u64 v[2:3], v[2:3], 0, v[30:31]
	global_load_dwordx4 v[22:25], v[6:7], off
	global_load_dwordx2 v[106:107], v[2:3], off
	v_lshl_add_u64 v[4:5], v[4:5], 0, v[154:155]
	global_load_dwordx4 v[18:21], v[4:5], off
	global_load_dwordx2 v[28:29], v[2:3], off offset:128
	v_mov_b32_e32 v119, v183
	v_mov_b32_e32 v121, v183
	v_mov_b32_e32 v123, v183
	v_mov_b32_e32 v125, v183
	v_mov_b32_e32 v127, v183
	v_add_u32_e32 v2, 0xa0, v32
	v_ashrrev_i32_e32 v3, 31, v2
	v_mad_i64_i32 v[4:5], s[28:29], v2, s51, v[184:185]
	v_lshl_add_u64 v[4:5], v[4:5], 0, s[14:15]
	v_lshlrev_b64 v[2:3], 11, v[2:3]
	v_lshl_add_u64 v[2:3], s[8:9], 0, v[2:3]
	v_lshl_add_u64 v[6:7], v[4:5], 0, v[186:187]
	v_lshl_add_u64 v[2:3], v[2:3], 0, v[30:31]
	global_load_dwordx4 v[14:17], v[6:7], off
	global_load_dwordx2 v[104:105], v[2:3], off
	v_lshl_add_u64 v[4:5], v[4:5], 0, v[154:155]
	global_load_dwordx4 v[10:13], v[4:5], off
	global_load_dwordx2 v[102:103], v[2:3], off offset:128
	v_add_u32_e32 v2, 0xb0, v32
	v_ashrrev_i32_e32 v3, 31, v2
	v_mad_i64_i32 v[4:5], s[28:29], v2, s51, v[184:185]
	v_lshl_add_u64 v[4:5], v[4:5], 0, s[14:15]
	v_lshlrev_b64 v[2:3], 11, v[2:3]
	v_lshl_add_u64 v[2:3], s[8:9], 0, v[2:3]
	v_lshl_add_u64 v[6:7], v[4:5], 0, v[186:187]
	v_lshl_add_u64 v[32:33], v[2:3], 0, v[30:31]
	global_load_dwordx4 v[6:9], v[6:7], off
	s_nop 0
	global_load_dwordx2 v[98:99], v[32:33], off
	v_lshl_add_u64 v[2:3], v[4:5], 0, v[154:155]
	global_load_dwordx4 v[2:5], v[2:3], off
	s_nop 0
	global_load_dwordx2 v[32:33], v[32:33], off offset:128
	s_waitcnt vmcnt(15)
	v_lshlrev_b32_e32 v182, 16, v108
	v_and_b32_e32 v108, 0xffff0000, v108
	v_lshlrev_b32_e32 v118, 16, v109
	v_and_b32_e32 v120, 0xffff0000, v109
	s_waitcnt vmcnt(14)
	v_cvt_pk_f32_fp8_e32 v[128:129], v26
	v_cvt_pk_f32_fp8_sdwa v[130:131], v26 src0_sel:WORD_1
	v_mov_b32_e32 v109, v183
	v_cvt_pk_f32_fp8_e32 v[132:133], v27
	v_mov_b32_e32 v135, v128
	v_mov_b32_e32 v128, v95
	v_pk_mul_f32 v[94:95], v[128:129], v[108:109]
	v_cvt_pk_f32_fp8_sdwa v[26:27], v27 src0_sel:WORD_1
	v_add_f32_e32 v108, v94, v95
	v_mov_b32_e32 v94, v96
	v_mov_b32_e32 v95, v130
	v_pk_mul_f32 v[94:95], v[94:95], v[118:119]
	v_mov_b32_e32 v130, v97
	v_add_f32_e32 v96, v94, v95
	v_pk_mul_f32 v[94:95], v[130:131], v[120:121]
	v_lshlrev_b32_e32 v122, 16, v110
	v_and_b32_e32 v110, 0xffff0000, v110
	v_lshlrev_b32_e32 v124, 16, v111
	v_and_b32_e32 v126, 0xffff0000, v111
	v_add_f32_e32 v97, v94, v95
	v_mov_b32_e32 v94, v90
	v_mov_b32_e32 v95, v132
	v_mov_b32_e32 v132, v91
	v_mov_b32_e32 v111, v183
	v_pk_mul_f32 v[94:95], v[94:95], v[122:123]
	v_pk_mul_f32 v[90:91], v[132:133], v[110:111]
	v_pk_mul_f32 v[134:135], v[134:135], v[182:183]
	v_add_f32_e32 v94, v94, v95
	v_add_f32_e32 v95, v90, v91
	v_mov_b32_e32 v90, v92
	v_mov_b32_e32 v91, v26
	v_mov_b32_e32 v26, v93
	v_add_f32_e32 v101, v134, v135
	v_pk_mul_f32 v[90:91], v[90:91], v[124:125]
	v_pk_mul_f32 v[26:27], v[26:27], v[126:127]
	v_add_f32_e32 v92, v90, v91
	v_add_f32_e32 v26, v26, v27
	v_mul_f32_e32 v27, 0x41800000, v101
	v_mul_f32_e32 v91, 0x41800000, v108
	v_cvt_pk_fp8_f32 v90, v27, v91
	v_mul_f32_e32 v27, 0x41800000, v94
	v_mul_f32_e32 v94, 0x41800000, v95
	v_cvt_pk_fp8_f32 v91, v27, v94
	v_mul_f32_e32 v93, 0x41800000, v96
	v_mul_f32_e32 v96, 0x41800000, v97
	v_mul_f32_e32 v27, 0x41800000, v92
	v_mul_f32_e32 v26, 0x41800000, v26
	v_cvt_pk_fp8_f32 v90, v93, v96 op_sel:[0,0,1]
	v_cvt_pk_fp8_f32 v91, v27, v26 op_sel:[0,0,1]
	v_pk_mul_f32 v[26:27], v[88:89], s[16:17] op_sel_hi:[1,0]
	s_waitcnt vmcnt(13)
	v_lshlrev_b32_e32 v182, 16, v112
	v_and_b32_e32 v88, 0xffff0000, v112
	v_lshlrev_b32_e32 v96, 16, v114
	v_and_b32_e32 v108, 0xffff0000, v114
	v_lshlrev_b32_e32 v110, 16, v115
	v_and_b32_e32 v112, 0xffff0000, v115
	s_waitcnt vmcnt(12)
	v_cvt_pk_f32_fp8_e32 v[114:115], v116
	v_cvt_pk_f32_fp8_sdwa v[118:119], v116 src0_sel:WORD_1
	v_cvt_pk_f32_fp8_e32 v[120:121], v117
	v_mov_b32_e32 v89, v183
	v_mov_b32_e32 v123, v114
	v_mov_b32_e32 v114, v87
	v_mov_b32_e32 v122, v86
	v_pk_mul_f32 v[86:87], v[114:115], v[88:89]
	v_lshlrev_b32_e32 v92, 16, v113
	v_and_b32_e32 v94, 0xffff0000, v113
	v_add_f32_e32 v88, v86, v87
	v_mov_b32_e32 v86, v26
	v_mov_b32_e32 v87, v118
	v_mov_b32_e32 v93, v183
	v_mov_b32_e32 v118, v27
	v_mov_b32_e32 v95, v183
	v_cvt_pk_f32_fp8_sdwa v[116:117], v117 src0_sel:WORD_1
	v_pk_mul_f32 v[86:87], v[86:87], v[92:93]
	v_pk_mul_f32 v[26:27], v[118:119], v[94:95]
	v_add_f32_e32 v86, v86, v87
	v_add_f32_e32 v87, v26, v27
	v_mov_b32_e32 v26, v82
	v_mov_b32_e32 v27, v120
	v_mov_b32_e32 v97, v183
	v_pk_mul_f32 v[26:27], v[26:27], v[96:97]
	v_mov_b32_e32 v120, v83
	v_add_f32_e32 v82, v26, v27
	v_pk_mul_f32 v[26:27], v[120:121], v[108:109]
	v_pk_mul_f32 v[122:123], v[122:123], v[182:183]
	v_add_f32_e32 v83, v26, v27
	v_mov_b32_e32 v26, v84
	v_mov_b32_e32 v27, v116
	v_pk_mul_f32 v[26:27], v[26:27], v[110:111]
	v_mov_b32_e32 v116, v85
	v_mov_b32_e32 v113, v183
	v_add_f32_e32 v101, v122, v123
	v_add_f32_e32 v84, v26, v27
	v_pk_mul_f32 v[26:27], v[116:117], v[112:113]
	v_mul_f32_e32 v88, 0x41800000, v88
	v_add_f32_e32 v85, v26, v27
	v_mul_f32_e32 v27, 0x41800000, v101
	v_cvt_pk_fp8_f32 v26, v27, v88
	v_mul_f32_e32 v82, 0x41800000, v82
	v_mul_f32_e32 v83, 0x41800000, v83
	v_cvt_pk_fp8_f32 v27, v82, v83
	v_mul_f32_e32 v82, 0x41800000, v84
	v_mul_f32_e32 v83, 0x41800000, v85
	s_waitcnt vmcnt(10)
	v_cvt_pk_f32_fp8_sdwa v[84:85], v107 src0_sel:WORD_1
	v_mul_f32_e32 v86, 0x41800000, v86
	v_mul_f32_e32 v87, 0x41800000, v87
	v_cvt_pk_fp8_f32 v26, v86, v87 op_sel:[0,0,1]
	v_lshlrev_b32_e32 v182, 16, v25
	v_mov_b32_e32 v86, v80
	v_mov_b32_e32 v87, v84
	v_pk_mul_f32 v[86:87], v[86:87], v[182:183]
	v_and_b32_e32 v182, 0xffff0000, v25
	v_add_f32_e32 v80, v86, v87
	v_mov_b32_e32 v84, v81
	v_mul_f32_e32 v86, 0x41800000, v80
	v_pk_mul_f32 v[80:81], v[84:85], v[182:183]
	v_cvt_pk_f32_fp8_e32 v[84:85], v107
	v_add_f32_e32 v87, v80, v81
	v_lshlrev_b32_e32 v182, 16, v24
	v_mov_b32_e32 v80, v78
	v_mov_b32_e32 v81, v84
	v_pk_mul_f32 v[80:81], v[80:81], v[182:183]
	v_and_b32_e32 v182, 0xffff0000, v24
	v_add_f32_e32 v25, v80, v81
	v_mov_b32_e32 v84, v79
	v_mul_f32_e32 v78, 0x41800000, v25
	v_pk_mul_f32 v[24:25], v[84:85], v[182:183]
	v_add_f32_e32 v24, v24, v25
	v_mul_f32_e32 v24, 0x41800000, v24
	v_cvt_pk_fp8_f32 v93, v78, v24
	v_pk_mul_f32 v[24:25], v[72:73], s[16:17] op_sel_hi:[1,0]
	v_cvt_pk_f32_fp8_sdwa v[72:73], v106 src0_sel:WORD_1
	v_mov_b32_e32 v78, v24
	v_lshlrev_b32_e32 v182, 16, v23
	v_mov_b32_e32 v79, v72
	v_mov_b32_e32 v72, v25
	v_cvt_pk_f32_fp8_e32 v[24:25], v106
	v_pk_mul_f32 v[78:79], v[78:79], v[182:183]
	v_and_b32_e32 v182, 0xffff0000, v23
	v_add_f32_e32 v80, v78, v79
	v_pk_mul_f32 v[72:73], v[72:73], v[182:183]
	v_lshlrev_b32_e32 v182, 16, v22
	v_mov_b32_e32 v78, v70
	v_mov_b32_e32 v79, v24
	v_pk_mul_f32 v[78:79], v[78:79], v[182:183]
	v_and_b32_e32 v182, 0xffff0000, v22
	v_add_f32_e32 v23, v78, v79
	v_mov_b32_e32 v24, v71
	v_mul_f32_e32 v70, 0x41800000, v23
	v_pk_mul_f32 v[22:23], v[24:25], v[182:183]
	v_pk_mul_f32 v[24:25], v[76:77], s[16:17] op_sel_hi:[1,0]
	v_add_f32_e32 v22, v22, v23
	v_mul_f32_e32 v22, 0x41800000, v22
	v_cvt_pk_fp8_f32 v92, v70, v22
	s_waitcnt vmcnt(8)
	v_cvt_pk_f32_fp8_sdwa v[70:71], v29 src0_sel:WORD_1
	v_add_f32_e32 v23, v72, v73
	v_pk_mul_f32 v[72:73], v[74:75], s[16:17] op_sel_hi:[1,0]
	v_lshlrev_b32_e32 v182, 16, v21
	v_mov_b32_e32 v74, v24
	v_mov_b32_e32 v75, v70
	v_pk_mul_f32 v[74:75], v[74:75], v[182:183]
	v_and_b32_e32 v182, 0xffff0000, v21
	v_add_f32_e32 v24, v74, v75
	v_mov_b32_e32 v70, v25
	v_mul_f32_e32 v74, 0x41800000, v24
	v_pk_mul_f32 v[24:25], v[70:71], v[182:183]
	v_cvt_pk_f32_fp8_e32 v[70:71], v29
	v_add_f32_e32 v75, v24, v25
	v_lshlrev_b32_e32 v182, 16, v20
	v_mov_b32_e32 v24, v72
	v_mov_b32_e32 v25, v70
	v_pk_mul_f32 v[24:25], v[24:25], v[182:183]
	v_and_b32_e32 v182, 0xffff0000, v20
	v_add_f32_e32 v21, v24, v25
	v_mov_b32_e32 v70, v73
	v_mul_f32_e32 v24, 0x41800000, v21
	v_pk_mul_f32 v[20:21], v[70:71], v[182:183]
	v_add_f32_e32 v20, v20, v21
	v_mul_f32_e32 v20, 0x41800000, v20
	v_cvt_pk_fp8_f32 v29, v24, v20
	v_cvt_pk_f32_fp8_sdwa v[24:25], v28 src0_sel:WORD_1
	v_pk_mul_f32 v[20:21], v[68:69], s[16:17] op_sel_hi:[1,0]
	v_lshlrev_b32_e32 v182, 16, v19
	v_mov_b32_e32 v68, v20
	v_mov_b32_e32 v69, v24
	v_mov_b32_e32 v24, v21
	v_cvt_pk_f32_fp8_e32 v[20:21], v28
	v_pk_mul_f32 v[68:69], v[68:69], v[182:183]
	v_and_b32_e32 v182, 0xffff0000, v19
	v_add_f32_e32 v70, v68, v69
	v_pk_mul_f32 v[24:25], v[24:25], v[182:183]
	v_lshlrev_b32_e32 v182, 16, v18
	v_mov_b32_e32 v68, v66
	v_mov_b32_e32 v69, v20
	v_pk_mul_f32 v[68:69], v[68:69], v[182:183]
	v_and_b32_e32 v182, 0xffff0000, v18
	v_add_f32_e32 v19, v68, v69
	v_mov_b32_e32 v20, v67
	v_mul_f32_e32 v66, 0x41800000, v19
	v_pk_mul_f32 v[18:19], v[20:21], v[182:183]
	v_add_f32_e32 v18, v18, v19
	v_mul_f32_e32 v18, 0x41800000, v18
	v_cvt_pk_fp8_f32 v28, v66, v18
	v_add_f32_e32 v19, v24, v25
	v_mul_f32_e32 v18, 0x41800000, v70
	v_mul_f32_e32 v19, 0x41800000, v19
	v_cvt_pk_fp8_f32 v27, v82, v83 op_sel:[0,0,1]
	v_or_b32_e32 v82, v100, v194
	v_cvt_pk_fp8_f32 v28, v18, v19 op_sel:[0,0,1]
	v_mul_f32_e32 v18, 0x41800000, v75
	v_ashrrev_i32_e32 v83, 31, v82
	v_mul_f32_e32 v22, 0x41800000, v80
	v_mul_f32_e32 v23, 0x41800000, v23
	v_cvt_pk_fp8_f32 v29, v74, v18 op_sel:[0,0,1]
	v_lshlrev_b64 v[82:83], 11, v[82:83]
	v_cvt_pk_fp8_f32 v92, v22, v23 op_sel:[0,0,1]
	v_mul_f32_e32 v22, 0x41800000, v87
	v_pk_mul_f32 v[18:19], v[56:57], s[16:17] op_sel_hi:[1,0]
	s_waitcnt vmcnt(6)
	v_cvt_pk_f32_fp8_e32 v[56:57], v104
	v_cvt_pk_fp8_f32 v93, v86, v22 op_sel:[0,0,1]
	v_lshl_add_u64 v[22:23], s[4:5], 0, v[82:83]
	v_lshl_add_u64 v[22:23], v[22:23], 0, v[30:31]
	v_cvt_pk_f32_fp8_sdwa v[66:67], v104 src0_sel:WORD_1
	v_lshl_add_u64 v[22:23], v[22:23], 0, v[174:175]
	v_permlane16_swap_b32_e32 v26, v28
	v_permlane16_swap_b32_e32 v27, v29
	v_pk_mul_f32 v[20:21], v[54:55], s[16:17] op_sel_hi:[1,0]
	global_store_dwordx4 v[22:23], v[26:29], off offset:128
	v_lshlrev_b32_e32 v182, 16, v14
	v_and_b32_e32 v14, 0xffff0000, v14
	v_lshlrev_b32_e32 v26, 16, v15
	v_and_b32_e32 v28, 0xffff0000, v15
	v_mov_b32_e32 v73, v56
	v_mov_b32_e32 v56, v21
	v_mov_b32_e32 v15, v183
	v_cvt_pk_f32_fp8_e32 v[68:69], v105
	v_pk_mul_f32 v[14:15], v[56:57], v[14:15]
	v_mov_b32_e32 v27, v183
	v_add_f32_e32 v21, v14, v15
	v_mov_b32_e32 v14, v18
	v_mov_b32_e32 v15, v66
	v_pk_mul_f32 v[14:15], v[14:15], v[26:27]
	v_mov_b32_e32 v66, v19
	v_mov_b32_e32 v29, v183
	v_pk_mul_f32 v[24:25], v[50:51], s[16:17] op_sel_hi:[1,0]
	v_cvt_pk_f32_fp8_sdwa v[70:71], v105 src0_sel:WORD_1
	v_add_f32_e32 v18, v14, v15
	v_pk_mul_f32 v[14:15], v[66:67], v[28:29]
	v_permlane16_swap_b32_e32 v90, v92
	v_permlane16_swap_b32_e32 v91, v93
	v_lshlrev_b32_e32 v50, 16, v16
	v_add_f32_e32 v19, v14, v15
	v_mov_b32_e32 v14, v24
	v_mov_b32_e32 v15, v68
	v_mov_b32_e32 v51, v183
	global_store_dwordx4 v[22:23], v[90:93], off
	v_pk_mul_f32 v[22:23], v[52:53], s[16:17] op_sel_hi:[1,0]
	v_and_b32_e32 v16, 0xffff0000, v16
	v_lshlrev_b32_e32 v52, 16, v17
	v_and_b32_e32 v54, 0xffff0000, v17
	v_pk_mul_f32 v[14:15], v[14:15], v[50:51]
	v_mov_b32_e32 v68, v25
	v_mov_b32_e32 v17, v183
	v_add_f32_e32 v24, v14, v15
	v_pk_mul_f32 v[14:15], v[68:69], v[16:17]
	v_mov_b32_e32 v72, v20
	v_add_f32_e32 v16, v14, v15
	v_mov_b32_e32 v14, v22
	v_mov_b32_e32 v15, v70
	v_mov_b32_e32 v53, v183
	v_pk_mul_f32 v[72:73], v[72:73], v[182:183]
	v_pk_mul_f32 v[14:15], v[14:15], v[52:53]
	v_mov_b32_e32 v70, v23
	v_mov_b32_e32 v55, v183
	v_add_f32_e32 v20, v72, v73
	v_add_f32_e32 v17, v14, v15
	v_pk_mul_f32 v[14:15], v[70:71], v[54:55]
	v_mul_f32_e32 v16, 0x41800000, v16
	v_add_f32_e32 v22, v14, v15
	v_mul_f32_e32 v15, 0x41800000, v20
	v_mul_f32_e32 v20, 0x41800000, v21
	v_cvt_pk_fp8_f32 v14, v15, v20
	v_mul_f32_e32 v20, 0x41800000, v24
	s_waitcnt vmcnt(6)
	v_cvt_pk_f32_fp8_e32 v[54:55], v102
	v_cvt_pk_fp8_f32 v15, v20, v16
	v_mul_f32_e32 v18, 0x41800000, v18
	v_mul_f32_e32 v19, 0x41800000, v19
	v_cvt_pk_f32_fp8_sdwa v[56:57], v102 src0_sel:WORD_1
	v_cvt_pk_fp8_f32 v14, v18, v19 op_sel:[0,0,1]
	v_pk_mul_f32 v[18:19], v[62:63], s[16:17] op_sel_hi:[1,0]
	v_mul_f32_e32 v16, 0x41800000, v17
	v_mul_f32_e32 v17, 0x41800000, v22
	v_lshlrev_b32_e32 v182, 16, v10
	v_and_b32_e32 v10, 0xffff0000, v10
	v_lshlrev_b32_e32 v24, 16, v11
	v_and_b32_e32 v26, 0xffff0000, v11
	v_mov_b32_e32 v63, v54
	v_mov_b32_e32 v54, v19
	v_mov_b32_e32 v11, v183
	v_cvt_pk_fp8_f32 v15, v16, v17 op_sel:[0,0,1]
	v_pk_mul_f32 v[16:17], v[64:65], s[16:17] op_sel_hi:[1,0]
	v_pk_mul_f32 v[22:23], v[58:59], s[16:17] op_sel_hi:[1,0]
	v_cvt_pk_f32_fp8_e32 v[58:59], v103
	v_pk_mul_f32 v[10:11], v[54:55], v[10:11]
	v_mov_b32_e32 v25, v183
	v_add_f32_e32 v19, v10, v11
	v_mov_b32_e32 v10, v16
	v_mov_b32_e32 v11, v56
	v_pk_mul_f32 v[10:11], v[10:11], v[24:25]
	v_mov_b32_e32 v56, v17
	v_pk_mul_f32 v[20:21], v[60:61], s[16:17] op_sel_hi:[1,0]
	v_cvt_pk_f32_fp8_sdwa v[60:61], v103 src0_sel:WORD_1
	v_add_f32_e32 v16, v10, v11
	v_pk_mul_f32 v[10:11], v[56:57], v[26:27]
	v_lshlrev_b32_e32 v28, 16, v12
	v_add_f32_e32 v17, v10, v11
	v_mov_b32_e32 v10, v22
	v_mov_b32_e32 v11, v58
	v_and_b32_e32 v12, 0xffff0000, v12
	v_lshlrev_b32_e32 v50, 16, v13
	v_and_b32_e32 v52, 0xffff0000, v13
	v_pk_mul_f32 v[10:11], v[10:11], v[28:29]
	v_mov_b32_e32 v58, v23
	v_mov_b32_e32 v13, v183
	v_add_f32_e32 v22, v10, v11
	v_pk_mul_f32 v[10:11], v[58:59], v[12:13]
	v_mov_b32_e32 v62, v18
	v_add_f32_e32 v12, v10, v11
	v_mov_b32_e32 v10, v20
	v_mov_b32_e32 v11, v60
	v_pk_mul_f32 v[62:63], v[62:63], v[182:183]
	v_pk_mul_f32 v[10:11], v[10:11], v[50:51]
	v_mov_b32_e32 v60, v21
	v_add_f32_e32 v18, v62, v63
	v_add_f32_e32 v13, v10, v11
	v_pk_mul_f32 v[10:11], v[60:61], v[52:53]
	v_mul_f32_e32 v12, 0x41800000, v12
	v_add_f32_e32 v20, v10, v11
	v_mul_f32_e32 v11, 0x41800000, v18
	v_mul_f32_e32 v18, 0x41800000, v19
	v_cvt_pk_fp8_f32 v10, v11, v18
	v_mul_f32_e32 v18, 0x41800000, v22
	v_cvt_pk_fp8_f32 v11, v18, v12
	s_waitcnt vmcnt(4)
	v_cvt_pk_f32_fp8_sdwa v[18:19], v99 src0_sel:WORD_1
	v_mul_f32_e32 v16, 0x41800000, v16
	v_mul_f32_e32 v17, 0x41800000, v17
	v_cvt_pk_fp8_f32 v10, v16, v17 op_sel:[0,0,1]
	v_pk_mul_f32 v[16:17], v[44:45], s[16:17] op_sel_hi:[1,0]
	v_lshlrev_b32_e32 v182, 16, v9
	v_mov_b32_e32 v22, v16
	v_mov_b32_e32 v23, v18
	v_pk_mul_f32 v[22:23], v[22:23], v[182:183]
	v_and_b32_e32 v182, 0xffff0000, v9
	v_add_f32_e32 v16, v22, v23
	v_mov_b32_e32 v18, v17
	v_mul_f32_e32 v24, 0x41800000, v16
	v_pk_mul_f32 v[16:17], v[18:19], v[182:183]
	v_cvt_pk_f32_fp8_e32 v[18:19], v99
	v_mul_f32_e32 v12, 0x41800000, v13
	v_mul_f32_e32 v13, 0x41800000, v20
	v_pk_mul_f32 v[20:21], v[42:43], s[16:17] op_sel_hi:[1,0]
	v_add_f32_e32 v25, v16, v17
	v_lshlrev_b32_e32 v182, 16, v8
	v_mov_b32_e32 v16, v20
	v_mov_b32_e32 v17, v18
	v_pk_mul_f32 v[16:17], v[16:17], v[182:183]
	v_and_b32_e32 v182, 0xffff0000, v8
	v_add_f32_e32 v9, v16, v17
	v_mov_b32_e32 v18, v21
	v_mul_f32_e32 v16, 0x41800000, v9
	v_pk_mul_f32 v[8:9], v[18:19], v[182:183]
	v_cvt_pk_f32_fp8_sdwa v[18:19], v98 src0_sel:WORD_1
	v_add_f32_e32 v8, v8, v9
	v_mul_f32_e32 v8, 0x41800000, v8
	v_cvt_pk_fp8_f32 v17, v16, v8
	v_pk_mul_f32 v[8:9], v[40:41], s[16:17] op_sel_hi:[1,0]
	v_mov_b32_e32 v23, v18
	v_mov_b32_e32 v22, v8
	v_mov_b32_e32 v18, v9
	v_cvt_pk_f32_fp8_e32 v[8:9], v98
	v_lshlrev_b32_e32 v182, 16, v7
	v_pk_mul_f32 v[20:21], v[38:39], s[16:17] op_sel_hi:[1,0]
	v_pk_mul_f32 v[22:23], v[22:23], v[182:183]
	v_and_b32_e32 v182, 0xffff0000, v7
	v_add_f32_e32 v26, v22, v23
	v_pk_mul_f32 v[18:19], v[18:19], v[182:183]
	v_lshlrev_b32_e32 v182, 16, v6
	v_mov_b32_e32 v22, v20
	v_mov_b32_e32 v23, v8
	v_pk_mul_f32 v[22:23], v[22:23], v[182:183]
	v_and_b32_e32 v182, 0xffff0000, v6
	v_add_f32_e32 v7, v22, v23
	v_mov_b32_e32 v8, v21
	v_mul_f32_e32 v20, 0x41800000, v7
	v_pk_mul_f32 v[6:7], v[8:9], v[182:183]
	v_add_f32_e32 v6, v6, v7
	v_mul_f32_e32 v6, 0x41800000, v6
	v_cvt_pk_fp8_f32 v16, v20, v6
	v_add_f32_e32 v7, v18, v19
	v_cvt_pk_fp8_f32 v11, v12, v13 op_sel:[0,0,1]
	v_or_b32_e32 v12, v100, v195
	v_mul_f32_e32 v6, 0x41800000, v26
	v_mul_f32_e32 v7, 0x41800000, v7
	v_ashrrev_i32_e32 v13, 31, v12
	v_cvt_pk_fp8_f32 v16, v6, v7 op_sel:[0,0,1]
	v_mul_f32_e32 v6, 0x41800000, v25
	v_lshlrev_b64 v[12:13], 11, v[12:13]
	v_cvt_pk_fp8_f32 v17, v24, v6 op_sel:[0,0,1]
	v_lshl_add_u64 v[6:7], s[4:5], 0, v[12:13]
	s_waitcnt vmcnt(2)
	v_cvt_pk_f32_fp8_sdwa v[12:13], v33 src0_sel:WORD_1
	v_lshl_add_u64 v[6:7], v[6:7], 0, v[30:31]
	v_permlane16_swap_b32_e32 v14, v16
	v_permlane16_swap_b32_e32 v15, v17
	v_lshl_add_u64 v[6:7], v[6:7], 0, v[174:175]
	v_pk_mul_f32 v[8:9], v[48:49], s[16:17] op_sel_hi:[1,0]
	global_store_dwordx4 v[6:7], v[14:17], off
	v_lshlrev_b32_e32 v182, 16, v5
	s_nop 0
	v_mov_b32_e32 v16, v8
	v_mov_b32_e32 v17, v12
	v_pk_mul_f32 v[16:17], v[16:17], v[182:183]
	v_and_b32_e32 v182, 0xffff0000, v5
	v_add_f32_e32 v8, v16, v17
	v_mov_b32_e32 v12, v9
	v_mul_f32_e32 v18, 0x41800000, v8
	v_pk_mul_f32 v[8:9], v[12:13], v[182:183]
	v_cvt_pk_f32_fp8_e32 v[12:13], v33
	v_pk_mul_f32 v[14:15], v[46:47], s[16:17] op_sel_hi:[1,0]
	v_add_f32_e32 v19, v8, v9
	v_lshlrev_b32_e32 v182, 16, v4
	v_mov_b32_e32 v8, v14
	v_mov_b32_e32 v9, v12
	v_pk_mul_f32 v[8:9], v[8:9], v[182:183]
	v_and_b32_e32 v182, 0xffff0000, v4
	v_add_f32_e32 v5, v8, v9
	v_mov_b32_e32 v12, v15
	v_mul_f32_e32 v8, 0x41800000, v5
	v_pk_mul_f32 v[4:5], v[12:13], v[182:183]
	v_add_f32_e32 v4, v4, v5
	v_mul_f32_e32 v4, 0x41800000, v4
	v_cvt_pk_fp8_f32 v13, v8, v4
	v_cvt_pk_f32_fp8_sdwa v[8:9], v32 src0_sel:WORD_1
	v_pk_mul_f32 v[4:5], v[36:37], s[16:17] op_sel_hi:[1,0]
	v_lshlrev_b32_e32 v182, 16, v3
	v_mov_b32_e32 v16, v4
	v_mov_b32_e32 v17, v8
	v_mov_b32_e32 v8, v5
	v_cvt_pk_f32_fp8_e32 v[4:5], v32
	v_pk_mul_f32 v[14:15], v[34:35], s[16:17] op_sel_hi:[1,0]
	v_pk_mul_f32 v[16:17], v[16:17], v[182:183]
	v_and_b32_e32 v182, 0xffff0000, v3
	v_add_f32_e32 v20, v16, v17
	v_pk_mul_f32 v[8:9], v[8:9], v[182:183]
	v_lshlrev_b32_e32 v182, 16, v2
	v_mov_b32_e32 v16, v14
	v_mov_b32_e32 v17, v4
	v_pk_mul_f32 v[16:17], v[16:17], v[182:183]
	v_and_b32_e32 v182, 0xffff0000, v2
	v_add_f32_e32 v3, v16, v17
	v_mov_b32_e32 v4, v15
	v_mul_f32_e32 v14, 0x41800000, v3
	v_pk_mul_f32 v[2:3], v[4:5], v[182:183]
	v_add_f32_e32 v2, v2, v3
	v_mul_f32_e32 v2, 0x41800000, v2
	v_cvt_pk_fp8_f32 v12, v14, v2
	v_add_f32_e32 v3, v8, v9
	v_mul_f32_e32 v2, 0x41800000, v20
	v_mul_f32_e32 v3, 0x41800000, v3
	v_cvt_pk_fp8_f32 v12, v2, v3 op_sel:[0,0,1]
	v_mul_f32_e32 v2, 0x41800000, v19
	v_cvt_pk_fp8_f32 v13, v18, v2 op_sel:[0,0,1]
	v_permlane16_swap_b32_e32 v10, v12
	s_nop 0
	v_permlane16_swap_b32_e32 v11, v13
	global_store_dwordx4 v[6:7], v[10:13], off offset:128
	s_cbranch_vccnz .LBB0_546
	s_andn2_b64 vcc, exec, s[0:1]
	s_cbranch_vccnz .LBB0_545
	s_barrier
	s_branch .LBB0_545

.LBB0_706:
	v_lshl_add_u64 v[8:9], s[92:93], 0, v[4:5]
	v_add_co_u32_e32 v10, vcc, 0x69400000, v8
	v_mov_b32_e32 v144, 0
	s_nop 0
	v_addc_co_u32_e32 v11, vcc, 0, v9, vcc
	global_load_dwordx2 v[160:161], v[10:11], off
	v_add_co_u32_e32 v8, vcc, s43, v8
	v_lshl_add_u32 v144, v144, 2, v132
	s_nop 0
	v_addc_co_u32_e32 v9, vcc, 0, v9, vcc
	global_load_dwordx2 v[162:163], v[10:11], off offset:512
	global_load_dwordx2 v[164:165], v[10:11], off offset:1024
	global_load_dwordx2 v[166:167], v[10:11], off offset:1536
	global_load_dwordx2 v[168:169], v[10:11], off offset:2048
	global_load_dwordx2 v[170:171], v[10:11], off offset:2560
	global_load_dwordx2 v[172:173], v[10:11], off offset:3072
	global_load_dwordx2 v[174:175], v[10:11], off offset:3584
	s_waitcnt vmcnt(0)
	v_lshlrev_b32_e32 v6, 16, v160
	v_and_b32_e32 v7, 0xffff0000, v160
	v_lshlrev_b32_e32 v70, 16, v161
	v_and_b32_e32 v71, 0xffff0000, v161
	v_add_f32_e32 v12, v6, v7
	v_add_f32_e32 v13, v70, v71
	v_add_f32_e32 v12, v12, v13
	v_add_f32_e32 v14, 0, v12
	v_lshlrev_b32_e32 v66, 16, v162
	v_and_b32_e32 v67, 0xffff0000, v162
	v_lshlrev_b32_e32 v68, 16, v163
	v_and_b32_e32 v69, 0xffff0000, v163
	v_add_f32_e32 v12, v66, v67
	v_add_f32_e32 v13, v68, v69
	v_add_f32_e32 v12, v12, v13
	v_add_f32_e32 v14, v14, v12
	v_lshlrev_b32_e32 v64, 16, v164
	v_and_b32_e32 v65, 0xffff0000, v164
	v_lshlrev_b32_e32 v62, 16, v165
	v_and_b32_e32 v63, 0xffff0000, v165
	v_add_f32_e32 v12, v64, v65
	v_add_f32_e32 v13, v62, v63
	v_add_f32_e32 v12, v12, v13
	v_add_f32_e32 v14, v14, v12
	v_lshlrev_b32_e32 v58, 16, v166
	v_and_b32_e32 v59, 0xffff0000, v166
	v_lshlrev_b32_e32 v60, 16, v167
	v_and_b32_e32 v61, 0xffff0000, v167
	v_add_f32_e32 v12, v58, v59
	v_add_f32_e32 v13, v60, v61
	v_add_f32_e32 v12, v12, v13
	v_add_f32_e32 v14, v14, v12
	v_lshlrev_b32_e32 v56, 16, v168
	v_and_b32_e32 v57, 0xffff0000, v168
	v_lshlrev_b32_e32 v54, 16, v169
	v_and_b32_e32 v55, 0xffff0000, v169
	v_add_f32_e32 v12, v56, v57
	v_add_f32_e32 v13, v54, v55
	v_add_f32_e32 v12, v12, v13
	v_add_f32_e32 v14, v14, v12
	v_lshlrev_b32_e32 v32, 16, v170
	v_and_b32_e32 v33, 0xffff0000, v170
	v_lshlrev_b32_e32 v52, 16, v171
	v_and_b32_e32 v53, 0xffff0000, v171
	v_add_f32_e32 v12, v32, v33
	v_add_f32_e32 v13, v52, v53
	v_add_f32_e32 v12, v12, v13
	v_add_f32_e32 v14, v14, v12
	v_lshlrev_b32_e32 v30, 16, v172
	v_and_b32_e32 v31, 0xffff0000, v172
	v_lshlrev_b32_e32 v28, 16, v173
	v_and_b32_e32 v29, 0xffff0000, v173
	v_add_f32_e32 v12, v30, v31
	v_add_f32_e32 v13, v28, v29
	v_add_f32_e32 v12, v12, v13
	v_add_f32_e32 v12, v14, v12
	v_lshlrev_b32_e32 v24, 16, v174
	v_and_b32_e32 v25, 0xffff0000, v174
	v_lshlrev_b32_e32 v26, 16, v175
	v_and_b32_e32 v27, 0xffff0000, v175
	v_add_f32_e32 v10, v24, v25
	v_add_f32_e32 v11, v26, v27
	v_add_f32_e32 v10, v10, v11
	v_add_f32_e32 v34, v12, v10
	global_load_dwordx2 v[22:23], v[8:9], off
	global_load_dwordx2 v[20:21], v[8:9], off offset:512
	global_load_dwordx2 v[18:19], v[8:9], off offset:1024
	global_load_dwordx2 v[16:17], v[8:9], off offset:1536
	global_load_dwordx2 v[14:15], v[8:9], off offset:2048
	global_load_dwordx2 v[12:13], v[8:9], off offset:2560
	global_load_dwordx2 v[10:11], v[8:9], off offset:3072
	s_nop 0
	global_load_dwordx2 v[8:9], v[8:9], off offset:3584
	v_add_f32_dpp v34, v34, v34 quad_perm:[1,0,3,2] row_mask:0xf bank_mask:0xf bound_ctrl:1
	s_nop 1
	v_add_f32_dpp v34, v34, v34 quad_perm:[2,3,0,1] row_mask:0xf bank_mask:0xf bound_ctrl:1
	s_nop 1
	v_add_f32_dpp v34, v34, v34 row_half_mirror row_mask:0xf bank_mask:0xf bound_ctrl:1
	s_nop 1
	v_add_f32_dpp v34, v34, v34 row_mirror row_mask:0xf bank_mask:0xf bound_ctrl:1
	v_mov_b32_e32 v145, v34
	s_nop 1
	v_permlane16_swap_b32_e32 v34, v145
	v_add_f32_e32 v34, v34, v145
	v_mov_b32_e32 v145, v34
	s_nop 1
	v_permlane32_swap_b32_e32 v34, v145
	v_add_f32_e32 v145, v34, v145
	v_fmac_f32_e32 v71, 0xba000000, v145
	v_fmac_f32_e32 v7, 0xba000000, v145
	v_fmac_f32_e32 v70, 0xba000000, v145
	v_fmac_f32_e32 v6, 0xba000000, v145
	v_mul_f32_e32 v34, v7, v7
	v_mul_f32_e32 v146, v71, v71
	v_fmac_f32_e32 v34, v6, v6
	v_fmac_f32_e32 v146, v70, v70
	v_fmac_f32_e32 v69, 0xba000000, v145
	v_fmac_f32_e32 v67, 0xba000000, v145
	v_add_f32_e32 v34, v34, v146
	v_fmac_f32_e32 v68, 0xba000000, v145
	v_fmac_f32_e32 v66, 0xba000000, v145
	v_mul_f32_e32 v146, v67, v67
	v_mul_f32_e32 v147, v69, v69
	v_fmac_f32_e32 v146, v66, v66
	v_fmac_f32_e32 v147, v68, v68
	v_add_f32_e32 v146, v146, v147
	v_fmac_f32_e32 v63, 0xba000000, v145
	v_fmac_f32_e32 v65, 0xba000000, v145
	v_add_f32_e32 v34, v34, v146
	v_fmac_f32_e32 v62, 0xba000000, v145
	v_fmac_f32_e32 v64, 0xba000000, v145
	v_mul_f32_e32 v146, v65, v65
	v_mul_f32_e32 v147, v63, v63
	v_fmac_f32_e32 v146, v64, v64
	v_fmac_f32_e32 v147, v62, v62
	v_add_f32_e32 v146, v146, v147
	v_fmac_f32_e32 v61, 0xba000000, v145
	v_fmac_f32_e32 v59, 0xba000000, v145
	v_add_f32_e32 v34, v146, v34
	v_fmac_f32_e32 v60, 0xba000000, v145
	v_fmac_f32_e32 v58, 0xba000000, v145
	v_mul_f32_e32 v146, v59, v59
	v_mul_f32_e32 v147, v61, v61
	v_fmac_f32_e32 v146, v58, v58
	v_fmac_f32_e32 v147, v60, v60
	v_add_f32_e32 v146, v146, v147
	v_fmac_f32_e32 v55, 0xba000000, v145
	v_fmac_f32_e32 v57, 0xba000000, v145
	v_add_f32_e32 v34, v146, v34
	v_fmac_f32_e32 v54, 0xba000000, v145
	v_fmac_f32_e32 v56, 0xba000000, v145
	v_mul_f32_e32 v146, v57, v57
	v_mul_f32_e32 v147, v55, v55
	v_fmac_f32_e32 v146, v56, v56
	v_fmac_f32_e32 v147, v54, v54
	v_add_f32_e32 v146, v146, v147
	v_fmac_f32_e32 v53, 0xba000000, v145
	v_fmac_f32_e32 v33, 0xba000000, v145
	v_add_f32_e32 v34, v146, v34
	v_fmac_f32_e32 v52, 0xba000000, v145
	v_fmac_f32_e32 v32, 0xba000000, v145
	v_mul_f32_e32 v146, v33, v33
	v_mul_f32_e32 v147, v53, v53
	v_fmac_f32_e32 v146, v32, v32
	v_fmac_f32_e32 v147, v52, v52
	v_add_f32_e32 v146, v146, v147
	v_fmac_f32_e32 v29, 0xba000000, v145
	v_fmac_f32_e32 v31, 0xba000000, v145
	v_add_f32_e32 v34, v146, v34
	v_fmac_f32_e32 v28, 0xba000000, v145
	v_fmac_f32_e32 v30, 0xba000000, v145
	v_mul_f32_e32 v146, v31, v31
	v_mul_f32_e32 v147, v29, v29
	v_fmac_f32_e32 v146, v30, v30
	v_fmac_f32_e32 v147, v28, v28
	v_add_f32_e32 v146, v146, v147
	v_fmac_f32_e32 v27, 0xba000000, v145
	v_fmac_f32_e32 v25, 0xba000000, v145
	v_add_f32_e32 v34, v146, v34
	v_fmac_f32_e32 v26, 0xba000000, v145
	v_fmac_f32_e32 v24, 0xba000000, v145
	v_mul_f32_e32 v146, v25, v25
	v_mul_f32_e32 v147, v27, v27
	v_fmac_f32_e32 v146, v24, v24
	v_fmac_f32_e32 v147, v26, v26
	v_add_f32_e32 v146, v146, v147
	v_add_f32_e32 v34, v146, v34
	s_nop 1
	v_add_f32_dpp v34, v34, v34 quad_perm:[1,0,3,2] row_mask:0xf bank_mask:0xf bound_ctrl:1
	s_nop 1
	v_add_f32_dpp v34, v34, v34 quad_perm:[2,3,0,1] row_mask:0xf bank_mask:0xf bound_ctrl:1
	s_nop 1
	v_add_f32_dpp v34, v34, v34 row_half_mirror row_mask:0xf bank_mask:0xf bound_ctrl:1
	s_nop 1
	v_add_f32_dpp v34, v34, v34 row_mirror row_mask:0xf bank_mask:0xf bound_ctrl:1
	v_mov_b32_e32 v146, v34
	s_nop 1
	v_permlane16_swap_b32_e32 v34, v146
	v_add_f32_e32 v34, v34, v146
	v_mov_b32_e32 v146, v34
	s_nop 1
	v_permlane32_swap_b32_e32 v34, v146
	v_add_f32_e32 v34, v34, v146
	v_fmamk_f32 v34, v34, 0x3a000000, v135
	v_cmp_gt_f32_e32 vcc, s44, v34
	v_mul_f32_e32 v146, 0x4f800000, v34
	s_nop 0
	v_cndmask_b32_e32 v34, v34, v146, vcc
	v_sqrt_f32_e32 v146, v34
	s_nop 0
	v_add_u32_e32 v147, -1, v146
	v_fma_f32 v148, -v147, v146, v34
	v_cmp_ge_f32_e64 s[12:13], 0, v148
	v_add_u32_e32 v148, 1, v146
	s_nop 0
	v_cndmask_b32_e64 v147, v146, v147, s[12:13]
	v_fma_f32 v146, -v148, v146, v34
	v_cmp_lt_f32_e64 s[12:13], 0, v146
	s_nop 1
	v_cndmask_b32_e64 v146, v147, v148, s[12:13]
	v_mul_f32_e32 v147, 0x37800000, v146
	v_cndmask_b32_e32 v146, v146, v147, vcc
	v_cmp_class_f32_e32 vcc, v34, v136
	s_nop 1
	v_cndmask_b32_e32 v34, v146, v34, vcc
	v_div_scale_f32 v146, s[12:13], v34, v34, 1.0
	v_rcp_f32_e32 v147, v146
	s_nop 0
	v_fma_f32 v148, -v146, v147, 1.0
	v_fmac_f32_e32 v147, v148, v147
	v_div_scale_f32 v148, vcc, 1.0, v34, 1.0
	v_mul_f32_e32 v149, v148, v147
	v_fma_f32 v150, -v146, v149, v148
	v_fmac_f32_e32 v149, v150, v147
	v_fma_f32 v146, -v146, v149, v148
	v_div_fmas_f32 v146, v146, v147, v149
	v_div_fixup_f32 v34, v146, v34, 1.0
	ds_read_b128 v[146:149], v144
	ds_read_b128 v[150:153], v144 offset:8192
	v_pk_mul_f32 v[6:7], v[6:7], v[34:35] op_sel_hi:[1,0]
	v_pk_mul_f32 v[70:71], v[70:71], v[34:35] op_sel_hi:[1,0]
	v_pk_mul_f32 v[66:67], v[66:67], v[34:35] op_sel_hi:[1,0]
	v_pk_mul_f32 v[68:69], v[68:69], v[34:35] op_sel_hi:[1,0]
	s_waitcnt lgkmcnt(0)
	v_pk_fma_f32 v[6:7], v[146:147], v[6:7], v[150:151]
	v_cvt_pk_fp8_f32 v146, v6, v7
	v_pk_fma_f32 v[70:71], v[148:149], v[70:71], v[152:153]
	v_lshl_add_u64 v[6:7], s[92:93], 0, v[2:3]
	v_pk_mul_f32 v[64:65], v[64:65], v[34:35] op_sel_hi:[1,0]
	v_cvt_pk_fp8_f32 v146, v70, v71 op_sel:[0,0,1]
	v_pk_mul_f32 v[62:63], v[62:63], v[34:35] op_sel_hi:[1,0]
	v_pk_mul_f32 v[58:59], v[58:59], v[34:35] op_sel_hi:[1,0]
	global_store_dword v[6:7], v146, off offset:-2048
	ds_read_b128 v[146:149], v144 offset:1024
	ds_read_b128 v[150:153], v144 offset:9216
	v_pk_mul_f32 v[60:61], v[60:61], v[34:35] op_sel_hi:[1,0]
	v_pk_mul_f32 v[56:57], v[56:57], v[34:35] op_sel_hi:[1,0]
	v_pk_mul_f32 v[54:55], v[54:55], v[34:35] op_sel_hi:[1,0]
	v_pk_mul_f32 v[32:33], v[32:33], v[34:35] op_sel_hi:[1,0]
	s_waitcnt lgkmcnt(0)
	v_pk_fma_f32 v[66:67], v[146:147], v[66:67], v[150:151]
	v_pk_fma_f32 v[68:69], v[148:149], v[68:69], v[152:153]
	v_cvt_pk_fp8_f32 v70, v66, v67
	v_pk_mul_f32 v[52:53], v[52:53], v[34:35] op_sel_hi:[1,0]
	v_pk_mul_f32 v[30:31], v[30:31], v[34:35] op_sel_hi:[1,0]
	v_pk_mul_f32 v[28:29], v[28:29], v[34:35] op_sel_hi:[1,0]
	v_cvt_pk_fp8_f32 v70, v68, v69 op_sel:[0,0,1]
	v_pk_mul_f32 v[24:25], v[24:25], v[34:35] op_sel_hi:[1,0]
	v_pk_mul_f32 v[26:27], v[26:27], v[34:35] op_sel_hi:[1,0]
	global_store_dword v[6:7], v70, off offset:-1792
	ds_read_b128 v[66:69], v144 offset:2048
	ds_read_b128 v[146:149], v144 offset:10240
	s_waitcnt lgkmcnt(0)
	v_pk_fma_f32 v[64:65], v[64:65], v[66:67], v[146:147]
	v_cvt_pk_fp8_f32 v66, v64, v65
	v_pk_fma_f32 v[62:63], v[62:63], v[68:69], v[148:149]
	s_nop 0
	v_cvt_pk_fp8_f32 v66, v62, v63 op_sel:[0,0,1]
	global_store_dword v[6:7], v66, off offset:-1536
	ds_read_b128 v[62:65], v144 offset:3072
	ds_read_b128 v[66:69], v144 offset:11264
	s_waitcnt lgkmcnt(0)
	v_pk_fma_f32 v[58:59], v[58:59], v[62:63], v[66:67]
	v_cvt_pk_fp8_f32 v62, v58, v59
	v_pk_fma_f32 v[60:61], v[60:61], v[64:65], v[68:69]
	s_nop 0
	v_cvt_pk_fp8_f32 v62, v60, v61 op_sel:[0,0,1]
	global_store_dword v[6:7], v62, off offset:-1280
	ds_read_b128 v[58:61], v144 offset:4096
	ds_read_b128 v[62:65], v144 offset:12288
	s_waitcnt lgkmcnt(0)
	v_pk_fma_f32 v[56:57], v[56:57], v[58:59], v[62:63]
	v_cvt_pk_fp8_f32 v58, v56, v57
	v_pk_fma_f32 v[54:55], v[54:55], v[60:61], v[64:65]
	s_nop 0
	v_cvt_pk_fp8_f32 v58, v54, v55 op_sel:[0,0,1]
	global_store_dword v[6:7], v58, off offset:-1024
	ds_read_b128 v[54:57], v144 offset:5120
	ds_read_b128 v[58:61], v144 offset:13312
	s_waitcnt lgkmcnt(0)
	v_pk_fma_f32 v[32:33], v[32:33], v[54:55], v[58:59]
	v_cvt_pk_fp8_f32 v54, v32, v33
	v_pk_fma_f32 v[52:53], v[52:53], v[56:57], v[60:61]
	v_cvt_pk_fp8_f32 v54, v52, v53 op_sel:[0,0,1]
	global_store_dword v[6:7], v54, off offset:-768
	ds_read_b128 v[52:55], v144 offset:6144
	ds_read_b128 v[56:59], v144 offset:14336
	s_waitcnt lgkmcnt(0)
	v_pk_fma_f32 v[30:31], v[30:31], v[52:53], v[56:57]
	s_nop 0
	v_cvt_pk_fp8_f32 v32, v30, v31
	v_pk_fma_f32 v[28:29], v[28:29], v[54:55], v[58:59]
	s_nop 0
	v_cvt_pk_fp8_f32 v32, v28, v29 op_sel:[0,0,1]
	global_store_dword v[6:7], v32, off offset:-512
	ds_read_b128 v[28:31], v144 offset:7168
	ds_read_b128 v[52:55], v144 offset:15360
	s_waitcnt lgkmcnt(0)
	v_pk_fma_f32 v[24:25], v[24:25], v[28:29], v[52:53]
	v_cvt_pk_fp8_f32 v28, v24, v25
	v_pk_fma_f32 v[26:27], v[26:27], v[30:31], v[54:55]
	s_nop 0
	v_cvt_pk_fp8_f32 v28, v26, v27 op_sel:[0,0,1]
	global_store_dword v[6:7], v28, off offset:-256
	s_and_saveexec_b64 s[12:13], s[8:9]
	s_cbranch_execz .LBB0_708
	s_add_i32 s70, s37, -8
	s_add_u32 s68, s92, s14
	v_mul_f32_e32 v24, 0x3a000000, v145
	s_addc_u32 s69, s93, s15
	v_mov_b32_e32 v25, v34
	v_mov_b32_e32 v26, s70
	ds_write_b64 v26, v[24:25]
	global_store_dwordx2 v137, v[24:25], s[68:69]
.LBB0_708:
	s_or_b64 exec, exec, s[12:13]
	s_waitcnt vmcnt(15)
	v_lshlrev_b32_e32 v58, 16, v22
	v_and_b32_e32 v59, 0xffff0000, v22
	v_lshlrev_b32_e32 v56, 16, v23
	v_and_b32_e32 v57, 0xffff0000, v23
	v_add_f32_e32 v22, v58, v59
	v_add_f32_e32 v23, v56, v57
	s_waitcnt vmcnt(14)
	v_lshlrev_b32_e32 v52, 16, v20
	v_and_b32_e32 v53, 0xffff0000, v20
	v_lshlrev_b32_e32 v54, 16, v21
	v_and_b32_e32 v55, 0xffff0000, v21
	v_add_f32_e32 v22, v22, v23
	v_add_f32_e32 v20, v52, v53
	v_add_f32_e32 v21, v54, v55
	s_waitcnt vmcnt(13)
	v_lshlrev_b32_e32 v32, 16, v18
	v_and_b32_e32 v33, 0xffff0000, v18
	v_lshlrev_b32_e32 v30, 16, v19
	v_and_b32_e32 v31, 0xffff0000, v19
	v_add_f32_e32 v22, 0, v22
	v_add_f32_e32 v20, v20, v21
	v_add_f32_e32 v18, v32, v33
	v_add_f32_e32 v19, v30, v31
	v_add_f32_e32 v20, v22, v20
	v_add_f32_e32 v18, v18, v19
	s_waitcnt vmcnt(12)
	v_lshlrev_b32_e32 v26, 16, v16
	v_and_b32_e32 v27, 0xffff0000, v16
	v_lshlrev_b32_e32 v28, 16, v17
	v_and_b32_e32 v29, 0xffff0000, v17
	v_add_f32_e32 v18, v20, v18
	v_add_f32_e32 v16, v26, v27
	v_add_f32_e32 v17, v28, v29
	s_waitcnt vmcnt(11)
	v_lshlrev_b32_e32 v22, 16, v14
	v_and_b32_e32 v23, 0xffff0000, v14
	v_lshlrev_b32_e32 v20, 16, v15
	v_and_b32_e32 v21, 0xffff0000, v15
	v_add_f32_e32 v16, v16, v17
	v_add_f32_e32 v14, v22, v23
	v_add_f32_e32 v15, v20, v21
	v_add_f32_e32 v16, v18, v16
	v_add_f32_e32 v14, v14, v15
	v_add_f32_e32 v14, v16, v14
	s_waitcnt vmcnt(10)
	v_lshlrev_b32_e32 v16, 16, v12
	v_and_b32_e32 v17, 0xffff0000, v12
	v_lshlrev_b32_e32 v18, 16, v13
	v_and_b32_e32 v19, 0xffff0000, v13
	v_add_f32_e32 v12, v16, v17
	v_add_f32_e32 v13, v18, v19
	v_add_f32_e32 v12, v12, v13
	v_add_f32_e32 v24, v14, v12
	s_waitcnt vmcnt(9)
	v_lshlrev_b32_e32 v14, 16, v10
	v_and_b32_e32 v15, 0xffff0000, v10
	v_lshlrev_b32_e32 v12, 16, v11
	v_and_b32_e32 v13, 0xffff0000, v11
	v_add_f32_e32 v10, v14, v15
	v_add_f32_e32 v11, v12, v13
	v_add_f32_e32 v10, v10, v11
	v_add_f32_e32 v24, v24, v10
	s_waitcnt vmcnt(8)
	v_lshlrev_b32_e32 v10, 16, v8
	v_and_b32_e32 v11, 0xffff0000, v8
	v_lshlrev_b32_e32 v8, 16, v9
	v_and_b32_e32 v9, 0xffff0000, v9
	v_add_f32_e32 v25, v10, v11
	v_add_f32_e32 v34, v8, v9
	v_add_f32_e32 v25, v25, v34
	v_add_f32_e32 v24, v24, v25
	s_nop 1
	v_add_f32_dpp v24, v24, v24 quad_perm:[1,0,3,2] row_mask:0xf bank_mask:0xf bound_ctrl:1
	s_nop 1
	v_add_f32_dpp v24, v24, v24 quad_perm:[2,3,0,1] row_mask:0xf bank_mask:0xf bound_ctrl:1
	s_nop 1
	v_add_f32_dpp v24, v24, v24 row_half_mirror row_mask:0xf bank_mask:0xf bound_ctrl:1
	s_nop 1
	v_add_f32_dpp v24, v24, v24 row_mirror row_mask:0xf bank_mask:0xf bound_ctrl:1
	v_mov_b32_e32 v25, v24
	s_nop 1
	v_permlane16_swap_b32_e32 v24, v25
	v_add_f32_e32 v24, v24, v25
	v_mov_b32_e32 v25, v24
	s_nop 1
	v_permlane32_swap_b32_e32 v24, v25
	v_add_f32_e32 v25, v24, v25
	v_fmac_f32_e32 v57, 0xba000000, v25
	v_fmac_f32_e32 v59, 0xba000000, v25
	v_fmac_f32_e32 v56, 0xba000000, v25
	v_fmac_f32_e32 v58, 0xba000000, v25
	v_mul_f32_e32 v24, v59, v59
	v_mul_f32_e32 v34, v57, v57
	v_fmac_f32_e32 v24, v58, v58
	v_fmac_f32_e32 v34, v56, v56
	v_fmac_f32_e32 v55, 0xba000000, v25
	v_fmac_f32_e32 v53, 0xba000000, v25
	v_add_f32_e32 v24, v24, v34
	v_fmac_f32_e32 v54, 0xba000000, v25
	v_fmac_f32_e32 v52, 0xba000000, v25
	v_mul_f32_e32 v34, v53, v53
	v_mul_f32_e32 v60, v55, v55
	v_fmac_f32_e32 v34, v52, v52
	v_fmac_f32_e32 v60, v54, v54
	v_add_f32_e32 v34, v34, v60
	v_fmac_f32_e32 v31, 0xba000000, v25
	v_fmac_f32_e32 v33, 0xba000000, v25
	v_add_f32_e32 v24, v24, v34
	v_fmac_f32_e32 v30, 0xba000000, v25
	v_fmac_f32_e32 v32, 0xba000000, v25
	v_mul_f32_e32 v34, v33, v33
	v_mul_f32_e32 v60, v31, v31
	v_fmac_f32_e32 v34, v32, v32
	v_fmac_f32_e32 v60, v30, v30
	v_add_f32_e32 v34, v34, v60
	v_fmac_f32_e32 v29, 0xba000000, v25
	v_fmac_f32_e32 v27, 0xba000000, v25
	v_add_f32_e32 v24, v34, v24
	v_fmac_f32_e32 v28, 0xba000000, v25
	v_fmac_f32_e32 v26, 0xba000000, v25
	v_mul_f32_e32 v34, v27, v27
	v_mul_f32_e32 v60, v29, v29
	v_fmac_f32_e32 v34, v26, v26
	v_fmac_f32_e32 v60, v28, v28
	v_add_f32_e32 v34, v34, v60
	v_fmac_f32_e32 v21, 0xba000000, v25
	v_fmac_f32_e32 v23, 0xba000000, v25
	v_add_f32_e32 v24, v34, v24
	v_fmac_f32_e32 v20, 0xba000000, v25
	v_fmac_f32_e32 v22, 0xba000000, v25
	v_mul_f32_e32 v34, v23, v23
	v_mul_f32_e32 v60, v21, v21
	v_fmac_f32_e32 v34, v22, v22
	v_fmac_f32_e32 v60, v20, v20
	v_add_f32_e32 v34, v34, v60
	v_fmac_f32_e32 v19, 0xba000000, v25
	v_fmac_f32_e32 v17, 0xba000000, v25
	v_add_f32_e32 v24, v34, v24
	v_fmac_f32_e32 v18, 0xba000000, v25
	v_fmac_f32_e32 v16, 0xba000000, v25
	v_mul_f32_e32 v34, v17, v17
	v_mul_f32_e32 v60, v19, v19
	v_fmac_f32_e32 v34, v16, v16
	v_fmac_f32_e32 v60, v18, v18
	v_add_f32_e32 v34, v34, v60
	v_fmac_f32_e32 v13, 0xba000000, v25
	v_fmac_f32_e32 v15, 0xba000000, v25
	v_add_f32_e32 v24, v34, v24
	v_fmac_f32_e32 v12, 0xba000000, v25
	v_fmac_f32_e32 v14, 0xba000000, v25
	v_mul_f32_e32 v34, v15, v15
	v_mul_f32_e32 v60, v13, v13
	v_fmac_f32_e32 v34, v14, v14
	v_fmac_f32_e32 v60, v12, v12
	v_add_f32_e32 v34, v34, v60
	v_fmac_f32_e32 v9, 0xba000000, v25
	v_fmac_f32_e32 v11, 0xba000000, v25
	v_add_f32_e32 v24, v34, v24
	v_fmac_f32_e32 v8, 0xba000000, v25
	v_fmac_f32_e32 v10, 0xba000000, v25
	v_mul_f32_e32 v34, v11, v11
	v_mul_f32_e32 v60, v9, v9
	v_fmac_f32_e32 v34, v10, v10
	v_fmac_f32_e32 v60, v8, v8
	v_add_f32_e32 v34, v34, v60
	v_add_f32_e32 v24, v34, v24
	s_nop 1
	v_add_f32_dpp v24, v24, v24 quad_perm:[1,0,3,2] row_mask:0xf bank_mask:0xf bound_ctrl:1
	s_nop 1
	v_add_f32_dpp v24, v24, v24 quad_perm:[2,3,0,1] row_mask:0xf bank_mask:0xf bound_ctrl:1
	s_nop 1
	v_add_f32_dpp v24, v24, v24 row_half_mirror row_mask:0xf bank_mask:0xf bound_ctrl:1
	s_nop 1
	v_add_f32_dpp v24, v24, v24 row_mirror row_mask:0xf bank_mask:0xf bound_ctrl:1
	v_mov_b32_e32 v34, v24
	s_nop 1
	v_permlane16_swap_b32_e32 v24, v34
	v_add_f32_e32 v24, v24, v34
	v_mov_b32_e32 v34, v24
	s_nop 1
	v_permlane32_swap_b32_e32 v24, v34
	v_add_f32_e32 v24, v24, v34
	v_fmamk_f32 v24, v24, 0x3a000000, v135
	v_cmp_gt_f32_e32 vcc, s44, v24
	v_mul_f32_e32 v34, 0x4f800000, v24
	s_nop 0
	v_cndmask_b32_e32 v24, v24, v34, vcc
	v_sqrt_f32_e32 v34, v24
	s_nop 0
	v_add_u32_e32 v60, -1, v34
	v_fma_f32 v61, -v60, v34, v24
	v_cmp_ge_f32_e64 s[12:13], 0, v61
	v_add_u32_e32 v61, 1, v34
	s_nop 0
	v_cndmask_b32_e64 v60, v34, v60, s[12:13]
	v_fma_f32 v34, -v61, v34, v24
	v_cmp_lt_f32_e64 s[12:13], 0, v34
	s_nop 1
	v_cndmask_b32_e64 v34, v60, v61, s[12:13]
	v_mul_f32_e32 v60, 0x37800000, v34
	v_cndmask_b32_e32 v34, v34, v60, vcc
	v_cmp_class_f32_e32 vcc, v24, v136
	s_nop 1
	v_cndmask_b32_e32 v24, v34, v24, vcc
	v_div_scale_f32 v34, s[12:13], v24, v24, 1.0
	v_rcp_f32_e32 v60, v34
	s_nop 0
	v_fma_f32 v61, -v34, v60, 1.0
	v_fmac_f32_e32 v60, v61, v60
	v_div_scale_f32 v61, vcc, 1.0, v24, 1.0
	v_mul_f32_e32 v62, v61, v60
	v_fma_f32 v63, -v34, v62, v61
	v_fmac_f32_e32 v62, v63, v60
	v_fma_f32 v34, -v34, v62, v61
	v_div_fmas_f32 v34, v34, v60, v62
	ds_read_b128 v[60:63], v144
	ds_read_b128 v[64:67], v144 offset:8192
	v_div_fixup_f32 v24, v34, v24, 1.0
	v_pk_mul_f32 v[58:59], v[58:59], v[24:25] op_sel_hi:[1,0]
	v_pk_mul_f32 v[56:57], v[56:57], v[24:25] op_sel_hi:[1,0]
	s_waitcnt lgkmcnt(0)
	v_pk_fma_f32 v[58:59], v[60:61], v[58:59], v[64:65]
	v_pk_fma_f32 v[56:57], v[62:63], v[56:57], v[66:67]
	v_cvt_pk_fp8_f32 v34, v58, v59
	v_pk_mul_f32 v[52:53], v[52:53], v[24:25] op_sel_hi:[1,0]
	v_pk_mul_f32 v[54:55], v[54:55], v[24:25] op_sel_hi:[1,0]
	v_pk_mul_f32 v[32:33], v[32:33], v[24:25] op_sel_hi:[1,0]
	v_cvt_pk_fp8_f32 v34, v56, v57 op_sel:[0,0,1]
	v_pk_mul_f32 v[30:31], v[30:31], v[24:25] op_sel_hi:[1,0]
	v_pk_mul_f32 v[26:27], v[26:27], v[24:25] op_sel_hi:[1,0]
	v_pk_mul_f32 v[28:29], v[28:29], v[24:25] op_sel_hi:[1,0]
	global_store_dword v[6:7], v34, off
	ds_read_b128 v[56:59], v144 offset:1024
	ds_read_b128 v[60:63], v144 offset:9216
	v_pk_mul_f32 v[22:23], v[22:23], v[24:25] op_sel_hi:[1,0]
	v_pk_mul_f32 v[20:21], v[20:21], v[24:25] op_sel_hi:[1,0]
	v_pk_mul_f32 v[16:17], v[16:17], v[24:25] op_sel_hi:[1,0]
	s_waitcnt lgkmcnt(0)
	v_pk_fma_f32 v[52:53], v[56:57], v[52:53], v[60:61]
	v_pk_fma_f32 v[54:55], v[58:59], v[54:55], v[62:63]
	v_cvt_pk_fp8_f32 v34, v52, v53
	v_pk_mul_f32 v[18:19], v[18:19], v[24:25] op_sel_hi:[1,0]
	v_pk_mul_f32 v[14:15], v[14:15], v[24:25] op_sel_hi:[1,0]
	v_pk_mul_f32 v[12:13], v[12:13], v[24:25] op_sel_hi:[1,0]
	v_cvt_pk_fp8_f32 v34, v54, v55 op_sel:[0,0,1]
	v_pk_mul_f32 v[10:11], v[10:11], v[24:25] op_sel_hi:[1,0]
	v_pk_mul_f32 v[8:9], v[8:9], v[24:25] op_sel_hi:[1,0]
	global_store_dword v[6:7], v34, off offset:256
	ds_read_b128 v[52:55], v144 offset:2048
	ds_read_b128 v[56:59], v144 offset:10240
	s_waitcnt lgkmcnt(0)
	v_pk_fma_f32 v[32:33], v[32:33], v[52:53], v[56:57]
	s_nop 0
	v_cvt_pk_fp8_f32 v34, v32, v33
	v_pk_fma_f32 v[30:31], v[30:31], v[54:55], v[58:59]
	s_nop 0
	v_cvt_pk_fp8_f32 v34, v30, v31 op_sel:[0,0,1]
	global_store_dword v[6:7], v34, off offset:512
	ds_read_b128 v[30:33], v144 offset:3072
	ds_read_b128 v[52:55], v144 offset:11264
	s_waitcnt lgkmcnt(0)
	v_pk_fma_f32 v[26:27], v[26:27], v[30:31], v[52:53]
	v_cvt_pk_fp8_f32 v30, v26, v27
	v_pk_fma_f32 v[28:29], v[28:29], v[32:33], v[54:55]
	s_nop 0
	v_cvt_pk_fp8_f32 v30, v28, v29 op_sel:[0,0,1]
	global_store_dword v[6:7], v30, off offset:768
	ds_read_b128 v[26:29], v144 offset:4096
	ds_read_b128 v[30:33], v144 offset:12288
	s_waitcnt lgkmcnt(0)
	v_pk_fma_f32 v[22:23], v[22:23], v[26:27], v[30:31]
	v_cvt_pk_fp8_f32 v26, v22, v23
	v_pk_fma_f32 v[20:21], v[20:21], v[28:29], v[32:33]
	s_nop 0
	v_cvt_pk_fp8_f32 v26, v20, v21 op_sel:[0,0,1]
	global_store_dword v[6:7], v26, off offset:1024
	ds_read_b128 v[20:23], v144 offset:5120
	ds_read_b128 v[26:29], v144 offset:13312
	s_waitcnt lgkmcnt(0)
	v_pk_fma_f32 v[16:17], v[16:17], v[20:21], v[26:27]
	v_cvt_pk_fp8_f32 v20, v16, v17
	v_pk_fma_f32 v[18:19], v[18:19], v[22:23], v[28:29]
	s_nop 0
	v_cvt_pk_fp8_f32 v20, v18, v19 op_sel:[0,0,1]
	global_store_dword v[6:7], v20, off offset:1280
	ds_read_b128 v[16:19], v144 offset:6144
	ds_read_b128 v[20:23], v144 offset:14336
	s_waitcnt lgkmcnt(0)
	v_pk_fma_f32 v[14:15], v[14:15], v[16:17], v[20:21]
	v_cvt_pk_fp8_f32 v16, v14, v15
	v_pk_fma_f32 v[12:13], v[12:13], v[18:19], v[22:23]
	s_nop 0
	v_cvt_pk_fp8_f32 v16, v12, v13 op_sel:[0,0,1]
	global_store_dword v[6:7], v16, off offset:1536
	ds_read_b128 v[12:15], v144 offset:7168
	ds_read_b128 v[16:19], v144 offset:15360
	s_waitcnt lgkmcnt(0)
	v_pk_fma_f32 v[10:11], v[10:11], v[12:13], v[16:17]
	v_cvt_pk_fp8_f32 v12, v10, v11
	v_pk_fma_f32 v[8:9], v[8:9], v[14:15], v[18:19]
	s_nop 0
	v_cvt_pk_fp8_f32 v12, v8, v9 op_sel:[0,0,1]
	global_store_dword v[6:7], v12, off offset:1792
	s_and_saveexec_b64 s[12:13], s[8:9]
	s_cbranch_execz .LBB0_705
	s_add_u32 s68, s92, s14
	v_mul_f32_e32 v6, 0x3a000000, v25
	s_addc_u32 s69, s93, s15
	v_mov_b32_e32 v7, v24
	v_mov_b32_e32 v8, s37
	ds_write_b64 v8, v[6:7]
	global_store_dwordx2 v137, v[6:7], s[68:69] offset:8
	s_branch .LBB0_705

.LBB0_926:
	s_add_i32 s8, s30, 0x25100
	v_mov_b32_e32 v2, s8
	s_lshl_b32 s8, s31, 11
	s_and_b32 s8, s8, 0x800
	s_nop 11
	v_add_u32_e32 v11, s8, v228
	ds_read_b32 v10, v2
	ds_read_b128 v[6:9], v11 offset:16
	ds_read_b128 v[14:17], v11 offset:512
	ds_read_b128 v[2:5], v11
	ds_read_b128 v[18:21], v11 offset:528
	s_and_b64 vcc, exec, s[6:7]
	s_waitcnt lgkmcnt(0)
	v_pk_fma_f32 v[26:27], v[190:191], s[20:21], v[6:7] op_sel_hi:[1,0,1]
	v_pk_add_f32 v[12:13], v[16:17], 1.0 op_sel_hi:[1,0]
	v_pk_fma_f32 v[22:23], v[194:195], s[20:21], v[2:3] op_sel_hi:[1,0,1]
	v_pk_add_f32 v[16:17], v[20:21], 1.0 op_sel_hi:[1,0]
	v_pk_fma_f32 v[20:21], v[196:197], s[20:21], v[4:5] op_sel_hi:[1,0,1]
	v_min_f32_e32 v22, 0x40e00000, v22
	v_min_f32_e32 v20, 0x40e00000, v20
	v_min_f32_e32 v21, 0x40e00000, v21
	v_min_f32_e32 v26, 0x40e00000, v26
	v_min_f32_e32 v23, 0x40e00000, v23
	v_min_f32_e32 v27, 0x40e00000, v27
	v_pk_mul_f32 v[36:37], v[20:21], s[22:23] op_sel_hi:[1,0]
	v_pk_mul_f32 v[38:39], v[22:23], s[22:23] op_sel_hi:[1,0]
	v_pk_mul_f32 v[42:43], v[26:27], s[22:23] op_sel_hi:[1,0]
	v_exp_f32_e32 v36, v36
	v_exp_f32_e32 v37, v37
	v_exp_f32_e32 v38, v38
	v_exp_f32_e32 v42, v42
	v_exp_f32_e32 v39, v39
	v_exp_f32_e32 v43, v43
	v_pk_add_f32 v[36:37], v[36:37], 1.0 op_sel_hi:[1,0]
	v_pk_fma_f32 v[24:25], v[192:193], s[20:21], v[8:9] op_sel_hi:[1,0,1]
	v_pk_add_f32 v[38:39], v[38:39], 1.0 op_sel_hi:[1,0]
	v_pk_add_f32 v[42:43], v[42:43], 1.0 op_sel_hi:[1,0]
	v_rcp_f32_e32 v36, v36
	v_rcp_f32_e32 v37, v37
	v_min_f32_e32 v24, 0x40e00000, v24
	v_min_f32_e32 v25, 0x40e00000, v25
	v_rcp_f32_e32 v38, v38
	v_rcp_f32_e32 v42, v42
	v_rcp_f32_e32 v39, v39
	v_rcp_f32_e32 v43, v43
	v_pk_mul_f32 v[40:41], v[24:25], s[22:23] op_sel_hi:[1,0]
	v_pk_add_f32 v[14:15], v[14:15], 1.0 op_sel_hi:[1,0]
	v_pk_add_f32 v[18:19], v[18:19], 1.0 op_sel_hi:[1,0]
	v_pk_fma_f32 v[28:29], v[188:189], s[20:21], v[12:13] op_sel_hi:[1,0,1]
	v_exp_f32_e32 v40, v40
	v_exp_f32_e32 v41, v41
	v_pk_fma_f32 v[30:31], v[186:187], s[20:21], v[14:15] op_sel_hi:[1,0,1]
	v_pk_fma_f32 v[34:35], v[182:183], s[20:21], v[18:19] op_sel_hi:[1,0,1]
	v_med3_f32 v28, v28, s56, v235
	v_med3_f32 v29, v29, s56, v235
	v_pk_mul_f32 v[20:21], v[20:21], v[36:37]
	v_med3_f32 v30, v30, s56, v235
	v_med3_f32 v34, v34, s56, v235
	v_med3_f32 v31, v31, s56, v235
	v_med3_f32 v35, v35, s56, v235
	v_pk_mul_f32 v[22:23], v[22:23], v[38:39]
	v_pk_mul_f32 v[28:29], v[28:29], v[20:21]
	v_pk_mul_f32 v[20:21], v[26:27], v[42:43]
	v_pk_mul_f32 v[22:23], v[30:31], v[22:23]
	v_pk_mul_f32 v[26:27], v[34:35], v[20:21]
	v_pk_add_f32 v[40:41], v[40:41], 1.0 op_sel_hi:[1,0]
	v_cvt_pk_fp8_f32 v20, v22, v23
	v_rcp_f32_e32 v40, v40
	v_rcp_f32_e32 v41, v41
	v_pk_fma_f32 v[32:33], v[184:185], s[20:21], v[16:17] op_sel_hi:[1,0,1]
	v_cvt_pk_fp8_f32 v20, v28, v29 op_sel:[0,0,1]
	v_pk_fma_f32 v[28:29], v[178:179], s[20:21], v[6:7] op_sel_hi:[1,0,1]
	v_med3_f32 v32, v32, s56, v235
	v_med3_f32 v33, v33, s56, v235
	v_pk_mul_f32 v[22:23], v[24:25], v[40:41]
	v_min_f32_e32 v28, 0x40e00000, v28
	v_min_f32_e32 v29, 0x40e00000, v29
	v_pk_mul_f32 v[22:23], v[32:33], v[22:23]
	v_pk_mul_f32 v[32:33], v[28:29], s[22:23] op_sel_hi:[1,0]
	v_exp_f32_e32 v32, v32
	v_exp_f32_e32 v33, v33
	v_cvt_pk_fp8_f32 v21, v26, v27
	v_pk_fma_f32 v[26:27], v[180:181], s[20:21], v[8:9] op_sel_hi:[1,0,1]
	v_pk_fma_f32 v[24:25], v[174:175], s[20:21], v[18:19] op_sel_hi:[1,0,1]
	v_min_f32_e32 v26, 0x40e00000, v26
	v_min_f32_e32 v27, 0x40e00000, v27
	v_pk_mul_f32 v[30:31], v[26:27], s[22:23] op_sel_hi:[1,0]
	v_pk_add_f32 v[32:33], v[32:33], 1.0 op_sel_hi:[1,0]
	v_exp_f32_e32 v30, v30
	v_exp_f32_e32 v31, v31
	v_rcp_f32_e32 v32, v32
	v_rcp_f32_e32 v33, v33
	v_cvt_pk_fp8_f32 v21, v22, v23 op_sel:[0,0,1]
	v_pk_fma_f32 v[22:23], v[176:177], s[20:21], v[16:17] op_sel_hi:[1,0,1]
	v_pk_add_f32 v[30:31], v[30:31], 1.0 op_sel_hi:[1,0]
	v_med3_f32 v34, v22, s56, v235
	v_rcp_f32_e32 v30, v30
	v_rcp_f32_e32 v31, v31
	v_med3_f32 v35, v23, s56, v235
	v_pk_mul_f32 v[22:23], v[28:29], v[32:33]
	v_pk_fma_f32 v[32:33], v[170:171], s[20:21], v[2:3] op_sel_hi:[1,0,1]
	v_pk_mul_f32 v[26:27], v[26:27], v[30:31]
	v_min_f32_e32 v32, 0x40e00000, v32
	v_min_f32_e32 v33, 0x40e00000, v33
	v_pk_mul_f32 v[36:37], v[32:33], s[22:23] op_sel_hi:[1,0]
	v_pk_fma_f32 v[30:31], v[172:173], s[20:21], v[4:5] op_sel_hi:[1,0,1]
	v_exp_f32_e32 v36, v36
	v_exp_f32_e32 v37, v37
	v_min_f32_e32 v30, 0x40e00000, v30
	v_min_f32_e32 v31, 0x40e00000, v31
	v_pk_mul_f32 v[38:39], v[30:31], s[22:23] op_sel_hi:[1,0]
	v_pk_add_f32 v[36:37], v[36:37], 1.0 op_sel_hi:[1,0]
	v_exp_f32_e32 v38, v38
	v_exp_f32_e32 v39, v39
	v_rcp_f32_e32 v36, v36
	v_rcp_f32_e32 v37, v37
	v_pk_fma_f32 v[28:29], v[166:167], s[20:21], v[14:15] op_sel_hi:[1,0,1]
	v_pk_add_f32 v[38:39], v[38:39], 1.0 op_sel_hi:[1,0]
	v_med3_f32 v24, v24, s56, v235
	v_med3_f32 v25, v25, s56, v235
	v_med3_f32 v28, v28, s56, v235
	v_med3_f32 v29, v29, s56, v235
	v_rcp_f32_e32 v38, v38
	v_rcp_f32_e32 v39, v39
	v_pk_mul_f32 v[32:33], v[32:33], v[36:37]
	v_pk_mul_f32 v[24:25], v[24:25], v[22:23]
	v_pk_mul_f32 v[28:29], v[28:29], v[32:33]
	v_cvt_pk_fp8_f32 v22, v28, v29
	v_cvt_pk_fp8_f32 v23, v24, v25
	v_pk_fma_f32 v[24:25], v[168:169], s[20:21], v[12:13] op_sel_hi:[1,0,1]
	v_pk_mul_f32 v[28:29], v[30:31], v[38:39]
	v_med3_f32 v24, v24, s56, v235
	v_med3_f32 v25, v25, s56, v235
	v_add_u32_e32 v11, s60, v10
	v_pk_mul_f32 v[24:25], v[24:25], v[28:29]
	v_lshl_add_u32 v44, v11, 8, v213
	v_cvt_pk_fp8_f32 v22, v24, v25 op_sel:[0,0,1]
	v_pk_mul_f32 v[24:25], v[34:35], v[26:27]
	v_lshl_or_b32 v10, s34, 7, v231
	v_cvt_pk_fp8_f32 v23, v24, v25 op_sel:[0,0,1]
	v_or_b32_e32 v24, v44, v229
	v_ashrrev_i32_e32 v25, 31, v24
	v_lshlrev_b64 v[24:25], 11, v[24:25]
	v_ashrrev_i32_e32 v11, 31, v10
	v_lshl_add_u64 v[24:25], s[14:15], 0, v[24:25]
	v_lshl_add_u64 v[24:25], v[24:25], 0, v[10:11]
	v_permlane16_swap_b32_e32 v20, v22
	v_permlane16_swap_b32_e32 v21, v23
	v_lshl_add_u64 v[24:25], v[24:25], 0, v[204:205]
	global_store_dwordx4 v[24:25], v[20:23], off
	v_pk_fma_f32 v[26:27], v[158:159], s[20:21], v[6:7] op_sel_hi:[1,0,1]
	v_pk_fma_f32 v[24:25], v[160:161], s[20:21], v[8:9] op_sel_hi:[1,0,1]
	v_pk_fma_f32 v[20:21], v[164:165], s[20:21], v[4:5] op_sel_hi:[1,0,1]
	v_pk_fma_f32 v[22:23], v[162:163], s[20:21], v[2:3] op_sel_hi:[1,0,1]
	v_min_f32_e32 v20, 0x40e00000, v20
	v_min_f32_e32 v21, 0x40e00000, v21
	v_min_f32_e32 v22, 0x40e00000, v22
	v_min_f32_e32 v26, 0x40e00000, v26
	v_min_f32_e32 v23, 0x40e00000, v23
	v_min_f32_e32 v27, 0x40e00000, v27
	v_pk_mul_f32 v[36:37], v[20:21], s[22:23] op_sel_hi:[1,0]
	v_pk_mul_f32 v[38:39], v[22:23], s[22:23] op_sel_hi:[1,0]
	v_pk_mul_f32 v[42:43], v[26:27], s[22:23] op_sel_hi:[1,0]
	v_exp_f32_e32 v36, v36
	v_exp_f32_e32 v37, v37
	v_exp_f32_e32 v38, v38
	v_exp_f32_e32 v42, v42
	v_exp_f32_e32 v39, v39
	v_exp_f32_e32 v43, v43
	v_pk_add_f32 v[36:37], v[36:37], 1.0 op_sel_hi:[1,0]
	v_min_f32_e32 v24, 0x40e00000, v24
	v_pk_add_f32 v[38:39], v[38:39], 1.0 op_sel_hi:[1,0]
	v_pk_add_f32 v[42:43], v[42:43], 1.0 op_sel_hi:[1,0]
	v_rcp_f32_e32 v36, v36
	v_rcp_f32_e32 v37, v37
	v_min_f32_e32 v25, 0x40e00000, v25
	v_rcp_f32_e32 v38, v38
	v_rcp_f32_e32 v42, v42
	v_rcp_f32_e32 v39, v39
	v_rcp_f32_e32 v43, v43
	v_pk_mul_f32 v[40:41], v[24:25], s[22:23] op_sel_hi:[1,0]
	v_pk_fma_f32 v[28:29], v[156:157], s[20:21], v[12:13] op_sel_hi:[1,0,1]
	v_exp_f32_e32 v40, v40
	v_exp_f32_e32 v41, v41
	v_pk_fma_f32 v[30:31], v[154:155], s[20:21], v[14:15] op_sel_hi:[1,0,1]
	v_pk_fma_f32 v[34:35], v[150:151], s[20:21], v[18:19] op_sel_hi:[1,0,1]
	v_med3_f32 v28, v28, s56, v235
	v_med3_f32 v29, v29, s56, v235
	v_pk_mul_f32 v[20:21], v[20:21], v[36:37]
	v_med3_f32 v30, v30, s56, v235
	v_med3_f32 v34, v34, s56, v235
	v_med3_f32 v31, v31, s56, v235
	v_med3_f32 v35, v35, s56, v235
	v_pk_mul_f32 v[22:23], v[22:23], v[38:39]
	v_pk_mul_f32 v[28:29], v[28:29], v[20:21]
	v_pk_mul_f32 v[20:21], v[26:27], v[42:43]
	v_pk_mul_f32 v[22:23], v[30:31], v[22:23]
	v_pk_mul_f32 v[26:27], v[34:35], v[20:21]
	v_pk_add_f32 v[40:41], v[40:41], 1.0 op_sel_hi:[1,0]
	v_cvt_pk_fp8_f32 v20, v22, v23
	v_rcp_f32_e32 v40, v40
	v_rcp_f32_e32 v41, v41
	v_pk_fma_f32 v[32:33], v[152:153], s[20:21], v[16:17] op_sel_hi:[1,0,1]
	v_cvt_pk_fp8_f32 v20, v28, v29 op_sel:[0,0,1]
	v_pk_fma_f32 v[28:29], v[146:147], s[20:21], v[6:7] op_sel_hi:[1,0,1]
	v_med3_f32 v32, v32, s56, v235
	v_med3_f32 v33, v33, s56, v235
	v_pk_mul_f32 v[22:23], v[24:25], v[40:41]
	v_min_f32_e32 v28, 0x40e00000, v28
	v_min_f32_e32 v29, 0x40e00000, v29
	v_pk_mul_f32 v[22:23], v[32:33], v[22:23]
	v_pk_mul_f32 v[32:33], v[28:29], s[22:23] op_sel_hi:[1,0]
	v_exp_f32_e32 v32, v32
	v_exp_f32_e32 v33, v33
	v_cvt_pk_fp8_f32 v21, v26, v27
	v_pk_fma_f32 v[26:27], v[148:149], s[20:21], v[8:9] op_sel_hi:[1,0,1]
	v_pk_fma_f32 v[24:25], v[142:143], s[20:21], v[18:19] op_sel_hi:[1,0,1]
	v_min_f32_e32 v26, 0x40e00000, v26
	v_min_f32_e32 v27, 0x40e00000, v27
	v_pk_mul_f32 v[30:31], v[26:27], s[22:23] op_sel_hi:[1,0]
	v_pk_add_f32 v[32:33], v[32:33], 1.0 op_sel_hi:[1,0]
	v_exp_f32_e32 v30, v30
	v_exp_f32_e32 v31, v31
	v_rcp_f32_e32 v32, v32
	v_rcp_f32_e32 v33, v33
	v_cvt_pk_fp8_f32 v21, v22, v23 op_sel:[0,0,1]
	v_pk_fma_f32 v[22:23], v[144:145], s[20:21], v[16:17] op_sel_hi:[1,0,1]
	v_pk_add_f32 v[30:31], v[30:31], 1.0 op_sel_hi:[1,0]
	v_med3_f32 v34, v22, s56, v235
	v_rcp_f32_e32 v30, v30
	v_rcp_f32_e32 v31, v31
	v_med3_f32 v35, v23, s56, v235
	v_pk_mul_f32 v[22:23], v[28:29], v[32:33]
	v_pk_fma_f32 v[32:33], v[138:139], s[20:21], v[2:3] op_sel_hi:[1,0,1]
	v_pk_mul_f32 v[26:27], v[26:27], v[30:31]
	v_min_f32_e32 v32, 0x40e00000, v32
	v_min_f32_e32 v33, 0x40e00000, v33
	v_pk_mul_f32 v[36:37], v[32:33], s[22:23] op_sel_hi:[1,0]
	v_pk_fma_f32 v[30:31], v[140:141], s[20:21], v[4:5] op_sel_hi:[1,0,1]
	v_exp_f32_e32 v36, v36
	v_exp_f32_e32 v37, v37
	v_min_f32_e32 v30, 0x40e00000, v30
	v_min_f32_e32 v31, 0x40e00000, v31
	v_pk_mul_f32 v[38:39], v[30:31], s[22:23] op_sel_hi:[1,0]
	v_pk_add_f32 v[36:37], v[36:37], 1.0 op_sel_hi:[1,0]
	v_exp_f32_e32 v38, v38
	v_exp_f32_e32 v39, v39
	v_rcp_f32_e32 v36, v36
	v_rcp_f32_e32 v37, v37
	v_pk_fma_f32 v[28:29], v[134:135], s[20:21], v[14:15] op_sel_hi:[1,0,1]
	v_pk_add_f32 v[38:39], v[38:39], 1.0 op_sel_hi:[1,0]
	v_med3_f32 v24, v24, s56, v235
	v_med3_f32 v25, v25, s56, v235
	v_med3_f32 v28, v28, s56, v235
	v_med3_f32 v29, v29, s56, v235
	v_rcp_f32_e32 v38, v38
	v_rcp_f32_e32 v39, v39
	v_pk_mul_f32 v[32:33], v[32:33], v[36:37]
	v_pk_mul_f32 v[24:25], v[24:25], v[22:23]
	v_pk_mul_f32 v[28:29], v[28:29], v[32:33]
	v_cvt_pk_fp8_f32 v22, v28, v29
	v_cvt_pk_fp8_f32 v23, v24, v25
	v_pk_fma_f32 v[24:25], v[136:137], s[20:21], v[12:13] op_sel_hi:[1,0,1]
	v_pk_mul_f32 v[28:29], v[30:31], v[38:39]
	v_med3_f32 v24, v24, s56, v235
	v_med3_f32 v25, v25, s56, v235
	v_pk_mul_f32 v[24:25], v[24:25], v[28:29]
	v_pk_fma_f32 v[28:29], v[124:125], s[20:21], v[12:13] op_sel_hi:[1,0,1]
	v_cvt_pk_fp8_f32 v22, v24, v25 op_sel:[0,0,1]
	v_pk_mul_f32 v[24:25], v[34:35], v[26:27]
	v_pk_fma_f32 v[26:27], v[126:127], s[20:21], v[6:7] op_sel_hi:[1,0,1]
	v_cvt_pk_fp8_f32 v23, v24, v25 op_sel:[0,0,1]
	v_or_b32_e32 v24, v44, v230
	v_ashrrev_i32_e32 v25, 31, v24
	v_lshlrev_b64 v[24:25], 11, v[24:25]
	v_lshl_add_u64 v[24:25], s[14:15], 0, v[24:25]
	v_lshl_add_u64 v[24:25], v[24:25], 0, v[10:11]
	v_permlane16_swap_b32_e32 v20, v22
	v_permlane16_swap_b32_e32 v21, v23
	v_lshl_add_u64 v[24:25], v[24:25], 0, v[204:205]
	global_store_dwordx4 v[24:25], v[20:23], off
	v_min_f32_e32 v26, 0x40e00000, v26
	v_min_f32_e32 v27, 0x40e00000, v27
	v_pk_fma_f32 v[20:21], v[132:133], s[20:21], v[4:5] op_sel_hi:[1,0,1]
	v_pk_fma_f32 v[22:23], v[130:131], s[20:21], v[2:3] op_sel_hi:[1,0,1]
	v_min_f32_e32 v20, 0x40e00000, v20
	v_min_f32_e32 v21, 0x40e00000, v21
	v_min_f32_e32 v22, 0x40e00000, v22
	v_min_f32_e32 v23, 0x40e00000, v23
	v_pk_mul_f32 v[36:37], v[20:21], s[22:23] op_sel_hi:[1,0]
	v_pk_mul_f32 v[38:39], v[22:23], s[22:23] op_sel_hi:[1,0]
	v_pk_mul_f32 v[42:43], v[26:27], s[22:23] op_sel_hi:[1,0]
	v_exp_f32_e32 v36, v36
	v_exp_f32_e32 v37, v37
	v_exp_f32_e32 v38, v38
	v_exp_f32_e32 v42, v42
	v_exp_f32_e32 v39, v39
	v_exp_f32_e32 v43, v43
	v_pk_add_f32 v[36:37], v[36:37], 1.0 op_sel_hi:[1,0]
	v_pk_fma_f32 v[24:25], v[128:129], s[20:21], v[8:9] op_sel_hi:[1,0,1]
	v_pk_add_f32 v[38:39], v[38:39], 1.0 op_sel_hi:[1,0]
	v_pk_add_f32 v[42:43], v[42:43], 1.0 op_sel_hi:[1,0]
	v_rcp_f32_e32 v36, v36
	v_rcp_f32_e32 v37, v37
	v_min_f32_e32 v24, 0x40e00000, v24
	v_min_f32_e32 v25, 0x40e00000, v25
	v_rcp_f32_e32 v38, v38
	v_rcp_f32_e32 v42, v42
	v_rcp_f32_e32 v39, v39
	v_rcp_f32_e32 v43, v43
	v_pk_mul_f32 v[40:41], v[24:25], s[22:23] op_sel_hi:[1,0]
	v_pk_fma_f32 v[30:31], v[122:123], s[20:21], v[14:15] op_sel_hi:[1,0,1]
	v_exp_f32_e32 v40, v40
	v_exp_f32_e32 v41, v41
	v_pk_fma_f32 v[34:35], v[118:119], s[20:21], v[18:19] op_sel_hi:[1,0,1]
	v_med3_f32 v28, v28, s56, v235
	v_med3_f32 v29, v29, s56, v235
	v_pk_mul_f32 v[20:21], v[20:21], v[36:37]
	v_med3_f32 v30, v30, s56, v235
	v_med3_f32 v34, v34, s56, v235
	v_med3_f32 v31, v31, s56, v235
	v_med3_f32 v35, v35, s56, v235
	v_pk_mul_f32 v[22:23], v[22:23], v[38:39]
	v_pk_mul_f32 v[28:29], v[28:29], v[20:21]
	v_pk_mul_f32 v[20:21], v[26:27], v[42:43]
	v_pk_mul_f32 v[22:23], v[30:31], v[22:23]
	v_pk_mul_f32 v[26:27], v[34:35], v[20:21]
	v_pk_add_f32 v[40:41], v[40:41], 1.0 op_sel_hi:[1,0]
	v_cvt_pk_fp8_f32 v20, v22, v23
	v_rcp_f32_e32 v40, v40
	v_rcp_f32_e32 v41, v41
	v_pk_fma_f32 v[32:33], v[120:121], s[20:21], v[16:17] op_sel_hi:[1,0,1]
	v_cvt_pk_fp8_f32 v20, v28, v29 op_sel:[0,0,1]
	v_pk_fma_f32 v[28:29], v[114:115], s[20:21], v[6:7] op_sel_hi:[1,0,1]
	v_med3_f32 v32, v32, s56, v235
	v_med3_f32 v33, v33, s56, v235
	v_pk_mul_f32 v[22:23], v[24:25], v[40:41]
	v_min_f32_e32 v28, 0x40e00000, v28
	v_min_f32_e32 v29, 0x40e00000, v29
	v_pk_mul_f32 v[22:23], v[32:33], v[22:23]
	v_pk_mul_f32 v[32:33], v[28:29], s[22:23] op_sel_hi:[1,0]
	v_exp_f32_e32 v32, v32
	v_exp_f32_e32 v33, v33
	v_cvt_pk_fp8_f32 v21, v26, v27
	v_pk_fma_f32 v[26:27], v[116:117], s[20:21], v[8:9] op_sel_hi:[1,0,1]
	v_pk_fma_f32 v[24:25], v[110:111], s[20:21], v[18:19] op_sel_hi:[1,0,1]
	v_min_f32_e32 v26, 0x40e00000, v26
	v_min_f32_e32 v27, 0x40e00000, v27
	v_pk_mul_f32 v[30:31], v[26:27], s[22:23] op_sel_hi:[1,0]
	v_pk_add_f32 v[32:33], v[32:33], 1.0 op_sel_hi:[1,0]
	v_exp_f32_e32 v30, v30
	v_exp_f32_e32 v31, v31
	v_rcp_f32_e32 v32, v32
	v_rcp_f32_e32 v33, v33
	v_cvt_pk_fp8_f32 v21, v22, v23 op_sel:[0,0,1]
	v_pk_fma_f32 v[22:23], v[112:113], s[20:21], v[16:17] op_sel_hi:[1,0,1]
	v_pk_add_f32 v[30:31], v[30:31], 1.0 op_sel_hi:[1,0]
	v_med3_f32 v34, v22, s56, v235
	v_rcp_f32_e32 v30, v30
	v_rcp_f32_e32 v31, v31
	v_med3_f32 v35, v23, s56, v235
	v_pk_mul_f32 v[22:23], v[28:29], v[32:33]
	v_pk_fma_f32 v[32:33], v[106:107], s[20:21], v[2:3] op_sel_hi:[1,0,1]
	v_pk_mul_f32 v[26:27], v[26:27], v[30:31]
	v_min_f32_e32 v32, 0x40e00000, v32
	v_min_f32_e32 v33, 0x40e00000, v33
	v_pk_mul_f32 v[36:37], v[32:33], s[22:23] op_sel_hi:[1,0]
	v_pk_fma_f32 v[30:31], v[108:109], s[20:21], v[4:5] op_sel_hi:[1,0,1]
	v_exp_f32_e32 v36, v36
	v_exp_f32_e32 v37, v37
	v_min_f32_e32 v30, 0x40e00000, v30
	v_min_f32_e32 v31, 0x40e00000, v31
	v_pk_mul_f32 v[38:39], v[30:31], s[22:23] op_sel_hi:[1,0]
	v_pk_add_f32 v[36:37], v[36:37], 1.0 op_sel_hi:[1,0]
	v_exp_f32_e32 v38, v38
	v_exp_f32_e32 v39, v39
	v_rcp_f32_e32 v36, v36
	v_rcp_f32_e32 v37, v37
	v_pk_fma_f32 v[28:29], v[102:103], s[20:21], v[14:15] op_sel_hi:[1,0,1]
	v_pk_add_f32 v[38:39], v[38:39], 1.0 op_sel_hi:[1,0]
	v_med3_f32 v24, v24, s56, v235
	v_med3_f32 v25, v25, s56, v235
	v_med3_f32 v28, v28, s56, v235
	v_med3_f32 v29, v29, s56, v235
	v_rcp_f32_e32 v38, v38
	v_rcp_f32_e32 v39, v39
	v_pk_mul_f32 v[32:33], v[32:33], v[36:37]
	v_pk_mul_f32 v[24:25], v[24:25], v[22:23]
	v_pk_mul_f32 v[28:29], v[28:29], v[32:33]
	v_cvt_pk_fp8_f32 v22, v28, v29
	v_cvt_pk_fp8_f32 v23, v24, v25
	v_pk_fma_f32 v[24:25], v[104:105], s[20:21], v[12:13] op_sel_hi:[1,0,1]
	v_pk_mul_f32 v[28:29], v[30:31], v[38:39]
	v_med3_f32 v24, v24, s56, v235
	v_med3_f32 v25, v25, s56, v235
	v_pk_mul_f32 v[24:25], v[24:25], v[28:29]
	v_add_u32_e32 v44, 0x80, v44
	v_cvt_pk_fp8_f32 v22, v24, v25 op_sel:[0,0,1]
	v_pk_mul_f32 v[24:25], v[34:35], v[26:27]
	v_pk_fma_f32 v[26:27], v[90:91], s[20:21], v[6:7] op_sel_hi:[1,0,1]
	v_cvt_pk_fp8_f32 v23, v24, v25 op_sel:[0,0,1]
	v_or_b32_e32 v24, v44, v229
	v_ashrrev_i32_e32 v25, 31, v24
	v_lshlrev_b64 v[24:25], 11, v[24:25]
	v_lshl_add_u64 v[24:25], s[14:15], 0, v[24:25]
	v_lshl_add_u64 v[24:25], v[24:25], 0, v[10:11]
	v_permlane16_swap_b32_e32 v20, v22
	v_permlane16_swap_b32_e32 v21, v23
	v_lshl_add_u64 v[24:25], v[24:25], 0, v[204:205]
	global_store_dwordx4 v[24:25], v[20:23], off
	v_min_f32_e32 v26, 0x40e00000, v26
	v_min_f32_e32 v27, 0x40e00000, v27
	v_pk_fma_f32 v[20:21], v[100:101], s[20:21], v[4:5] op_sel_hi:[1,0,1]
	v_pk_fma_f32 v[22:23], v[98:99], s[20:21], v[2:3] op_sel_hi:[1,0,1]
	v_min_f32_e32 v20, 0x40e00000, v20
	v_min_f32_e32 v21, 0x40e00000, v21
	v_pk_mul_f32 v[36:37], v[20:21], s[22:23] op_sel_hi:[1,0]
	v_pk_mul_f32 v[42:43], v[26:27], s[22:23] op_sel_hi:[1,0]
	v_exp_f32_e32 v36, v36
	v_exp_f32_e32 v37, v37
	v_min_f32_e32 v22, 0x40e00000, v22
	v_min_f32_e32 v23, 0x40e00000, v23
	v_exp_f32_e32 v42, v42
	v_exp_f32_e32 v43, v43
	v_pk_fma_f32 v[24:25], v[92:93], s[20:21], v[8:9] op_sel_hi:[1,0,1]
	v_pk_mul_f32 v[38:39], v[22:23], s[22:23] op_sel_hi:[1,0]
	v_min_f32_e32 v24, 0x40e00000, v24
	v_min_f32_e32 v25, 0x40e00000, v25
	v_exp_f32_e32 v38, v38
	v_exp_f32_e32 v39, v39
	v_pk_mul_f32 v[40:41], v[24:25], s[22:23] op_sel_hi:[1,0]
	v_pk_add_f32 v[36:37], v[36:37], 1.0 op_sel_hi:[1,0]
	v_exp_f32_e32 v40, v40
	v_exp_f32_e32 v41, v41
	v_pk_add_f32 v[42:43], v[42:43], 1.0 op_sel_hi:[1,0]
	v_rcp_f32_e32 v36, v36
	v_rcp_f32_e32 v37, v37
	v_rcp_f32_e32 v42, v42
	v_rcp_f32_e32 v43, v43
	v_pk_add_f32 v[38:39], v[38:39], 1.0 op_sel_hi:[1,0]
	v_pk_fma_f32 v[28:29], v[96:97], s[20:21], v[12:13] op_sel_hi:[1,0,1]
	v_rcp_f32_e32 v38, v38
	v_rcp_f32_e32 v39, v39
	v_pk_fma_f32 v[34:35], v[86:87], s[20:21], v[18:19] op_sel_hi:[1,0,1]
	v_med3_f32 v28, v28, s56, v235
	v_med3_f32 v29, v29, s56, v235
	v_pk_add_f32 v[40:41], v[40:41], 1.0 op_sel_hi:[1,0]
	v_pk_mul_f32 v[20:21], v[20:21], v[36:37]
	v_med3_f32 v34, v34, s56, v235
	v_med3_f32 v35, v35, s56, v235
	v_rcp_f32_e32 v40, v40
	v_rcp_f32_e32 v41, v41
	v_pk_mul_f32 v[28:29], v[28:29], v[20:21]
	v_pk_mul_f32 v[20:21], v[26:27], v[42:43]
	v_pk_fma_f32 v[30:31], v[94:95], s[20:21], v[14:15] op_sel_hi:[1,0,1]
	v_pk_mul_f32 v[26:27], v[34:35], v[20:21]
	v_med3_f32 v30, v30, s56, v235
	v_med3_f32 v31, v31, s56, v235
	v_pk_mul_f32 v[22:23], v[22:23], v[38:39]
	v_cvt_pk_fp8_f32 v21, v26, v27
	v_pk_fma_f32 v[32:33], v[88:89], s[20:21], v[16:17] op_sel_hi:[1,0,1]
	v_pk_mul_f32 v[22:23], v[30:31], v[22:23]
	v_pk_fma_f32 v[6:7], v[78:79], s[20:21], v[6:7] op_sel_hi:[1,0,1]
	v_med3_f32 v32, v32, s56, v235
	v_med3_f32 v33, v33, s56, v235
	v_cvt_pk_fp8_f32 v20, v22, v23
	v_pk_mul_f32 v[22:23], v[24:25], v[40:41]
	v_pk_fma_f32 v[8:9], v[80:81], s[20:21], v[8:9] op_sel_hi:[1,0,1]
	v_min_f32_e32 v6, 0x40e00000, v6
	v_min_f32_e32 v7, 0x40e00000, v7
	v_pk_mul_f32 v[22:23], v[32:33], v[22:23]
	v_min_f32_e32 v8, 0x40e00000, v8
	v_min_f32_e32 v9, 0x40e00000, v9
	v_pk_mul_f32 v[24:25], v[6:7], s[22:23] op_sel_hi:[1,0]
	v_cvt_pk_fp8_f32 v21, v22, v23 op_sel:[0,0,1]
	v_pk_mul_f32 v[22:23], v[8:9], s[22:23] op_sel_hi:[1,0]
	v_exp_f32_e32 v24, v24
	v_exp_f32_e32 v25, v25
	v_exp_f32_e32 v22, v22
	v_exp_f32_e32 v23, v23
	v_pk_fma_f32 v[18:19], v[82:83], s[20:21], v[18:19] op_sel_hi:[1,0,1]
	v_pk_add_f32 v[24:25], v[24:25], 1.0 op_sel_hi:[1,0]
	v_med3_f32 v18, v18, s56, v235
	v_pk_add_f32 v[22:23], v[22:23], 1.0 op_sel_hi:[1,0]
	v_rcp_f32_e32 v24, v24
	v_rcp_f32_e32 v25, v25
	v_rcp_f32_e32 v22, v22
	v_rcp_f32_e32 v23, v23
	v_med3_f32 v19, v19, s56, v235
	v_pk_mul_f32 v[6:7], v[6:7], v[24:25]
	v_pk_fma_f32 v[2:3], v[70:71], s[20:21], v[2:3] op_sel_hi:[1,0,1]
	v_pk_mul_f32 v[8:9], v[8:9], v[22:23]
	v_pk_mul_f32 v[6:7], v[18:19], v[6:7]
	v_min_f32_e32 v2, 0x40e00000, v2
	v_min_f32_e32 v3, 0x40e00000, v3
	v_cvt_pk_fp8_f32 v23, v6, v7
	v_pk_fma_f32 v[6:7], v[76:77], s[20:21], v[12:13] op_sel_hi:[1,0,1]
	v_pk_fma_f32 v[12:13], v[74:75], s[20:21], v[14:15] op_sel_hi:[1,0,1]
	v_pk_mul_f32 v[14:15], v[2:3], s[22:23] op_sel_hi:[1,0]
	v_pk_fma_f32 v[4:5], v[72:73], s[20:21], v[4:5] op_sel_hi:[1,0,1]
	v_exp_f32_e32 v14, v14
	v_exp_f32_e32 v15, v15
	v_min_f32_e32 v4, 0x40e00000, v4
	v_min_f32_e32 v5, 0x40e00000, v5
	v_pk_mul_f32 v[18:19], v[4:5], s[22:23] op_sel_hi:[1,0]
	v_pk_add_f32 v[14:15], v[14:15], 1.0 op_sel_hi:[1,0]
	v_exp_f32_e32 v18, v18
	v_exp_f32_e32 v19, v19
	v_rcp_f32_e32 v14, v14
	v_rcp_f32_e32 v15, v15
	v_med3_f32 v12, v12, s56, v235
	v_pk_add_f32 v[18:19], v[18:19], 1.0 op_sel_hi:[1,0]
	v_med3_f32 v13, v13, s56, v235
	v_rcp_f32_e32 v18, v18
	v_rcp_f32_e32 v19, v19
	v_pk_mul_f32 v[2:3], v[2:3], v[14:15]
	v_pk_mul_f32 v[2:3], v[12:13], v[2:3]
	v_pk_fma_f32 v[16:17], v[84:85], s[20:21], v[16:17] op_sel_hi:[1,0,1]
	v_cvt_pk_fp8_f32 v22, v2, v3
	v_med3_f32 v6, v6, s56, v235
	v_med3_f32 v7, v7, s56, v235
	v_pk_mul_f32 v[2:3], v[4:5], v[18:19]
	v_med3_f32 v16, v16, s56, v235
	v_med3_f32 v17, v17, s56, v235
	v_pk_mul_f32 v[2:3], v[6:7], v[2:3]
	v_cvt_pk_fp8_f32 v20, v28, v29 op_sel:[0,0,1]
	v_cvt_pk_fp8_f32 v22, v2, v3 op_sel:[0,0,1]
	v_pk_mul_f32 v[2:3], v[16:17], v[8:9]
	s_mov_b64 s[6:7], -1
	v_cvt_pk_fp8_f32 v23, v2, v3 op_sel:[0,0,1]
	v_or_b32_e32 v2, v44, v230
	v_ashrrev_i32_e32 v3, 31, v2
	v_lshlrev_b64 v[2:3], 11, v[2:3]
	v_lshl_add_u64 v[2:3], s[14:15], 0, v[2:3]
	v_lshl_add_u64 v[2:3], v[2:3], 0, v[10:11]
	v_permlane16_swap_b32_e32 v20, v22
	v_permlane16_swap_b32_e32 v21, v23
	v_lshl_add_u64 v[2:3], v[2:3], 0, v[204:205]
	global_store_dwordx4 v[2:3], v[20:23], off
	s_cbranch_vccnz .LBB0_907
	s_andn2_b64 vcc, exec, s[0:1]
	s_cbranch_vccnz .LBB0_906
	s_barrier
	s_branch .LBB0_906

.LBB0_932:
	v_mul_f32_e32 v147, 0x42800000, v50
	v_mul_f32_e32 v149, 0x42800000, v58
	v_cvt_pk_fp8_f32 v148, v147, v149
	v_mul_f32_e32 v147, 0x42800000, v74
	v_mul_f32_e32 v152, 0x42800000, v82
	v_cvt_pk_fp8_f32 v149, v147, v152
	v_mul_f32_e32 v150, 0x42800000, v62
	v_mul_f32_e32 v151, 0x42800000, v70
	v_cvt_pk_fp8_f32 v148, v150, v151 op_sel:[0,0,1]
	v_mul_f32_e32 v147, 0x42800000, v86
	v_mul_f32_e32 v150, 0x42800000, v94
	v_cvt_pk_fp8_f32 v149, v147, v150 op_sel:[0,0,1]
	v_mul_f32_e32 v147, 0x42800000, v98
	v_mul_f32_e32 v151, 0x42800000, v102
	v_cvt_pk_fp8_f32 v150, v147, v151
	v_mul_f32_e32 v147, 0x42800000, v114
	v_mul_f32_e32 v154, 0x42800000, v118
	v_cvt_pk_fp8_f32 v151, v147, v154
	v_mul_f32_e32 v152, 0x42800000, v106
	v_mul_f32_e32 v153, 0x42800000, v110
	v_cvt_pk_fp8_f32 v150, v152, v153 op_sel:[0,0,1]
	v_mul_f32_e32 v147, 0x42800000, v122
	v_mul_f32_e32 v152, 0x42800000, v126
	v_cvt_pk_fp8_f32 v151, v147, v152 op_sel:[0,0,1]
	v_mul_f32_e32 v147, 0x42800000, v51
	v_mul_f32_e32 v153, 0x42800000, v59
	v_cvt_pk_fp8_f32 v152, v147, v153
	v_mul_f32_e32 v147, 0x42800000, v75
	v_mul_f32_e32 v156, 0x42800000, v83
	v_cvt_pk_fp8_f32 v153, v147, v156
	v_mul_f32_e32 v154, 0x42800000, v63
	v_mul_f32_e32 v155, 0x42800000, v71
	v_cvt_pk_fp8_f32 v152, v154, v155 op_sel:[0,0,1]
	v_mul_f32_e32 v147, 0x42800000, v87
	v_mul_f32_e32 v154, 0x42800000, v95
	v_cvt_pk_fp8_f32 v153, v147, v154 op_sel:[0,0,1]
	v_mul_f32_e32 v147, 0x42800000, v99
	v_mul_f32_e32 v155, 0x42800000, v103
	v_cvt_pk_fp8_f32 v154, v147, v155
	v_mul_f32_e32 v147, 0x42800000, v115
	v_mul_f32_e32 v158, 0x42800000, v119
	v_cvt_pk_fp8_f32 v155, v147, v158
	v_mul_f32_e32 v156, 0x42800000, v107
	v_mul_f32_e32 v157, 0x42800000, v111
	v_cvt_pk_fp8_f32 v154, v156, v157 op_sel:[0,0,1]
	v_mul_f32_e32 v147, 0x42800000, v123
	v_mul_f32_e32 v156, 0x42800000, v127
	v_cvt_pk_fp8_f32 v155, v147, v156 op_sel:[0,0,1]
	v_mul_f32_e32 v147, 0x42800000, v52
	v_mul_f32_e32 v157, 0x42800000, v60
	v_cvt_pk_fp8_f32 v156, v147, v157
	v_mul_f32_e32 v147, 0x42800000, v76
	v_mul_f32_e32 v160, 0x42800000, v84
	v_cvt_pk_fp8_f32 v157, v147, v160
	s_ashr_i32 s0, s28, 31
	s_lshr_b32 s0, s0, 20
	v_mul_f32_e32 v158, 0x42800000, v64
	v_mul_f32_e32 v159, 0x42800000, v72
	s_add_i32 s0, s28, s0
	v_cvt_pk_fp8_f32 v156, v158, v159 op_sel:[0,0,1]
	v_mul_f32_e32 v147, 0x42800000, v88
	v_mul_f32_e32 v158, 0x42800000, v96
	s_and_b32 s0, s0, 0xfffff000
	v_cvt_pk_fp8_f32 v157, v147, v158 op_sel:[0,0,1]
	v_mul_f32_e32 v147, 0x42800000, v100
	v_mul_f32_e32 v159, 0x42800000, v104
	s_sub_i32 s1, s28, s0
	v_cvt_pk_fp8_f32 v158, v147, v159
	v_mul_f32_e32 v147, 0x42800000, v116
	v_mul_f32_e32 v162, 0x42800000, v120
	s_sext_i32_i16 s0, s1
	v_cvt_pk_fp8_f32 v159, v147, v162
	s_bfe_u32 s0, s0, 0x70018
	s_add_i32 s0, s1, s0
	v_mul_f32_e32 v160, 0x42800000, v108
	v_mul_f32_e32 v161, 0x42800000, v112
	s_sext_i32_i16 s4, s0
	v_cvt_pk_fp8_f32 v158, v160, v161 op_sel:[0,0,1]
	v_mul_f32_e32 v147, 0x42800000, v124
	v_mul_f32_e32 v160, 0x42800000, v128
	s_lshr_b32 s0, s4, 7
	s_and_b32 s4, s4, 0xffffff80
	v_cvt_pk_fp8_f32 v159, v147, v160 op_sel:[0,0,1]
	v_mul_f32_e32 v147, 0x42800000, v53
	v_mul_f32_e32 v161, 0x42800000, v61
	s_sub_i32 s4, s1, s4
	v_cvt_pk_fp8_f32 v160, v147, v161
	v_mul_f32_e32 v147, 0x42800000, v77
	v_mul_f32_e32 v164, 0x42800000, v85
	s_bfe_u32 s1, s4, 0x3001c
	v_cvt_pk_fp8_f32 v161, v147, v164
	s_add_i32 s1, s4, s1
	s_sext_i32_i16 s1, s1
	v_mul_f32_e32 v162, 0x42800000, v65
	v_mul_f32_e32 v163, 0x42800000, v73
	s_add_i32 s27, s28, s90
	v_cvt_pk_fp8_f32 v160, v162, v163 op_sel:[0,0,1]
	v_mul_f32_e32 v147, 0x42800000, v89
	v_mul_f32_e32 v162, 0x42800000, v97
	s_ashr_i32 s28, s1, 3
	s_bfe_i64 s[0:1], s[0:1], 0x100000
	v_cvt_pk_fp8_f32 v161, v147, v162 op_sel:[0,0,1]
	v_mul_f32_e32 v147, 0x42800000, v101
	v_mul_f32_e32 v163, 0x42800000, v105
	s_lshl_b64 s[0:1], s[0:1], 22
	v_cvt_pk_fp8_f32 v162, v147, v163
	v_mul_f32_e32 v147, 0x42800000, v117
	v_mul_f32_e32 v166, 0x42800000, v121
	s_add_u32 s0, s5, s0
	v_cvt_pk_fp8_f32 v163, v147, v166
	s_addc_u32 s1, s6, s1
	s_lshl_b32 s29, s28, 7
	s_ashr_i32 s30, s29, 31
	v_mul_f32_e32 v164, 0x42800000, v109
	v_mul_f32_e32 v165, 0x42800000, v113
	s_add_u32 s0, s0, s29
	v_cvt_pk_fp8_f32 v162, v164, v165 op_sel:[0,0,1]
	v_mul_f32_e32 v147, 0x42800000, v125
	v_mul_f32_e32 v164, 0x42800000, v129
	s_addc_u32 s1, s1, s30
	s_lshl_b32 s4, s4, 8
	s_lshl_b32 s28, s28, 11
	v_cvt_pk_fp8_f32 v163, v147, v164 op_sel:[0,0,1]
	s_sub_i32 s4, s4, s28
	ds_write_b128 v142, v[148:151] offset:36864
	ds_write_b128 v142, v[152:155] offset:37008
	ds_write_b128 v142, v[156:159] offset:37152
	ds_write_b128 v142, v[160:163] offset:37296
	s_waitcnt lgkmcnt(0)
	s_barrier
	v_add_u32_e32 v152, s4, v138
	ds_read_b128 v[148:151], v143 offset:36864
	v_ashrrev_i32_e32 v153, 31, v152
	v_lshlrev_b64 v[152:153], 11, v[152:153]
	v_lshl_add_u64 v[152:153], s[0:1], 0, v[152:153]
	v_lshl_add_u64 v[156:157], v[152:153], 0, v[132:133]
	ds_read_b128 v[152:155], v144 offset:36864
	s_waitcnt lgkmcnt(1)
	global_store_dwordx4 v[156:157], v[148:151], off nt
	s_cmpk_gt_i32 s27, 0xfff
	s_nop 0
	v_add_u32_e32 v148, s4, v139
	v_ashrrev_i32_e32 v149, 31, v148
	v_lshlrev_b64 v[148:149], 11, v[148:149]
	v_lshl_add_u64 v[148:149], s[0:1], 0, v[148:149]
	v_lshl_add_u64 v[148:149], v[148:149], 0, v[134:135]
	s_waitcnt lgkmcnt(0)
	global_store_dwordx4 v[148:149], v[152:155], off nt
	ds_read_b128 v[148:151], v145 offset:36864
	s_nop 0
	v_add_u32_e32 v152, s4, v140
	v_ashrrev_i32_e32 v153, 31, v152
	v_lshlrev_b64 v[152:153], 11, v[152:153]
	v_lshl_add_u64 v[152:153], s[0:1], 0, v[152:153]
	v_lshl_add_u64 v[156:157], v[152:153], 0, v[132:133]
	ds_read_b128 v[152:155], v146 offset:36864
	s_waitcnt lgkmcnt(1)
	global_store_dwordx4 v[156:157], v[148:151], off nt
	s_nop 1
	v_add_u32_e32 v148, s4, v141
	v_ashrrev_i32_e32 v149, 31, v148
	v_lshlrev_b64 v[148:149], 11, v[148:149]
	v_lshl_add_u64 v[148:149], s[0:1], 0, v[148:149]
	v_lshl_add_u64 v[148:149], v[148:149], 0, v[136:137]
	s_cselect_b64 s[0:1], -1, 0
	s_waitcnt lgkmcnt(0)
	global_store_dwordx4 v[148:149], v[152:155], off nt

.Lcvdn_a:
	v_mul_f32_e32 v147, 0x42800000, v30
	v_mul_f32_e32 v149, 0x42800000, v2
	v_cvt_pk_fp8_f32 v148, v147, v149
	v_mul_f32_e32 v147, 0x42800000, v14
	v_mul_f32_e32 v152, 0x42800000, v18
	v_cvt_pk_fp8_f32 v149, v147, v152
	v_mul_f32_e32 v150, 0x42800000, v6
	v_mul_f32_e32 v151, 0x42800000, v10
	v_cvt_pk_fp8_f32 v148, v150, v151 op_sel:[0,0,1]
	v_mul_f32_e32 v147, 0x42800000, v22
	v_mul_f32_e32 v150, 0x42800000, v26
	v_cvt_pk_fp8_f32 v149, v147, v150 op_sel:[0,0,1]
	v_mul_f32_e32 v147, 0x42800000, v34
	v_mul_f32_e32 v151, 0x42800000, v38
	v_cvt_pk_fp8_f32 v150, v147, v151
	v_mul_f32_e32 v147, 0x42800000, v54
	v_mul_f32_e32 v154, 0x42800000, v66
	v_cvt_pk_fp8_f32 v151, v147, v154
	v_mul_f32_e32 v152, 0x42800000, v42
	v_mul_f32_e32 v153, 0x42800000, v46
	v_cvt_pk_fp8_f32 v150, v152, v153 op_sel:[0,0,1]
	v_mul_f32_e32 v147, 0x42800000, v78
	v_mul_f32_e32 v152, 0x42800000, v90
	v_cvt_pk_fp8_f32 v151, v147, v152 op_sel:[0,0,1]
	v_mul_f32_e32 v147, 0x42800000, v31
	v_mul_f32_e32 v153, 0x42800000, v3
	v_cvt_pk_fp8_f32 v152, v147, v153
	v_mul_f32_e32 v147, 0x42800000, v15
	v_mul_f32_e32 v156, 0x42800000, v19
	v_cvt_pk_fp8_f32 v153, v147, v156
	v_mul_f32_e32 v154, 0x42800000, v7
	v_mul_f32_e32 v155, 0x42800000, v11
	v_cvt_pk_fp8_f32 v152, v154, v155 op_sel:[0,0,1]
	v_mul_f32_e32 v147, 0x42800000, v23
	v_mul_f32_e32 v154, 0x42800000, v27
	v_cvt_pk_fp8_f32 v153, v147, v154 op_sel:[0,0,1]
	v_mul_f32_e32 v147, 0x42800000, v35
	v_mul_f32_e32 v155, 0x42800000, v39
	v_cvt_pk_fp8_f32 v154, v147, v155
	v_mul_f32_e32 v147, 0x42800000, v55
	v_mul_f32_e32 v158, 0x42800000, v67
	v_cvt_pk_fp8_f32 v155, v147, v158
	v_mul_f32_e32 v156, 0x42800000, v43
	v_mul_f32_e32 v157, 0x42800000, v47
	v_cvt_pk_fp8_f32 v154, v156, v157 op_sel:[0,0,1]
	v_mul_f32_e32 v147, 0x42800000, v79
	v_mul_f32_e32 v156, 0x42800000, v91
	v_cvt_pk_fp8_f32 v155, v147, v156 op_sel:[0,0,1]
	v_mul_f32_e32 v147, 0x42800000, v32
	v_mul_f32_e32 v157, 0x42800000, v4
	v_cvt_pk_fp8_f32 v156, v147, v157
	v_mul_f32_e32 v147, 0x42800000, v16
	v_mul_f32_e32 v160, 0x42800000, v20
	v_cvt_pk_fp8_f32 v157, v147, v160
	s_ashr_i32 s4, s27, 31
	s_lshr_b32 s4, s4, 20
	v_mul_f32_e32 v158, 0x42800000, v8
	v_mul_f32_e32 v159, 0x42800000, v12
	s_add_i32 s4, s27, s4
	v_cvt_pk_fp8_f32 v156, v158, v159 op_sel:[0,0,1]
	v_mul_f32_e32 v147, 0x42800000, v24
	v_mul_f32_e32 v158, 0x42800000, v28
	s_and_b32 s4, s4, 0xfffff000
	v_cvt_pk_fp8_f32 v157, v147, v158 op_sel:[0,0,1]
	v_mul_f32_e32 v147, 0x42800000, v36
	v_mul_f32_e32 v159, 0x42800000, v40
	s_sub_i32 s29, s27, s4
	v_cvt_pk_fp8_f32 v158, v147, v159
	v_mul_f32_e32 v147, 0x42800000, v56
	v_mul_f32_e32 v162, 0x42800000, v68
	s_sext_i32_i16 s4, s29
	v_cvt_pk_fp8_f32 v159, v147, v162
	s_bfe_u32 s4, s4, 0x70018
	s_add_i32 s4, s29, s4
	v_mul_f32_e32 v160, 0x42800000, v44
	v_mul_f32_e32 v161, 0x42800000, v48
	s_sext_i32_i16 s30, s4
	v_cvt_pk_fp8_f32 v158, v160, v161 op_sel:[0,0,1]
	v_mul_f32_e32 v147, 0x42800000, v80
	v_mul_f32_e32 v160, 0x42800000, v92
	s_lshr_b32 s4, s30, 7
	s_and_b32 s30, s30, 0xffffff80
	v_cvt_pk_fp8_f32 v159, v147, v160 op_sel:[0,0,1]
	v_mul_f32_e32 v147, 0x42800000, v33
	v_mul_f32_e32 v161, 0x42800000, v5
	s_sub_i32 s29, s29, s30
	v_cvt_pk_fp8_f32 v160, v147, v161
	v_mul_f32_e32 v147, 0x42800000, v17
	v_mul_f32_e32 v164, 0x42800000, v21
	s_bfe_u32 s30, s29, 0x3001c
	v_cvt_pk_fp8_f32 v161, v147, v164
	s_add_i32 s30, s29, s30
	s_sext_i32_i16 s30, s30
	v_mul_f32_e32 v162, 0x42800000, v9
	v_mul_f32_e32 v163, 0x42800000, v13
	v_cvt_pk_fp8_f32 v160, v162, v163 op_sel:[0,0,1]
	v_mul_f32_e32 v147, 0x42800000, v25
	v_mul_f32_e32 v162, 0x42800000, v29
	s_ashr_i32 s34, s30, 3
	s_bfe_i64 s[30:31], s[4:5], 0x100000
	v_cvt_pk_fp8_f32 v161, v147, v162 op_sel:[0,0,1]
	v_mul_f32_e32 v147, 0x42800000, v37
	v_mul_f32_e32 v163, 0x42800000, v41
	s_lshl_b64 s[30:31], s[30:31], 22
	v_cvt_pk_fp8_f32 v162, v147, v163
	v_mul_f32_e32 v147, 0x42800000, v57
	v_mul_f32_e32 v166, 0x42800000, v69
	s_add_u32 s4, s5, s30
	v_cvt_pk_fp8_f32 v163, v147, v166
	s_addc_u32 s31, s6, s31
	s_lshl_b32 s30, s34, 7
	s_ashr_i32 s35, s30, 31
	v_mul_f32_e32 v164, 0x42800000, v45
	v_mul_f32_e32 v165, 0x42800000, v49
	s_add_u32 s30, s4, s30
	v_cvt_pk_fp8_f32 v162, v164, v165 op_sel:[0,0,1]
	v_mul_f32_e32 v147, 0x42800000, v81
	v_mul_f32_e32 v164, 0x42800000, v93
	s_addc_u32 s31, s31, s35
	s_lshl_b32 s4, s29, 8
	s_lshl_b32 s29, s34, 11
	v_cvt_pk_fp8_f32 v163, v147, v164 op_sel:[0,0,1]
	s_sub_i32 s4, s4, s29
	ds_write_b128 v142, v[148:151]
	ds_write_b128 v142, v[152:155] offset:144
	ds_write_b128 v142, v[156:159] offset:288
	ds_write_b128 v142, v[160:163] offset:432
	s_waitcnt lgkmcnt(0)
	s_barrier
	v_add_u32_e32 v152, s4, v138
	ds_read_b128 v[148:151], v143
	v_ashrrev_i32_e32 v153, 31, v152
	v_lshlrev_b64 v[152:153], 11, v[152:153]
	v_lshl_add_u64 v[152:153], s[30:31], 0, v[152:153]
	v_lshl_add_u64 v[156:157], v[152:153], 0, v[132:133]
	ds_read_b128 v[152:155], v144
	s_waitcnt lgkmcnt(1)
	global_store_dwordx4 v[156:157], v[148:151], off nt
	s_andn2_b64 vcc, exec, s[0:1]
	s_mov_b64 s[0:1], -1
	v_add_u32_e32 v148, s4, v139
	v_ashrrev_i32_e32 v149, 31, v148
	v_lshlrev_b64 v[148:149], 11, v[148:149]
	v_lshl_add_u64 v[148:149], s[30:31], 0, v[148:149]
	v_lshl_add_u64 v[148:149], v[148:149], 0, v[134:135]
	s_waitcnt lgkmcnt(0)
	global_store_dwordx4 v[148:149], v[152:155], off nt
	ds_read_b128 v[148:151], v145
	s_nop 0
	v_add_u32_e32 v152, s4, v140
	v_ashrrev_i32_e32 v153, 31, v152
	v_lshlrev_b64 v[152:153], 11, v[152:153]
	v_lshl_add_u64 v[152:153], s[30:31], 0, v[152:153]
	v_lshl_add_u64 v[156:157], v[152:153], 0, v[132:133]
	ds_read_b128 v[152:155], v146
	s_waitcnt lgkmcnt(1)
	global_store_dwordx4 v[156:157], v[148:151], off nt
	s_nop 1
	v_add_u32_e32 v148, s4, v141
	v_ashrrev_i32_e32 v149, 31, v148
	v_lshlrev_b64 v[148:149], 11, v[148:149]
	v_lshl_add_u64 v[148:149], s[30:31], 0, v[148:149]
	v_lshl_add_u64 v[148:149], v[148:149], 0, v[136:137]
	s_waitcnt lgkmcnt(0)
	global_store_dwordx4 v[148:149], v[152:155], off nt
	s_cbranch_vccnz .LBB0_933
	s_add_i32 s0, s26, s27
	s_cmpk_gt_i32 s0, 0xfff
	s_cbranch_scc1 .Lcvdn_t
	s_ashr_i32 s1, s0, 31
	s_lshr_b32 s1, s1, 20
	s_add_i32 s1, s0, s1
	s_and_b32 s1, s1, 0xfffff000
	s_sub_i32 s1, s0, s1
	s_sext_i32_i16 s0, s1
	s_bfe_u32 s0, s0, 0x70018
	s_add_i32 s0, s1, s0
	s_sext_i32_i16 s4, s0
	s_lshr_b32 s0, s4, 7
	s_and_b32 s4, s4, 0xffffff80
	s_sub_i32 s4, s1, s4
	s_bfe_u32 s1, s4, 0x3001c
	s_add_i32 s1, s4, s1
	s_sext_i32_i16 s1, s1
	s_ashr_i32 s27, s1, 3
	s_bfe_i64 s[0:1], s[0:1], 0x100000
	v_readlane_b32 s36, v254, 32
	s_lshl_b64 s[0:1], s[0:1], 24
	v_readlane_b32 s50, v254, 46
	v_readlane_b32 s51, v254, 47
	s_add_u32 s29, s50, s0
	s_addc_u32 s30, s51, s1
	s_lshl_b32 s0, s27, 7
	s_add_i32 s0, s0, s7
	s_ashr_i32 s1, s0, 31
	s_lshl_b64 s[0:1], s[0:1], 13
	s_add_u32 s29, s29, s0
	s_addc_u32 s30, s30, s1
	s_lshl_b32 s0, s27, 11
	s_lshl_b32 s1, s4, 8
	s_sub_i32 s0, s1, s0
	s_ashr_i32 s1, s0, 31
	s_lshl_b64 s[0:1], s[0:1], 2
	s_add_u32 s0, s29, s0
	s_addc_u32 s1, s30, s1
	v_lshl_add_u64 v[78:79], s[0:1], 0, v[130:131]
	v_add_co_u32_e32 v2, vcc, s8, v78
	v_readlane_b32 s37, v254, 33
	s_nop 0
	v_addc_co_u32_e32 v3, vcc, 0, v79, vcc
	v_add_co_u32_e32 v6, vcc, s9, v78
	global_load_dwordx4 v[30:33], v[78:79], off nt
	s_nop 0
	global_load_dwordx4 v[2:5], v[2:3], off nt
	v_addc_co_u32_e32 v7, vcc, 0, v79, vcc
	v_add_co_u32_e32 v10, vcc, s10, v78
	v_readlane_b32 s38, v254, 34
	s_nop 0
	v_addc_co_u32_e32 v11, vcc, 0, v79, vcc
	v_add_co_u32_e32 v14, vcc, s11, v78
	global_load_dwordx4 v[6:9], v[6:7], off nt
	s_nop 0
	global_load_dwordx4 v[10:13], v[10:11], off nt
	v_addc_co_u32_e32 v15, vcc, 0, v79, vcc
	v_add_co_u32_e32 v18, vcc, s16, v78
	v_readlane_b32 s39, v254, 35
	s_nop 0
	v_addc_co_u32_e32 v19, vcc, 0, v79, vcc
	v_add_co_u32_e32 v22, vcc, s17, v78
	global_load_dwordx4 v[14:17], v[14:15], off nt
	s_nop 0
	global_load_dwordx4 v[18:21], v[18:19], off nt
	v_addc_co_u32_e32 v23, vcc, 0, v79, vcc
	v_add_co_u32_e32 v26, vcc, s18, v78
	v_readlane_b32 s40, v254, 36
	s_nop 0
	v_addc_co_u32_e32 v27, vcc, 0, v79, vcc
	v_add_co_u32_e32 v34, vcc, s19, v78
	global_load_dwordx4 v[22:25], v[22:23], off nt
	s_nop 0
	global_load_dwordx4 v[26:29], v[26:27], off nt
	v_addc_co_u32_e32 v35, vcc, 0, v79, vcc
	v_add_co_u32_e32 v38, vcc, s20, v78
	v_readlane_b32 s41, v254, 37
	s_nop 0
	v_addc_co_u32_e32 v39, vcc, 0, v79, vcc
	v_add_co_u32_e32 v42, vcc, s22, v78
	global_load_dwordx4 v[34:37], v[34:35], off nt
	s_nop 0
	global_load_dwordx4 v[38:41], v[38:39], off nt
	v_addc_co_u32_e32 v43, vcc, 0, v79, vcc
	v_add_co_u32_e32 v46, vcc, s24, v78
	v_readlane_b32 s42, v254, 38
	s_nop 0
	v_addc_co_u32_e32 v47, vcc, 0, v79, vcc
	v_add_co_u32_e32 v54, vcc, s25, v78
	global_load_dwordx4 v[42:45], v[42:43], off nt
	s_nop 0
	global_load_dwordx4 v[46:49], v[46:47], off nt
	v_addc_co_u32_e32 v55, vcc, 0, v79, vcc
	v_add_co_u32_e32 v66, vcc, 0x1a000, v78
	v_readlane_b32 s43, v254, 39
	s_nop 0
	v_addc_co_u32_e32 v67, vcc, 0, v79, vcc
	v_add_co_u32_e32 v80, vcc, 0x1c000, v78
	global_load_dwordx4 v[54:57], v[54:55], off nt
	s_nop 0
	global_load_dwordx4 v[66:69], v[66:67], off nt
	v_addc_co_u32_e32 v81, vcc, 0, v79, vcc
	v_add_co_u32_e32 v90, vcc, 0x1e000, v78
	v_readlane_b32 s44, v254, 40
	s_nop 0
	v_addc_co_u32_e32 v91, vcc, 0, v79, vcc
	global_load_dwordx4 v[78:81], v[80:81], off nt
	s_nop 0
	global_load_dwordx4 v[90:93], v[90:91], off nt
	v_readlane_b32 s45, v254, 41
	v_readlane_b32 s46, v254, 42
	v_readlane_b32 s47, v254, 43
	v_readlane_b32 s48, v254, 44
	v_readlane_b32 s49, v254, 45
	s_waitcnt vmcnt(20)
	s_branch .LBB0_932

.LBB0_963:
	s_add_i32 s8, s60, 0x25100
	v_mov_b32_e32 v2, s8
	s_lshl_b32 s8, s59, 11
	s_and_b32 s8, s8, 0x800
	s_nop 11
	v_add_u32_e32 v11, s8, v228
	ds_read_b32 v10, v2
	ds_read_b128 v[6:9], v11 offset:16
	ds_read_b128 v[14:17], v11 offset:512
	ds_read_b128 v[2:5], v11
	ds_read_b128 v[18:21], v11 offset:528
	s_and_b64 vcc, exec, s[6:7]
	s_waitcnt lgkmcnt(0)
	v_pk_fma_f32 v[26:27], v[190:191], s[20:21], v[6:7] op_sel_hi:[1,0,1]
	v_pk_add_f32 v[12:13], v[16:17], 1.0 op_sel_hi:[1,0]
	v_pk_fma_f32 v[22:23], v[194:195], s[20:21], v[2:3] op_sel_hi:[1,0,1]
	v_pk_add_f32 v[16:17], v[20:21], 1.0 op_sel_hi:[1,0]
	v_pk_fma_f32 v[20:21], v[196:197], s[20:21], v[4:5] op_sel_hi:[1,0,1]
	v_min_f32_e32 v22, 0x40e00000, v22
	v_min_f32_e32 v20, 0x40e00000, v20
	v_min_f32_e32 v21, 0x40e00000, v21
	v_min_f32_e32 v26, 0x40e00000, v26
	v_min_f32_e32 v23, 0x40e00000, v23
	v_min_f32_e32 v27, 0x40e00000, v27
	v_pk_mul_f32 v[36:37], v[20:21], s[22:23] op_sel_hi:[1,0]
	v_pk_mul_f32 v[38:39], v[22:23], s[22:23] op_sel_hi:[1,0]
	v_pk_mul_f32 v[42:43], v[26:27], s[22:23] op_sel_hi:[1,0]
	v_exp_f32_e32 v36, v36
	v_exp_f32_e32 v37, v37
	v_exp_f32_e32 v38, v38
	v_exp_f32_e32 v42, v42
	v_exp_f32_e32 v39, v39
	v_exp_f32_e32 v43, v43
	v_pk_add_f32 v[36:37], v[36:37], 1.0 op_sel_hi:[1,0]
	v_pk_fma_f32 v[24:25], v[192:193], s[20:21], v[8:9] op_sel_hi:[1,0,1]
	v_pk_add_f32 v[38:39], v[38:39], 1.0 op_sel_hi:[1,0]
	v_pk_add_f32 v[42:43], v[42:43], 1.0 op_sel_hi:[1,0]
	v_rcp_f32_e32 v36, v36
	v_rcp_f32_e32 v37, v37
	v_min_f32_e32 v24, 0x40e00000, v24
	v_min_f32_e32 v25, 0x40e00000, v25
	v_rcp_f32_e32 v38, v38
	v_rcp_f32_e32 v42, v42
	v_rcp_f32_e32 v39, v39
	v_rcp_f32_e32 v43, v43
	v_pk_mul_f32 v[40:41], v[24:25], s[22:23] op_sel_hi:[1,0]
	v_pk_add_f32 v[14:15], v[14:15], 1.0 op_sel_hi:[1,0]
	v_pk_add_f32 v[18:19], v[18:19], 1.0 op_sel_hi:[1,0]
	v_pk_fma_f32 v[28:29], v[188:189], s[20:21], v[12:13] op_sel_hi:[1,0,1]
	v_exp_f32_e32 v40, v40
	v_exp_f32_e32 v41, v41
	v_pk_fma_f32 v[30:31], v[186:187], s[20:21], v[14:15] op_sel_hi:[1,0,1]
	v_pk_fma_f32 v[34:35], v[182:183], s[20:21], v[18:19] op_sel_hi:[1,0,1]
	v_med3_f32 v28, v28, s54, v235
	v_med3_f32 v29, v29, s54, v235
	v_pk_mul_f32 v[20:21], v[20:21], v[36:37]
	v_med3_f32 v30, v30, s54, v235
	v_med3_f32 v34, v34, s54, v235
	v_med3_f32 v31, v31, s54, v235
	v_med3_f32 v35, v35, s54, v235
	v_pk_mul_f32 v[22:23], v[22:23], v[38:39]
	v_pk_mul_f32 v[28:29], v[28:29], v[20:21]
	v_pk_mul_f32 v[20:21], v[26:27], v[42:43]
	v_pk_mul_f32 v[22:23], v[30:31], v[22:23]
	v_pk_mul_f32 v[26:27], v[34:35], v[20:21]
	v_pk_add_f32 v[40:41], v[40:41], 1.0 op_sel_hi:[1,0]
	v_cvt_pk_fp8_f32 v20, v22, v23
	v_rcp_f32_e32 v40, v40
	v_rcp_f32_e32 v41, v41
	v_pk_fma_f32 v[32:33], v[184:185], s[20:21], v[16:17] op_sel_hi:[1,0,1]
	v_cvt_pk_fp8_f32 v20, v28, v29 op_sel:[0,0,1]
	v_pk_fma_f32 v[28:29], v[178:179], s[20:21], v[6:7] op_sel_hi:[1,0,1]
	v_med3_f32 v32, v32, s54, v235
	v_med3_f32 v33, v33, s54, v235
	v_pk_mul_f32 v[22:23], v[24:25], v[40:41]
	v_min_f32_e32 v28, 0x40e00000, v28
	v_min_f32_e32 v29, 0x40e00000, v29
	v_pk_mul_f32 v[22:23], v[32:33], v[22:23]
	v_pk_mul_f32 v[32:33], v[28:29], s[22:23] op_sel_hi:[1,0]
	v_exp_f32_e32 v32, v32
	v_exp_f32_e32 v33, v33
	v_cvt_pk_fp8_f32 v21, v26, v27
	v_pk_fma_f32 v[26:27], v[180:181], s[20:21], v[8:9] op_sel_hi:[1,0,1]
	v_pk_fma_f32 v[24:25], v[174:175], s[20:21], v[18:19] op_sel_hi:[1,0,1]
	v_min_f32_e32 v26, 0x40e00000, v26
	v_min_f32_e32 v27, 0x40e00000, v27
	v_pk_mul_f32 v[30:31], v[26:27], s[22:23] op_sel_hi:[1,0]
	v_pk_add_f32 v[32:33], v[32:33], 1.0 op_sel_hi:[1,0]
	v_exp_f32_e32 v30, v30
	v_exp_f32_e32 v31, v31
	v_rcp_f32_e32 v32, v32
	v_rcp_f32_e32 v33, v33
	v_cvt_pk_fp8_f32 v21, v22, v23 op_sel:[0,0,1]
	v_pk_fma_f32 v[22:23], v[176:177], s[20:21], v[16:17] op_sel_hi:[1,0,1]
	v_pk_add_f32 v[30:31], v[30:31], 1.0 op_sel_hi:[1,0]
	v_med3_f32 v34, v22, s54, v235
	v_rcp_f32_e32 v30, v30
	v_rcp_f32_e32 v31, v31
	v_med3_f32 v35, v23, s54, v235
	v_pk_mul_f32 v[22:23], v[28:29], v[32:33]
	v_pk_fma_f32 v[32:33], v[170:171], s[20:21], v[2:3] op_sel_hi:[1,0,1]
	v_pk_mul_f32 v[26:27], v[26:27], v[30:31]
	v_min_f32_e32 v32, 0x40e00000, v32
	v_min_f32_e32 v33, 0x40e00000, v33
	v_pk_mul_f32 v[36:37], v[32:33], s[22:23] op_sel_hi:[1,0]
	v_pk_fma_f32 v[30:31], v[172:173], s[20:21], v[4:5] op_sel_hi:[1,0,1]
	v_exp_f32_e32 v36, v36
	v_exp_f32_e32 v37, v37
	v_min_f32_e32 v30, 0x40e00000, v30
	v_min_f32_e32 v31, 0x40e00000, v31
	v_pk_mul_f32 v[38:39], v[30:31], s[22:23] op_sel_hi:[1,0]
	v_pk_add_f32 v[36:37], v[36:37], 1.0 op_sel_hi:[1,0]
	v_exp_f32_e32 v38, v38
	v_exp_f32_e32 v39, v39
	v_rcp_f32_e32 v36, v36
	v_rcp_f32_e32 v37, v37
	v_pk_fma_f32 v[28:29], v[166:167], s[20:21], v[14:15] op_sel_hi:[1,0,1]
	v_pk_add_f32 v[38:39], v[38:39], 1.0 op_sel_hi:[1,0]
	v_med3_f32 v24, v24, s54, v235
	v_med3_f32 v25, v25, s54, v235
	v_med3_f32 v28, v28, s54, v235
	v_med3_f32 v29, v29, s54, v235
	v_rcp_f32_e32 v38, v38
	v_rcp_f32_e32 v39, v39
	v_pk_mul_f32 v[32:33], v[32:33], v[36:37]
	v_pk_mul_f32 v[24:25], v[24:25], v[22:23]
	v_pk_mul_f32 v[28:29], v[28:29], v[32:33]
	v_cvt_pk_fp8_f32 v22, v28, v29
	v_cvt_pk_fp8_f32 v23, v24, v25
	v_pk_fma_f32 v[24:25], v[168:169], s[20:21], v[12:13] op_sel_hi:[1,0,1]
	v_pk_mul_f32 v[28:29], v[30:31], v[38:39]
	v_med3_f32 v24, v24, s54, v235
	v_med3_f32 v25, v25, s54, v235
	v_add_u32_e32 v11, s58, v10
	v_pk_mul_f32 v[24:25], v[24:25], v[28:29]
	v_lshl_add_u32 v44, v11, 8, v213
	v_cvt_pk_fp8_f32 v22, v24, v25 op_sel:[0,0,1]
	v_pk_mul_f32 v[24:25], v[34:35], v[26:27]
	v_lshl_or_b32 v10, s30, 7, v231
	v_cvt_pk_fp8_f32 v23, v24, v25 op_sel:[0,0,1]
	v_or_b32_e32 v24, v44, v229
	v_ashrrev_i32_e32 v25, 31, v24
	v_lshlrev_b64 v[24:25], 11, v[24:25]
	v_ashrrev_i32_e32 v11, 31, v10
	v_lshl_add_u64 v[24:25], s[14:15], 0, v[24:25]
	v_lshl_add_u64 v[24:25], v[24:25], 0, v[10:11]
	v_permlane16_swap_b32_e32 v20, v22
	v_permlane16_swap_b32_e32 v21, v23
	v_lshl_add_u64 v[24:25], v[24:25], 0, v[204:205]
	global_store_dwordx4 v[24:25], v[20:23], off
	v_pk_fma_f32 v[26:27], v[158:159], s[20:21], v[6:7] op_sel_hi:[1,0,1]
	v_pk_fma_f32 v[24:25], v[160:161], s[20:21], v[8:9] op_sel_hi:[1,0,1]
	v_pk_fma_f32 v[20:21], v[164:165], s[20:21], v[4:5] op_sel_hi:[1,0,1]
	v_pk_fma_f32 v[22:23], v[162:163], s[20:21], v[2:3] op_sel_hi:[1,0,1]
	v_min_f32_e32 v20, 0x40e00000, v20
	v_min_f32_e32 v21, 0x40e00000, v21
	v_min_f32_e32 v22, 0x40e00000, v22
	v_min_f32_e32 v26, 0x40e00000, v26
	v_min_f32_e32 v23, 0x40e00000, v23
	v_min_f32_e32 v27, 0x40e00000, v27
	v_pk_mul_f32 v[36:37], v[20:21], s[22:23] op_sel_hi:[1,0]
	v_pk_mul_f32 v[38:39], v[22:23], s[22:23] op_sel_hi:[1,0]
	v_pk_mul_f32 v[42:43], v[26:27], s[22:23] op_sel_hi:[1,0]
	v_exp_f32_e32 v36, v36
	v_exp_f32_e32 v37, v37
	v_exp_f32_e32 v38, v38
	v_exp_f32_e32 v42, v42
	v_exp_f32_e32 v39, v39
	v_exp_f32_e32 v43, v43
	v_pk_add_f32 v[36:37], v[36:37], 1.0 op_sel_hi:[1,0]
	v_min_f32_e32 v24, 0x40e00000, v24
	v_pk_add_f32 v[38:39], v[38:39], 1.0 op_sel_hi:[1,0]
	v_pk_add_f32 v[42:43], v[42:43], 1.0 op_sel_hi:[1,0]
	v_rcp_f32_e32 v36, v36
	v_rcp_f32_e32 v37, v37
	v_min_f32_e32 v25, 0x40e00000, v25
	v_rcp_f32_e32 v38, v38
	v_rcp_f32_e32 v42, v42
	v_rcp_f32_e32 v39, v39
	v_rcp_f32_e32 v43, v43
	v_pk_mul_f32 v[40:41], v[24:25], s[22:23] op_sel_hi:[1,0]
	v_pk_fma_f32 v[28:29], v[156:157], s[20:21], v[12:13] op_sel_hi:[1,0,1]
	v_exp_f32_e32 v40, v40
	v_exp_f32_e32 v41, v41
	v_pk_fma_f32 v[30:31], v[154:155], s[20:21], v[14:15] op_sel_hi:[1,0,1]
	v_pk_fma_f32 v[34:35], v[150:151], s[20:21], v[18:19] op_sel_hi:[1,0,1]
	v_med3_f32 v28, v28, s54, v235
	v_med3_f32 v29, v29, s54, v235
	v_pk_mul_f32 v[20:21], v[20:21], v[36:37]
	v_med3_f32 v30, v30, s54, v235
	v_med3_f32 v34, v34, s54, v235
	v_med3_f32 v31, v31, s54, v235
	v_med3_f32 v35, v35, s54, v235
	v_pk_mul_f32 v[22:23], v[22:23], v[38:39]
	v_pk_mul_f32 v[28:29], v[28:29], v[20:21]
	v_pk_mul_f32 v[20:21], v[26:27], v[42:43]
	v_pk_mul_f32 v[22:23], v[30:31], v[22:23]
	v_pk_mul_f32 v[26:27], v[34:35], v[20:21]
	v_pk_add_f32 v[40:41], v[40:41], 1.0 op_sel_hi:[1,0]
	v_cvt_pk_fp8_f32 v20, v22, v23
	v_rcp_f32_e32 v40, v40
	v_rcp_f32_e32 v41, v41
	v_pk_fma_f32 v[32:33], v[152:153], s[20:21], v[16:17] op_sel_hi:[1,0,1]
	v_cvt_pk_fp8_f32 v20, v28, v29 op_sel:[0,0,1]
	v_pk_fma_f32 v[28:29], v[146:147], s[20:21], v[6:7] op_sel_hi:[1,0,1]
	v_med3_f32 v32, v32, s54, v235
	v_med3_f32 v33, v33, s54, v235
	v_pk_mul_f32 v[22:23], v[24:25], v[40:41]
	v_min_f32_e32 v28, 0x40e00000, v28
	v_min_f32_e32 v29, 0x40e00000, v29
	v_pk_mul_f32 v[22:23], v[32:33], v[22:23]
	v_pk_mul_f32 v[32:33], v[28:29], s[22:23] op_sel_hi:[1,0]
	v_exp_f32_e32 v32, v32
	v_exp_f32_e32 v33, v33
	v_cvt_pk_fp8_f32 v21, v26, v27
	v_pk_fma_f32 v[26:27], v[148:149], s[20:21], v[8:9] op_sel_hi:[1,0,1]
	v_pk_fma_f32 v[24:25], v[142:143], s[20:21], v[18:19] op_sel_hi:[1,0,1]
	v_min_f32_e32 v26, 0x40e00000, v26
	v_min_f32_e32 v27, 0x40e00000, v27
	v_pk_mul_f32 v[30:31], v[26:27], s[22:23] op_sel_hi:[1,0]
	v_pk_add_f32 v[32:33], v[32:33], 1.0 op_sel_hi:[1,0]
	v_exp_f32_e32 v30, v30
	v_exp_f32_e32 v31, v31
	v_rcp_f32_e32 v32, v32
	v_rcp_f32_e32 v33, v33
	v_cvt_pk_fp8_f32 v21, v22, v23 op_sel:[0,0,1]
	v_pk_fma_f32 v[22:23], v[144:145], s[20:21], v[16:17] op_sel_hi:[1,0,1]
	v_pk_add_f32 v[30:31], v[30:31], 1.0 op_sel_hi:[1,0]
	v_med3_f32 v34, v22, s54, v235
	v_rcp_f32_e32 v30, v30
	v_rcp_f32_e32 v31, v31
	v_med3_f32 v35, v23, s54, v235
	v_pk_mul_f32 v[22:23], v[28:29], v[32:33]
	v_pk_fma_f32 v[32:33], v[138:139], s[20:21], v[2:3] op_sel_hi:[1,0,1]
	v_pk_mul_f32 v[26:27], v[26:27], v[30:31]
	v_min_f32_e32 v32, 0x40e00000, v32
	v_min_f32_e32 v33, 0x40e00000, v33
	v_pk_mul_f32 v[36:37], v[32:33], s[22:23] op_sel_hi:[1,0]
	v_pk_fma_f32 v[30:31], v[140:141], s[20:21], v[4:5] op_sel_hi:[1,0,1]
	v_exp_f32_e32 v36, v36
	v_exp_f32_e32 v37, v37
	v_min_f32_e32 v30, 0x40e00000, v30
	v_min_f32_e32 v31, 0x40e00000, v31
	v_pk_mul_f32 v[38:39], v[30:31], s[22:23] op_sel_hi:[1,0]
	v_pk_add_f32 v[36:37], v[36:37], 1.0 op_sel_hi:[1,0]
	v_exp_f32_e32 v38, v38
	v_exp_f32_e32 v39, v39
	v_rcp_f32_e32 v36, v36
	v_rcp_f32_e32 v37, v37
	v_pk_fma_f32 v[28:29], v[134:135], s[20:21], v[14:15] op_sel_hi:[1,0,1]
	v_pk_add_f32 v[38:39], v[38:39], 1.0 op_sel_hi:[1,0]
	v_med3_f32 v24, v24, s54, v235
	v_med3_f32 v25, v25, s54, v235
	v_med3_f32 v28, v28, s54, v235
	v_med3_f32 v29, v29, s54, v235
	v_rcp_f32_e32 v38, v38
	v_rcp_f32_e32 v39, v39
	v_pk_mul_f32 v[32:33], v[32:33], v[36:37]
	v_pk_mul_f32 v[24:25], v[24:25], v[22:23]
	v_pk_mul_f32 v[28:29], v[28:29], v[32:33]
	v_cvt_pk_fp8_f32 v22, v28, v29
	v_cvt_pk_fp8_f32 v23, v24, v25
	v_pk_fma_f32 v[24:25], v[136:137], s[20:21], v[12:13] op_sel_hi:[1,0,1]
	v_pk_mul_f32 v[28:29], v[30:31], v[38:39]
	v_med3_f32 v24, v24, s54, v235
	v_med3_f32 v25, v25, s54, v235
	v_pk_mul_f32 v[24:25], v[24:25], v[28:29]
	v_pk_fma_f32 v[28:29], v[124:125], s[20:21], v[12:13] op_sel_hi:[1,0,1]
	v_cvt_pk_fp8_f32 v22, v24, v25 op_sel:[0,0,1]
	v_pk_mul_f32 v[24:25], v[34:35], v[26:27]
	v_pk_fma_f32 v[26:27], v[126:127], s[20:21], v[6:7] op_sel_hi:[1,0,1]
	v_cvt_pk_fp8_f32 v23, v24, v25 op_sel:[0,0,1]
	v_or_b32_e32 v24, v44, v230
	v_ashrrev_i32_e32 v25, 31, v24
	v_lshlrev_b64 v[24:25], 11, v[24:25]
	v_lshl_add_u64 v[24:25], s[14:15], 0, v[24:25]
	v_lshl_add_u64 v[24:25], v[24:25], 0, v[10:11]
	v_permlane16_swap_b32_e32 v20, v22
	v_permlane16_swap_b32_e32 v21, v23
	v_lshl_add_u64 v[24:25], v[24:25], 0, v[204:205]
	global_store_dwordx4 v[24:25], v[20:23], off
	v_min_f32_e32 v26, 0x40e00000, v26
	v_min_f32_e32 v27, 0x40e00000, v27
	v_pk_fma_f32 v[20:21], v[132:133], s[20:21], v[4:5] op_sel_hi:[1,0,1]
	v_pk_fma_f32 v[22:23], v[130:131], s[20:21], v[2:3] op_sel_hi:[1,0,1]
	v_min_f32_e32 v20, 0x40e00000, v20
	v_min_f32_e32 v21, 0x40e00000, v21
	v_min_f32_e32 v22, 0x40e00000, v22
	v_min_f32_e32 v23, 0x40e00000, v23
	v_pk_mul_f32 v[36:37], v[20:21], s[22:23] op_sel_hi:[1,0]
	v_pk_mul_f32 v[38:39], v[22:23], s[22:23] op_sel_hi:[1,0]
	v_pk_mul_f32 v[42:43], v[26:27], s[22:23] op_sel_hi:[1,0]
	v_exp_f32_e32 v36, v36
	v_exp_f32_e32 v37, v37
	v_exp_f32_e32 v38, v38
	v_exp_f32_e32 v42, v42
	v_exp_f32_e32 v39, v39
	v_exp_f32_e32 v43, v43
	v_pk_add_f32 v[36:37], v[36:37], 1.0 op_sel_hi:[1,0]
	v_pk_fma_f32 v[24:25], v[128:129], s[20:21], v[8:9] op_sel_hi:[1,0,1]
	v_pk_add_f32 v[38:39], v[38:39], 1.0 op_sel_hi:[1,0]
	v_pk_add_f32 v[42:43], v[42:43], 1.0 op_sel_hi:[1,0]
	v_rcp_f32_e32 v36, v36
	v_rcp_f32_e32 v37, v37
	v_min_f32_e32 v24, 0x40e00000, v24
	v_min_f32_e32 v25, 0x40e00000, v25
	v_rcp_f32_e32 v38, v38
	v_rcp_f32_e32 v42, v42
	v_rcp_f32_e32 v39, v39
	v_rcp_f32_e32 v43, v43
	v_pk_mul_f32 v[40:41], v[24:25], s[22:23] op_sel_hi:[1,0]
	v_pk_fma_f32 v[30:31], v[122:123], s[20:21], v[14:15] op_sel_hi:[1,0,1]
	v_exp_f32_e32 v40, v40
	v_exp_f32_e32 v41, v41
	v_pk_fma_f32 v[34:35], v[118:119], s[20:21], v[18:19] op_sel_hi:[1,0,1]
	v_med3_f32 v28, v28, s54, v235
	v_med3_f32 v29, v29, s54, v235
	v_pk_mul_f32 v[20:21], v[20:21], v[36:37]
	v_med3_f32 v30, v30, s54, v235
	v_med3_f32 v34, v34, s54, v235
	v_med3_f32 v31, v31, s54, v235
	v_med3_f32 v35, v35, s54, v235
	v_pk_mul_f32 v[22:23], v[22:23], v[38:39]
	v_pk_mul_f32 v[28:29], v[28:29], v[20:21]
	v_pk_mul_f32 v[20:21], v[26:27], v[42:43]
	v_pk_mul_f32 v[22:23], v[30:31], v[22:23]
	v_pk_mul_f32 v[26:27], v[34:35], v[20:21]
	v_pk_add_f32 v[40:41], v[40:41], 1.0 op_sel_hi:[1,0]
	v_cvt_pk_fp8_f32 v20, v22, v23
	v_rcp_f32_e32 v40, v40
	v_rcp_f32_e32 v41, v41
	v_pk_fma_f32 v[32:33], v[120:121], s[20:21], v[16:17] op_sel_hi:[1,0,1]
	v_cvt_pk_fp8_f32 v20, v28, v29 op_sel:[0,0,1]
	v_pk_fma_f32 v[28:29], v[114:115], s[20:21], v[6:7] op_sel_hi:[1,0,1]
	v_med3_f32 v32, v32, s54, v235
	v_med3_f32 v33, v33, s54, v235
	v_pk_mul_f32 v[22:23], v[24:25], v[40:41]
	v_min_f32_e32 v28, 0x40e00000, v28
	v_min_f32_e32 v29, 0x40e00000, v29
	v_pk_mul_f32 v[22:23], v[32:33], v[22:23]
	v_pk_mul_f32 v[32:33], v[28:29], s[22:23] op_sel_hi:[1,0]
	v_exp_f32_e32 v32, v32
	v_exp_f32_e32 v33, v33
	v_cvt_pk_fp8_f32 v21, v26, v27
	v_pk_fma_f32 v[26:27], v[116:117], s[20:21], v[8:9] op_sel_hi:[1,0,1]
	v_pk_fma_f32 v[24:25], v[110:111], s[20:21], v[18:19] op_sel_hi:[1,0,1]
	v_min_f32_e32 v26, 0x40e00000, v26
	v_min_f32_e32 v27, 0x40e00000, v27
	v_pk_mul_f32 v[30:31], v[26:27], s[22:23] op_sel_hi:[1,0]
	v_pk_add_f32 v[32:33], v[32:33], 1.0 op_sel_hi:[1,0]
	v_exp_f32_e32 v30, v30
	v_exp_f32_e32 v31, v31
	v_rcp_f32_e32 v32, v32
	v_rcp_f32_e32 v33, v33
	v_cvt_pk_fp8_f32 v21, v22, v23 op_sel:[0,0,1]
	v_pk_fma_f32 v[22:23], v[112:113], s[20:21], v[16:17] op_sel_hi:[1,0,1]
	v_pk_add_f32 v[30:31], v[30:31], 1.0 op_sel_hi:[1,0]
	v_med3_f32 v34, v22, s54, v235
	v_rcp_f32_e32 v30, v30
	v_rcp_f32_e32 v31, v31
	v_med3_f32 v35, v23, s54, v235
	v_pk_mul_f32 v[22:23], v[28:29], v[32:33]
	v_pk_fma_f32 v[32:33], v[106:107], s[20:21], v[2:3] op_sel_hi:[1,0,1]
	v_pk_mul_f32 v[26:27], v[26:27], v[30:31]
	v_min_f32_e32 v32, 0x40e00000, v32
	v_min_f32_e32 v33, 0x40e00000, v33
	v_pk_mul_f32 v[36:37], v[32:33], s[22:23] op_sel_hi:[1,0]
	v_pk_fma_f32 v[30:31], v[108:109], s[20:21], v[4:5] op_sel_hi:[1,0,1]
	v_exp_f32_e32 v36, v36
	v_exp_f32_e32 v37, v37
	v_min_f32_e32 v30, 0x40e00000, v30
	v_min_f32_e32 v31, 0x40e00000, v31
	v_pk_mul_f32 v[38:39], v[30:31], s[22:23] op_sel_hi:[1,0]
	v_pk_add_f32 v[36:37], v[36:37], 1.0 op_sel_hi:[1,0]
	v_exp_f32_e32 v38, v38
	v_exp_f32_e32 v39, v39
	v_rcp_f32_e32 v36, v36
	v_rcp_f32_e32 v37, v37
	v_pk_fma_f32 v[28:29], v[102:103], s[20:21], v[14:15] op_sel_hi:[1,0,1]
	v_pk_add_f32 v[38:39], v[38:39], 1.0 op_sel_hi:[1,0]
	v_med3_f32 v24, v24, s54, v235
	v_med3_f32 v25, v25, s54, v235
	v_med3_f32 v28, v28, s54, v235
	v_med3_f32 v29, v29, s54, v235
	v_rcp_f32_e32 v38, v38
	v_rcp_f32_e32 v39, v39
	v_pk_mul_f32 v[32:33], v[32:33], v[36:37]
	v_pk_mul_f32 v[24:25], v[24:25], v[22:23]
	v_pk_mul_f32 v[28:29], v[28:29], v[32:33]
	v_cvt_pk_fp8_f32 v22, v28, v29
	v_cvt_pk_fp8_f32 v23, v24, v25
	v_pk_fma_f32 v[24:25], v[104:105], s[20:21], v[12:13] op_sel_hi:[1,0,1]
	v_pk_mul_f32 v[28:29], v[30:31], v[38:39]
	v_med3_f32 v24, v24, s54, v235
	v_med3_f32 v25, v25, s54, v235
	v_pk_mul_f32 v[24:25], v[24:25], v[28:29]
	v_add_u32_e32 v44, 0x80, v44
	v_cvt_pk_fp8_f32 v22, v24, v25 op_sel:[0,0,1]
	v_pk_mul_f32 v[24:25], v[34:35], v[26:27]
	v_pk_fma_f32 v[26:27], v[90:91], s[20:21], v[6:7] op_sel_hi:[1,0,1]
	v_cvt_pk_fp8_f32 v23, v24, v25 op_sel:[0,0,1]
	v_or_b32_e32 v24, v44, v229
	v_ashrrev_i32_e32 v25, 31, v24
	v_lshlrev_b64 v[24:25], 11, v[24:25]
	v_lshl_add_u64 v[24:25], s[14:15], 0, v[24:25]
	v_lshl_add_u64 v[24:25], v[24:25], 0, v[10:11]
	v_permlane16_swap_b32_e32 v20, v22
	v_permlane16_swap_b32_e32 v21, v23
	v_lshl_add_u64 v[24:25], v[24:25], 0, v[204:205]
	global_store_dwordx4 v[24:25], v[20:23], off
	v_min_f32_e32 v26, 0x40e00000, v26
	v_min_f32_e32 v27, 0x40e00000, v27
	v_pk_fma_f32 v[20:21], v[100:101], s[20:21], v[4:5] op_sel_hi:[1,0,1]
	v_pk_fma_f32 v[22:23], v[98:99], s[20:21], v[2:3] op_sel_hi:[1,0,1]
	v_min_f32_e32 v20, 0x40e00000, v20
	v_min_f32_e32 v21, 0x40e00000, v21
	v_pk_mul_f32 v[36:37], v[20:21], s[22:23] op_sel_hi:[1,0]
	v_pk_mul_f32 v[42:43], v[26:27], s[22:23] op_sel_hi:[1,0]
	v_exp_f32_e32 v36, v36
	v_exp_f32_e32 v37, v37
	v_min_f32_e32 v22, 0x40e00000, v22
	v_min_f32_e32 v23, 0x40e00000, v23
	v_exp_f32_e32 v42, v42
	v_exp_f32_e32 v43, v43
	v_pk_fma_f32 v[24:25], v[92:93], s[20:21], v[8:9] op_sel_hi:[1,0,1]
	v_pk_mul_f32 v[38:39], v[22:23], s[22:23] op_sel_hi:[1,0]
	v_min_f32_e32 v24, 0x40e00000, v24
	v_min_f32_e32 v25, 0x40e00000, v25
	v_exp_f32_e32 v38, v38
	v_exp_f32_e32 v39, v39
	v_pk_mul_f32 v[40:41], v[24:25], s[22:23] op_sel_hi:[1,0]
	v_pk_add_f32 v[36:37], v[36:37], 1.0 op_sel_hi:[1,0]
	v_exp_f32_e32 v40, v40
	v_exp_f32_e32 v41, v41
	v_pk_add_f32 v[42:43], v[42:43], 1.0 op_sel_hi:[1,0]
	v_rcp_f32_e32 v36, v36
	v_rcp_f32_e32 v37, v37
	v_rcp_f32_e32 v42, v42
	v_rcp_f32_e32 v43, v43
	v_pk_add_f32 v[38:39], v[38:39], 1.0 op_sel_hi:[1,0]
	v_pk_fma_f32 v[28:29], v[96:97], s[20:21], v[12:13] op_sel_hi:[1,0,1]
	v_rcp_f32_e32 v38, v38
	v_rcp_f32_e32 v39, v39
	v_pk_fma_f32 v[34:35], v[86:87], s[20:21], v[18:19] op_sel_hi:[1,0,1]
	v_med3_f32 v28, v28, s54, v235
	v_med3_f32 v29, v29, s54, v235
	v_pk_add_f32 v[40:41], v[40:41], 1.0 op_sel_hi:[1,0]
	v_pk_mul_f32 v[20:21], v[20:21], v[36:37]
	v_med3_f32 v34, v34, s54, v235
	v_med3_f32 v35, v35, s54, v235
	v_rcp_f32_e32 v40, v40
	v_rcp_f32_e32 v41, v41
	v_pk_mul_f32 v[28:29], v[28:29], v[20:21]
	v_pk_mul_f32 v[20:21], v[26:27], v[42:43]
	v_pk_fma_f32 v[30:31], v[94:95], s[20:21], v[14:15] op_sel_hi:[1,0,1]
	v_pk_mul_f32 v[26:27], v[34:35], v[20:21]
	v_med3_f32 v30, v30, s54, v235
	v_med3_f32 v31, v31, s54, v235
	v_pk_mul_f32 v[22:23], v[22:23], v[38:39]
	v_cvt_pk_fp8_f32 v21, v26, v27
	v_pk_fma_f32 v[32:33], v[88:89], s[20:21], v[16:17] op_sel_hi:[1,0,1]
	v_pk_mul_f32 v[22:23], v[30:31], v[22:23]
	v_pk_fma_f32 v[6:7], v[78:79], s[20:21], v[6:7] op_sel_hi:[1,0,1]
	v_med3_f32 v32, v32, s54, v235
	v_med3_f32 v33, v33, s54, v235
	v_cvt_pk_fp8_f32 v20, v22, v23
	v_pk_mul_f32 v[22:23], v[24:25], v[40:41]
	v_pk_fma_f32 v[8:9], v[80:81], s[20:21], v[8:9] op_sel_hi:[1,0,1]
	v_min_f32_e32 v6, 0x40e00000, v6
	v_min_f32_e32 v7, 0x40e00000, v7
	v_pk_mul_f32 v[22:23], v[32:33], v[22:23]
	v_min_f32_e32 v8, 0x40e00000, v8
	v_min_f32_e32 v9, 0x40e00000, v9
	v_pk_mul_f32 v[24:25], v[6:7], s[22:23] op_sel_hi:[1,0]
	v_cvt_pk_fp8_f32 v21, v22, v23 op_sel:[0,0,1]
	v_pk_mul_f32 v[22:23], v[8:9], s[22:23] op_sel_hi:[1,0]
	v_exp_f32_e32 v24, v24
	v_exp_f32_e32 v25, v25
	v_exp_f32_e32 v22, v22
	v_exp_f32_e32 v23, v23
	v_pk_fma_f32 v[18:19], v[82:83], s[20:21], v[18:19] op_sel_hi:[1,0,1]
	v_pk_add_f32 v[24:25], v[24:25], 1.0 op_sel_hi:[1,0]
	v_med3_f32 v18, v18, s54, v235
	v_pk_add_f32 v[22:23], v[22:23], 1.0 op_sel_hi:[1,0]
	v_rcp_f32_e32 v24, v24
	v_rcp_f32_e32 v25, v25
	v_rcp_f32_e32 v22, v22
	v_rcp_f32_e32 v23, v23
	v_med3_f32 v19, v19, s54, v235
	v_pk_mul_f32 v[6:7], v[6:7], v[24:25]
	v_pk_fma_f32 v[2:3], v[70:71], s[20:21], v[2:3] op_sel_hi:[1,0,1]
	v_pk_mul_f32 v[8:9], v[8:9], v[22:23]
	v_pk_mul_f32 v[6:7], v[18:19], v[6:7]
	v_min_f32_e32 v2, 0x40e00000, v2
	v_min_f32_e32 v3, 0x40e00000, v3
	v_cvt_pk_fp8_f32 v23, v6, v7
	v_pk_fma_f32 v[6:7], v[76:77], s[20:21], v[12:13] op_sel_hi:[1,0,1]
	v_pk_fma_f32 v[12:13], v[74:75], s[20:21], v[14:15] op_sel_hi:[1,0,1]
	v_pk_mul_f32 v[14:15], v[2:3], s[22:23] op_sel_hi:[1,0]
	v_pk_fma_f32 v[4:5], v[72:73], s[20:21], v[4:5] op_sel_hi:[1,0,1]
	v_exp_f32_e32 v14, v14
	v_exp_f32_e32 v15, v15
	v_min_f32_e32 v4, 0x40e00000, v4
	v_min_f32_e32 v5, 0x40e00000, v5
	v_pk_mul_f32 v[18:19], v[4:5], s[22:23] op_sel_hi:[1,0]
	v_pk_add_f32 v[14:15], v[14:15], 1.0 op_sel_hi:[1,0]
	v_exp_f32_e32 v18, v18
	v_exp_f32_e32 v19, v19
	v_rcp_f32_e32 v14, v14
	v_rcp_f32_e32 v15, v15
	v_med3_f32 v12, v12, s54, v235
	v_pk_add_f32 v[18:19], v[18:19], 1.0 op_sel_hi:[1,0]
	v_med3_f32 v13, v13, s54, v235
	v_rcp_f32_e32 v18, v18
	v_rcp_f32_e32 v19, v19
	v_pk_mul_f32 v[2:3], v[2:3], v[14:15]
	v_pk_mul_f32 v[2:3], v[12:13], v[2:3]
	v_pk_fma_f32 v[16:17], v[84:85], s[20:21], v[16:17] op_sel_hi:[1,0,1]
	v_cvt_pk_fp8_f32 v22, v2, v3
	v_med3_f32 v6, v6, s54, v235
	v_med3_f32 v7, v7, s54, v235
	v_pk_mul_f32 v[2:3], v[4:5], v[18:19]
	v_med3_f32 v16, v16, s54, v235
	v_med3_f32 v17, v17, s54, v235
	v_pk_mul_f32 v[2:3], v[6:7], v[2:3]
	v_cvt_pk_fp8_f32 v20, v28, v29 op_sel:[0,0,1]
	v_cvt_pk_fp8_f32 v22, v2, v3 op_sel:[0,0,1]
	v_pk_mul_f32 v[2:3], v[16:17], v[8:9]
	s_mov_b64 s[6:7], -1
	v_cvt_pk_fp8_f32 v23, v2, v3 op_sel:[0,0,1]
	v_or_b32_e32 v2, v44, v230
	v_ashrrev_i32_e32 v3, 31, v2
	v_lshlrev_b64 v[2:3], 11, v[2:3]
	v_lshl_add_u64 v[2:3], s[14:15], 0, v[2:3]
	v_lshl_add_u64 v[2:3], v[2:3], 0, v[10:11]
	v_permlane16_swap_b32_e32 v20, v22
	v_permlane16_swap_b32_e32 v21, v23
	v_lshl_add_u64 v[2:3], v[2:3], 0, v[204:205]
	global_store_dwordx4 v[2:3], v[20:23], off
	s_cbranch_vccnz .LBB0_944
	s_andn2_b64 vcc, exec, s[0:1]
	s_cbranch_vccnz .LBB0_943
	s_barrier
	s_branch .LBB0_943

.LBB0_1132:
	s_lshl_b32 s8, s59, 11
	s_and_b32 s8, s8, 0x800
	s_add_i32 s8, s8, 0
	s_add_i32 s9, s62, 0x25100
	s_add_i32 s8, s8, 0x25500
	v_mov_b32_e32 v2, s9
	s_lshl_b32 s9, s50, 2
	s_nop 11
	s_add_i32 s9, s8, s9
	v_lshl_add_u32 v4, v226, 2, s8
	v_lshl_add_u32 v3, v227, 2, s9
	ds_read_b32 v23, v2
	ds_read_b128 v[10:13], v3
	v_mov_b32_e32 v2, s61
	v_add_u32_e32 v22, 0x400, v4
	ds_read2_b32 v[18:19], v22 offset1:16
	ds_read_b128 v[6:9], v3 offset:528
	ds_read_b32 v25, v2
	ds_read_b128 v[14:17], v3 offset:16
	ds_read_b128 v[2:5], v3 offset:512
	v_add_u32_e32 v20, s60, v226
	s_waitcnt lgkmcnt(0)
	v_mul_f32_e32 v18, 0x41800000, v18
	v_cmp_lt_i32_e32 vcc, v20, v25
	ds_read2_b32 v[20:21], v22 offset0:32 offset1:48
	v_mul_f32_e32 v19, 0x41800000, v19
	v_cndmask_b32_e32 v32, 0, v18, vcc
	v_add_u32_e32 v18, s60, v229
	v_cmp_lt_i32_e32 vcc, v18, v25
	v_add_u32_e32 v18, s60, v230
	v_pk_fma_f32 v[30:31], v[196:197], s[16:17], v[12:13] op_sel_hi:[1,0,1]
	v_cndmask_b32_e32 v38, 0, v19, vcc
	s_waitcnt lgkmcnt(0)
	v_mul_f32_e32 v19, 0x41800000, v20
	v_cmp_lt_i32_e32 vcc, v18, v25
	v_pk_mul_f32 v[36:37], v[30:31], v[32:33] op_sel_hi:[1,0]
	v_pk_fma_f32 v[30:31], v[190:191], s[16:17], v[14:15] op_sel_hi:[1,0,1]
	v_cndmask_b32_e32 v40, 0, v19, vcc
	ds_read2_b32 v[18:19], v22 offset0:128 offset1:144
	v_pk_mul_f32 v[42:43], v[30:31], v[32:33] op_sel_hi:[1,0]
	v_add_u32_e32 v20, s60, v231
	v_pk_fma_f32 v[34:35], v[194:195], s[16:17], v[10:11] op_sel_hi:[1,0,1]
	v_cvt_pk_fp8_f32 v31, v42, v43
	v_mul_f32_e32 v21, 0x41800000, v21
	v_cmp_lt_i32_e32 vcc, v20, v25
	v_add_u32_e32 v20, s60, v232
	v_pk_mul_f32 v[34:35], v[34:35], v[32:33] op_sel_hi:[1,0]
	v_cndmask_b32_e32 v28, 0, v21, vcc
	v_cmp_lt_i32_e32 vcc, v20, v25
	ds_read2_b32 v[20:21], v22 offset0:160 offset1:176
	v_cvt_pk_fp8_f32 v30, v34, v35
	v_pk_fma_f32 v[34:35], v[192:193], s[16:17], v[16:17] op_sel_hi:[1,0,1]
	s_waitcnt lgkmcnt(0)
	v_mul_f32_e32 v18, 0x41800000, v18
	v_pk_mul_f32 v[34:35], v[34:35], v[32:33] op_sel_hi:[1,0]
	v_cndmask_b32_e32 v26, 0, v18, vcc
	v_cvt_pk_fp8_f32 v31, v34, v35 op_sel:[0,0,1]
	v_pk_fma_f32 v[34:35], v[188:189], s[16:17], v[4:5] op_sel_hi:[1,0,1]
	v_add_u32_e32 v18, s60, v233
	v_pk_mul_f32 v[42:43], v[34:35], v[32:33] op_sel_hi:[1,0]
	v_pk_fma_f32 v[34:35], v[178:179], s[16:17], v[6:7] op_sel_hi:[1,0,1]
	v_mul_f32_e32 v19, 0x41800000, v19
	v_cmp_lt_i32_e32 vcc, v18, v25
	v_add_u32_e32 v18, s60, v234
	v_pk_mul_f32 v[44:45], v[34:35], v[32:33] op_sel_hi:[1,0]
	v_cndmask_b32_e32 v24, 0, v19, vcc
	v_mul_f32_e32 v19, 0x41800000, v20
	v_cmp_lt_i32_e32 vcc, v18, v25
	v_add_u32_e32 v18, s60, v235
	v_cvt_pk_fp8_f32 v30, v36, v37 op_sel:[0,0,1]
	v_pk_fma_f32 v[36:37], v[186:187], s[16:17], v[2:3] op_sel_hi:[1,0,1]
	v_cvt_pk_fp8_f32 v35, v44, v45
	v_cndmask_b32_e32 v22, 0, v19, vcc
	v_mul_f32_e32 v19, 0x41800000, v21
	v_cmp_lt_i32_e32 vcc, v18, v25
	v_pk_mul_f32 v[36:37], v[36:37], v[32:33] op_sel_hi:[1,0]
	s_nop 0
	v_cndmask_b32_e32 v18, 0, v19, vcc
	v_add_u32_e32 v19, s58, v23
	v_cvt_pk_fp8_f32 v34, v36, v37
	v_pk_fma_f32 v[36:37], v[180:181], s[16:17], v[8:9] op_sel_hi:[1,0,1]
	v_lshl_add_u32 v19, v19, 8, v226
	v_pk_mul_f32 v[32:33], v[36:37], v[32:33] op_sel_hi:[1,0]
	v_pk_fma_f32 v[46:47], v[174:175], s[16:17], v[10:11] op_sel_hi:[1,0,1]
	v_cvt_pk_fp8_f32 v35, v32, v33 op_sel:[0,0,1]
	v_or_b32_e32 v32, v19, v236
	v_ashrrev_i32_e32 v33, 31, v32
	v_lshlrev_b64 v[36:37], 11, v[32:33]
	v_pk_fma_f32 v[32:33], v[182:183], s[16:17], v[14:15] op_sel_hi:[1,0,1]
	v_pk_mul_f32 v[46:47], v[46:47], v[38:39] op_sel_hi:[1,0]
	v_pk_mul_f32 v[44:45], v[32:33], v[38:39] op_sel_hi:[1,0]
	v_cvt_pk_fp8_f32 v32, v46, v47
	v_cvt_pk_fp8_f32 v33, v44, v45
	v_cvt_pk_fp8_f32 v34, v42, v43 op_sel:[0,0,1]
	v_pk_fma_f32 v[42:43], v[184:185], s[16:17], v[16:17] op_sel_hi:[1,0,1]
	v_pk_fma_f32 v[44:45], v[176:177], s[16:17], v[12:13] op_sel_hi:[1,0,1]
	v_pk_mul_f32 v[42:43], v[42:43], v[38:39] op_sel_hi:[1,0]
	v_pk_mul_f32 v[44:45], v[44:45], v[38:39] op_sel_hi:[1,0]
	v_cvt_pk_fp8_f32 v33, v42, v43 op_sel:[0,0,1]
	v_cvt_pk_fp8_f32 v32, v44, v45 op_sel:[0,0,1]
	v_lshl_or_b32 v20, s26, 8, v238
	v_ashrrev_i32_e32 v21, 31, v20
	v_lshl_add_u64 v[36:37], s[4:5], 0, v[36:37]
	v_lshl_add_u64 v[36:37], v[36:37], 0, v[20:21]
	v_permlane16_swap_b32_e32 v30, v32
	v_permlane16_swap_b32_e32 v31, v33
	v_lshl_add_u64 v[42:43], v[36:37], 0, v[214:215]
	global_store_dwordx4 v[42:43], v[30:33], off
	v_pk_fma_f32 v[44:45], v[162:163], s[16:17], v[2:3] op_sel_hi:[1,0,1]
	s_nop 0
	v_pk_fma_f32 v[32:33], v[170:171], s[16:17], v[6:7] op_sel_hi:[1,0,1]
	v_pk_mul_f32 v[44:45], v[44:45], v[38:39] op_sel_hi:[1,0]
	v_pk_mul_f32 v[32:33], v[32:33], v[38:39] op_sel_hi:[1,0]
	v_cvt_pk_fp8_f32 v36, v44, v45
	v_cvt_pk_fp8_f32 v37, v32, v33
	v_pk_fma_f32 v[30:31], v[172:173], s[16:17], v[8:9] op_sel_hi:[1,0,1]
	v_pk_fma_f32 v[32:33], v[164:165], s[16:17], v[4:5] op_sel_hi:[1,0,1]
	v_pk_mul_f32 v[30:31], v[30:31], v[38:39] op_sel_hi:[1,0]
	v_pk_mul_f32 v[32:33], v[32:33], v[38:39] op_sel_hi:[1,0]
	v_cvt_pk_fp8_f32 v37, v30, v31 op_sel:[0,0,1]
	v_cvt_pk_fp8_f32 v36, v32, v33 op_sel:[0,0,1]
	v_pk_fma_f32 v[30:31], v[168:169], s[16:17], v[12:13] op_sel_hi:[1,0,1]
	v_pk_fma_f32 v[32:33], v[166:167], s[16:17], v[10:11] op_sel_hi:[1,0,1]
	v_permlane16_swap_b32_e32 v35, v37
	v_permlane16_swap_b32_e32 v34, v36
	global_store_dwordx4 v[42:43], v[34:37], off offset:128
	v_pk_mul_f32 v[32:33], v[32:33], v[40:41] op_sel_hi:[1,0]
	v_pk_fma_f32 v[42:43], v[142:143], s[16:17], v[10:11] op_sel_hi:[1,0,1]
	v_pk_mul_f32 v[34:35], v[30:31], v[40:41] op_sel_hi:[1,0]
	v_pk_fma_f32 v[30:31], v[158:159], s[16:17], v[14:15] op_sel_hi:[1,0,1]
	v_pk_mul_f32 v[42:43], v[42:43], v[28:29] op_sel_hi:[1,0]
	v_pk_mul_f32 v[36:37], v[30:31], v[40:41] op_sel_hi:[1,0]
	v_cvt_pk_fp8_f32 v30, v32, v33
	v_cvt_pk_fp8_f32 v31, v36, v37
	v_pk_fma_f32 v[32:33], v[160:161], s[16:17], v[16:17] op_sel_hi:[1,0,1]
	v_cvt_pk_fp8_f32 v30, v34, v35 op_sel:[0,0,1]
	v_pk_fma_f32 v[34:35], v[154:155], s[16:17], v[2:3] op_sel_hi:[1,0,1]
	v_pk_mul_f32 v[32:33], v[32:33], v[40:41] op_sel_hi:[1,0]
	v_pk_mul_f32 v[36:37], v[34:35], v[40:41] op_sel_hi:[1,0]
	v_pk_fma_f32 v[34:35], v[146:147], s[16:17], v[6:7] op_sel_hi:[1,0,1]
	v_cvt_pk_fp8_f32 v31, v32, v33 op_sel:[0,0,1]
	v_pk_mul_f32 v[38:39], v[34:35], v[40:41] op_sel_hi:[1,0]
	v_cvt_pk_fp8_f32 v34, v36, v37
	v_pk_fma_f32 v[32:33], v[156:157], s[16:17], v[4:5] op_sel_hi:[1,0,1]
	v_cvt_pk_fp8_f32 v35, v38, v39
	v_pk_mul_f32 v[32:33], v[32:33], v[40:41] op_sel_hi:[1,0]
	v_pk_fma_f32 v[36:37], v[148:149], s[16:17], v[8:9] op_sel_hi:[1,0,1]
	v_cvt_pk_fp8_f32 v34, v32, v33 op_sel:[0,0,1]
	v_or_b32_e32 v32, v19, v237
	v_pk_mul_f32 v[36:37], v[36:37], v[40:41] op_sel_hi:[1,0]
	v_ashrrev_i32_e32 v33, 31, v32
	v_cvt_pk_fp8_f32 v35, v36, v37 op_sel:[0,0,1]
	v_lshlrev_b64 v[36:37], 11, v[32:33]
	v_pk_fma_f32 v[32:33], v[150:151], s[16:17], v[14:15] op_sel_hi:[1,0,1]
	v_pk_fma_f32 v[38:39], v[152:153], s[16:17], v[16:17] op_sel_hi:[1,0,1]
	v_pk_mul_f32 v[40:41], v[32:33], v[28:29] op_sel_hi:[1,0]
	v_cvt_pk_fp8_f32 v32, v42, v43
	v_cvt_pk_fp8_f32 v33, v40, v41
	v_pk_fma_f32 v[40:41], v[144:145], s[16:17], v[12:13] op_sel_hi:[1,0,1]
	v_pk_mul_f32 v[38:39], v[38:39], v[28:29] op_sel_hi:[1,0]
	v_pk_mul_f32 v[40:41], v[40:41], v[28:29] op_sel_hi:[1,0]
	v_cvt_pk_fp8_f32 v33, v38, v39 op_sel:[0,0,1]
	v_cvt_pk_fp8_f32 v32, v40, v41 op_sel:[0,0,1]
	v_lshl_add_u64 v[36:37], s[4:5], 0, v[36:37]
	v_lshl_add_u64 v[36:37], v[36:37], 0, v[20:21]
	v_permlane16_swap_b32_e32 v31, v33
	v_permlane16_swap_b32_e32 v30, v32
	v_lshl_add_u64 v[38:39], v[36:37], 0, v[214:215]
	global_store_dwordx4 v[38:39], v[30:33], off
	v_pk_fma_f32 v[40:41], v[138:139], s[16:17], v[2:3] op_sel_hi:[1,0,1]
	s_nop 0
	v_pk_fma_f32 v[32:33], v[134:135], s[16:17], v[6:7] op_sel_hi:[1,0,1]
	v_pk_mul_f32 v[40:41], v[40:41], v[28:29] op_sel_hi:[1,0]
	v_pk_mul_f32 v[32:33], v[32:33], v[28:29] op_sel_hi:[1,0]
	v_cvt_pk_fp8_f32 v36, v40, v41
	v_cvt_pk_fp8_f32 v37, v32, v33
	v_pk_fma_f32 v[30:31], v[136:137], s[16:17], v[8:9] op_sel_hi:[1,0,1]
	v_pk_fma_f32 v[32:33], v[140:141], s[16:17], v[4:5] op_sel_hi:[1,0,1]
	v_add_u32_e32 v19, 0x80, v19
	v_pk_mul_f32 v[32:33], v[32:33], v[28:29] op_sel_hi:[1,0]
	v_pk_mul_f32 v[28:29], v[30:31], v[28:29] op_sel_hi:[1,0]
	v_cvt_pk_fp8_f32 v36, v32, v33 op_sel:[0,0,1]
	v_cvt_pk_fp8_f32 v37, v28, v29 op_sel:[0,0,1]
	v_pk_fma_f32 v[28:29], v[132:133], s[16:17], v[12:13] op_sel_hi:[1,0,1]
	v_pk_fma_f32 v[30:31], v[130:131], s[16:17], v[10:11] op_sel_hi:[1,0,1]
	v_permlane16_swap_b32_e32 v34, v36
	v_permlane16_swap_b32_e32 v35, v37
	v_pk_mul_f32 v[32:33], v[28:29], v[26:27] op_sel_hi:[1,0]
	v_pk_fma_f32 v[28:29], v[126:127], s[16:17], v[14:15] op_sel_hi:[1,0,1]
	global_store_dwordx4 v[38:39], v[34:37], off offset:128
	v_pk_mul_f32 v[30:31], v[30:31], v[26:27] op_sel_hi:[1,0]
	v_pk_fma_f32 v[38:39], v[110:111], s[16:17], v[10:11] op_sel_hi:[1,0,1]
	v_pk_mul_f32 v[34:35], v[28:29], v[26:27] op_sel_hi:[1,0]
	v_cvt_pk_fp8_f32 v28, v30, v31
	v_cvt_pk_fp8_f32 v29, v34, v35
	v_pk_fma_f32 v[30:31], v[128:129], s[16:17], v[16:17] op_sel_hi:[1,0,1]
	v_cvt_pk_fp8_f32 v28, v32, v33 op_sel:[0,0,1]
	v_pk_fma_f32 v[32:33], v[122:123], s[16:17], v[2:3] op_sel_hi:[1,0,1]
	v_pk_mul_f32 v[30:31], v[30:31], v[26:27] op_sel_hi:[1,0]
	v_pk_mul_f32 v[34:35], v[32:33], v[26:27] op_sel_hi:[1,0]
	v_pk_fma_f32 v[32:33], v[118:119], s[16:17], v[6:7] op_sel_hi:[1,0,1]
	v_cvt_pk_fp8_f32 v29, v30, v31 op_sel:[0,0,1]
	v_pk_mul_f32 v[36:37], v[32:33], v[26:27] op_sel_hi:[1,0]
	v_cvt_pk_fp8_f32 v32, v34, v35
	v_pk_fma_f32 v[30:31], v[124:125], s[16:17], v[4:5] op_sel_hi:[1,0,1]
	v_pk_mul_f32 v[30:31], v[30:31], v[26:27] op_sel_hi:[1,0]
	v_cvt_pk_fp8_f32 v33, v36, v37
	v_cvt_pk_fp8_f32 v32, v30, v31 op_sel:[0,0,1]
	v_pk_fma_f32 v[30:31], v[114:115], s[16:17], v[14:15] op_sel_hi:[1,0,1]
	v_pk_mul_f32 v[38:39], v[38:39], v[24:25] op_sel_hi:[1,0]
	v_pk_mul_f32 v[36:37], v[30:31], v[24:25] op_sel_hi:[1,0]
	v_cvt_pk_fp8_f32 v30, v38, v39
	v_cvt_pk_fp8_f32 v31, v36, v37
	v_pk_fma_f32 v[34:35], v[120:121], s[16:17], v[8:9] op_sel_hi:[1,0,1]
	v_pk_fma_f32 v[36:37], v[112:113], s[16:17], v[12:13] op_sel_hi:[1,0,1]
	v_pk_mul_f32 v[26:27], v[34:35], v[26:27] op_sel_hi:[1,0]
	v_pk_fma_f32 v[34:35], v[116:117], s[16:17], v[16:17] op_sel_hi:[1,0,1]
	v_cvt_pk_fp8_f32 v33, v26, v27 op_sel:[0,0,1]
	v_or_b32_e32 v26, v19, v236
	v_pk_mul_f32 v[36:37], v[36:37], v[24:25] op_sel_hi:[1,0]
	v_pk_mul_f32 v[34:35], v[34:35], v[24:25] op_sel_hi:[1,0]
	v_ashrrev_i32_e32 v27, 31, v26
	v_cvt_pk_fp8_f32 v30, v36, v37 op_sel:[0,0,1]
	v_cvt_pk_fp8_f32 v31, v34, v35 op_sel:[0,0,1]
	v_lshlrev_b64 v[26:27], 11, v[26:27]
	v_lshl_add_u64 v[26:27], s[4:5], 0, v[26:27]
	v_lshl_add_u64 v[26:27], v[26:27], 0, v[20:21]
	v_permlane16_swap_b32_e32 v28, v30
	v_permlane16_swap_b32_e32 v29, v31
	v_lshl_add_u64 v[26:27], v[26:27], 0, v[214:215]
	global_store_dwordx4 v[26:27], v[28:31], off
	v_pk_fma_f32 v[36:37], v[102:103], s[16:17], v[2:3] op_sel_hi:[1,0,1]
	s_nop 0
	v_pk_fma_f32 v[30:31], v[106:107], s[16:17], v[6:7] op_sel_hi:[1,0,1]
	v_pk_mul_f32 v[36:37], v[36:37], v[24:25] op_sel_hi:[1,0]
	v_pk_mul_f32 v[30:31], v[30:31], v[24:25] op_sel_hi:[1,0]
	v_cvt_pk_fp8_f32 v34, v36, v37
	v_cvt_pk_fp8_f32 v35, v30, v31
	v_pk_fma_f32 v[28:29], v[108:109], s[16:17], v[8:9] op_sel_hi:[1,0,1]
	v_pk_fma_f32 v[30:31], v[104:105], s[16:17], v[4:5] op_sel_hi:[1,0,1]
	s_and_b64 vcc, exec, s[6:7]
	v_pk_mul_f32 v[30:31], v[30:31], v[24:25] op_sel_hi:[1,0]
	v_pk_mul_f32 v[24:25], v[28:29], v[24:25] op_sel_hi:[1,0]
	v_cvt_pk_fp8_f32 v34, v30, v31 op_sel:[0,0,1]
	v_cvt_pk_fp8_f32 v35, v24, v25 op_sel:[0,0,1]
	v_pk_fma_f32 v[24:25], v[100:101], s[16:17], v[12:13] op_sel_hi:[1,0,1]
	s_mov_b64 s[6:7], -1
	v_permlane16_swap_b32_e32 v32, v34
	v_permlane16_swap_b32_e32 v33, v35
	global_store_dwordx4 v[26:27], v[32:35], off offset:128
	v_pk_fma_f32 v[26:27], v[98:99], s[16:17], v[10:11] op_sel_hi:[1,0,1]
	v_pk_mul_f32 v[28:29], v[24:25], v[22:23] op_sel_hi:[1,0]
	v_pk_fma_f32 v[24:25], v[90:91], s[16:17], v[14:15] op_sel_hi:[1,0,1]
	v_pk_mul_f32 v[26:27], v[26:27], v[22:23] op_sel_hi:[1,0]
	v_pk_mul_f32 v[30:31], v[24:25], v[22:23] op_sel_hi:[1,0]
	v_cvt_pk_fp8_f32 v24, v26, v27
	v_cvt_pk_fp8_f32 v25, v30, v31
	v_pk_fma_f32 v[26:27], v[92:93], s[16:17], v[16:17] op_sel_hi:[1,0,1]
	v_cvt_pk_fp8_f32 v24, v28, v29 op_sel:[0,0,1]
	v_pk_fma_f32 v[28:29], v[94:95], s[16:17], v[2:3] op_sel_hi:[1,0,1]
	v_pk_mul_f32 v[26:27], v[26:27], v[22:23] op_sel_hi:[1,0]
	v_pk_mul_f32 v[30:31], v[28:29], v[22:23] op_sel_hi:[1,0]
	v_pk_fma_f32 v[28:29], v[86:87], s[16:17], v[6:7] op_sel_hi:[1,0,1]
	v_cvt_pk_fp8_f32 v25, v26, v27 op_sel:[0,0,1]
	v_pk_mul_f32 v[32:33], v[28:29], v[22:23] op_sel_hi:[1,0]
	v_cvt_pk_fp8_f32 v28, v30, v31
	v_pk_fma_f32 v[26:27], v[96:97], s[16:17], v[4:5] op_sel_hi:[1,0,1]
	v_pk_fma_f32 v[30:31], v[88:89], s[16:17], v[8:9] op_sel_hi:[1,0,1]
	v_pk_mul_f32 v[26:27], v[26:27], v[22:23] op_sel_hi:[1,0]
	v_pk_fma_f32 v[10:11], v[78:79], s[16:17], v[10:11] op_sel_hi:[1,0,1]
	v_pk_fma_f32 v[2:3], v[70:71], s[16:17], v[2:3] op_sel_hi:[1,0,1]
	v_pk_mul_f32 v[22:23], v[30:31], v[22:23] op_sel_hi:[1,0]
	v_cvt_pk_fp8_f32 v28, v26, v27 op_sel:[0,0,1]
	v_pk_fma_f32 v[14:15], v[82:83], s[16:17], v[14:15] op_sel_hi:[1,0,1]
	v_pk_mul_f32 v[10:11], v[10:11], v[18:19] op_sel_hi:[1,0]
	v_pk_fma_f32 v[6:7], v[74:75], s[16:17], v[6:7] op_sel_hi:[1,0,1]
	v_pk_mul_f32 v[2:3], v[2:3], v[18:19] op_sel_hi:[1,0]
	v_cvt_pk_fp8_f32 v29, v32, v33
	v_pk_mul_f32 v[14:15], v[14:15], v[18:19] op_sel_hi:[1,0]
	v_cvt_pk_fp8_f32 v26, v10, v11
	v_pk_mul_f32 v[6:7], v[6:7], v[18:19] op_sel_hi:[1,0]
	v_cvt_pk_fp8_f32 v30, v2, v3
	v_cvt_pk_fp8_f32 v27, v14, v15
	v_cvt_pk_fp8_f32 v31, v6, v7
	v_pk_fma_f32 v[10:11], v[80:81], s[16:17], v[12:13] op_sel_hi:[1,0,1]
	v_pk_fma_f32 v[2:3], v[72:73], s[16:17], v[4:5] op_sel_hi:[1,0,1]
	v_pk_fma_f32 v[16:17], v[84:85], s[16:17], v[16:17] op_sel_hi:[1,0,1]
	v_pk_mul_f32 v[10:11], v[10:11], v[18:19] op_sel_hi:[1,0]
	v_pk_fma_f32 v[8:9], v[76:77], s[16:17], v[8:9] op_sel_hi:[1,0,1]
	v_pk_mul_f32 v[2:3], v[2:3], v[18:19] op_sel_hi:[1,0]
	v_cvt_pk_fp8_f32 v29, v22, v23 op_sel:[0,0,1]
	v_or_b32_e32 v22, v19, v237
	v_cvt_pk_fp8_f32 v26, v10, v11 op_sel:[0,0,1]
	v_pk_mul_f32 v[10:11], v[16:17], v[18:19] op_sel_hi:[1,0]
	v_cvt_pk_fp8_f32 v30, v2, v3 op_sel:[0,0,1]
	v_pk_mul_f32 v[2:3], v[8:9], v[18:19] op_sel_hi:[1,0]
	v_ashrrev_i32_e32 v23, 31, v22
	v_cvt_pk_fp8_f32 v27, v10, v11 op_sel:[0,0,1]
	v_cvt_pk_fp8_f32 v31, v2, v3 op_sel:[0,0,1]
	v_lshlrev_b64 v[22:23], 11, v[22:23]
	v_lshl_add_u64 v[10:11], s[4:5], 0, v[22:23]
	v_lshl_add_u64 v[10:11], v[10:11], 0, v[20:21]
	v_permlane16_swap_b32_e32 v24, v26
	v_permlane16_swap_b32_e32 v25, v27
	v_lshl_add_u64 v[10:11], v[10:11], 0, v[214:215]
	v_permlane16_swap_b32_e32 v28, v30
	v_permlane16_swap_b32_e32 v29, v31
	global_store_dwordx4 v[10:11], v[24:27], off
	global_store_dwordx4 v[10:11], v[28:31], off offset:128
	s_cbranch_vccnz .LBB0_1109
	s_andn2_b64 vcc, exec, s[0:1]
	s_cbranch_vccnz .LBB0_1108
	s_barrier
	s_branch .LBB0_1108
